# fused-epilogue row-statistics shuffles (shfl_xor 16/32) via v_permlane16/32_swap instead of ds_bpermute round trips (324 sites, same sums)
# baseline (speedup 1.0000x reference)
.LBB0_502:
	v_mov_b32_e32 v0, v142
	s_nop 1
	v_permlane32_swap_b32_e32 v0, v142
	s_nop 2
	v_mov_b32_e32 v36, v2
	v_lshlrev_b64 v[34:35], 11, v[130:131]
	v_lshl_add_u64 v[34:35], v[128:129], 0, v[34:35]
	s_mov_b32 s5, 32
	s_waitcnt lgkmcnt(0)
	v_add_f32_e32 v0, v142, v0
	v_div_scale_f32 v2, s[8:9], v0, v0, 1.0
	v_rcp_f32_e32 v37, v2
	v_div_scale_f32 v38, vcc, 1.0, v0, 1.0
	s_mov_b64 s[22:23], 0
	v_fma_f32 v39, -v2, v37, 1.0
	v_fmac_f32_e32 v37, v39, v37
	v_mul_f32_e32 v39, v38, v37
	v_fma_f32 v40, -v2, v39, v38
	v_fmac_f32_e32 v39, v40, v37
	v_fma_f32 v2, -v2, v39, v38
	v_div_fmas_f32 v2, v2, v37, v39
	v_div_fixup_f32 v0, v2, v0, 1.0
	v_mov_b32_e32 v37, v4
	v_pk_mul_f32 v[36:37], v[36:37], v[0:1] op_sel_hi:[1,0]
	v_mov_b32_e32 v4, v3
	v_pk_mul_f32 v[2:3], v[4:5], v[0:1] op_sel_hi:[1,0]
	v_and_b32_sdwa v4, v37, v228 dst_sel:DWORD dst_unused:UNUSED_PAD src0_sel:WORD_1 src1_sel:DWORD
	v_and_b32_sdwa v5, v36, v228 dst_sel:DWORD dst_unused:UNUSED_PAD src0_sel:WORD_1 src1_sel:DWORD
	v_add3_u32 v5, v36, v5, s55
	v_add3_u32 v4, v37, v4, s55
	v_and_b32_sdwa v36, v3, v228 dst_sel:DWORD dst_unused:UNUSED_PAD src0_sel:WORD_1 src1_sel:DWORD
	v_and_b32_sdwa v37, v2, v228 dst_sel:DWORD dst_unused:UNUSED_PAD src0_sel:WORD_1 src1_sel:DWORD
	v_add3_u32 v3, v3, v36, s55
	v_add3_u32 v2, v2, v37, s55
	v_and_b32_e32 v3, 0xffff0000, v3
	v_and_b32_e32 v2, 0xffff0000, v2
	v_or_b32_sdwa v3, v3, v4 dst_sel:DWORD dst_unused:UNUSED_PAD src0_sel:DWORD src1_sel:WORD_1
	v_or_b32_sdwa v2, v2, v5 dst_sel:DWORD dst_unused:UNUSED_PAD src0_sel:DWORD src1_sel:WORD_1
	global_store_dwordx2 v[34:35], v[2:3], off
	v_mov_b32_e32 v2, v6
	v_mov_b32_e32 v3, v8
	v_pk_mul_f32 v[2:3], v[2:3], v[0:1] op_sel_hi:[1,0]
	v_mov_b32_e32 v8, v7
	v_pk_mul_f32 v[4:5], v[8:9], v[0:1] op_sel_hi:[1,0]
	v_and_b32_sdwa v6, v3, v228 dst_sel:DWORD dst_unused:UNUSED_PAD src0_sel:WORD_1 src1_sel:DWORD
	v_and_b32_sdwa v7, v2, v228 dst_sel:DWORD dst_unused:UNUSED_PAD src0_sel:WORD_1 src1_sel:DWORD
	v_add3_u32 v2, v2, v7, s55
	v_add3_u32 v3, v3, v6, s55
	v_and_b32_sdwa v6, v5, v228 dst_sel:DWORD dst_unused:UNUSED_PAD src0_sel:WORD_1 src1_sel:DWORD
	v_and_b32_sdwa v7, v4, v228 dst_sel:DWORD dst_unused:UNUSED_PAD src0_sel:WORD_1 src1_sel:DWORD
	v_add3_u32 v5, v5, v6, s55
	v_add3_u32 v4, v4, v7, s55
	v_and_b32_e32 v5, 0xffff0000, v5
	v_and_b32_e32 v4, 0xffff0000, v4
	v_or_b32_sdwa v3, v5, v3 dst_sel:DWORD dst_unused:UNUSED_PAD src0_sel:DWORD src1_sel:WORD_1
	v_or_b32_sdwa v2, v4, v2 dst_sel:DWORD dst_unused:UNUSED_PAD src0_sel:DWORD src1_sel:WORD_1
	global_store_dwordx2 v[34:35], v[2:3], off offset:16
	v_mov_b32_e32 v2, v10
	v_mov_b32_e32 v3, v12
	v_pk_mul_f32 v[2:3], v[2:3], v[0:1] op_sel_hi:[1,0]
	v_mov_b32_e32 v12, v11
	v_pk_mul_f32 v[4:5], v[12:13], v[0:1] op_sel_hi:[1,0]
	v_and_b32_sdwa v6, v3, v228 dst_sel:DWORD dst_unused:UNUSED_PAD src0_sel:WORD_1 src1_sel:DWORD
	v_and_b32_sdwa v7, v2, v228 dst_sel:DWORD dst_unused:UNUSED_PAD src0_sel:WORD_1 src1_sel:DWORD
	v_add3_u32 v2, v2, v7, s55
	v_add3_u32 v3, v3, v6, s55
	v_and_b32_sdwa v6, v5, v228 dst_sel:DWORD dst_unused:UNUSED_PAD src0_sel:WORD_1 src1_sel:DWORD
	v_and_b32_sdwa v7, v4, v228 dst_sel:DWORD dst_unused:UNUSED_PAD src0_sel:WORD_1 src1_sel:DWORD
	v_add3_u32 v5, v5, v6, s55
	v_add3_u32 v4, v4, v7, s55
	v_and_b32_e32 v5, 0xffff0000, v5
	v_and_b32_e32 v4, 0xffff0000, v4
	v_or_b32_sdwa v3, v5, v3 dst_sel:DWORD dst_unused:UNUSED_PAD src0_sel:DWORD src1_sel:WORD_1
	v_or_b32_sdwa v2, v4, v2 dst_sel:DWORD dst_unused:UNUSED_PAD src0_sel:DWORD src1_sel:WORD_1
	global_store_dwordx2 v[34:35], v[2:3], off offset:32
	v_mov_b32_e32 v2, v14
	v_mov_b32_e32 v3, v16
	v_pk_mul_f32 v[2:3], v[2:3], v[0:1] op_sel_hi:[1,0]
	v_mov_b32_e32 v16, v15
	v_pk_mul_f32 v[4:5], v[16:17], v[0:1] op_sel_hi:[1,0]
	v_and_b32_sdwa v6, v3, v228 dst_sel:DWORD dst_unused:UNUSED_PAD src0_sel:WORD_1 src1_sel:DWORD
	v_and_b32_sdwa v7, v2, v228 dst_sel:DWORD dst_unused:UNUSED_PAD src0_sel:WORD_1 src1_sel:DWORD
	v_add3_u32 v2, v2, v7, s55
	v_add3_u32 v3, v3, v6, s55
	v_and_b32_sdwa v6, v5, v228 dst_sel:DWORD dst_unused:UNUSED_PAD src0_sel:WORD_1 src1_sel:DWORD
	v_and_b32_sdwa v7, v4, v228 dst_sel:DWORD dst_unused:UNUSED_PAD src0_sel:WORD_1 src1_sel:DWORD
	v_add3_u32 v5, v5, v6, s55
	v_add3_u32 v4, v4, v7, s55
	v_and_b32_e32 v5, 0xffff0000, v5
	v_and_b32_e32 v4, 0xffff0000, v4
	v_or_b32_sdwa v3, v5, v3 dst_sel:DWORD dst_unused:UNUSED_PAD src0_sel:DWORD src1_sel:WORD_1
	v_or_b32_sdwa v2, v4, v2 dst_sel:DWORD dst_unused:UNUSED_PAD src0_sel:DWORD src1_sel:WORD_1
	global_store_dwordx2 v[34:35], v[2:3], off offset:48
	v_mov_b32_e32 v2, v18
	v_mov_b32_e32 v3, v20
	v_pk_mul_f32 v[2:3], v[2:3], v[0:1] op_sel_hi:[1,0]
	v_mov_b32_e32 v20, v19
	v_pk_mul_f32 v[4:5], v[20:21], v[0:1] op_sel_hi:[1,0]
	v_and_b32_sdwa v6, v3, v228 dst_sel:DWORD dst_unused:UNUSED_PAD src0_sel:WORD_1 src1_sel:DWORD
	v_and_b32_sdwa v7, v2, v228 dst_sel:DWORD dst_unused:UNUSED_PAD src0_sel:WORD_1 src1_sel:DWORD
	v_add3_u32 v2, v2, v7, s55
	v_add3_u32 v3, v3, v6, s55
	v_and_b32_sdwa v6, v5, v228 dst_sel:DWORD dst_unused:UNUSED_PAD src0_sel:WORD_1 src1_sel:DWORD
	v_and_b32_sdwa v7, v4, v228 dst_sel:DWORD dst_unused:UNUSED_PAD src0_sel:WORD_1 src1_sel:DWORD
	v_add3_u32 v5, v5, v6, s55
	v_add3_u32 v4, v4, v7, s55
	v_and_b32_e32 v5, 0xffff0000, v5
	v_and_b32_e32 v4, 0xffff0000, v4
	v_or_b32_sdwa v3, v5, v3 dst_sel:DWORD dst_unused:UNUSED_PAD src0_sel:DWORD src1_sel:WORD_1
	v_or_b32_sdwa v2, v4, v2 dst_sel:DWORD dst_unused:UNUSED_PAD src0_sel:DWORD src1_sel:WORD_1
	global_store_dwordx2 v[34:35], v[2:3], off offset:64
	v_mov_b32_e32 v2, v22
	v_mov_b32_e32 v3, v24
	v_pk_mul_f32 v[2:3], v[2:3], v[0:1] op_sel_hi:[1,0]
	v_mov_b32_e32 v24, v23
	v_pk_mul_f32 v[4:5], v[24:25], v[0:1] op_sel_hi:[1,0]
	v_and_b32_sdwa v6, v3, v228 dst_sel:DWORD dst_unused:UNUSED_PAD src0_sel:WORD_1 src1_sel:DWORD
	v_and_b32_sdwa v7, v2, v228 dst_sel:DWORD dst_unused:UNUSED_PAD src0_sel:WORD_1 src1_sel:DWORD
	v_add3_u32 v2, v2, v7, s55
	v_add3_u32 v3, v3, v6, s55
	v_and_b32_sdwa v6, v5, v228 dst_sel:DWORD dst_unused:UNUSED_PAD src0_sel:WORD_1 src1_sel:DWORD
	v_and_b32_sdwa v7, v4, v228 dst_sel:DWORD dst_unused:UNUSED_PAD src0_sel:WORD_1 src1_sel:DWORD
	v_add3_u32 v5, v5, v6, s55
	v_add3_u32 v4, v4, v7, s55
	v_and_b32_e32 v5, 0xffff0000, v5
	v_and_b32_e32 v4, 0xffff0000, v4
	v_or_b32_sdwa v3, v5, v3 dst_sel:DWORD dst_unused:UNUSED_PAD src0_sel:DWORD src1_sel:WORD_1
	v_or_b32_sdwa v2, v4, v2 dst_sel:DWORD dst_unused:UNUSED_PAD src0_sel:DWORD src1_sel:WORD_1
	global_store_dwordx2 v[34:35], v[2:3], off offset:80
	v_mov_b32_e32 v2, v26
	v_mov_b32_e32 v3, v28
	v_pk_mul_f32 v[2:3], v[2:3], v[0:1] op_sel_hi:[1,0]
	v_mov_b32_e32 v28, v27
	v_pk_mul_f32 v[4:5], v[28:29], v[0:1] op_sel_hi:[1,0]
	v_and_b32_sdwa v6, v3, v228 dst_sel:DWORD dst_unused:UNUSED_PAD src0_sel:WORD_1 src1_sel:DWORD
	v_and_b32_sdwa v7, v2, v228 dst_sel:DWORD dst_unused:UNUSED_PAD src0_sel:WORD_1 src1_sel:DWORD
	v_add3_u32 v2, v2, v7, s55
	v_add3_u32 v3, v3, v6, s55
	v_and_b32_sdwa v6, v5, v228 dst_sel:DWORD dst_unused:UNUSED_PAD src0_sel:WORD_1 src1_sel:DWORD
	v_and_b32_sdwa v7, v4, v228 dst_sel:DWORD dst_unused:UNUSED_PAD src0_sel:WORD_1 src1_sel:DWORD
	v_add3_u32 v5, v5, v6, s55
	v_add3_u32 v4, v4, v7, s55
	v_and_b32_e32 v5, 0xffff0000, v5
	v_and_b32_e32 v4, 0xffff0000, v4
	v_or_b32_sdwa v3, v5, v3 dst_sel:DWORD dst_unused:UNUSED_PAD src0_sel:DWORD src1_sel:WORD_1
	v_or_b32_sdwa v2, v4, v2 dst_sel:DWORD dst_unused:UNUSED_PAD src0_sel:DWORD src1_sel:WORD_1
	global_store_dwordx2 v[34:35], v[2:3], off offset:96
	v_mov_b32_e32 v2, v30
	v_mov_b32_e32 v3, v32
	v_pk_mul_f32 v[2:3], v[2:3], v[0:1] op_sel_hi:[1,0]
	v_mov_b32_e32 v32, v31
	v_pk_mul_f32 v[4:5], v[32:33], v[0:1] op_sel_hi:[1,0]
	v_and_b32_sdwa v0, v3, v228 dst_sel:DWORD dst_unused:UNUSED_PAD src0_sel:WORD_1 src1_sel:DWORD
	v_and_b32_sdwa v6, v2, v228 dst_sel:DWORD dst_unused:UNUSED_PAD src0_sel:WORD_1 src1_sel:DWORD
	v_add3_u32 v2, v2, v6, s55
	v_add3_u32 v0, v3, v0, s55
	v_and_b32_sdwa v3, v5, v228 dst_sel:DWORD dst_unused:UNUSED_PAD src0_sel:WORD_1 src1_sel:DWORD
	v_and_b32_sdwa v6, v4, v228 dst_sel:DWORD dst_unused:UNUSED_PAD src0_sel:WORD_1 src1_sel:DWORD
	v_add3_u32 v3, v5, v3, s55
	v_add3_u32 v4, v4, v6, s55
	v_and_b32_e32 v3, 0xffff0000, v3
	v_and_b32_e32 v4, 0xffff0000, v4
	v_or_b32_sdwa v3, v3, v0 dst_sel:DWORD dst_unused:UNUSED_PAD src0_sel:DWORD src1_sel:WORD_1
	v_or_b32_sdwa v2, v4, v2 dst_sel:DWORD dst_unused:UNUSED_PAD src0_sel:DWORD src1_sel:WORD_1
	s_and_b64 vcc, exec, s[20:21]
	global_store_dwordx2 v[34:35], v[2:3], off offset:112
	s_cbranch_vccnz .LBB0_490

.LBB0_594:
	s_lshl_b32 s4, s21, 5
	s_lshl_b32 s5, s20, 8
	v_lshrrev_b32_e32 v0, 1, v166
	s_or_b32 s4, s5, s4
	v_and_or_b32 v220, v0, 24, s4
	s_lshl_b32 s37, s83, 8
	v_add_u32_e32 v118, s37, v240
	v_ashrrev_i32_e32 v221, 31, v220
	v_lshl_add_u64 v[120:121], v[220:221], 1, s[6:7]
	s_mov_b64 s[4:5], 0x4000000
	v_ashrrev_i32_e32 v119, 31, v118
	v_lshl_add_u64 v[120:121], v[120:121], 0, s[4:5]
	v_lshlrev_b64 v[224:225], 11, v[118:119]
	v_lshl_add_u64 v[126:127], v[120:121], 0, v[224:225]
	s_barrier
	global_load_dwordx4 v[206:209], v[126:127], off
	global_load_dwordx4 v[202:205], v[126:127], off offset:256
	v_or_b32_e32 v126, 16, v118
	v_ashrrev_i32_e32 v127, 31, v126
	v_lshlrev_b64 v[126:127], 11, v[126:127]
	v_lshl_add_u64 v[126:127], v[120:121], 0, v[126:127]
	global_load_dwordx4 v[198:201], v[126:127], off
	global_load_dwordx4 v[194:197], v[126:127], off offset:256
	v_or_b32_e32 v126, 32, v118
	v_ashrrev_i32_e32 v127, 31, v126
	v_lshlrev_b64 v[126:127], 11, v[126:127]
	v_lshl_add_u64 v[126:127], v[120:121], 0, v[126:127]
	global_load_dwordx4 v[190:193], v[126:127], off
	global_load_dwordx4 v[186:189], v[126:127], off offset:256
	v_or_b32_e32 v126, 48, v118
	v_ashrrev_i32_e32 v127, 31, v126
	v_lshlrev_b64 v[126:127], 11, v[126:127]
	v_lshl_add_u64 v[126:127], v[120:121], 0, v[126:127]
	global_load_dwordx4 v[174:177], v[126:127], off
	global_load_dwordx4 v[162:165], v[126:127], off offset:256
	v_add_u32_e32 v126, 0x80, v118
	v_ashrrev_i32_e32 v127, 31, v126
	v_lshlrev_b64 v[126:127], 11, v[126:127]
	v_lshl_add_u64 v[126:127], v[120:121], 0, v[126:127]
	global_load_dwordx4 v[158:161], v[126:127], off
	global_load_dwordx4 v[154:157], v[126:127], off offset:256
	v_add_u32_e32 v126, 0x90, v118
	v_ashrrev_i32_e32 v127, 31, v126
	v_lshlrev_b64 v[126:127], 11, v[126:127]
	v_lshl_add_u64 v[126:127], v[120:121], 0, v[126:127]
	global_load_dwordx4 v[150:153], v[126:127], off
	global_load_dwordx4 v[146:149], v[126:127], off offset:256
	v_add_u32_e32 v126, 0xa0, v118
	v_add_u32_e32 v118, 0xb0, v118
	v_ashrrev_i32_e32 v127, 31, v126
	v_ashrrev_i32_e32 v119, 31, v118
	v_lshlrev_b64 v[126:127], 11, v[126:127]
	v_lshlrev_b64 v[118:119], 11, v[118:119]
	v_lshl_add_u64 v[126:127], v[120:121], 0, v[126:127]
	v_lshl_add_u64 v[118:119], v[120:121], 0, v[118:119]
	global_load_dwordx4 v[142:145], v[126:127], off
	global_load_dwordx4 v[138:141], v[126:127], off offset:256
	s_nop 0
	global_load_dwordx4 v[126:129], v[118:119], off
	s_nop 0
	global_load_dwordx4 v[118:121], v[118:119], off offset:256
	v_and_b32_e32 v168, 64, v231
	v_xor_b32_e32 v0, 16, v231
	v_add_u32_e32 v168, 64, v168
	v_cmp_lt_i32_e32 vcc, v0, v168
	v_mul_f32_e32 v169, v137, v137
	v_fmac_f32_e32 v169, v136, v136
	v_cndmask_b32_e32 v0, v231, v0, vcc
	v_lshlrev_b32_e32 v241, 2, v0
	v_mul_f32_e32 v0, v135, v135
	v_fmac_f32_e32 v0, v134, v134
	v_add_f32_e32 v0, v0, v169
	v_mul_f32_e32 v169, v131, v131
	v_mul_f32_e32 v170, v133, v133
	v_fmac_f32_e32 v169, v130, v130
	v_fmac_f32_e32 v170, v132, v132
	v_add_f32_e32 v169, v169, v170
	v_add_f32_e32 v0, v169, v0
	v_mul_f32_e32 v169, v123, v123
	v_mul_f32_e32 v170, v125, v125
	v_fmac_f32_e32 v169, v122, v122
	v_fmac_f32_e32 v170, v124, v124
	v_add_f32_e32 v169, v169, v170
	v_add_f32_e32 v0, v169, v0
	v_mul_f32_e32 v169, v115, v115
	v_mul_f32_e32 v170, v117, v117
	v_fmac_f32_e32 v169, v114, v114
	v_fmac_f32_e32 v170, v116, v116
	v_add_f32_e32 v169, v169, v170
	v_add_f32_e32 v0, v169, v0
	v_mov_b32_e32 v169, v0
	s_nop 1
	v_permlane16_swap_b32_e32 v169, v0
	v_xor_b32_e32 v170, 32, v231
	v_cmp_lt_i32_e32 vcc, v170, v168
	s_lshl_b32 s4, s21, 2
	s_add_i32 s36, s4, 0
	v_cndmask_b32_e32 v168, v231, v170, vcc
	v_lshlrev_b32_e32 v242, 2, v168
	s_waitcnt lgkmcnt(0)
	v_add_f32_e32 v168, v0, v169
	v_mov_b32_e32 v169, v168
	s_nop 1
	v_permlane32_swap_b32_e32 v169, v168
	v_and_b32_e32 v0, 63, v166
	v_cmp_gt_u32_e64 s[42:43], 16, v0
	s_and_saveexec_b64 s[6:7], s[42:43]
	s_load_dwordx2 s[90:91], s[0:1], 0xb0
	v_readlane_b32 s64, v252, 3
	v_readlane_b32 s65, v255, 10
	v_readlane_b32 s68, v255, 11
	v_readlane_b32 s74, v255, 12
	v_readlane_b32 s95, v255, 13
	s_movk_i32 s92, 0x2b20
	s_cbranch_execz .LBB0_596
	s_lshl_b32 s4, s82, 10
	s_add_i32 s4, s36, s4
	s_waitcnt lgkmcnt(0)
	v_add_f32_e32 v168, v168, v169
	v_lshl_add_u32 v169, v167, 4, s4
	ds_write_b32 v169, v168
.LBB0_596:
	s_or_b64 exec, exec, s[6:7]
	v_mul_f32_e32 v168, v111, v111
	s_waitcnt lgkmcnt(0)
	v_mul_f32_e32 v169, v113, v113
	v_fmac_f32_e32 v168, v110, v110
	v_fmac_f32_e32 v169, v112, v112
	v_add_f32_e32 v168, v168, v169
	v_mul_f32_e32 v169, v107, v107
	v_mul_f32_e32 v170, v109, v109
	v_fmac_f32_e32 v169, v106, v106
	v_fmac_f32_e32 v170, v108, v108
	v_add_f32_e32 v169, v169, v170
	v_add_f32_e32 v168, v169, v168
	v_mul_f32_e32 v169, v103, v103
	v_mul_f32_e32 v170, v105, v105
	v_fmac_f32_e32 v169, v102, v102
	v_fmac_f32_e32 v170, v104, v104
	v_add_f32_e32 v169, v169, v170
	v_add_f32_e32 v168, v169, v168
	v_mul_f32_e32 v169, v99, v99
	v_mul_f32_e32 v170, v101, v101
	v_fmac_f32_e32 v169, v98, v98
	v_fmac_f32_e32 v170, v100, v100
	v_add_f32_e32 v169, v169, v170
	v_add_f32_e32 v168, v169, v168
	v_mov_b32_e32 v169, v168
	s_nop 1
	v_permlane16_swap_b32_e32 v169, v168
	s_waitcnt lgkmcnt(0)
	v_add_f32_e32 v168, v168, v169
	v_mov_b32_e32 v169, v168
	s_nop 1
	v_permlane32_swap_b32_e32 v169, v168
	s_and_saveexec_b64 s[6:7], s[42:43]
	s_cbranch_execz .LBB0_598
	s_lshl_b32 s4, s82, 10
	s_add_i32 s4, s36, s4
	s_waitcnt lgkmcnt(0)
	v_add_f32_e32 v168, v168, v169
	v_lshl_add_u32 v169, v167, 4, s4
	ds_write_b32 v169, v168 offset:256
.LBB0_598:
	s_or_b64 exec, exec, s[6:7]
	v_mul_f32_e32 v168, v95, v95
	s_waitcnt lgkmcnt(0)
	v_mul_f32_e32 v169, v97, v97
	v_fmac_f32_e32 v168, v94, v94
	v_fmac_f32_e32 v169, v96, v96
	v_add_f32_e32 v168, v168, v169
	v_mul_f32_e32 v169, v91, v91
	v_mul_f32_e32 v170, v93, v93
	v_fmac_f32_e32 v169, v90, v90
	v_fmac_f32_e32 v170, v92, v92
	v_add_f32_e32 v169, v169, v170
	v_add_f32_e32 v168, v169, v168
	v_mul_f32_e32 v169, v87, v87
	v_mul_f32_e32 v170, v89, v89
	v_fmac_f32_e32 v169, v86, v86
	v_fmac_f32_e32 v170, v88, v88
	v_add_f32_e32 v169, v169, v170
	v_add_f32_e32 v168, v169, v168
	v_mul_f32_e32 v169, v83, v83
	v_mul_f32_e32 v170, v85, v85
	v_fmac_f32_e32 v169, v82, v82
	v_fmac_f32_e32 v170, v84, v84
	v_add_f32_e32 v169, v169, v170
	v_add_f32_e32 v168, v169, v168
	v_mov_b32_e32 v169, v168
	s_nop 1
	v_permlane16_swap_b32_e32 v169, v168
	s_waitcnt lgkmcnt(0)
	v_add_f32_e32 v168, v168, v169
	v_mov_b32_e32 v169, v168
	s_nop 1
	v_permlane32_swap_b32_e32 v169, v168
	s_and_saveexec_b64 s[6:7], s[42:43]
	s_cbranch_execz .LBB0_600
	s_lshl_b32 s4, s82, 10
	s_add_i32 s4, s36, s4
	s_waitcnt lgkmcnt(0)
	v_add_f32_e32 v168, v168, v169
	v_lshl_add_u32 v169, v167, 4, s4
	ds_write_b32 v169, v168 offset:512
.LBB0_600:
	s_or_b64 exec, exec, s[6:7]
	v_mul_f32_e32 v168, v79, v79
	s_waitcnt lgkmcnt(0)
	v_mul_f32_e32 v169, v81, v81
	v_fmac_f32_e32 v168, v78, v78
	v_fmac_f32_e32 v169, v80, v80
	v_add_f32_e32 v168, v168, v169
	v_mul_f32_e32 v169, v75, v75
	v_mul_f32_e32 v170, v77, v77
	v_fmac_f32_e32 v169, v74, v74
	v_fmac_f32_e32 v170, v76, v76
	v_add_f32_e32 v169, v169, v170
	v_add_f32_e32 v168, v169, v168
	v_mul_f32_e32 v169, v71, v71
	v_mul_f32_e32 v170, v73, v73
	v_fmac_f32_e32 v169, v70, v70
	v_fmac_f32_e32 v170, v72, v72
	v_add_f32_e32 v169, v169, v170
	v_add_f32_e32 v168, v169, v168
	v_mul_f32_e32 v169, v67, v67
	v_mul_f32_e32 v170, v69, v69
	v_fmac_f32_e32 v169, v66, v66
	v_fmac_f32_e32 v170, v68, v68
	v_add_f32_e32 v169, v169, v170
	v_add_f32_e32 v168, v169, v168
	v_mov_b32_e32 v169, v168
	s_nop 1
	v_permlane16_swap_b32_e32 v169, v168
	s_waitcnt lgkmcnt(0)
	v_add_f32_e32 v168, v168, v169
	v_mov_b32_e32 v169, v168
	s_nop 1
	v_permlane32_swap_b32_e32 v169, v168
	s_and_saveexec_b64 s[6:7], s[42:43]
	s_cbranch_execz .LBB0_602
	s_lshl_b32 s4, s82, 10
	s_add_i32 s4, s36, s4
	s_waitcnt lgkmcnt(0)
	v_add_f32_e32 v168, v168, v169
	v_lshl_add_u32 v169, v167, 4, s4
	ds_write_b32 v169, v168 offset:768
.LBB0_602:
	s_or_b64 exec, exec, s[6:7]
	v_mul_f32_e32 v168, v63, v63
	s_waitcnt lgkmcnt(0)
	v_mul_f32_e32 v169, v65, v65
	v_fmac_f32_e32 v168, v62, v62
	v_fmac_f32_e32 v169, v64, v64
	v_add_f32_e32 v168, v168, v169
	v_mul_f32_e32 v169, v59, v59
	v_mul_f32_e32 v170, v61, v61
	v_fmac_f32_e32 v169, v58, v58
	v_fmac_f32_e32 v170, v60, v60
	v_add_f32_e32 v169, v169, v170
	v_add_f32_e32 v168, v169, v168
	v_mul_f32_e32 v169, v55, v55
	v_mul_f32_e32 v170, v57, v57
	v_fmac_f32_e32 v169, v54, v54
	v_fmac_f32_e32 v170, v56, v56
	v_add_f32_e32 v169, v169, v170
	v_add_f32_e32 v168, v169, v168
	v_mul_f32_e32 v169, v51, v51
	v_mul_f32_e32 v170, v53, v53
	v_fmac_f32_e32 v169, v50, v50
	v_fmac_f32_e32 v170, v52, v52
	v_add_f32_e32 v169, v169, v170
	v_add_f32_e32 v168, v169, v168
	v_mov_b32_e32 v169, v168
	s_nop 1
	v_permlane16_swap_b32_e32 v169, v168
	s_waitcnt lgkmcnt(0)
	v_add_f32_e32 v168, v168, v169
	v_mov_b32_e32 v169, v168
	s_nop 1
	v_permlane32_swap_b32_e32 v169, v168
	s_and_saveexec_b64 s[6:7], s[42:43]
	s_cbranch_execz .LBB0_604
	s_lshl_b32 s4, s82, 10
	s_add_i32 s4, s36, s4
	s_waitcnt lgkmcnt(0)
	v_add_f32_e32 v168, v168, v169
	v_lshl_add_u32 v169, v167, 4, s4
	ds_write_b32 v169, v168 offset:2048
.LBB0_604:
	s_or_b64 exec, exec, s[6:7]
	v_mul_f32_e32 v168, v47, v47
	s_waitcnt lgkmcnt(0)
	v_mul_f32_e32 v169, v49, v49
	v_fmac_f32_e32 v168, v46, v46
	v_fmac_f32_e32 v169, v48, v48
	v_add_f32_e32 v168, v168, v169
	v_mul_f32_e32 v169, v43, v43
	v_mul_f32_e32 v170, v45, v45
	v_fmac_f32_e32 v169, v42, v42
	v_fmac_f32_e32 v170, v44, v44
	v_add_f32_e32 v169, v169, v170
	v_add_f32_e32 v168, v169, v168
	v_mul_f32_e32 v169, v39, v39
	v_mul_f32_e32 v170, v41, v41
	v_fmac_f32_e32 v169, v38, v38
	v_fmac_f32_e32 v170, v40, v40
	v_add_f32_e32 v169, v169, v170
	v_add_f32_e32 v168, v169, v168
	v_mul_f32_e32 v169, v35, v35
	v_mul_f32_e32 v170, v37, v37
	v_fmac_f32_e32 v169, v34, v34
	v_fmac_f32_e32 v170, v36, v36
	v_add_f32_e32 v169, v169, v170
	v_add_f32_e32 v168, v169, v168
	v_mov_b32_e32 v169, v168
	s_nop 1
	v_permlane16_swap_b32_e32 v169, v168
	s_waitcnt lgkmcnt(0)
	v_add_f32_e32 v168, v168, v169
	v_mov_b32_e32 v169, v168
	s_nop 1
	v_permlane32_swap_b32_e32 v169, v168
	s_and_saveexec_b64 s[6:7], s[42:43]
	s_cbranch_execz .LBB0_606
	s_lshl_b32 s4, s82, 10
	s_add_i32 s4, s36, s4
	s_waitcnt lgkmcnt(0)
	v_add_f32_e32 v168, v168, v169
	v_lshl_add_u32 v169, v167, 4, s4
	ds_write_b32 v169, v168 offset:2304
.LBB0_606:
	s_or_b64 exec, exec, s[6:7]
	v_mul_f32_e32 v168, v31, v31
	s_waitcnt lgkmcnt(0)
	v_mul_f32_e32 v169, v33, v33
	v_fmac_f32_e32 v168, v30, v30
	v_fmac_f32_e32 v169, v32, v32
	v_add_f32_e32 v168, v168, v169
	v_mul_f32_e32 v169, v27, v27
	v_mul_f32_e32 v170, v29, v29
	v_fmac_f32_e32 v169, v26, v26
	v_fmac_f32_e32 v170, v28, v28
	v_add_f32_e32 v169, v169, v170
	v_add_f32_e32 v168, v169, v168
	v_mul_f32_e32 v169, v23, v23
	v_mul_f32_e32 v170, v25, v25
	v_fmac_f32_e32 v169, v22, v22
	v_fmac_f32_e32 v170, v24, v24
	v_add_f32_e32 v169, v169, v170
	v_add_f32_e32 v168, v169, v168
	v_mul_f32_e32 v169, v19, v19
	v_mul_f32_e32 v170, v21, v21
	v_fmac_f32_e32 v169, v18, v18
	v_fmac_f32_e32 v170, v20, v20
	v_add_f32_e32 v169, v169, v170
	v_add_f32_e32 v168, v169, v168
	v_mov_b32_e32 v169, v168
	s_nop 1
	v_permlane16_swap_b32_e32 v169, v168
	s_waitcnt lgkmcnt(0)
	v_add_f32_e32 v168, v168, v169
	v_mov_b32_e32 v169, v168
	s_nop 1
	v_permlane32_swap_b32_e32 v169, v168
	s_and_saveexec_b64 s[6:7], s[42:43]
	s_cbranch_execz .LBB0_608
	s_lshl_b32 s4, s82, 10
	s_add_i32 s4, s36, s4
	s_waitcnt lgkmcnt(0)
	v_add_f32_e32 v168, v168, v169
	v_lshl_add_u32 v169, v167, 4, s4
	ds_write_b32 v169, v168 offset:2560
.LBB0_608:
	s_or_b64 exec, exec, s[6:7]
	v_mul_f32_e32 v168, v15, v15
	s_waitcnt lgkmcnt(0)
	v_mul_f32_e32 v169, v17, v17
	v_fmac_f32_e32 v168, v14, v14
	v_fmac_f32_e32 v169, v16, v16
	v_add_f32_e32 v168, v168, v169
	v_mul_f32_e32 v169, v11, v11
	v_mul_f32_e32 v170, v13, v13
	v_fmac_f32_e32 v169, v10, v10
	v_fmac_f32_e32 v170, v12, v12
	v_add_f32_e32 v169, v169, v170
	v_add_f32_e32 v168, v169, v168
	v_mul_f32_e32 v169, v7, v7
	v_mul_f32_e32 v170, v9, v9
	v_fmac_f32_e32 v169, v6, v6
	v_fmac_f32_e32 v170, v8, v8
	v_add_f32_e32 v169, v169, v170
	v_add_f32_e32 v168, v169, v168
	v_mul_f32_e32 v169, v3, v3
	v_mul_f32_e32 v170, v5, v5
	v_fmac_f32_e32 v169, v2, v2
	v_fmac_f32_e32 v170, v4, v4
	v_add_f32_e32 v169, v169, v170
	v_add_f32_e32 v168, v169, v168
	v_mov_b32_e32 v169, v168
	s_nop 1
	v_permlane16_swap_b32_e32 v169, v168
	s_waitcnt lgkmcnt(0)
	v_add_f32_e32 v168, v168, v169
	v_mov_b32_e32 v169, v168
	s_nop 1
	v_permlane32_swap_b32_e32 v169, v168
	s_and_saveexec_b64 s[6:7], s[42:43]
	s_cbranch_execz .LBB0_610
	s_lshl_b32 s4, s82, 10
	s_add_i32 s4, s36, s4
	s_waitcnt lgkmcnt(0)
	v_add_f32_e32 v168, v168, v169
	v_lshl_add_u32 v167, v167, 4, s4
	ds_write_b32 v167, v168 offset:2816

.LBB0_636:
	s_waitcnt vmcnt(0)
	v_lshlrev_b32_e32 v216, 16, v206
	v_and_b32_e32 v217, 0xffff0000, v206
	v_lshlrev_b32_e32 v206, 16, v207
	v_and_b32_e32 v207, 0xffff0000, v207
	s_waitcnt lgkmcnt(0)
	v_pk_mul_f32 v[136:137], v[136:137], v[0:1] op_sel_hi:[1,0]
	v_pk_mul_f32 v[134:135], v[134:135], v[0:1] op_sel_hi:[1,0]
	v_lshlrev_b32_e32 v218, 16, v208
	v_and_b32_e32 v219, 0xffff0000, v208
	v_lshlrev_b32_e32 v208, 16, v209
	v_and_b32_e32 v209, 0xffff0000, v209
	v_pk_fma_f32 v[136:137], v[184:185], v[136:137], v[206:207]
	v_pk_fma_f32 v[134:135], v[182:183], v[134:135], v[216:217]
	v_pk_mul_f32 v[132:133], v[132:133], v[0:1] op_sel_hi:[1,0]
	v_pk_mul_f32 v[130:131], v[130:131], v[0:1] op_sel_hi:[1,0]
	v_pk_fma_f32 v[206:207], v[180:181], v[132:133], v[208:209]
	v_pk_fma_f32 v[132:133], v[178:179], v[130:131], v[218:219]
	v_mul_f32_e32 v130, v135, v135
	v_mul_f32_e32 v131, v137, v137
	v_fmac_f32_e32 v130, v134, v134
	v_fmac_f32_e32 v131, v136, v136
	v_add_f32_e32 v130, v130, v131
	v_mul_f32_e32 v131, v133, v133
	v_mul_f32_e32 v208, v207, v207
	v_fmac_f32_e32 v131, v132, v132
	v_fmac_f32_e32 v208, v206, v206
	v_add_f32_e32 v131, v131, v208
	v_add_f32_e32 v208, v130, v131
	v_cvt_pk_bf16_f32 v130, v134, v135
	v_cvt_pk_bf16_f32 v131, v136, v137
	v_lshlrev_b32_e32 v134, 16, v202
	v_and_b32_e32 v135, 0xffff0000, v202
	v_lshlrev_b32_e32 v136, 16, v203
	v_and_b32_e32 v137, 0xffff0000, v203
	v_pk_mul_f32 v[124:125], v[124:125], v[0:1] op_sel_hi:[1,0]
	v_pk_mul_f32 v[122:123], v[122:123], v[0:1] op_sel_hi:[1,0]
	v_lshlrev_b32_e32 v202, 16, v204
	v_and_b32_e32 v203, 0xffff0000, v204
	v_pk_fma_f32 v[124:125], v[172:173], v[124:125], v[136:137]
	v_pk_fma_f32 v[122:123], v[170:171], v[122:123], v[134:135]
	v_pk_mul_f32 v[114:115], v[114:115], v[0:1] op_sel_hi:[1,0]
	v_lshlrev_b32_e32 v204, 16, v205
	v_and_b32_e32 v205, 0xffff0000, v205
	v_pk_mul_f32 v[116:117], v[116:117], v[0:1] op_sel_hi:[1,0]
	v_pk_fma_f32 v[134:135], v[166:167], v[114:115], v[202:203]
	v_mul_f32_e32 v0, v123, v123
	v_mul_f32_e32 v114, v125, v125
	v_pk_fma_f32 v[116:117], v[168:169], v[116:117], v[204:205]
	v_fmac_f32_e32 v0, v122, v122
	v_fmac_f32_e32 v114, v124, v124
	v_add_f32_e32 v0, v0, v114
	v_mul_f32_e32 v114, v135, v135
	v_mul_f32_e32 v115, v117, v117
	v_fmac_f32_e32 v114, v134, v134
	v_fmac_f32_e32 v115, v116, v116
	v_add_f32_e32 v114, v114, v115
	v_add_f32_e32 v0, v0, v114
	v_add_f32_e32 v0, v208, v0
	v_mov_b32_e32 v202, v0
	s_nop 1
	v_permlane16_swap_b32_e32 v202, v0
	s_add_u32 s6, s22, s24
	s_addc_u32 s7, s23, s25
	v_lshl_add_u64 v[114:115], s[6:7], 0, v[224:225]
	v_lshl_add_u64 v[136:137], v[220:221], 1, v[114:115]
	s_waitcnt lgkmcnt(0)
	v_add_f32_e32 v0, v0, v202
	v_mov_b32_e32 v114, v0
	s_nop 1
	v_permlane32_swap_b32_e32 v114, v0
	v_cvt_pk_bf16_f32 v132, v132, v133
	v_cvt_pk_bf16_f32 v133, v206, v207
	global_store_dwordx4 v[136:137], v[130:133], off
	v_cvt_pk_bf16_f32 v122, v122, v123
	v_cvt_pk_bf16_f32 v123, v124, v125
	v_cvt_pk_bf16_f32 v124, v134, v135
	v_cvt_pk_bf16_f32 v125, v116, v117
	global_store_dwordx4 v[136:137], v[122:125], off offset:256
	s_and_saveexec_b64 s[8:9], s[42:43]
	s_cbranch_execz .LBB0_638
	v_lshl_add_u32 v115, v240, 4, s36
	s_waitcnt lgkmcnt(0)
	v_add_f32_e32 v0, v0, v114
	ds_write_b32 v115, v0 offset:6144

.LBB0_640:
	v_lshlrev_b32_e32 v122, 16, v198
	v_and_b32_e32 v123, 0xffff0000, v198
	v_lshlrev_b32_e32 v124, 16, v199
	v_and_b32_e32 v125, 0xffff0000, v199
	s_waitcnt lgkmcnt(0)
	v_pk_mul_f32 v[112:113], v[112:113], v[0:1] op_sel_hi:[1,0]
	v_pk_mul_f32 v[110:111], v[110:111], v[0:1] op_sel_hi:[1,0]
	v_lshlrev_b32_e32 v130, 16, v200
	v_and_b32_e32 v131, 0xffff0000, v200
	v_lshlrev_b32_e32 v132, 16, v201
	v_and_b32_e32 v133, 0xffff0000, v201
	v_pk_fma_f32 v[112:113], v[184:185], v[112:113], v[124:125]
	v_pk_fma_f32 v[110:111], v[182:183], v[110:111], v[122:123]
	v_pk_mul_f32 v[108:109], v[108:109], v[0:1] op_sel_hi:[1,0]
	v_pk_mul_f32 v[106:107], v[106:107], v[0:1] op_sel_hi:[1,0]
	v_pk_fma_f32 v[122:123], v[180:181], v[108:109], v[132:133]
	v_pk_fma_f32 v[108:109], v[178:179], v[106:107], v[130:131]
	v_mul_f32_e32 v106, v111, v111
	v_mul_f32_e32 v107, v113, v113
	v_fmac_f32_e32 v106, v110, v110
	v_fmac_f32_e32 v107, v112, v112
	v_add_f32_e32 v106, v106, v107
	v_mul_f32_e32 v107, v109, v109
	v_mul_f32_e32 v115, v123, v123
	v_fmac_f32_e32 v107, v108, v108
	v_fmac_f32_e32 v115, v122, v122
	v_add_f32_e32 v107, v107, v115
	v_add_f32_e32 v115, v106, v107
	v_cvt_pk_bf16_f32 v106, v110, v111
	v_cvt_pk_bf16_f32 v107, v112, v113
	v_lshlrev_b32_e32 v110, 16, v194
	v_and_b32_e32 v111, 0xffff0000, v194
	v_lshlrev_b32_e32 v112, 16, v195
	v_and_b32_e32 v113, 0xffff0000, v195
	v_pk_mul_f32 v[104:105], v[104:105], v[0:1] op_sel_hi:[1,0]
	v_pk_mul_f32 v[102:103], v[102:103], v[0:1] op_sel_hi:[1,0]
	v_cvt_pk_bf16_f32 v108, v108, v109
	v_cvt_pk_bf16_f32 v109, v122, v123
	v_lshlrev_b32_e32 v122, 16, v196
	v_and_b32_e32 v123, 0xffff0000, v196
	v_pk_fma_f32 v[104:105], v[172:173], v[104:105], v[112:113]
	v_pk_fma_f32 v[102:103], v[170:171], v[102:103], v[110:111]
	v_pk_mul_f32 v[98:99], v[98:99], v[0:1] op_sel_hi:[1,0]
	v_lshlrev_b32_e32 v124, 16, v197
	v_and_b32_e32 v125, 0xffff0000, v197
	v_pk_mul_f32 v[100:101], v[100:101], v[0:1] op_sel_hi:[1,0]
	v_pk_fma_f32 v[112:113], v[166:167], v[98:99], v[122:123]
	v_mul_f32_e32 v0, v103, v103
	v_mul_f32_e32 v98, v105, v105
	v_pk_fma_f32 v[110:111], v[168:169], v[100:101], v[124:125]
	v_fmac_f32_e32 v0, v102, v102
	v_fmac_f32_e32 v98, v104, v104
	v_add_f32_e32 v0, v0, v98
	v_mul_f32_e32 v98, v113, v113
	v_mul_f32_e32 v99, v111, v111
	v_fmac_f32_e32 v98, v112, v112
	v_fmac_f32_e32 v99, v110, v110
	v_add_f32_e32 v98, v98, v99
	v_add_f32_e32 v0, v0, v98
	v_add_f32_e32 v0, v115, v0
	v_mov_b32_e32 v101, v0
	s_nop 1
	v_permlane16_swap_b32_e32 v101, v0
	v_or_b32_e32 v114, 16, v240
	v_add_u32_e32 v116, s37, v114
	v_ashrrev_i32_e32 v117, 31, v116
	v_lshlrev_b64 v[116:117], 11, v[116:117]
	v_lshl_add_u64 v[98:99], s[6:7], 0, v[116:117]
	s_waitcnt lgkmcnt(0)
	v_add_f32_e32 v0, v0, v101
	v_lshl_add_u64 v[116:117], v[220:221], 1, v[98:99]
	v_mov_b32_e32 v98, v0
	s_nop 1
	v_permlane32_swap_b32_e32 v98, v0
	global_store_dwordx4 v[116:117], v[106:109], off
	v_cvt_pk_bf16_f32 v100, v102, v103
	v_cvt_pk_bf16_f32 v101, v104, v105
	v_cvt_pk_bf16_f32 v102, v112, v113
	v_cvt_pk_bf16_f32 v103, v110, v111
	global_store_dwordx4 v[116:117], v[100:103], off offset:256
	s_and_saveexec_b64 s[8:9], s[42:43]
	s_cbranch_execz .LBB0_642
	v_lshl_add_u32 v99, v114, 4, s36
	s_waitcnt lgkmcnt(0)
	v_add_f32_e32 v0, v0, v98
	ds_write_b32 v99, v0 offset:6144

.LBB0_644:
	v_lshlrev_b32_e32 v102, 16, v190
	v_and_b32_e32 v103, 0xffff0000, v190
	v_lshlrev_b32_e32 v104, 16, v191
	v_and_b32_e32 v105, 0xffff0000, v191
	s_waitcnt lgkmcnt(0)
	v_pk_mul_f32 v[96:97], v[96:97], v[0:1] op_sel_hi:[1,0]
	v_pk_mul_f32 v[94:95], v[94:95], v[0:1] op_sel_hi:[1,0]
	v_lshlrev_b32_e32 v106, 16, v192
	v_and_b32_e32 v107, 0xffff0000, v192
	v_lshlrev_b32_e32 v108, 16, v193
	v_and_b32_e32 v109, 0xffff0000, v193
	v_pk_fma_f32 v[96:97], v[184:185], v[96:97], v[104:105]
	v_pk_fma_f32 v[94:95], v[182:183], v[94:95], v[102:103]
	v_pk_mul_f32 v[92:93], v[92:93], v[0:1] op_sel_hi:[1,0]
	v_pk_mul_f32 v[90:91], v[90:91], v[0:1] op_sel_hi:[1,0]
	v_pk_fma_f32 v[102:103], v[180:181], v[92:93], v[108:109]
	v_pk_fma_f32 v[92:93], v[178:179], v[90:91], v[106:107]
	v_mul_f32_e32 v90, v95, v95
	v_mul_f32_e32 v91, v97, v97
	v_fmac_f32_e32 v90, v94, v94
	v_fmac_f32_e32 v91, v96, v96
	v_add_f32_e32 v90, v90, v91
	v_mul_f32_e32 v91, v93, v93
	v_mul_f32_e32 v99, v103, v103
	v_fmac_f32_e32 v91, v92, v92
	v_fmac_f32_e32 v99, v102, v102
	v_add_f32_e32 v91, v91, v99
	v_add_f32_e32 v99, v90, v91
	v_cvt_pk_bf16_f32 v90, v94, v95
	v_cvt_pk_bf16_f32 v91, v96, v97
	v_lshlrev_b32_e32 v94, 16, v186
	v_and_b32_e32 v95, 0xffff0000, v186
	v_lshlrev_b32_e32 v96, 16, v187
	v_and_b32_e32 v97, 0xffff0000, v187
	v_pk_mul_f32 v[88:89], v[88:89], v[0:1] op_sel_hi:[1,0]
	v_pk_mul_f32 v[86:87], v[86:87], v[0:1] op_sel_hi:[1,0]
	v_cvt_pk_bf16_f32 v92, v92, v93
	v_cvt_pk_bf16_f32 v93, v102, v103
	v_lshlrev_b32_e32 v102, 16, v188
	v_and_b32_e32 v103, 0xffff0000, v188
	v_pk_fma_f32 v[88:89], v[172:173], v[88:89], v[96:97]
	v_pk_fma_f32 v[86:87], v[170:171], v[86:87], v[94:95]
	v_pk_mul_f32 v[82:83], v[82:83], v[0:1] op_sel_hi:[1,0]
	v_lshlrev_b32_e32 v104, 16, v189
	v_and_b32_e32 v105, 0xffff0000, v189
	v_pk_mul_f32 v[84:85], v[84:85], v[0:1] op_sel_hi:[1,0]
	v_pk_fma_f32 v[96:97], v[166:167], v[82:83], v[102:103]
	v_mul_f32_e32 v0, v87, v87
	v_mul_f32_e32 v82, v89, v89
	v_pk_fma_f32 v[94:95], v[168:169], v[84:85], v[104:105]
	v_fmac_f32_e32 v0, v86, v86
	v_fmac_f32_e32 v82, v88, v88
	v_add_f32_e32 v0, v0, v82
	v_mul_f32_e32 v82, v97, v97
	v_mul_f32_e32 v83, v95, v95
	v_fmac_f32_e32 v82, v96, v96
	v_fmac_f32_e32 v83, v94, v94
	v_add_f32_e32 v82, v82, v83
	v_add_f32_e32 v0, v0, v82
	v_add_f32_e32 v0, v99, v0
	v_mov_b32_e32 v85, v0
	s_nop 1
	v_permlane16_swap_b32_e32 v85, v0
	v_or_b32_e32 v98, 32, v240
	v_add_u32_e32 v100, s37, v98
	v_ashrrev_i32_e32 v101, 31, v100
	v_lshlrev_b64 v[100:101], 11, v[100:101]
	v_lshl_add_u64 v[82:83], s[6:7], 0, v[100:101]
	s_waitcnt lgkmcnt(0)
	v_add_f32_e32 v0, v0, v85
	v_lshl_add_u64 v[100:101], v[220:221], 1, v[82:83]
	v_mov_b32_e32 v82, v0
	s_nop 1
	v_permlane32_swap_b32_e32 v82, v0
	global_store_dwordx4 v[100:101], v[90:93], off
	v_cvt_pk_bf16_f32 v84, v86, v87
	v_cvt_pk_bf16_f32 v85, v88, v89
	v_cvt_pk_bf16_f32 v86, v96, v97
	v_cvt_pk_bf16_f32 v87, v94, v95
	global_store_dwordx4 v[100:101], v[84:87], off offset:256
	s_and_saveexec_b64 s[8:9], s[42:43]
	s_cbranch_execz .LBB0_646
	v_lshl_add_u32 v83, v98, 4, s36
	s_waitcnt lgkmcnt(0)
	v_add_f32_e32 v0, v0, v82
	ds_write_b32 v83, v0 offset:6144

.LBB0_648:
	v_lshlrev_b32_e32 v86, 16, v174
	v_and_b32_e32 v87, 0xffff0000, v174
	v_lshlrev_b32_e32 v88, 16, v175
	v_and_b32_e32 v89, 0xffff0000, v175
	s_waitcnt lgkmcnt(0)
	v_pk_mul_f32 v[80:81], v[80:81], v[0:1] op_sel_hi:[1,0]
	v_pk_mul_f32 v[78:79], v[78:79], v[0:1] op_sel_hi:[1,0]
	v_lshlrev_b32_e32 v90, 16, v176
	v_and_b32_e32 v91, 0xffff0000, v176
	v_lshlrev_b32_e32 v92, 16, v177
	v_and_b32_e32 v93, 0xffff0000, v177
	v_pk_fma_f32 v[80:81], v[184:185], v[80:81], v[88:89]
	v_pk_fma_f32 v[78:79], v[182:183], v[78:79], v[86:87]
	v_pk_mul_f32 v[76:77], v[76:77], v[0:1] op_sel_hi:[1,0]
	v_pk_mul_f32 v[74:75], v[74:75], v[0:1] op_sel_hi:[1,0]
	v_pk_fma_f32 v[86:87], v[180:181], v[76:77], v[92:93]
	v_pk_fma_f32 v[76:77], v[178:179], v[74:75], v[90:91]
	v_mul_f32_e32 v74, v79, v79
	v_mul_f32_e32 v75, v81, v81
	v_fmac_f32_e32 v74, v78, v78
	v_fmac_f32_e32 v75, v80, v80
	v_add_f32_e32 v74, v74, v75
	v_mul_f32_e32 v75, v77, v77
	v_mul_f32_e32 v83, v87, v87
	v_fmac_f32_e32 v75, v76, v76
	v_fmac_f32_e32 v83, v86, v86
	v_add_f32_e32 v75, v75, v83
	v_add_f32_e32 v83, v74, v75
	v_cvt_pk_bf16_f32 v74, v78, v79
	v_cvt_pk_bf16_f32 v75, v80, v81
	v_lshlrev_b32_e32 v78, 16, v162
	v_and_b32_e32 v79, 0xffff0000, v162
	v_lshlrev_b32_e32 v80, 16, v163
	v_and_b32_e32 v81, 0xffff0000, v163
	v_pk_mul_f32 v[72:73], v[72:73], v[0:1] op_sel_hi:[1,0]
	v_pk_mul_f32 v[70:71], v[70:71], v[0:1] op_sel_hi:[1,0]
	v_cvt_pk_bf16_f32 v76, v76, v77
	v_cvt_pk_bf16_f32 v77, v86, v87
	v_lshlrev_b32_e32 v86, 16, v164
	v_and_b32_e32 v87, 0xffff0000, v164
	v_pk_fma_f32 v[72:73], v[172:173], v[72:73], v[80:81]
	v_pk_fma_f32 v[70:71], v[170:171], v[70:71], v[78:79]
	v_pk_mul_f32 v[66:67], v[66:67], v[0:1] op_sel_hi:[1,0]
	v_lshlrev_b32_e32 v88, 16, v165
	v_and_b32_e32 v89, 0xffff0000, v165
	v_pk_mul_f32 v[68:69], v[68:69], v[0:1] op_sel_hi:[1,0]
	v_pk_fma_f32 v[80:81], v[166:167], v[66:67], v[86:87]
	v_mul_f32_e32 v0, v71, v71
	v_mul_f32_e32 v66, v73, v73
	v_pk_fma_f32 v[78:79], v[168:169], v[68:69], v[88:89]
	v_fmac_f32_e32 v0, v70, v70
	v_fmac_f32_e32 v66, v72, v72
	v_add_f32_e32 v0, v0, v66
	v_mul_f32_e32 v66, v81, v81
	v_mul_f32_e32 v67, v79, v79
	v_fmac_f32_e32 v66, v80, v80
	v_fmac_f32_e32 v67, v78, v78
	v_add_f32_e32 v66, v66, v67
	v_add_f32_e32 v0, v0, v66
	v_add_f32_e32 v0, v83, v0
	v_mov_b32_e32 v69, v0
	s_nop 1
	v_permlane16_swap_b32_e32 v69, v0
	v_or_b32_e32 v82, 48, v240
	v_add_u32_e32 v84, s37, v82
	v_ashrrev_i32_e32 v85, 31, v84
	v_lshlrev_b64 v[84:85], 11, v[84:85]
	v_lshl_add_u64 v[66:67], s[6:7], 0, v[84:85]
	s_waitcnt lgkmcnt(0)
	v_add_f32_e32 v0, v0, v69
	v_lshl_add_u64 v[84:85], v[220:221], 1, v[66:67]
	v_mov_b32_e32 v66, v0
	s_nop 1
	v_permlane32_swap_b32_e32 v66, v0
	global_store_dwordx4 v[84:85], v[74:77], off
	v_cvt_pk_bf16_f32 v68, v70, v71
	v_cvt_pk_bf16_f32 v69, v72, v73
	v_cvt_pk_bf16_f32 v70, v80, v81
	v_cvt_pk_bf16_f32 v71, v78, v79
	global_store_dwordx4 v[84:85], v[68:71], off offset:256
	s_and_saveexec_b64 s[8:9], s[42:43]
	s_cbranch_execz .LBB0_650
	v_lshl_add_u32 v67, v82, 4, s36
	s_waitcnt lgkmcnt(0)
	v_add_f32_e32 v0, v0, v66
	ds_write_b32 v67, v0 offset:6144

.LBB0_652:
	v_lshlrev_b32_e32 v70, 16, v158
	v_and_b32_e32 v71, 0xffff0000, v158
	v_lshlrev_b32_e32 v72, 16, v159
	v_and_b32_e32 v73, 0xffff0000, v159
	s_waitcnt lgkmcnt(0)
	v_pk_mul_f32 v[64:65], v[64:65], v[0:1] op_sel_hi:[1,0]
	v_pk_mul_f32 v[62:63], v[62:63], v[0:1] op_sel_hi:[1,0]
	v_lshlrev_b32_e32 v74, 16, v160
	v_and_b32_e32 v75, 0xffff0000, v160
	v_lshlrev_b32_e32 v76, 16, v161
	v_and_b32_e32 v77, 0xffff0000, v161
	v_pk_fma_f32 v[64:65], v[184:185], v[64:65], v[72:73]
	v_pk_fma_f32 v[62:63], v[182:183], v[62:63], v[70:71]
	v_pk_mul_f32 v[60:61], v[60:61], v[0:1] op_sel_hi:[1,0]
	v_pk_mul_f32 v[58:59], v[58:59], v[0:1] op_sel_hi:[1,0]
	v_pk_fma_f32 v[70:71], v[180:181], v[60:61], v[76:77]
	v_pk_fma_f32 v[60:61], v[178:179], v[58:59], v[74:75]
	v_mul_f32_e32 v58, v63, v63
	v_mul_f32_e32 v59, v65, v65
	v_fmac_f32_e32 v58, v62, v62
	v_fmac_f32_e32 v59, v64, v64
	v_add_f32_e32 v58, v58, v59
	v_mul_f32_e32 v59, v61, v61
	v_mul_f32_e32 v67, v71, v71
	v_fmac_f32_e32 v59, v60, v60
	v_fmac_f32_e32 v67, v70, v70
	v_add_f32_e32 v59, v59, v67
	v_add_f32_e32 v67, v58, v59
	v_cvt_pk_bf16_f32 v58, v62, v63
	v_cvt_pk_bf16_f32 v59, v64, v65
	v_lshlrev_b32_e32 v62, 16, v154
	v_and_b32_e32 v63, 0xffff0000, v154
	v_lshlrev_b32_e32 v64, 16, v155
	v_and_b32_e32 v65, 0xffff0000, v155
	v_pk_mul_f32 v[56:57], v[56:57], v[0:1] op_sel_hi:[1,0]
	v_pk_mul_f32 v[54:55], v[54:55], v[0:1] op_sel_hi:[1,0]
	v_cvt_pk_bf16_f32 v60, v60, v61
	v_cvt_pk_bf16_f32 v61, v70, v71
	v_lshlrev_b32_e32 v70, 16, v156
	v_and_b32_e32 v71, 0xffff0000, v156
	v_pk_fma_f32 v[56:57], v[172:173], v[56:57], v[64:65]
	v_pk_fma_f32 v[54:55], v[170:171], v[54:55], v[62:63]
	v_pk_mul_f32 v[50:51], v[50:51], v[0:1] op_sel_hi:[1,0]
	v_lshlrev_b32_e32 v72, 16, v157
	v_and_b32_e32 v73, 0xffff0000, v157
	v_pk_mul_f32 v[52:53], v[52:53], v[0:1] op_sel_hi:[1,0]
	v_pk_fma_f32 v[64:65], v[166:167], v[50:51], v[70:71]
	v_mul_f32_e32 v0, v55, v55
	v_mul_f32_e32 v50, v57, v57
	v_pk_fma_f32 v[62:63], v[168:169], v[52:53], v[72:73]
	v_fmac_f32_e32 v0, v54, v54
	v_fmac_f32_e32 v50, v56, v56
	v_add_f32_e32 v0, v0, v50
	v_mul_f32_e32 v50, v65, v65
	v_mul_f32_e32 v51, v63, v63
	v_fmac_f32_e32 v50, v64, v64
	v_fmac_f32_e32 v51, v62, v62
	v_add_f32_e32 v50, v50, v51
	v_add_f32_e32 v0, v0, v50
	v_add_f32_e32 v0, v67, v0
	v_mov_b32_e32 v53, v0
	s_nop 1
	v_permlane16_swap_b32_e32 v53, v0
	v_add_u32_e32 v66, 0x80, v240
	v_add_u32_e32 v68, s37, v66
	v_ashrrev_i32_e32 v69, 31, v68
	v_lshlrev_b64 v[68:69], 11, v[68:69]
	v_lshl_add_u64 v[50:51], s[6:7], 0, v[68:69]
	s_waitcnt lgkmcnt(0)
	v_add_f32_e32 v0, v0, v53
	v_lshl_add_u64 v[68:69], v[220:221], 1, v[50:51]
	v_mov_b32_e32 v50, v0
	s_nop 1
	v_permlane32_swap_b32_e32 v50, v0
	global_store_dwordx4 v[68:69], v[58:61], off
	v_cvt_pk_bf16_f32 v52, v54, v55
	v_cvt_pk_bf16_f32 v53, v56, v57
	v_cvt_pk_bf16_f32 v54, v64, v65
	v_cvt_pk_bf16_f32 v55, v62, v63
	global_store_dwordx4 v[68:69], v[52:55], off offset:256
	s_and_saveexec_b64 s[8:9], s[42:43]
	s_cbranch_execz .LBB0_654
	v_lshl_add_u32 v51, v66, 4, s36
	s_waitcnt lgkmcnt(0)
	v_add_f32_e32 v0, v0, v50
	ds_write_b32 v51, v0 offset:6144

.LBB0_656:
	v_lshlrev_b32_e32 v54, 16, v150
	v_and_b32_e32 v55, 0xffff0000, v150
	v_lshlrev_b32_e32 v56, 16, v151
	v_and_b32_e32 v57, 0xffff0000, v151
	s_waitcnt lgkmcnt(0)
	v_pk_mul_f32 v[48:49], v[48:49], v[0:1] op_sel_hi:[1,0]
	v_pk_mul_f32 v[46:47], v[46:47], v[0:1] op_sel_hi:[1,0]
	v_lshlrev_b32_e32 v58, 16, v152
	v_and_b32_e32 v59, 0xffff0000, v152
	v_lshlrev_b32_e32 v60, 16, v153
	v_and_b32_e32 v61, 0xffff0000, v153
	v_pk_fma_f32 v[48:49], v[184:185], v[48:49], v[56:57]
	v_pk_fma_f32 v[46:47], v[182:183], v[46:47], v[54:55]
	v_pk_mul_f32 v[44:45], v[44:45], v[0:1] op_sel_hi:[1,0]
	v_pk_mul_f32 v[42:43], v[42:43], v[0:1] op_sel_hi:[1,0]
	v_pk_fma_f32 v[54:55], v[180:181], v[44:45], v[60:61]
	v_pk_fma_f32 v[44:45], v[178:179], v[42:43], v[58:59]
	v_mul_f32_e32 v42, v47, v47
	v_mul_f32_e32 v43, v49, v49
	v_fmac_f32_e32 v42, v46, v46
	v_fmac_f32_e32 v43, v48, v48
	v_add_f32_e32 v42, v42, v43
	v_mul_f32_e32 v43, v45, v45
	v_mul_f32_e32 v51, v55, v55
	v_fmac_f32_e32 v43, v44, v44
	v_fmac_f32_e32 v51, v54, v54
	v_add_f32_e32 v43, v43, v51
	v_add_f32_e32 v51, v42, v43
	v_cvt_pk_bf16_f32 v42, v46, v47
	v_cvt_pk_bf16_f32 v43, v48, v49
	v_lshlrev_b32_e32 v46, 16, v146
	v_and_b32_e32 v47, 0xffff0000, v146
	v_lshlrev_b32_e32 v48, 16, v147
	v_and_b32_e32 v49, 0xffff0000, v147
	v_pk_mul_f32 v[40:41], v[40:41], v[0:1] op_sel_hi:[1,0]
	v_pk_mul_f32 v[38:39], v[38:39], v[0:1] op_sel_hi:[1,0]
	v_cvt_pk_bf16_f32 v44, v44, v45
	v_cvt_pk_bf16_f32 v45, v54, v55
	v_lshlrev_b32_e32 v54, 16, v148
	v_and_b32_e32 v55, 0xffff0000, v148
	v_pk_fma_f32 v[40:41], v[172:173], v[40:41], v[48:49]
	v_pk_fma_f32 v[38:39], v[170:171], v[38:39], v[46:47]
	v_pk_mul_f32 v[34:35], v[34:35], v[0:1] op_sel_hi:[1,0]
	v_lshlrev_b32_e32 v56, 16, v149
	v_and_b32_e32 v57, 0xffff0000, v149
	v_pk_mul_f32 v[36:37], v[36:37], v[0:1] op_sel_hi:[1,0]
	v_pk_fma_f32 v[48:49], v[166:167], v[34:35], v[54:55]
	v_mul_f32_e32 v0, v39, v39
	v_mul_f32_e32 v34, v41, v41
	v_pk_fma_f32 v[46:47], v[168:169], v[36:37], v[56:57]
	v_fmac_f32_e32 v0, v38, v38
	v_fmac_f32_e32 v34, v40, v40
	v_add_f32_e32 v0, v0, v34
	v_mul_f32_e32 v34, v49, v49
	v_mul_f32_e32 v35, v47, v47
	v_fmac_f32_e32 v34, v48, v48
	v_fmac_f32_e32 v35, v46, v46
	v_add_f32_e32 v34, v34, v35
	v_add_f32_e32 v0, v0, v34
	v_add_f32_e32 v0, v51, v0
	v_mov_b32_e32 v37, v0
	s_nop 1
	v_permlane16_swap_b32_e32 v37, v0
	v_add_u32_e32 v50, 0x90, v240
	v_add_u32_e32 v52, s37, v50
	v_ashrrev_i32_e32 v53, 31, v52
	v_lshlrev_b64 v[52:53], 11, v[52:53]
	v_lshl_add_u64 v[34:35], s[6:7], 0, v[52:53]
	s_waitcnt lgkmcnt(0)
	v_add_f32_e32 v0, v0, v37
	v_lshl_add_u64 v[52:53], v[220:221], 1, v[34:35]
	v_mov_b32_e32 v34, v0
	s_nop 1
	v_permlane32_swap_b32_e32 v34, v0
	global_store_dwordx4 v[52:53], v[42:45], off
	v_cvt_pk_bf16_f32 v36, v38, v39
	v_cvt_pk_bf16_f32 v37, v40, v41
	v_cvt_pk_bf16_f32 v38, v48, v49
	v_cvt_pk_bf16_f32 v39, v46, v47
	global_store_dwordx4 v[52:53], v[36:39], off offset:256
	s_and_saveexec_b64 s[8:9], s[42:43]
	s_cbranch_execz .LBB0_658
	v_lshl_add_u32 v35, v50, 4, s36
	s_waitcnt lgkmcnt(0)
	v_add_f32_e32 v0, v0, v34
	ds_write_b32 v35, v0 offset:6144

.LBB0_660:
	v_lshlrev_b32_e32 v38, 16, v142
	v_and_b32_e32 v39, 0xffff0000, v142
	v_lshlrev_b32_e32 v40, 16, v143
	v_and_b32_e32 v41, 0xffff0000, v143
	s_waitcnt lgkmcnt(0)
	v_pk_mul_f32 v[32:33], v[32:33], v[0:1] op_sel_hi:[1,0]
	v_pk_mul_f32 v[30:31], v[30:31], v[0:1] op_sel_hi:[1,0]
	v_lshlrev_b32_e32 v42, 16, v144
	v_and_b32_e32 v43, 0xffff0000, v144
	v_lshlrev_b32_e32 v44, 16, v145
	v_and_b32_e32 v45, 0xffff0000, v145
	v_pk_fma_f32 v[32:33], v[184:185], v[32:33], v[40:41]
	v_pk_fma_f32 v[30:31], v[182:183], v[30:31], v[38:39]
	v_pk_mul_f32 v[28:29], v[28:29], v[0:1] op_sel_hi:[1,0]
	v_pk_mul_f32 v[26:27], v[26:27], v[0:1] op_sel_hi:[1,0]
	v_pk_fma_f32 v[38:39], v[180:181], v[28:29], v[44:45]
	v_pk_fma_f32 v[28:29], v[178:179], v[26:27], v[42:43]
	v_mul_f32_e32 v26, v31, v31
	v_mul_f32_e32 v27, v33, v33
	v_fmac_f32_e32 v26, v30, v30
	v_fmac_f32_e32 v27, v32, v32
	v_add_f32_e32 v26, v26, v27
	v_mul_f32_e32 v27, v29, v29
	v_mul_f32_e32 v35, v39, v39
	v_fmac_f32_e32 v27, v28, v28
	v_fmac_f32_e32 v35, v38, v38
	v_add_f32_e32 v27, v27, v35
	v_add_f32_e32 v35, v26, v27
	v_cvt_pk_bf16_f32 v26, v30, v31
	v_cvt_pk_bf16_f32 v27, v32, v33
	v_lshlrev_b32_e32 v30, 16, v138
	v_and_b32_e32 v31, 0xffff0000, v138
	v_lshlrev_b32_e32 v32, 16, v139
	v_and_b32_e32 v33, 0xffff0000, v139
	v_pk_mul_f32 v[24:25], v[24:25], v[0:1] op_sel_hi:[1,0]
	v_pk_mul_f32 v[22:23], v[22:23], v[0:1] op_sel_hi:[1,0]
	v_cvt_pk_bf16_f32 v28, v28, v29
	v_cvt_pk_bf16_f32 v29, v38, v39
	v_lshlrev_b32_e32 v38, 16, v140
	v_and_b32_e32 v39, 0xffff0000, v140
	v_pk_fma_f32 v[24:25], v[172:173], v[24:25], v[32:33]
	v_pk_fma_f32 v[22:23], v[170:171], v[22:23], v[30:31]
	v_pk_mul_f32 v[18:19], v[18:19], v[0:1] op_sel_hi:[1,0]
	v_lshlrev_b32_e32 v40, 16, v141
	v_and_b32_e32 v41, 0xffff0000, v141
	v_pk_mul_f32 v[20:21], v[20:21], v[0:1] op_sel_hi:[1,0]
	v_pk_fma_f32 v[32:33], v[166:167], v[18:19], v[38:39]
	v_mul_f32_e32 v0, v23, v23
	v_mul_f32_e32 v18, v25, v25
	v_pk_fma_f32 v[30:31], v[168:169], v[20:21], v[40:41]
	v_fmac_f32_e32 v0, v22, v22
	v_fmac_f32_e32 v18, v24, v24
	v_add_f32_e32 v0, v0, v18
	v_mul_f32_e32 v18, v33, v33
	v_mul_f32_e32 v19, v31, v31
	v_fmac_f32_e32 v18, v32, v32
	v_fmac_f32_e32 v19, v30, v30
	v_add_f32_e32 v18, v18, v19
	v_add_f32_e32 v0, v0, v18
	v_add_f32_e32 v0, v35, v0
	v_mov_b32_e32 v21, v0
	s_nop 1
	v_permlane16_swap_b32_e32 v21, v0
	v_add_u32_e32 v34, 0xa0, v240
	v_add_u32_e32 v36, s37, v34
	v_ashrrev_i32_e32 v37, 31, v36
	v_lshlrev_b64 v[36:37], 11, v[36:37]
	v_lshl_add_u64 v[18:19], s[6:7], 0, v[36:37]
	s_waitcnt lgkmcnt(0)
	v_add_f32_e32 v0, v0, v21
	v_lshl_add_u64 v[36:37], v[220:221], 1, v[18:19]
	v_mov_b32_e32 v18, v0
	s_nop 1
	v_permlane32_swap_b32_e32 v18, v0
	global_store_dwordx4 v[36:37], v[26:29], off
	v_cvt_pk_bf16_f32 v20, v22, v23
	v_cvt_pk_bf16_f32 v21, v24, v25
	v_cvt_pk_bf16_f32 v22, v32, v33
	v_cvt_pk_bf16_f32 v23, v30, v31
	global_store_dwordx4 v[36:37], v[20:23], off offset:256
	s_and_saveexec_b64 s[8:9], s[42:43]
	s_cbranch_execz .LBB0_662
	v_lshl_add_u32 v19, v34, 4, s36
	s_waitcnt lgkmcnt(0)
	v_add_f32_e32 v0, v0, v18
	ds_write_b32 v19, v0 offset:6144

.LBB0_664:
	v_lshlrev_b32_e32 v22, 16, v126
	v_and_b32_e32 v23, 0xffff0000, v126
	v_lshlrev_b32_e32 v24, 16, v127
	v_and_b32_e32 v25, 0xffff0000, v127
	s_waitcnt lgkmcnt(0)
	v_pk_mul_f32 v[16:17], v[16:17], v[0:1] op_sel_hi:[1,0]
	v_pk_mul_f32 v[14:15], v[14:15], v[0:1] op_sel_hi:[1,0]
	v_lshlrev_b32_e32 v26, 16, v128
	v_and_b32_e32 v27, 0xffff0000, v128
	v_lshlrev_b32_e32 v28, 16, v129
	v_and_b32_e32 v29, 0xffff0000, v129
	v_pk_fma_f32 v[16:17], v[184:185], v[16:17], v[24:25]
	v_pk_fma_f32 v[14:15], v[182:183], v[14:15], v[22:23]
	v_pk_mul_f32 v[12:13], v[12:13], v[0:1] op_sel_hi:[1,0]
	v_pk_mul_f32 v[10:11], v[10:11], v[0:1] op_sel_hi:[1,0]
	v_pk_fma_f32 v[22:23], v[180:181], v[12:13], v[28:29]
	v_pk_fma_f32 v[12:13], v[178:179], v[10:11], v[26:27]
	v_mul_f32_e32 v10, v15, v15
	v_mul_f32_e32 v11, v17, v17
	v_fmac_f32_e32 v10, v14, v14
	v_fmac_f32_e32 v11, v16, v16
	v_add_f32_e32 v10, v10, v11
	v_mul_f32_e32 v11, v13, v13
	v_mul_f32_e32 v19, v23, v23
	v_fmac_f32_e32 v11, v12, v12
	v_fmac_f32_e32 v19, v22, v22
	v_add_f32_e32 v11, v11, v19
	v_add_f32_e32 v19, v10, v11
	v_cvt_pk_bf16_f32 v10, v14, v15
	v_cvt_pk_bf16_f32 v11, v16, v17
	v_lshlrev_b32_e32 v14, 16, v118
	v_and_b32_e32 v15, 0xffff0000, v118
	v_lshlrev_b32_e32 v16, 16, v119
	v_and_b32_e32 v17, 0xffff0000, v119
	v_pk_mul_f32 v[8:9], v[8:9], v[0:1] op_sel_hi:[1,0]
	v_pk_mul_f32 v[6:7], v[6:7], v[0:1] op_sel_hi:[1,0]
	v_cvt_pk_bf16_f32 v12, v12, v13
	v_cvt_pk_bf16_f32 v13, v22, v23
	v_lshlrev_b32_e32 v22, 16, v120
	v_and_b32_e32 v23, 0xffff0000, v120
	v_pk_fma_f32 v[8:9], v[172:173], v[8:9], v[16:17]
	v_pk_fma_f32 v[6:7], v[170:171], v[6:7], v[14:15]
	v_pk_mul_f32 v[2:3], v[2:3], v[0:1] op_sel_hi:[1,0]
	v_lshlrev_b32_e32 v24, 16, v121
	v_and_b32_e32 v25, 0xffff0000, v121
	v_pk_mul_f32 v[4:5], v[4:5], v[0:1] op_sel_hi:[1,0]
	v_pk_fma_f32 v[16:17], v[166:167], v[2:3], v[22:23]
	v_mul_f32_e32 v0, v7, v7
	v_mul_f32_e32 v2, v9, v9
	v_pk_fma_f32 v[14:15], v[168:169], v[4:5], v[24:25]
	v_fmac_f32_e32 v0, v6, v6
	v_fmac_f32_e32 v2, v8, v8
	v_add_f32_e32 v0, v0, v2
	v_mul_f32_e32 v2, v17, v17
	v_mul_f32_e32 v3, v15, v15
	v_fmac_f32_e32 v2, v16, v16
	v_fmac_f32_e32 v3, v14, v14
	v_add_f32_e32 v2, v2, v3
	v_add_f32_e32 v0, v0, v2
	v_add_f32_e32 v0, v19, v0
	v_mov_b32_e32 v5, v0
	s_nop 1
	v_permlane16_swap_b32_e32 v5, v0
	v_add_u32_e32 v18, 0xb0, v240
	v_add_u32_e32 v20, s37, v18
	v_ashrrev_i32_e32 v21, 31, v20
	v_lshlrev_b64 v[20:21], 11, v[20:21]
	v_lshl_add_u64 v[2:3], s[6:7], 0, v[20:21]
	s_waitcnt lgkmcnt(0)
	v_add_f32_e32 v0, v0, v5
	v_lshl_add_u64 v[20:21], v[220:221], 1, v[2:3]
	v_mov_b32_e32 v2, v0
	s_nop 1
	v_permlane32_swap_b32_e32 v2, v0
	global_store_dwordx4 v[20:21], v[10:13], off
	v_cvt_pk_bf16_f32 v4, v6, v7
	v_cvt_pk_bf16_f32 v5, v8, v9
	v_cvt_pk_bf16_f32 v6, v16, v17
	v_cvt_pk_bf16_f32 v7, v14, v15
	global_store_dwordx4 v[20:21], v[4:7], off offset:256
	s_and_saveexec_b64 s[6:7], s[42:43]
	s_cbranch_execz .LBB0_666
	v_lshl_add_u32 v3, v18, 4, s36
	s_waitcnt lgkmcnt(0)
	v_add_f32_e32 v0, v0, v2
	ds_write_b32 v3, v0 offset:6144

.LBB0_692:
	s_lshl_b32 s5, s19, 5
	s_lshl_b32 s8, s18, 8
	v_lshrrev_b32_e32 v0, 1, v239
	s_add_i32 s4, s92, 64
	s_or_b32 s5, s8, s5
	v_and_or_b32 v220, v0, 24, s5
	s_lshl_b32 s35, s4, 8
	v_add_u32_e32 v118, s35, v240
	v_ashrrev_i32_e32 v221, 31, v220
	v_lshl_add_u64 v[120:121], v[220:221], 1, s[6:7]
	s_mov_b64 s[6:7], 0x4000000
	v_ashrrev_i32_e32 v119, 31, v118
	v_lshl_add_u64 v[120:121], v[120:121], 0, s[6:7]
	v_lshlrev_b64 v[224:225], 11, v[118:119]
	v_lshl_add_u64 v[126:127], v[120:121], 0, v[224:225]
	s_barrier
	global_load_dwordx4 v[206:209], v[126:127], off
	global_load_dwordx4 v[202:205], v[126:127], off offset:256
	v_or_b32_e32 v126, 16, v118
	v_ashrrev_i32_e32 v127, 31, v126
	v_lshlrev_b64 v[126:127], 11, v[126:127]
	v_lshl_add_u64 v[126:127], v[120:121], 0, v[126:127]
	global_load_dwordx4 v[198:201], v[126:127], off
	global_load_dwordx4 v[194:197], v[126:127], off offset:256
	v_or_b32_e32 v126, 32, v118
	v_ashrrev_i32_e32 v127, 31, v126
	v_lshlrev_b64 v[126:127], 11, v[126:127]
	v_lshl_add_u64 v[126:127], v[120:121], 0, v[126:127]
	global_load_dwordx4 v[190:193], v[126:127], off
	global_load_dwordx4 v[186:189], v[126:127], off offset:256
	v_or_b32_e32 v126, 48, v118
	v_ashrrev_i32_e32 v127, 31, v126
	v_lshlrev_b64 v[126:127], 11, v[126:127]
	v_lshl_add_u64 v[126:127], v[120:121], 0, v[126:127]
	global_load_dwordx4 v[174:177], v[126:127], off
	global_load_dwordx4 v[162:165], v[126:127], off offset:256
	v_add_u32_e32 v126, 0x80, v118
	v_ashrrev_i32_e32 v127, 31, v126
	v_lshlrev_b64 v[126:127], 11, v[126:127]
	v_lshl_add_u64 v[126:127], v[120:121], 0, v[126:127]
	global_load_dwordx4 v[158:161], v[126:127], off
	global_load_dwordx4 v[154:157], v[126:127], off offset:256
	v_add_u32_e32 v126, 0x90, v118
	v_ashrrev_i32_e32 v127, 31, v126
	v_lshlrev_b64 v[126:127], 11, v[126:127]
	v_lshl_add_u64 v[126:127], v[120:121], 0, v[126:127]
	global_load_dwordx4 v[150:153], v[126:127], off
	global_load_dwordx4 v[146:149], v[126:127], off offset:256
	v_add_u32_e32 v126, 0xa0, v118
	v_add_u32_e32 v118, 0xb0, v118
	v_ashrrev_i32_e32 v127, 31, v126
	v_ashrrev_i32_e32 v119, 31, v118
	v_lshlrev_b64 v[126:127], 11, v[126:127]
	v_lshlrev_b64 v[118:119], 11, v[118:119]
	v_lshl_add_u64 v[126:127], v[120:121], 0, v[126:127]
	v_lshl_add_u64 v[118:119], v[120:121], 0, v[118:119]
	global_load_dwordx4 v[142:145], v[126:127], off
	global_load_dwordx4 v[138:141], v[126:127], off offset:256
	s_nop 0
	global_load_dwordx4 v[126:129], v[118:119], off
	s_nop 0
	global_load_dwordx4 v[118:121], v[118:119], off offset:256
	v_and_b32_e32 v167, 64, v231
	v_xor_b32_e32 v0, 16, v231
	v_add_u32_e32 v167, 64, v167
	v_cmp_lt_i32_e32 vcc, v0, v167
	v_mul_f32_e32 v168, v137, v137
	v_fmac_f32_e32 v168, v136, v136
	v_cndmask_b32_e32 v0, v231, v0, vcc
	v_lshlrev_b32_e32 v241, 2, v0
	v_mul_f32_e32 v0, v135, v135
	v_fmac_f32_e32 v0, v134, v134
	v_add_f32_e32 v0, v0, v168
	v_mul_f32_e32 v168, v131, v131
	v_mul_f32_e32 v169, v133, v133
	v_fmac_f32_e32 v168, v130, v130
	v_fmac_f32_e32 v169, v132, v132
	v_add_f32_e32 v168, v168, v169
	v_add_f32_e32 v0, v168, v0
	v_mul_f32_e32 v168, v123, v123
	v_mul_f32_e32 v169, v125, v125
	v_fmac_f32_e32 v168, v122, v122
	v_fmac_f32_e32 v169, v124, v124
	v_add_f32_e32 v168, v168, v169
	v_add_f32_e32 v0, v168, v0
	v_mul_f32_e32 v168, v115, v115
	v_mul_f32_e32 v169, v117, v117
	v_fmac_f32_e32 v168, v114, v114
	v_fmac_f32_e32 v169, v116, v116
	v_add_f32_e32 v168, v168, v169
	v_add_f32_e32 v0, v168, v0
	v_mov_b32_e32 v168, v0
	s_nop 1
	v_permlane16_swap_b32_e32 v168, v0
	v_xor_b32_e32 v169, 32, v231
	v_cmp_lt_i32_e32 vcc, v169, v167
	s_lshl_b32 s5, s19, 2
	s_add_i32 s34, s5, 0
	v_cndmask_b32_e32 v167, v231, v169, vcc
	v_lshlrev_b32_e32 v242, 2, v167
	s_waitcnt lgkmcnt(0)
	v_add_f32_e32 v167, v0, v168
	v_mov_b32_e32 v168, v167
	s_nop 1
	v_permlane32_swap_b32_e32 v168, v167
	v_and_b32_e32 v0, 63, v239
	v_cmp_gt_u32_e64 s[40:41], 16, v0
	s_and_saveexec_b64 s[6:7], s[40:41]
	s_load_dwordx2 s[90:91], s[0:1], 0xb0
	v_readlane_b32 s64, v252, 3
	v_readlane_b32 s65, v255, 10
	v_readlane_b32 s68, v255, 11
	s_cbranch_execz .LBB0_694
	s_lshl_b32 s5, s76, 10
	s_add_i32 s5, s34, s5
	s_waitcnt lgkmcnt(0)
	v_add_f32_e32 v167, v167, v168
	v_lshl_add_u32 v168, v166, 4, s5
	ds_write_b32 v168, v167
.LBB0_694:
	s_or_b64 exec, exec, s[6:7]
	v_mul_f32_e32 v167, v111, v111
	s_waitcnt lgkmcnt(0)
	v_mul_f32_e32 v168, v113, v113
	v_fmac_f32_e32 v167, v110, v110
	v_fmac_f32_e32 v168, v112, v112
	v_add_f32_e32 v167, v167, v168
	v_mul_f32_e32 v168, v107, v107
	v_mul_f32_e32 v169, v109, v109
	v_fmac_f32_e32 v168, v106, v106
	v_fmac_f32_e32 v169, v108, v108
	v_add_f32_e32 v168, v168, v169
	v_add_f32_e32 v167, v168, v167
	v_mul_f32_e32 v168, v103, v103
	v_mul_f32_e32 v169, v105, v105
	v_fmac_f32_e32 v168, v102, v102
	v_fmac_f32_e32 v169, v104, v104
	v_add_f32_e32 v168, v168, v169
	v_add_f32_e32 v167, v168, v167
	v_mul_f32_e32 v168, v99, v99
	v_mul_f32_e32 v169, v101, v101
	v_fmac_f32_e32 v168, v98, v98
	v_fmac_f32_e32 v169, v100, v100
	v_add_f32_e32 v168, v168, v169
	v_add_f32_e32 v167, v168, v167
	v_mov_b32_e32 v168, v167
	s_nop 1
	v_permlane16_swap_b32_e32 v168, v167
	s_waitcnt lgkmcnt(0)
	v_add_f32_e32 v167, v167, v168
	v_mov_b32_e32 v168, v167
	s_nop 1
	v_permlane32_swap_b32_e32 v168, v167
	s_and_saveexec_b64 s[6:7], s[40:41]
	s_movk_i32 s92, 0x2b20
	s_cbranch_execz .LBB0_696
	s_lshl_b32 s5, s76, 10
	s_add_i32 s5, s34, s5
	s_waitcnt lgkmcnt(0)
	v_add_f32_e32 v167, v167, v168
	v_lshl_add_u32 v168, v166, 4, s5
	ds_write_b32 v168, v167 offset:256
.LBB0_696:
	s_or_b64 exec, exec, s[6:7]
	v_mul_f32_e32 v167, v95, v95
	s_waitcnt lgkmcnt(0)
	v_mul_f32_e32 v168, v97, v97
	v_fmac_f32_e32 v167, v94, v94
	v_fmac_f32_e32 v168, v96, v96
	v_add_f32_e32 v167, v167, v168
	v_mul_f32_e32 v168, v91, v91
	v_mul_f32_e32 v169, v93, v93
	v_fmac_f32_e32 v168, v90, v90
	v_fmac_f32_e32 v169, v92, v92
	v_add_f32_e32 v168, v168, v169
	v_add_f32_e32 v167, v168, v167
	v_mul_f32_e32 v168, v87, v87
	v_mul_f32_e32 v169, v89, v89
	v_fmac_f32_e32 v168, v86, v86
	v_fmac_f32_e32 v169, v88, v88
	v_add_f32_e32 v168, v168, v169
	v_add_f32_e32 v167, v168, v167
	v_mul_f32_e32 v168, v83, v83
	v_mul_f32_e32 v169, v85, v85
	v_fmac_f32_e32 v168, v82, v82
	v_fmac_f32_e32 v169, v84, v84
	v_add_f32_e32 v168, v168, v169
	v_add_f32_e32 v167, v168, v167
	v_mov_b32_e32 v168, v167
	s_nop 1
	v_permlane16_swap_b32_e32 v168, v167
	s_waitcnt lgkmcnt(0)
	v_add_f32_e32 v167, v167, v168
	v_mov_b32_e32 v168, v167
	s_nop 1
	v_permlane32_swap_b32_e32 v168, v167
	s_and_saveexec_b64 s[6:7], s[40:41]
	s_cbranch_execz .LBB0_698
	s_lshl_b32 s5, s76, 10
	s_add_i32 s5, s34, s5
	s_waitcnt lgkmcnt(0)
	v_add_f32_e32 v167, v167, v168
	v_lshl_add_u32 v168, v166, 4, s5
	ds_write_b32 v168, v167 offset:512
.LBB0_698:
	s_or_b64 exec, exec, s[6:7]
	v_mul_f32_e32 v167, v79, v79
	s_waitcnt lgkmcnt(0)
	v_mul_f32_e32 v168, v81, v81
	v_fmac_f32_e32 v167, v78, v78
	v_fmac_f32_e32 v168, v80, v80
	v_add_f32_e32 v167, v167, v168
	v_mul_f32_e32 v168, v75, v75
	v_mul_f32_e32 v169, v77, v77
	v_fmac_f32_e32 v168, v74, v74
	v_fmac_f32_e32 v169, v76, v76
	v_add_f32_e32 v168, v168, v169
	v_add_f32_e32 v167, v168, v167
	v_mul_f32_e32 v168, v71, v71
	v_mul_f32_e32 v169, v73, v73
	v_fmac_f32_e32 v168, v70, v70
	v_fmac_f32_e32 v169, v72, v72
	v_add_f32_e32 v168, v168, v169
	v_add_f32_e32 v167, v168, v167
	v_mul_f32_e32 v168, v67, v67
	v_mul_f32_e32 v169, v69, v69
	v_fmac_f32_e32 v168, v66, v66
	v_fmac_f32_e32 v169, v68, v68
	v_add_f32_e32 v168, v168, v169
	v_add_f32_e32 v167, v168, v167
	v_mov_b32_e32 v168, v167
	s_nop 1
	v_permlane16_swap_b32_e32 v168, v167
	s_waitcnt lgkmcnt(0)
	v_add_f32_e32 v167, v167, v168
	v_mov_b32_e32 v168, v167
	s_nop 1
	v_permlane32_swap_b32_e32 v168, v167
	s_and_saveexec_b64 s[6:7], s[40:41]
	s_cbranch_execz .LBB0_700
	s_lshl_b32 s5, s76, 10
	s_add_i32 s5, s34, s5
	s_waitcnt lgkmcnt(0)
	v_add_f32_e32 v167, v167, v168
	v_lshl_add_u32 v168, v166, 4, s5
	ds_write_b32 v168, v167 offset:768
.LBB0_700:
	s_or_b64 exec, exec, s[6:7]
	v_mul_f32_e32 v167, v63, v63
	s_waitcnt lgkmcnt(0)
	v_mul_f32_e32 v168, v65, v65
	v_fmac_f32_e32 v167, v62, v62
	v_fmac_f32_e32 v168, v64, v64
	v_add_f32_e32 v167, v167, v168
	v_mul_f32_e32 v168, v59, v59
	v_mul_f32_e32 v169, v61, v61
	v_fmac_f32_e32 v168, v58, v58
	v_fmac_f32_e32 v169, v60, v60
	v_add_f32_e32 v168, v168, v169
	v_add_f32_e32 v167, v168, v167
	v_mul_f32_e32 v168, v55, v55
	v_mul_f32_e32 v169, v57, v57
	v_fmac_f32_e32 v168, v54, v54
	v_fmac_f32_e32 v169, v56, v56
	v_add_f32_e32 v168, v168, v169
	v_add_f32_e32 v167, v168, v167
	v_mul_f32_e32 v168, v51, v51
	v_mul_f32_e32 v169, v53, v53
	v_fmac_f32_e32 v168, v50, v50
	v_fmac_f32_e32 v169, v52, v52
	v_add_f32_e32 v168, v168, v169
	v_add_f32_e32 v167, v168, v167
	v_mov_b32_e32 v168, v167
	s_nop 1
	v_permlane16_swap_b32_e32 v168, v167
	s_waitcnt lgkmcnt(0)
	v_add_f32_e32 v167, v167, v168
	v_mov_b32_e32 v168, v167
	s_nop 1
	v_permlane32_swap_b32_e32 v168, v167
	s_and_saveexec_b64 s[6:7], s[40:41]
	s_cbranch_execz .LBB0_702
	s_lshl_b32 s5, s76, 10
	s_add_i32 s5, s34, s5
	s_waitcnt lgkmcnt(0)
	v_add_f32_e32 v167, v167, v168
	v_lshl_add_u32 v168, v166, 4, s5
	ds_write_b32 v168, v167 offset:2048
.LBB0_702:
	s_or_b64 exec, exec, s[6:7]
	v_mul_f32_e32 v167, v47, v47
	s_waitcnt lgkmcnt(0)
	v_mul_f32_e32 v168, v49, v49
	v_fmac_f32_e32 v167, v46, v46
	v_fmac_f32_e32 v168, v48, v48
	v_add_f32_e32 v167, v167, v168
	v_mul_f32_e32 v168, v43, v43
	v_mul_f32_e32 v169, v45, v45
	v_fmac_f32_e32 v168, v42, v42
	v_fmac_f32_e32 v169, v44, v44
	v_add_f32_e32 v168, v168, v169
	v_add_f32_e32 v167, v168, v167
	v_mul_f32_e32 v168, v39, v39
	v_mul_f32_e32 v169, v41, v41
	v_fmac_f32_e32 v168, v38, v38
	v_fmac_f32_e32 v169, v40, v40
	v_add_f32_e32 v168, v168, v169
	v_add_f32_e32 v167, v168, v167
	v_mul_f32_e32 v168, v35, v35
	v_mul_f32_e32 v169, v37, v37
	v_fmac_f32_e32 v168, v34, v34
	v_fmac_f32_e32 v169, v36, v36
	v_add_f32_e32 v168, v168, v169
	v_add_f32_e32 v167, v168, v167
	v_mov_b32_e32 v168, v167
	s_nop 1
	v_permlane16_swap_b32_e32 v168, v167
	s_waitcnt lgkmcnt(0)
	v_add_f32_e32 v167, v167, v168
	v_mov_b32_e32 v168, v167
	s_nop 1
	v_permlane32_swap_b32_e32 v168, v167
	s_and_saveexec_b64 s[6:7], s[40:41]
	s_cbranch_execz .LBB0_704
	s_lshl_b32 s5, s76, 10
	s_add_i32 s5, s34, s5
	s_waitcnt lgkmcnt(0)
	v_add_f32_e32 v167, v167, v168
	v_lshl_add_u32 v168, v166, 4, s5
	ds_write_b32 v168, v167 offset:2304
.LBB0_704:
	s_or_b64 exec, exec, s[6:7]
	v_mul_f32_e32 v167, v31, v31
	s_waitcnt lgkmcnt(0)
	v_mul_f32_e32 v168, v33, v33
	v_fmac_f32_e32 v167, v30, v30
	v_fmac_f32_e32 v168, v32, v32
	v_add_f32_e32 v167, v167, v168
	v_mul_f32_e32 v168, v27, v27
	v_mul_f32_e32 v169, v29, v29
	v_fmac_f32_e32 v168, v26, v26
	v_fmac_f32_e32 v169, v28, v28
	v_add_f32_e32 v168, v168, v169
	v_add_f32_e32 v167, v168, v167
	v_mul_f32_e32 v168, v23, v23
	v_mul_f32_e32 v169, v25, v25
	v_fmac_f32_e32 v168, v22, v22
	v_fmac_f32_e32 v169, v24, v24
	v_add_f32_e32 v168, v168, v169
	v_add_f32_e32 v167, v168, v167
	v_mul_f32_e32 v168, v19, v19
	v_mul_f32_e32 v169, v21, v21
	v_fmac_f32_e32 v168, v18, v18
	v_fmac_f32_e32 v169, v20, v20
	v_add_f32_e32 v168, v168, v169
	v_add_f32_e32 v167, v168, v167
	v_mov_b32_e32 v168, v167
	s_nop 1
	v_permlane16_swap_b32_e32 v168, v167
	s_waitcnt lgkmcnt(0)
	v_add_f32_e32 v167, v167, v168
	v_mov_b32_e32 v168, v167
	s_nop 1
	v_permlane32_swap_b32_e32 v168, v167
	s_and_saveexec_b64 s[6:7], s[40:41]
	s_cbranch_execz .LBB0_706
	s_lshl_b32 s5, s76, 10
	s_add_i32 s5, s34, s5
	s_waitcnt lgkmcnt(0)
	v_add_f32_e32 v167, v167, v168
	v_lshl_add_u32 v168, v166, 4, s5
	ds_write_b32 v168, v167 offset:2560
.LBB0_706:
	s_or_b64 exec, exec, s[6:7]
	v_mul_f32_e32 v167, v15, v15
	s_waitcnt lgkmcnt(0)
	v_mul_f32_e32 v168, v17, v17
	v_fmac_f32_e32 v167, v14, v14
	v_fmac_f32_e32 v168, v16, v16
	v_add_f32_e32 v167, v167, v168
	v_mul_f32_e32 v168, v11, v11
	v_mul_f32_e32 v169, v13, v13
	v_fmac_f32_e32 v168, v10, v10
	v_fmac_f32_e32 v169, v12, v12
	v_add_f32_e32 v168, v168, v169
	v_add_f32_e32 v167, v168, v167
	v_mul_f32_e32 v168, v7, v7
	v_mul_f32_e32 v169, v9, v9
	v_fmac_f32_e32 v168, v6, v6
	v_fmac_f32_e32 v169, v8, v8
	v_add_f32_e32 v168, v168, v169
	v_add_f32_e32 v167, v168, v167
	v_mul_f32_e32 v168, v3, v3
	v_mul_f32_e32 v169, v5, v5
	v_fmac_f32_e32 v168, v2, v2
	v_fmac_f32_e32 v169, v4, v4
	v_add_f32_e32 v168, v168, v169
	v_add_f32_e32 v167, v168, v167
	v_mov_b32_e32 v168, v167
	s_nop 1
	v_permlane16_swap_b32_e32 v168, v167
	s_waitcnt lgkmcnt(0)
	v_add_f32_e32 v167, v167, v168
	v_mov_b32_e32 v168, v167
	s_nop 1
	v_permlane32_swap_b32_e32 v168, v167
	s_and_saveexec_b64 s[6:7], s[40:41]
	s_cbranch_execz .LBB0_708
	s_lshl_b32 s5, s76, 10
	s_add_i32 s5, s34, s5
	s_waitcnt lgkmcnt(0)
	v_add_f32_e32 v167, v167, v168
	v_lshl_add_u32 v166, v166, 4, s5
	ds_write_b32 v166, v167 offset:2816

.LBB0_734:
	s_waitcnt vmcnt(0)
	v_lshlrev_b32_e32 v216, 16, v206
	v_and_b32_e32 v217, 0xffff0000, v206
	v_lshlrev_b32_e32 v206, 16, v207
	v_and_b32_e32 v207, 0xffff0000, v207
	s_waitcnt lgkmcnt(0)
	v_pk_mul_f32 v[136:137], v[136:137], v[0:1] op_sel_hi:[1,0]
	v_pk_mul_f32 v[134:135], v[134:135], v[0:1] op_sel_hi:[1,0]
	v_lshlrev_b32_e32 v218, 16, v208
	v_and_b32_e32 v219, 0xffff0000, v208
	v_lshlrev_b32_e32 v208, 16, v209
	v_and_b32_e32 v209, 0xffff0000, v209
	v_pk_fma_f32 v[136:137], v[184:185], v[136:137], v[206:207]
	v_pk_fma_f32 v[134:135], v[182:183], v[134:135], v[216:217]
	v_pk_mul_f32 v[132:133], v[132:133], v[0:1] op_sel_hi:[1,0]
	v_pk_mul_f32 v[130:131], v[130:131], v[0:1] op_sel_hi:[1,0]
	v_pk_fma_f32 v[206:207], v[180:181], v[132:133], v[208:209]
	v_pk_fma_f32 v[132:133], v[178:179], v[130:131], v[218:219]
	v_mul_f32_e32 v130, v135, v135
	v_mul_f32_e32 v131, v137, v137
	v_fmac_f32_e32 v130, v134, v134
	v_fmac_f32_e32 v131, v136, v136
	v_add_f32_e32 v130, v130, v131
	v_mul_f32_e32 v131, v133, v133
	v_mul_f32_e32 v208, v207, v207
	v_fmac_f32_e32 v131, v132, v132
	v_fmac_f32_e32 v208, v206, v206
	v_add_f32_e32 v131, v131, v208
	v_add_f32_e32 v208, v130, v131
	v_cvt_pk_bf16_f32 v130, v134, v135
	v_cvt_pk_bf16_f32 v131, v136, v137
	v_lshlrev_b32_e32 v134, 16, v202
	v_and_b32_e32 v135, 0xffff0000, v202
	v_lshlrev_b32_e32 v136, 16, v203
	v_and_b32_e32 v137, 0xffff0000, v203
	v_pk_mul_f32 v[124:125], v[124:125], v[0:1] op_sel_hi:[1,0]
	v_pk_mul_f32 v[122:123], v[122:123], v[0:1] op_sel_hi:[1,0]
	v_lshlrev_b32_e32 v202, 16, v204
	v_and_b32_e32 v203, 0xffff0000, v204
	v_pk_fma_f32 v[124:125], v[172:173], v[124:125], v[136:137]
	v_pk_fma_f32 v[122:123], v[170:171], v[122:123], v[134:135]
	v_pk_mul_f32 v[114:115], v[114:115], v[0:1] op_sel_hi:[1,0]
	v_lshlrev_b32_e32 v204, 16, v205
	v_and_b32_e32 v205, 0xffff0000, v205
	v_pk_mul_f32 v[116:117], v[116:117], v[0:1] op_sel_hi:[1,0]
	v_pk_fma_f32 v[134:135], v[166:167], v[114:115], v[202:203]
	v_mul_f32_e32 v0, v123, v123
	v_mul_f32_e32 v114, v125, v125
	v_pk_fma_f32 v[116:117], v[168:169], v[116:117], v[204:205]
	v_fmac_f32_e32 v0, v122, v122
	v_fmac_f32_e32 v114, v124, v124
	v_add_f32_e32 v0, v0, v114
	v_mul_f32_e32 v114, v135, v135
	v_mul_f32_e32 v115, v117, v117
	v_fmac_f32_e32 v114, v134, v134
	v_fmac_f32_e32 v115, v116, v116
	v_add_f32_e32 v114, v114, v115
	v_add_f32_e32 v0, v0, v114
	v_add_f32_e32 v0, v208, v0
	v_mov_b32_e32 v202, v0
	s_nop 1
	v_permlane16_swap_b32_e32 v202, v0
	s_add_u32 s6, s20, s22
	s_addc_u32 s7, s21, s23
	v_lshl_add_u64 v[114:115], s[6:7], 0, v[224:225]
	v_lshl_add_u64 v[136:137], v[220:221], 1, v[114:115]
	s_waitcnt lgkmcnt(0)
	v_add_f32_e32 v0, v0, v202
	v_mov_b32_e32 v114, v0
	s_nop 1
	v_permlane32_swap_b32_e32 v114, v0
	v_cvt_pk_bf16_f32 v132, v132, v133
	v_cvt_pk_bf16_f32 v133, v206, v207
	global_store_dwordx4 v[136:137], v[130:133], off
	v_cvt_pk_bf16_f32 v122, v122, v123
	v_cvt_pk_bf16_f32 v123, v124, v125
	v_cvt_pk_bf16_f32 v124, v134, v135
	v_cvt_pk_bf16_f32 v125, v116, v117
	global_store_dwordx4 v[136:137], v[122:125], off offset:256
	s_and_saveexec_b64 s[8:9], s[40:41]
	s_cbranch_execz .LBB0_736
	v_lshl_add_u32 v115, v240, 4, s34
	s_waitcnt lgkmcnt(0)
	v_add_f32_e32 v0, v0, v114
	ds_write_b32 v115, v0 offset:6144

.LBB0_738:
	v_lshlrev_b32_e32 v122, 16, v198
	v_and_b32_e32 v123, 0xffff0000, v198
	v_lshlrev_b32_e32 v124, 16, v199
	v_and_b32_e32 v125, 0xffff0000, v199
	s_waitcnt lgkmcnt(0)
	v_pk_mul_f32 v[112:113], v[112:113], v[0:1] op_sel_hi:[1,0]
	v_pk_mul_f32 v[110:111], v[110:111], v[0:1] op_sel_hi:[1,0]
	v_lshlrev_b32_e32 v130, 16, v200
	v_and_b32_e32 v131, 0xffff0000, v200
	v_lshlrev_b32_e32 v132, 16, v201
	v_and_b32_e32 v133, 0xffff0000, v201
	v_pk_fma_f32 v[112:113], v[184:185], v[112:113], v[124:125]
	v_pk_fma_f32 v[110:111], v[182:183], v[110:111], v[122:123]
	v_pk_mul_f32 v[108:109], v[108:109], v[0:1] op_sel_hi:[1,0]
	v_pk_mul_f32 v[106:107], v[106:107], v[0:1] op_sel_hi:[1,0]
	v_pk_fma_f32 v[122:123], v[180:181], v[108:109], v[132:133]
	v_pk_fma_f32 v[108:109], v[178:179], v[106:107], v[130:131]
	v_mul_f32_e32 v106, v111, v111
	v_mul_f32_e32 v107, v113, v113
	v_fmac_f32_e32 v106, v110, v110
	v_fmac_f32_e32 v107, v112, v112
	v_add_f32_e32 v106, v106, v107
	v_mul_f32_e32 v107, v109, v109
	v_mul_f32_e32 v115, v123, v123
	v_fmac_f32_e32 v107, v108, v108
	v_fmac_f32_e32 v115, v122, v122
	v_add_f32_e32 v107, v107, v115
	v_add_f32_e32 v115, v106, v107
	v_cvt_pk_bf16_f32 v106, v110, v111
	v_cvt_pk_bf16_f32 v107, v112, v113
	v_lshlrev_b32_e32 v110, 16, v194
	v_and_b32_e32 v111, 0xffff0000, v194
	v_lshlrev_b32_e32 v112, 16, v195
	v_and_b32_e32 v113, 0xffff0000, v195
	v_pk_mul_f32 v[104:105], v[104:105], v[0:1] op_sel_hi:[1,0]
	v_pk_mul_f32 v[102:103], v[102:103], v[0:1] op_sel_hi:[1,0]
	v_cvt_pk_bf16_f32 v108, v108, v109
	v_cvt_pk_bf16_f32 v109, v122, v123
	v_lshlrev_b32_e32 v122, 16, v196
	v_and_b32_e32 v123, 0xffff0000, v196
	v_pk_fma_f32 v[104:105], v[172:173], v[104:105], v[112:113]
	v_pk_fma_f32 v[102:103], v[170:171], v[102:103], v[110:111]
	v_pk_mul_f32 v[98:99], v[98:99], v[0:1] op_sel_hi:[1,0]
	v_lshlrev_b32_e32 v124, 16, v197
	v_and_b32_e32 v125, 0xffff0000, v197
	v_pk_mul_f32 v[100:101], v[100:101], v[0:1] op_sel_hi:[1,0]
	v_pk_fma_f32 v[112:113], v[166:167], v[98:99], v[122:123]
	v_mul_f32_e32 v0, v103, v103
	v_mul_f32_e32 v98, v105, v105
	v_pk_fma_f32 v[110:111], v[168:169], v[100:101], v[124:125]
	v_fmac_f32_e32 v0, v102, v102
	v_fmac_f32_e32 v98, v104, v104
	v_add_f32_e32 v0, v0, v98
	v_mul_f32_e32 v98, v113, v113
	v_mul_f32_e32 v99, v111, v111
	v_fmac_f32_e32 v98, v112, v112
	v_fmac_f32_e32 v99, v110, v110
	v_add_f32_e32 v98, v98, v99
	v_add_f32_e32 v0, v0, v98
	v_add_f32_e32 v0, v115, v0
	v_mov_b32_e32 v101, v0
	s_nop 1
	v_permlane16_swap_b32_e32 v101, v0
	v_or_b32_e32 v114, 16, v240
	v_add_u32_e32 v116, s35, v114
	v_ashrrev_i32_e32 v117, 31, v116
	v_lshlrev_b64 v[116:117], 11, v[116:117]
	v_lshl_add_u64 v[98:99], s[6:7], 0, v[116:117]
	s_waitcnt lgkmcnt(0)
	v_add_f32_e32 v0, v0, v101
	v_lshl_add_u64 v[116:117], v[220:221], 1, v[98:99]
	v_mov_b32_e32 v98, v0
	s_nop 1
	v_permlane32_swap_b32_e32 v98, v0
	global_store_dwordx4 v[116:117], v[106:109], off
	v_cvt_pk_bf16_f32 v100, v102, v103
	v_cvt_pk_bf16_f32 v101, v104, v105
	v_cvt_pk_bf16_f32 v102, v112, v113
	v_cvt_pk_bf16_f32 v103, v110, v111
	global_store_dwordx4 v[116:117], v[100:103], off offset:256
	s_and_saveexec_b64 s[8:9], s[40:41]
	s_cbranch_execz .LBB0_740
	v_lshl_add_u32 v99, v114, 4, s34
	s_waitcnt lgkmcnt(0)
	v_add_f32_e32 v0, v0, v98
	ds_write_b32 v99, v0 offset:6144

.LBB0_742:
	v_lshlrev_b32_e32 v102, 16, v190
	v_and_b32_e32 v103, 0xffff0000, v190
	v_lshlrev_b32_e32 v104, 16, v191
	v_and_b32_e32 v105, 0xffff0000, v191
	s_waitcnt lgkmcnt(0)
	v_pk_mul_f32 v[96:97], v[96:97], v[0:1] op_sel_hi:[1,0]
	v_pk_mul_f32 v[94:95], v[94:95], v[0:1] op_sel_hi:[1,0]
	v_lshlrev_b32_e32 v106, 16, v192
	v_and_b32_e32 v107, 0xffff0000, v192
	v_lshlrev_b32_e32 v108, 16, v193
	v_and_b32_e32 v109, 0xffff0000, v193
	v_pk_fma_f32 v[96:97], v[184:185], v[96:97], v[104:105]
	v_pk_fma_f32 v[94:95], v[182:183], v[94:95], v[102:103]
	v_pk_mul_f32 v[92:93], v[92:93], v[0:1] op_sel_hi:[1,0]
	v_pk_mul_f32 v[90:91], v[90:91], v[0:1] op_sel_hi:[1,0]
	v_pk_fma_f32 v[102:103], v[180:181], v[92:93], v[108:109]
	v_pk_fma_f32 v[92:93], v[178:179], v[90:91], v[106:107]
	v_mul_f32_e32 v90, v95, v95
	v_mul_f32_e32 v91, v97, v97
	v_fmac_f32_e32 v90, v94, v94
	v_fmac_f32_e32 v91, v96, v96
	v_add_f32_e32 v90, v90, v91
	v_mul_f32_e32 v91, v93, v93
	v_mul_f32_e32 v99, v103, v103
	v_fmac_f32_e32 v91, v92, v92
	v_fmac_f32_e32 v99, v102, v102
	v_add_f32_e32 v91, v91, v99
	v_add_f32_e32 v99, v90, v91
	v_cvt_pk_bf16_f32 v90, v94, v95
	v_cvt_pk_bf16_f32 v91, v96, v97
	v_lshlrev_b32_e32 v94, 16, v186
	v_and_b32_e32 v95, 0xffff0000, v186
	v_lshlrev_b32_e32 v96, 16, v187
	v_and_b32_e32 v97, 0xffff0000, v187
	v_pk_mul_f32 v[88:89], v[88:89], v[0:1] op_sel_hi:[1,0]
	v_pk_mul_f32 v[86:87], v[86:87], v[0:1] op_sel_hi:[1,0]
	v_cvt_pk_bf16_f32 v92, v92, v93
	v_cvt_pk_bf16_f32 v93, v102, v103
	v_lshlrev_b32_e32 v102, 16, v188
	v_and_b32_e32 v103, 0xffff0000, v188
	v_pk_fma_f32 v[88:89], v[172:173], v[88:89], v[96:97]
	v_pk_fma_f32 v[86:87], v[170:171], v[86:87], v[94:95]
	v_pk_mul_f32 v[82:83], v[82:83], v[0:1] op_sel_hi:[1,0]
	v_lshlrev_b32_e32 v104, 16, v189
	v_and_b32_e32 v105, 0xffff0000, v189
	v_pk_mul_f32 v[84:85], v[84:85], v[0:1] op_sel_hi:[1,0]
	v_pk_fma_f32 v[96:97], v[166:167], v[82:83], v[102:103]
	v_mul_f32_e32 v0, v87, v87
	v_mul_f32_e32 v82, v89, v89
	v_pk_fma_f32 v[94:95], v[168:169], v[84:85], v[104:105]
	v_fmac_f32_e32 v0, v86, v86
	v_fmac_f32_e32 v82, v88, v88
	v_add_f32_e32 v0, v0, v82
	v_mul_f32_e32 v82, v97, v97
	v_mul_f32_e32 v83, v95, v95
	v_fmac_f32_e32 v82, v96, v96
	v_fmac_f32_e32 v83, v94, v94
	v_add_f32_e32 v82, v82, v83
	v_add_f32_e32 v0, v0, v82
	v_add_f32_e32 v0, v99, v0
	v_mov_b32_e32 v85, v0
	s_nop 1
	v_permlane16_swap_b32_e32 v85, v0
	v_or_b32_e32 v98, 32, v240
	v_add_u32_e32 v100, s35, v98
	v_ashrrev_i32_e32 v101, 31, v100
	v_lshlrev_b64 v[100:101], 11, v[100:101]
	v_lshl_add_u64 v[82:83], s[6:7], 0, v[100:101]
	s_waitcnt lgkmcnt(0)
	v_add_f32_e32 v0, v0, v85
	v_lshl_add_u64 v[100:101], v[220:221], 1, v[82:83]
	v_mov_b32_e32 v82, v0
	s_nop 1
	v_permlane32_swap_b32_e32 v82, v0
	global_store_dwordx4 v[100:101], v[90:93], off
	v_cvt_pk_bf16_f32 v84, v86, v87
	v_cvt_pk_bf16_f32 v85, v88, v89
	v_cvt_pk_bf16_f32 v86, v96, v97
	v_cvt_pk_bf16_f32 v87, v94, v95
	global_store_dwordx4 v[100:101], v[84:87], off offset:256
	s_and_saveexec_b64 s[8:9], s[40:41]
	s_cbranch_execz .LBB0_744
	v_lshl_add_u32 v83, v98, 4, s34
	s_waitcnt lgkmcnt(0)
	v_add_f32_e32 v0, v0, v82
	ds_write_b32 v83, v0 offset:6144

.LBB0_746:
	v_lshlrev_b32_e32 v86, 16, v174
	v_and_b32_e32 v87, 0xffff0000, v174
	v_lshlrev_b32_e32 v88, 16, v175
	v_and_b32_e32 v89, 0xffff0000, v175
	s_waitcnt lgkmcnt(0)
	v_pk_mul_f32 v[80:81], v[80:81], v[0:1] op_sel_hi:[1,0]
	v_pk_mul_f32 v[78:79], v[78:79], v[0:1] op_sel_hi:[1,0]
	v_lshlrev_b32_e32 v90, 16, v176
	v_and_b32_e32 v91, 0xffff0000, v176
	v_lshlrev_b32_e32 v92, 16, v177
	v_and_b32_e32 v93, 0xffff0000, v177
	v_pk_fma_f32 v[80:81], v[184:185], v[80:81], v[88:89]
	v_pk_fma_f32 v[78:79], v[182:183], v[78:79], v[86:87]
	v_pk_mul_f32 v[76:77], v[76:77], v[0:1] op_sel_hi:[1,0]
	v_pk_mul_f32 v[74:75], v[74:75], v[0:1] op_sel_hi:[1,0]
	v_pk_fma_f32 v[86:87], v[180:181], v[76:77], v[92:93]
	v_pk_fma_f32 v[76:77], v[178:179], v[74:75], v[90:91]
	v_mul_f32_e32 v74, v79, v79
	v_mul_f32_e32 v75, v81, v81
	v_fmac_f32_e32 v74, v78, v78
	v_fmac_f32_e32 v75, v80, v80
	v_add_f32_e32 v74, v74, v75
	v_mul_f32_e32 v75, v77, v77
	v_mul_f32_e32 v83, v87, v87
	v_fmac_f32_e32 v75, v76, v76
	v_fmac_f32_e32 v83, v86, v86
	v_add_f32_e32 v75, v75, v83
	v_add_f32_e32 v83, v74, v75
	v_cvt_pk_bf16_f32 v74, v78, v79
	v_cvt_pk_bf16_f32 v75, v80, v81
	v_lshlrev_b32_e32 v78, 16, v162
	v_and_b32_e32 v79, 0xffff0000, v162
	v_lshlrev_b32_e32 v80, 16, v163
	v_and_b32_e32 v81, 0xffff0000, v163
	v_pk_mul_f32 v[72:73], v[72:73], v[0:1] op_sel_hi:[1,0]
	v_pk_mul_f32 v[70:71], v[70:71], v[0:1] op_sel_hi:[1,0]
	v_cvt_pk_bf16_f32 v76, v76, v77
	v_cvt_pk_bf16_f32 v77, v86, v87
	v_lshlrev_b32_e32 v86, 16, v164
	v_and_b32_e32 v87, 0xffff0000, v164
	v_pk_fma_f32 v[72:73], v[172:173], v[72:73], v[80:81]
	v_pk_fma_f32 v[70:71], v[170:171], v[70:71], v[78:79]
	v_pk_mul_f32 v[66:67], v[66:67], v[0:1] op_sel_hi:[1,0]
	v_lshlrev_b32_e32 v88, 16, v165
	v_and_b32_e32 v89, 0xffff0000, v165
	v_pk_mul_f32 v[68:69], v[68:69], v[0:1] op_sel_hi:[1,0]
	v_pk_fma_f32 v[80:81], v[166:167], v[66:67], v[86:87]
	v_mul_f32_e32 v0, v71, v71
	v_mul_f32_e32 v66, v73, v73
	v_pk_fma_f32 v[78:79], v[168:169], v[68:69], v[88:89]
	v_fmac_f32_e32 v0, v70, v70
	v_fmac_f32_e32 v66, v72, v72
	v_add_f32_e32 v0, v0, v66
	v_mul_f32_e32 v66, v81, v81
	v_mul_f32_e32 v67, v79, v79
	v_fmac_f32_e32 v66, v80, v80
	v_fmac_f32_e32 v67, v78, v78
	v_add_f32_e32 v66, v66, v67
	v_add_f32_e32 v0, v0, v66
	v_add_f32_e32 v0, v83, v0
	v_mov_b32_e32 v69, v0
	s_nop 1
	v_permlane16_swap_b32_e32 v69, v0
	v_or_b32_e32 v82, 48, v240
	v_add_u32_e32 v84, s35, v82
	v_ashrrev_i32_e32 v85, 31, v84
	v_lshlrev_b64 v[84:85], 11, v[84:85]
	v_lshl_add_u64 v[66:67], s[6:7], 0, v[84:85]
	s_waitcnt lgkmcnt(0)
	v_add_f32_e32 v0, v0, v69
	v_lshl_add_u64 v[84:85], v[220:221], 1, v[66:67]
	v_mov_b32_e32 v66, v0
	s_nop 1
	v_permlane32_swap_b32_e32 v66, v0
	global_store_dwordx4 v[84:85], v[74:77], off
	v_cvt_pk_bf16_f32 v68, v70, v71
	v_cvt_pk_bf16_f32 v69, v72, v73
	v_cvt_pk_bf16_f32 v70, v80, v81
	v_cvt_pk_bf16_f32 v71, v78, v79
	global_store_dwordx4 v[84:85], v[68:71], off offset:256
	s_and_saveexec_b64 s[8:9], s[40:41]
	s_cbranch_execz .LBB0_748
	v_lshl_add_u32 v67, v82, 4, s34
	s_waitcnt lgkmcnt(0)
	v_add_f32_e32 v0, v0, v66
	ds_write_b32 v67, v0 offset:6144

.LBB0_750:
	v_lshlrev_b32_e32 v70, 16, v158
	v_and_b32_e32 v71, 0xffff0000, v158
	v_lshlrev_b32_e32 v72, 16, v159
	v_and_b32_e32 v73, 0xffff0000, v159
	s_waitcnt lgkmcnt(0)
	v_pk_mul_f32 v[64:65], v[64:65], v[0:1] op_sel_hi:[1,0]
	v_pk_mul_f32 v[62:63], v[62:63], v[0:1] op_sel_hi:[1,0]
	v_lshlrev_b32_e32 v74, 16, v160
	v_and_b32_e32 v75, 0xffff0000, v160
	v_lshlrev_b32_e32 v76, 16, v161
	v_and_b32_e32 v77, 0xffff0000, v161
	v_pk_fma_f32 v[64:65], v[184:185], v[64:65], v[72:73]
	v_pk_fma_f32 v[62:63], v[182:183], v[62:63], v[70:71]
	v_pk_mul_f32 v[60:61], v[60:61], v[0:1] op_sel_hi:[1,0]
	v_pk_mul_f32 v[58:59], v[58:59], v[0:1] op_sel_hi:[1,0]
	v_pk_fma_f32 v[70:71], v[180:181], v[60:61], v[76:77]
	v_pk_fma_f32 v[60:61], v[178:179], v[58:59], v[74:75]
	v_mul_f32_e32 v58, v63, v63
	v_mul_f32_e32 v59, v65, v65
	v_fmac_f32_e32 v58, v62, v62
	v_fmac_f32_e32 v59, v64, v64
	v_add_f32_e32 v58, v58, v59
	v_mul_f32_e32 v59, v61, v61
	v_mul_f32_e32 v67, v71, v71
	v_fmac_f32_e32 v59, v60, v60
	v_fmac_f32_e32 v67, v70, v70
	v_add_f32_e32 v59, v59, v67
	v_add_f32_e32 v67, v58, v59
	v_cvt_pk_bf16_f32 v58, v62, v63
	v_cvt_pk_bf16_f32 v59, v64, v65
	v_lshlrev_b32_e32 v62, 16, v154
	v_and_b32_e32 v63, 0xffff0000, v154
	v_lshlrev_b32_e32 v64, 16, v155
	v_and_b32_e32 v65, 0xffff0000, v155
	v_pk_mul_f32 v[56:57], v[56:57], v[0:1] op_sel_hi:[1,0]
	v_pk_mul_f32 v[54:55], v[54:55], v[0:1] op_sel_hi:[1,0]
	v_cvt_pk_bf16_f32 v60, v60, v61
	v_cvt_pk_bf16_f32 v61, v70, v71
	v_lshlrev_b32_e32 v70, 16, v156
	v_and_b32_e32 v71, 0xffff0000, v156
	v_pk_fma_f32 v[56:57], v[172:173], v[56:57], v[64:65]
	v_pk_fma_f32 v[54:55], v[170:171], v[54:55], v[62:63]
	v_pk_mul_f32 v[50:51], v[50:51], v[0:1] op_sel_hi:[1,0]
	v_lshlrev_b32_e32 v72, 16, v157
	v_and_b32_e32 v73, 0xffff0000, v157
	v_pk_mul_f32 v[52:53], v[52:53], v[0:1] op_sel_hi:[1,0]
	v_pk_fma_f32 v[64:65], v[166:167], v[50:51], v[70:71]
	v_mul_f32_e32 v0, v55, v55
	v_mul_f32_e32 v50, v57, v57
	v_pk_fma_f32 v[62:63], v[168:169], v[52:53], v[72:73]
	v_fmac_f32_e32 v0, v54, v54
	v_fmac_f32_e32 v50, v56, v56
	v_add_f32_e32 v0, v0, v50
	v_mul_f32_e32 v50, v65, v65
	v_mul_f32_e32 v51, v63, v63
	v_fmac_f32_e32 v50, v64, v64
	v_fmac_f32_e32 v51, v62, v62
	v_add_f32_e32 v50, v50, v51
	v_add_f32_e32 v0, v0, v50
	v_add_f32_e32 v0, v67, v0
	v_mov_b32_e32 v53, v0
	s_nop 1
	v_permlane16_swap_b32_e32 v53, v0
	v_add_u32_e32 v66, 0x80, v240
	v_add_u32_e32 v68, s35, v66
	v_ashrrev_i32_e32 v69, 31, v68
	v_lshlrev_b64 v[68:69], 11, v[68:69]
	v_lshl_add_u64 v[50:51], s[6:7], 0, v[68:69]
	s_waitcnt lgkmcnt(0)
	v_add_f32_e32 v0, v0, v53
	v_lshl_add_u64 v[68:69], v[220:221], 1, v[50:51]
	v_mov_b32_e32 v50, v0
	s_nop 1
	v_permlane32_swap_b32_e32 v50, v0
	global_store_dwordx4 v[68:69], v[58:61], off
	v_cvt_pk_bf16_f32 v52, v54, v55
	v_cvt_pk_bf16_f32 v53, v56, v57
	v_cvt_pk_bf16_f32 v54, v64, v65
	v_cvt_pk_bf16_f32 v55, v62, v63
	global_store_dwordx4 v[68:69], v[52:55], off offset:256
	s_and_saveexec_b64 s[8:9], s[40:41]
	s_cbranch_execz .LBB0_752
	v_lshl_add_u32 v51, v66, 4, s34
	s_waitcnt lgkmcnt(0)
	v_add_f32_e32 v0, v0, v50
	ds_write_b32 v51, v0 offset:6144

.LBB0_754:
	v_lshlrev_b32_e32 v54, 16, v150
	v_and_b32_e32 v55, 0xffff0000, v150
	v_lshlrev_b32_e32 v56, 16, v151
	v_and_b32_e32 v57, 0xffff0000, v151
	s_waitcnt lgkmcnt(0)
	v_pk_mul_f32 v[48:49], v[48:49], v[0:1] op_sel_hi:[1,0]
	v_pk_mul_f32 v[46:47], v[46:47], v[0:1] op_sel_hi:[1,0]
	v_lshlrev_b32_e32 v58, 16, v152
	v_and_b32_e32 v59, 0xffff0000, v152
	v_lshlrev_b32_e32 v60, 16, v153
	v_and_b32_e32 v61, 0xffff0000, v153
	v_pk_fma_f32 v[48:49], v[184:185], v[48:49], v[56:57]
	v_pk_fma_f32 v[46:47], v[182:183], v[46:47], v[54:55]
	v_pk_mul_f32 v[44:45], v[44:45], v[0:1] op_sel_hi:[1,0]
	v_pk_mul_f32 v[42:43], v[42:43], v[0:1] op_sel_hi:[1,0]
	v_pk_fma_f32 v[54:55], v[180:181], v[44:45], v[60:61]
	v_pk_fma_f32 v[44:45], v[178:179], v[42:43], v[58:59]
	v_mul_f32_e32 v42, v47, v47
	v_mul_f32_e32 v43, v49, v49
	v_fmac_f32_e32 v42, v46, v46
	v_fmac_f32_e32 v43, v48, v48
	v_add_f32_e32 v42, v42, v43
	v_mul_f32_e32 v43, v45, v45
	v_mul_f32_e32 v51, v55, v55
	v_fmac_f32_e32 v43, v44, v44
	v_fmac_f32_e32 v51, v54, v54
	v_add_f32_e32 v43, v43, v51
	v_add_f32_e32 v51, v42, v43
	v_cvt_pk_bf16_f32 v42, v46, v47
	v_cvt_pk_bf16_f32 v43, v48, v49
	v_lshlrev_b32_e32 v46, 16, v146
	v_and_b32_e32 v47, 0xffff0000, v146
	v_lshlrev_b32_e32 v48, 16, v147
	v_and_b32_e32 v49, 0xffff0000, v147
	v_pk_mul_f32 v[40:41], v[40:41], v[0:1] op_sel_hi:[1,0]
	v_pk_mul_f32 v[38:39], v[38:39], v[0:1] op_sel_hi:[1,0]
	v_cvt_pk_bf16_f32 v44, v44, v45
	v_cvt_pk_bf16_f32 v45, v54, v55
	v_lshlrev_b32_e32 v54, 16, v148
	v_and_b32_e32 v55, 0xffff0000, v148
	v_pk_fma_f32 v[40:41], v[172:173], v[40:41], v[48:49]
	v_pk_fma_f32 v[38:39], v[170:171], v[38:39], v[46:47]
	v_pk_mul_f32 v[34:35], v[34:35], v[0:1] op_sel_hi:[1,0]
	v_lshlrev_b32_e32 v56, 16, v149
	v_and_b32_e32 v57, 0xffff0000, v149
	v_pk_mul_f32 v[36:37], v[36:37], v[0:1] op_sel_hi:[1,0]
	v_pk_fma_f32 v[48:49], v[166:167], v[34:35], v[54:55]
	v_mul_f32_e32 v0, v39, v39
	v_mul_f32_e32 v34, v41, v41
	v_pk_fma_f32 v[46:47], v[168:169], v[36:37], v[56:57]
	v_fmac_f32_e32 v0, v38, v38
	v_fmac_f32_e32 v34, v40, v40
	v_add_f32_e32 v0, v0, v34
	v_mul_f32_e32 v34, v49, v49
	v_mul_f32_e32 v35, v47, v47
	v_fmac_f32_e32 v34, v48, v48
	v_fmac_f32_e32 v35, v46, v46
	v_add_f32_e32 v34, v34, v35
	v_add_f32_e32 v0, v0, v34
	v_add_f32_e32 v0, v51, v0
	v_mov_b32_e32 v37, v0
	s_nop 1
	v_permlane16_swap_b32_e32 v37, v0
	v_add_u32_e32 v50, 0x90, v240
	v_add_u32_e32 v52, s35, v50
	v_ashrrev_i32_e32 v53, 31, v52
	v_lshlrev_b64 v[52:53], 11, v[52:53]
	v_lshl_add_u64 v[34:35], s[6:7], 0, v[52:53]
	s_waitcnt lgkmcnt(0)
	v_add_f32_e32 v0, v0, v37
	v_lshl_add_u64 v[52:53], v[220:221], 1, v[34:35]
	v_mov_b32_e32 v34, v0
	s_nop 1
	v_permlane32_swap_b32_e32 v34, v0
	global_store_dwordx4 v[52:53], v[42:45], off
	v_cvt_pk_bf16_f32 v36, v38, v39
	v_cvt_pk_bf16_f32 v37, v40, v41
	v_cvt_pk_bf16_f32 v38, v48, v49
	v_cvt_pk_bf16_f32 v39, v46, v47
	global_store_dwordx4 v[52:53], v[36:39], off offset:256
	s_and_saveexec_b64 s[8:9], s[40:41]
	s_cbranch_execz .LBB0_756
	v_lshl_add_u32 v35, v50, 4, s34
	s_waitcnt lgkmcnt(0)
	v_add_f32_e32 v0, v0, v34
	ds_write_b32 v35, v0 offset:6144

.LBB0_758:
	v_lshlrev_b32_e32 v38, 16, v142
	v_and_b32_e32 v39, 0xffff0000, v142
	v_lshlrev_b32_e32 v40, 16, v143
	v_and_b32_e32 v41, 0xffff0000, v143
	s_waitcnt lgkmcnt(0)
	v_pk_mul_f32 v[32:33], v[32:33], v[0:1] op_sel_hi:[1,0]
	v_pk_mul_f32 v[30:31], v[30:31], v[0:1] op_sel_hi:[1,0]
	v_lshlrev_b32_e32 v42, 16, v144
	v_and_b32_e32 v43, 0xffff0000, v144
	v_lshlrev_b32_e32 v44, 16, v145
	v_and_b32_e32 v45, 0xffff0000, v145
	v_pk_fma_f32 v[32:33], v[184:185], v[32:33], v[40:41]
	v_pk_fma_f32 v[30:31], v[182:183], v[30:31], v[38:39]
	v_pk_mul_f32 v[28:29], v[28:29], v[0:1] op_sel_hi:[1,0]
	v_pk_mul_f32 v[26:27], v[26:27], v[0:1] op_sel_hi:[1,0]
	v_pk_fma_f32 v[38:39], v[180:181], v[28:29], v[44:45]
	v_pk_fma_f32 v[28:29], v[178:179], v[26:27], v[42:43]
	v_mul_f32_e32 v26, v31, v31
	v_mul_f32_e32 v27, v33, v33
	v_fmac_f32_e32 v26, v30, v30
	v_fmac_f32_e32 v27, v32, v32
	v_add_f32_e32 v26, v26, v27
	v_mul_f32_e32 v27, v29, v29
	v_mul_f32_e32 v35, v39, v39
	v_fmac_f32_e32 v27, v28, v28
	v_fmac_f32_e32 v35, v38, v38
	v_add_f32_e32 v27, v27, v35
	v_add_f32_e32 v35, v26, v27
	v_cvt_pk_bf16_f32 v26, v30, v31
	v_cvt_pk_bf16_f32 v27, v32, v33
	v_lshlrev_b32_e32 v30, 16, v138
	v_and_b32_e32 v31, 0xffff0000, v138
	v_lshlrev_b32_e32 v32, 16, v139
	v_and_b32_e32 v33, 0xffff0000, v139
	v_pk_mul_f32 v[24:25], v[24:25], v[0:1] op_sel_hi:[1,0]
	v_pk_mul_f32 v[22:23], v[22:23], v[0:1] op_sel_hi:[1,0]
	v_cvt_pk_bf16_f32 v28, v28, v29
	v_cvt_pk_bf16_f32 v29, v38, v39
	v_lshlrev_b32_e32 v38, 16, v140
	v_and_b32_e32 v39, 0xffff0000, v140
	v_pk_fma_f32 v[24:25], v[172:173], v[24:25], v[32:33]
	v_pk_fma_f32 v[22:23], v[170:171], v[22:23], v[30:31]
	v_pk_mul_f32 v[18:19], v[18:19], v[0:1] op_sel_hi:[1,0]
	v_lshlrev_b32_e32 v40, 16, v141
	v_and_b32_e32 v41, 0xffff0000, v141
	v_pk_mul_f32 v[20:21], v[20:21], v[0:1] op_sel_hi:[1,0]
	v_pk_fma_f32 v[32:33], v[166:167], v[18:19], v[38:39]
	v_mul_f32_e32 v0, v23, v23
	v_mul_f32_e32 v18, v25, v25
	v_pk_fma_f32 v[30:31], v[168:169], v[20:21], v[40:41]
	v_fmac_f32_e32 v0, v22, v22
	v_fmac_f32_e32 v18, v24, v24
	v_add_f32_e32 v0, v0, v18
	v_mul_f32_e32 v18, v33, v33
	v_mul_f32_e32 v19, v31, v31
	v_fmac_f32_e32 v18, v32, v32
	v_fmac_f32_e32 v19, v30, v30
	v_add_f32_e32 v18, v18, v19
	v_add_f32_e32 v0, v0, v18
	v_add_f32_e32 v0, v35, v0
	v_mov_b32_e32 v21, v0
	s_nop 1
	v_permlane16_swap_b32_e32 v21, v0
	v_add_u32_e32 v34, 0xa0, v240
	v_add_u32_e32 v36, s35, v34
	v_ashrrev_i32_e32 v37, 31, v36
	v_lshlrev_b64 v[36:37], 11, v[36:37]
	v_lshl_add_u64 v[18:19], s[6:7], 0, v[36:37]
	s_waitcnt lgkmcnt(0)
	v_add_f32_e32 v0, v0, v21
	v_lshl_add_u64 v[36:37], v[220:221], 1, v[18:19]
	v_mov_b32_e32 v18, v0
	s_nop 1
	v_permlane32_swap_b32_e32 v18, v0
	global_store_dwordx4 v[36:37], v[26:29], off
	v_cvt_pk_bf16_f32 v20, v22, v23
	v_cvt_pk_bf16_f32 v21, v24, v25
	v_cvt_pk_bf16_f32 v22, v32, v33
	v_cvt_pk_bf16_f32 v23, v30, v31
	global_store_dwordx4 v[36:37], v[20:23], off offset:256
	s_and_saveexec_b64 s[8:9], s[40:41]
	s_cbranch_execz .LBB0_760
	v_lshl_add_u32 v19, v34, 4, s34
	s_waitcnt lgkmcnt(0)
	v_add_f32_e32 v0, v0, v18
	ds_write_b32 v19, v0 offset:6144

.LBB0_762:
	v_lshlrev_b32_e32 v22, 16, v126
	v_and_b32_e32 v23, 0xffff0000, v126
	v_lshlrev_b32_e32 v24, 16, v127
	v_and_b32_e32 v25, 0xffff0000, v127
	s_waitcnt lgkmcnt(0)
	v_pk_mul_f32 v[16:17], v[16:17], v[0:1] op_sel_hi:[1,0]
	v_pk_mul_f32 v[14:15], v[14:15], v[0:1] op_sel_hi:[1,0]
	v_lshlrev_b32_e32 v26, 16, v128
	v_and_b32_e32 v27, 0xffff0000, v128
	v_lshlrev_b32_e32 v28, 16, v129
	v_and_b32_e32 v29, 0xffff0000, v129
	v_pk_fma_f32 v[16:17], v[184:185], v[16:17], v[24:25]
	v_pk_fma_f32 v[14:15], v[182:183], v[14:15], v[22:23]
	v_pk_mul_f32 v[12:13], v[12:13], v[0:1] op_sel_hi:[1,0]
	v_pk_mul_f32 v[10:11], v[10:11], v[0:1] op_sel_hi:[1,0]
	v_pk_fma_f32 v[22:23], v[180:181], v[12:13], v[28:29]
	v_pk_fma_f32 v[12:13], v[178:179], v[10:11], v[26:27]
	v_mul_f32_e32 v10, v15, v15
	v_mul_f32_e32 v11, v17, v17
	v_fmac_f32_e32 v10, v14, v14
	v_fmac_f32_e32 v11, v16, v16
	v_add_f32_e32 v10, v10, v11
	v_mul_f32_e32 v11, v13, v13
	v_mul_f32_e32 v19, v23, v23
	v_fmac_f32_e32 v11, v12, v12
	v_fmac_f32_e32 v19, v22, v22
	v_add_f32_e32 v11, v11, v19
	v_add_f32_e32 v19, v10, v11
	v_cvt_pk_bf16_f32 v10, v14, v15
	v_cvt_pk_bf16_f32 v11, v16, v17
	v_lshlrev_b32_e32 v14, 16, v118
	v_and_b32_e32 v15, 0xffff0000, v118
	v_lshlrev_b32_e32 v16, 16, v119
	v_and_b32_e32 v17, 0xffff0000, v119
	v_pk_mul_f32 v[8:9], v[8:9], v[0:1] op_sel_hi:[1,0]
	v_pk_mul_f32 v[6:7], v[6:7], v[0:1] op_sel_hi:[1,0]
	v_cvt_pk_bf16_f32 v12, v12, v13
	v_cvt_pk_bf16_f32 v13, v22, v23
	v_lshlrev_b32_e32 v22, 16, v120
	v_and_b32_e32 v23, 0xffff0000, v120
	v_pk_fma_f32 v[8:9], v[172:173], v[8:9], v[16:17]
	v_pk_fma_f32 v[6:7], v[170:171], v[6:7], v[14:15]
	v_pk_mul_f32 v[2:3], v[2:3], v[0:1] op_sel_hi:[1,0]
	v_lshlrev_b32_e32 v24, 16, v121
	v_and_b32_e32 v25, 0xffff0000, v121
	v_pk_mul_f32 v[4:5], v[4:5], v[0:1] op_sel_hi:[1,0]
	v_pk_fma_f32 v[16:17], v[166:167], v[2:3], v[22:23]
	v_mul_f32_e32 v0, v7, v7
	v_mul_f32_e32 v2, v9, v9
	v_pk_fma_f32 v[14:15], v[168:169], v[4:5], v[24:25]
	v_fmac_f32_e32 v0, v6, v6
	v_fmac_f32_e32 v2, v8, v8
	v_add_f32_e32 v0, v0, v2
	v_mul_f32_e32 v2, v17, v17
	v_mul_f32_e32 v3, v15, v15
	v_fmac_f32_e32 v2, v16, v16
	v_fmac_f32_e32 v3, v14, v14
	v_add_f32_e32 v2, v2, v3
	v_add_f32_e32 v0, v0, v2
	v_add_f32_e32 v0, v19, v0
	v_mov_b32_e32 v5, v0
	s_nop 1
	v_permlane16_swap_b32_e32 v5, v0
	v_add_u32_e32 v18, 0xb0, v240
	v_add_u32_e32 v20, s35, v18
	v_ashrrev_i32_e32 v21, 31, v20
	v_lshlrev_b64 v[20:21], 11, v[20:21]
	v_lshl_add_u64 v[2:3], s[6:7], 0, v[20:21]
	s_waitcnt lgkmcnt(0)
	v_add_f32_e32 v0, v0, v5
	v_lshl_add_u64 v[20:21], v[220:221], 1, v[2:3]
	v_mov_b32_e32 v2, v0
	s_nop 1
	v_permlane32_swap_b32_e32 v2, v0
	global_store_dwordx4 v[20:21], v[10:13], off
	v_cvt_pk_bf16_f32 v4, v6, v7
	v_cvt_pk_bf16_f32 v5, v8, v9
	v_cvt_pk_bf16_f32 v6, v16, v17
	v_cvt_pk_bf16_f32 v7, v14, v15
	global_store_dwordx4 v[20:21], v[4:7], off offset:256
	s_and_saveexec_b64 s[6:7], s[40:41]
	s_cbranch_execz .LBB0_764
	v_lshl_add_u32 v3, v18, 4, s34
	s_waitcnt lgkmcnt(0)
	v_add_f32_e32 v0, v0, v2
	ds_write_b32 v3, v0 offset:6144

.LBB0_1024:
	v_mov_b32_e32 v0, v205
	s_nop 1
	v_permlane32_swap_b32_e32 v0, v205
	s_waitcnt lgkmcnt(0)
	v_add_f32_e32 v0, v205, v0
	v_div_scale_f32 v66, s[6:7], v0, v0, 1.0
	v_rcp_f32_e32 v67, v66
	v_readlane_b32 s6, v253, 8
	v_readlane_b32 s7, v253, 9
	v_fma_f32 v68, -v66, v67, 1.0
	v_fmac_f32_e32 v67, v68, v67
	v_div_scale_f32 v68, vcc, 1.0, v0, 1.0
	v_mul_f32_e32 v69, v68, v67
	v_fma_f32 v70, -v66, v69, v68
	v_fmac_f32_e32 v69, v70, v67
	v_fma_f32 v66, -v66, v69, v68
	v_div_fmas_f32 v66, v66, v67, v69
	v_div_fixup_f32 v72, v66, v0, 1.0
	s_andn2_b64 vcc, exec, s[6:7]
	s_cbranch_vccnz .LBB0_1026
	v_mul_f32_e32 v0, v50, v72
	v_mul_f32_e32 v66, v51, v72
	ds_write2st64_b32 v242, v0, v66 offset1:1
	v_mul_f32_e32 v0, v52, v72
	v_mul_f32_e32 v66, v53, v72
	ds_write2st64_b32 v242, v0, v66 offset0:2 offset1:3
	v_mul_f32_e32 v0, v54, v72
	v_mul_f32_e32 v66, v55, v72
	ds_write2st64_b32 v242, v0, v66 offset0:4 offset1:5
	v_mul_f32_e32 v0, v56, v72
	v_mul_f32_e32 v66, v57, v72
	ds_write2st64_b32 v242, v0, v66 offset0:6 offset1:7
	v_mul_f32_e32 v0, v58, v72
	v_mul_f32_e32 v66, v59, v72
	ds_write2st64_b32 v242, v0, v66 offset0:8 offset1:9
	v_mul_f32_e32 v0, v60, v72
	v_mul_f32_e32 v66, v61, v72
	ds_write2st64_b32 v242, v0, v66 offset0:10 offset1:11
	v_mul_f32_e32 v0, v62, v72
	v_mul_f32_e32 v66, v63, v72
	ds_write2st64_b32 v242, v0, v66 offset0:12 offset1:13
	v_mul_f32_e32 v0, v64, v72
	v_mul_f32_e32 v66, v65, v72
	ds_write2st64_b32 v242, v0, v66 offset0:14 offset1:15
	v_mul_f32_e32 v0, v34, v72
	v_mul_f32_e32 v66, v35, v72
	ds_write2st64_b32 v242, v0, v66 offset0:16 offset1:17
	v_mul_f32_e32 v0, v36, v72
	v_mul_f32_e32 v66, v37, v72
	ds_write2st64_b32 v242, v0, v66 offset0:18 offset1:19
	v_mul_f32_e32 v0, v38, v72
	v_mul_f32_e32 v66, v39, v72
	ds_write2st64_b32 v242, v0, v66 offset0:20 offset1:21
	v_mul_f32_e32 v0, v40, v72
	v_mul_f32_e32 v66, v41, v72
	ds_write2st64_b32 v242, v0, v66 offset0:22 offset1:23
	v_mul_f32_e32 v0, v42, v72
	v_mul_f32_e32 v66, v43, v72
	ds_write2st64_b32 v242, v0, v66 offset0:24 offset1:25
	v_mul_f32_e32 v0, v44, v72
	v_mul_f32_e32 v66, v45, v72
	ds_write2st64_b32 v242, v0, v66 offset0:26 offset1:27
	v_mul_f32_e32 v0, v46, v72
	v_mul_f32_e32 v66, v47, v72
	ds_write2st64_b32 v242, v0, v66 offset0:28 offset1:29
	v_mul_f32_e32 v0, v48, v72
	v_mul_f32_e32 v66, v49, v72
	ds_write2st64_b32 v242, v0, v66 offset0:30 offset1:31
	v_mul_f32_e32 v0, v18, v72
	v_mul_f32_e32 v66, v19, v72
	ds_write2st64_b32 v242, v0, v66 offset0:32 offset1:33
	v_mul_f32_e32 v0, v20, v72
	v_mul_f32_e32 v66, v21, v72
	ds_write2st64_b32 v242, v0, v66 offset0:34 offset1:35
	v_mul_f32_e32 v0, v22, v72
	v_mul_f32_e32 v66, v23, v72
	ds_write2st64_b32 v242, v0, v66 offset0:36 offset1:37
	v_mul_f32_e32 v0, v24, v72
	v_mul_f32_e32 v66, v25, v72
	ds_write2st64_b32 v242, v0, v66 offset0:38 offset1:39
	v_mul_f32_e32 v0, v26, v72
	v_mul_f32_e32 v66, v27, v72
	ds_write2st64_b32 v242, v0, v66 offset0:40 offset1:41
	v_mul_f32_e32 v0, v28, v72
	v_mul_f32_e32 v66, v29, v72
	ds_write2st64_b32 v242, v0, v66 offset0:42 offset1:43
	v_mul_f32_e32 v0, v30, v72
	v_mul_f32_e32 v66, v31, v72
	ds_write2st64_b32 v242, v0, v66 offset0:44 offset1:45
	v_mul_f32_e32 v0, v32, v72
	v_mul_f32_e32 v66, v33, v72
	ds_write2st64_b32 v242, v0, v66 offset0:46 offset1:47
	v_mul_f32_e32 v0, v2, v72
	v_mul_f32_e32 v66, v3, v72
	ds_write2st64_b32 v242, v0, v66 offset0:48 offset1:49
	v_mul_f32_e32 v0, v4, v72
	v_mul_f32_e32 v66, v5, v72
	ds_write2st64_b32 v242, v0, v66 offset0:50 offset1:51
	v_mul_f32_e32 v0, v6, v72
	v_mul_f32_e32 v66, v7, v72
	ds_write2st64_b32 v242, v0, v66 offset0:52 offset1:53
	v_mul_f32_e32 v0, v8, v72
	v_mul_f32_e32 v66, v9, v72
	ds_write2st64_b32 v242, v0, v66 offset0:54 offset1:55
	v_mul_f32_e32 v0, v10, v72
	v_mul_f32_e32 v66, v11, v72
	ds_write2st64_b32 v242, v0, v66 offset0:56 offset1:57
	v_mul_f32_e32 v0, v12, v72
	v_mul_f32_e32 v66, v13, v72
	ds_write2st64_b32 v242, v0, v66 offset0:58 offset1:59
	v_mul_f32_e32 v0, v14, v72
	v_mul_f32_e32 v66, v15, v72
	ds_write2st64_b32 v242, v0, v66 offset0:60 offset1:61
	v_mul_f32_e32 v0, v16, v72
	v_mul_f32_e32 v66, v17, v72
	ds_write2st64_b32 v242, v0, v66 offset0:62 offset1:63
.LBB0_1026:
	v_readlane_b32 s6, v253, 10
	v_readlane_b32 s7, v253, 11
	s_andn2_b64 vcc, exec, s[6:7]
	s_waitcnt lgkmcnt(0)
	s_barrier
	s_cbranch_vccnz .LBB0_1000
	ds_read2st64_b32 v[74:75], v243 offset1:1
	ds_read2st64_b32 v[76:77], v243 offset0:2 offset1:3
	ds_read2st64_b32 v[78:79], v243 offset0:4 offset1:5
	ds_read2st64_b32 v[82:83], v243 offset0:6 offset1:7
	ds_read2st64_b32 v[118:119], v243 offset0:8 offset1:9
	ds_read2st64_b32 v[120:121], v243 offset0:10 offset1:11
	ds_read2st64_b32 v[122:123], v243 offset0:12 offset1:13
	ds_read2st64_b32 v[124:125], v243 offset0:14 offset1:15
	ds_read2st64_b32 v[126:127], v243 offset0:16 offset1:17
	ds_read2st64_b32 v[128:129], v243 offset0:18 offset1:19
	s_waitcnt vmcnt(3)
	ds_read2st64_b32 v[130:131], v243 offset0:20 offset1:21
	ds_read2st64_b32 v[132:133], v243 offset0:22 offset1:23
	s_waitcnt vmcnt(2)
	ds_read2st64_b32 v[134:135], v243 offset0:24 offset1:25
	ds_read2st64_b32 v[136:137], v243 offset0:26 offset1:27
	s_waitcnt vmcnt(1)
	ds_read2st64_b32 v[138:139], v243 offset0:28 offset1:29
	ds_read2st64_b32 v[140:141], v243 offset0:30 offset1:31
	ds_read2st64_b32 v[114:115], v243 offset0:32 offset1:33
	ds_read2st64_b32 v[116:117], v243 offset0:34 offset1:35
	ds_read2st64_b32 v[110:111], v243 offset0:36 offset1:37
	ds_read2st64_b32 v[112:113], v243 offset0:38 offset1:39
	ds_read2st64_b32 v[106:107], v243 offset0:40 offset1:41
	ds_read2st64_b32 v[108:109], v243 offset0:42 offset1:43
	ds_read2st64_b32 v[102:103], v243 offset0:44 offset1:45
	ds_read2st64_b32 v[104:105], v243 offset0:46 offset1:47
	ds_read2st64_b32 v[98:99], v243 offset0:48 offset1:49
	ds_read2st64_b32 v[100:101], v243 offset0:50 offset1:51
	ds_read2st64_b32 v[94:95], v243 offset0:52 offset1:53
	ds_read2st64_b32 v[96:97], v243 offset0:54 offset1:55
	ds_read2st64_b32 v[68:69], v243 offset0:56 offset1:57
	ds_read2st64_b32 v[70:71], v243 offset0:58 offset1:59
	ds_read2st64_b32 v[80:81], v243 offset0:60 offset1:61
	ds_read2st64_b32 v[84:85], v243 offset0:62 offset1:63
	v_mov_b32_e32 v184, v10
	s_movk_i32 s4, 0xc00
	v_mov_b32_e32 v205, v1
	s_waitcnt lgkmcnt(3)
	v_mov_b32_e32 v73, v68
	v_mul_f32_e32 v0, v185, v68
	v_pk_fma_f32 v[66:67], v[184:185], v[72:73], v[0:1] op_sel_hi:[1,1,0] neg_lo:[0,0,1] neg_hi:[0,0,1]
	v_mov_b32_e32 v184, v11
	v_mov_b32_e32 v73, v69
	s_waitcnt lgkmcnt(2)
	v_pk_mul_f32 v[10:11], v[196:197], v[70:71]
	v_mul_f32_e32 v0, v185, v69
	v_pk_fma_f32 v[70:71], v[12:13], v[72:73], v[10:11] op_sel_hi:[1,0,1] neg_lo:[0,0,1] neg_hi:[0,0,1]
	s_waitcnt lgkmcnt(1)
	v_pk_mul_f32 v[10:11], v[196:197], v[80:81]
	v_mov_b32_e32 v80, v50
	v_pk_fma_f32 v[14:15], v[14:15], v[72:73], v[10:11] op_sel_hi:[1,0,1] neg_lo:[0,0,1] neg_hi:[0,0,1]
	s_waitcnt lgkmcnt(0)
	v_pk_mul_f32 v[10:11], v[196:197], v[84:85]
	v_mov_b32_e32 v84, v74
	v_mov_b32_e32 v85, v76
	v_mov_b32_e32 v76, v75
	v_mov_b32_e32 v81, v52
	v_pk_mul_f32 v[84:85], v[196:197], v[84:85]
	v_mov_b32_e32 v52, v51
	v_pk_mul_f32 v[50:51], v[196:197], v[76:77]
	v_pk_fma_f32 v[84:85], v[80:81], v[72:73], v[84:85] op_sel_hi:[1,0,1] neg_lo:[0,0,1] neg_hi:[0,0,1]
	v_pk_fma_f32 v[86:87], v[52:53], v[72:73], v[50:51] op_sel_hi:[1,0,1] neg_lo:[0,0,1] neg_hi:[0,0,1]
	s_waitcnt vmcnt(0)
	v_pk_mul_f32 v[142:143], v[84:85], v[84:85]
	v_pk_mul_f32 v[144:145], v[86:87], v[86:87]
	v_mov_b32_e32 v52, v78
	v_mov_b32_e32 v53, v82
	v_pk_fma_f32 v[68:69], v[184:185], v[72:73], v[0:1] op_sel_hi:[1,1,0] neg_lo:[0,0,1] neg_hi:[0,0,1]
	v_mov_b32_e32 v50, v54
	v_mov_b32_e32 v51, v56
	v_pk_mul_f32 v[52:53], v[196:197], v[52:53]
	v_mov_b32_e32 v82, v79
	v_add_f32_e32 v0, v142, v144
	v_pk_fma_f32 v[80:81], v[50:51], v[72:73], v[52:53] op_sel_hi:[1,0,1] neg_lo:[0,0,1] neg_hi:[0,0,1]
	v_mov_b32_e32 v56, v55
	v_pk_mul_f32 v[50:51], v[196:197], v[82:83]
	v_add_f32_e32 v0, v0, v143
	v_pk_mul_f32 v[146:147], v[80:81], v[80:81]
	v_pk_fma_f32 v[82:83], v[56:57], v[72:73], v[50:51] op_sel_hi:[1,0,1] neg_lo:[0,0,1] neg_hi:[0,0,1]
	v_add_f32_e32 v0, v0, v145
	v_pk_mul_f32 v[148:149], v[82:83], v[82:83]
	v_mov_b32_e32 v52, v118
	v_mov_b32_e32 v53, v120
	v_add_f32_e32 v0, v0, v146
	v_mov_b32_e32 v50, v58
	v_mov_b32_e32 v51, v60
	v_pk_mul_f32 v[52:53], v[196:197], v[52:53]
	v_mov_b32_e32 v120, v119
	v_add_f32_e32 v0, v0, v148
	v_pk_fma_f32 v[76:77], v[50:51], v[72:73], v[52:53] op_sel_hi:[1,0,1] neg_lo:[0,0,1] neg_hi:[0,0,1]
	v_mov_b32_e32 v60, v59
	v_pk_mul_f32 v[50:51], v[196:197], v[120:121]
	v_add_f32_e32 v0, v0, v147
	v_pk_mul_f32 v[150:151], v[76:77], v[76:77]
	v_pk_fma_f32 v[78:79], v[60:61], v[72:73], v[50:51] op_sel_hi:[1,0,1] neg_lo:[0,0,1] neg_hi:[0,0,1]
	v_add_f32_e32 v0, v0, v149
	v_pk_mul_f32 v[118:119], v[78:79], v[78:79]
	v_mov_b32_e32 v52, v122
	v_mov_b32_e32 v53, v124
	v_add_f32_e32 v0, v0, v150
	v_mov_b32_e32 v50, v62
	v_mov_b32_e32 v51, v64
	v_pk_mul_f32 v[52:53], v[196:197], v[52:53]
	v_mov_b32_e32 v124, v123
	v_add_f32_e32 v0, v0, v118
	v_pk_fma_f32 v[74:75], v[50:51], v[72:73], v[52:53] op_sel_hi:[1,0,1] neg_lo:[0,0,1] neg_hi:[0,0,1]
	v_mov_b32_e32 v64, v63
	v_pk_mul_f32 v[50:51], v[196:197], v[124:125]
	v_add_f32_e32 v0, v0, v151
	v_pk_fma_f32 v[16:17], v[16:17], v[72:73], v[10:11] op_sel_hi:[1,0,1] neg_lo:[0,0,1] neg_hi:[0,0,1]
	global_load_dwordx4 v[10:13], v[186:187], off
	v_pk_mul_f32 v[120:121], v[74:75], v[74:75]
	v_pk_fma_f32 v[62:63], v[64:65], v[72:73], v[50:51] op_sel_hi:[1,0,1] neg_lo:[0,0,1] neg_hi:[0,0,1]
	v_add_f32_e32 v0, v0, v119
	v_pk_mul_f32 v[64:65], v[62:63], v[62:63]
	v_mov_b32_e32 v52, v126
	v_mov_b32_e32 v53, v128
	v_add_f32_e32 v0, v0, v120
	v_mov_b32_e32 v50, v34
	v_mov_b32_e32 v51, v36
	v_pk_mul_f32 v[52:53], v[196:197], v[52:53]
	v_mov_b32_e32 v128, v127
	v_add_f32_e32 v0, v0, v64
	v_pk_fma_f32 v[58:59], v[50:51], v[72:73], v[52:53] op_sel_hi:[1,0,1] neg_lo:[0,0,1] neg_hi:[0,0,1]
	v_mov_b32_e32 v36, v35
	v_pk_mul_f32 v[34:35], v[196:197], v[128:129]
	v_add_f32_e32 v0, v0, v121
	v_pk_mul_f32 v[122:123], v[58:59], v[58:59]
	v_pk_fma_f32 v[60:61], v[36:37], v[72:73], v[34:35] op_sel_hi:[1,0,1] neg_lo:[0,0,1] neg_hi:[0,0,1]
	v_add_f32_e32 v0, v0, v65
	v_pk_mul_f32 v[124:125], v[60:61], v[60:61]
	v_mov_b32_e32 v36, v130
	v_mov_b32_e32 v37, v132
	v_add_f32_e32 v0, v0, v122
	v_mov_b32_e32 v34, v38
	v_mov_b32_e32 v35, v40
	v_pk_mul_f32 v[36:37], v[196:197], v[36:37]
	v_mov_b32_e32 v132, v131
	v_add_f32_e32 v0, v0, v124
	v_pk_fma_f32 v[54:55], v[34:35], v[72:73], v[36:37] op_sel_hi:[1,0,1] neg_lo:[0,0,1] neg_hi:[0,0,1]
	v_mov_b32_e32 v40, v39
	v_pk_mul_f32 v[34:35], v[196:197], v[132:133]
	v_add_f32_e32 v0, v0, v123
	v_pk_mul_f32 v[126:127], v[54:55], v[54:55]
	v_pk_fma_f32 v[56:57], v[40:41], v[72:73], v[34:35] op_sel_hi:[1,0,1] neg_lo:[0,0,1] neg_hi:[0,0,1]
	v_add_f32_e32 v0, v0, v125
	v_pk_mul_f32 v[128:129], v[56:57], v[56:57]
	v_mov_b32_e32 v36, v134
	v_mov_b32_e32 v37, v136
	v_add_f32_e32 v0, v0, v126
	v_mov_b32_e32 v34, v42
	v_mov_b32_e32 v35, v44
	v_pk_mul_f32 v[36:37], v[196:197], v[36:37]
	v_mov_b32_e32 v136, v135
	v_add_f32_e32 v0, v0, v128
	v_pk_fma_f32 v[50:51], v[34:35], v[72:73], v[36:37] op_sel_hi:[1,0,1] neg_lo:[0,0,1] neg_hi:[0,0,1]
	v_mov_b32_e32 v44, v43
	v_pk_mul_f32 v[34:35], v[196:197], v[136:137]
	v_add_f32_e32 v0, v0, v127
	v_pk_mul_f32 v[130:131], v[50:51], v[50:51]
	v_pk_fma_f32 v[52:53], v[44:45], v[72:73], v[34:35] op_sel_hi:[1,0,1] neg_lo:[0,0,1] neg_hi:[0,0,1]
	v_add_f32_e32 v0, v0, v129
	v_pk_mul_f32 v[132:133], v[52:53], v[52:53]
	v_mov_b32_e32 v36, v138
	v_mov_b32_e32 v37, v140
	v_add_f32_e32 v0, v0, v130
	v_mov_b32_e32 v34, v46
	v_mov_b32_e32 v35, v48
	v_pk_mul_f32 v[36:37], v[196:197], v[36:37]
	v_mov_b32_e32 v140, v139
	v_add_f32_e32 v0, v0, v132
	v_pk_fma_f32 v[44:45], v[34:35], v[72:73], v[36:37] op_sel_hi:[1,0,1] neg_lo:[0,0,1] neg_hi:[0,0,1]
	v_mov_b32_e32 v48, v47
	v_pk_mul_f32 v[34:35], v[196:197], v[140:141]
	v_add_f32_e32 v0, v0, v131
	v_pk_mul_f32 v[134:135], v[44:45], v[44:45]
	v_pk_fma_f32 v[46:47], v[48:49], v[72:73], v[34:35] op_sel_hi:[1,0,1] neg_lo:[0,0,1] neg_hi:[0,0,1]
	v_add_f32_e32 v0, v0, v133
	v_pk_mul_f32 v[48:49], v[46:47], v[46:47]
	v_mov_b32_e32 v36, v114
	v_mov_b32_e32 v37, v116
	v_add_f32_e32 v0, v0, v134
	v_mov_b32_e32 v34, v18
	v_mov_b32_e32 v35, v20
	v_pk_mul_f32 v[36:37], v[196:197], v[36:37]
	v_mov_b32_e32 v116, v115
	v_add_f32_e32 v0, v0, v48
	v_pk_fma_f32 v[40:41], v[34:35], v[72:73], v[36:37] op_sel_hi:[1,0,1] neg_lo:[0,0,1] neg_hi:[0,0,1]
	v_mov_b32_e32 v20, v19
	v_pk_mul_f32 v[18:19], v[196:197], v[116:117]
	v_add_f32_e32 v0, v0, v135
	v_pk_mul_f32 v[136:137], v[40:41], v[40:41]
	v_pk_fma_f32 v[42:43], v[20:21], v[72:73], v[18:19] op_sel_hi:[1,0,1] neg_lo:[0,0,1] neg_hi:[0,0,1]
	v_add_f32_e32 v0, v0, v49
	v_pk_mul_f32 v[114:115], v[42:43], v[42:43]
	v_mov_b32_e32 v20, v110
	v_mov_b32_e32 v21, v112
	v_add_f32_e32 v0, v0, v136
	v_mov_b32_e32 v18, v22
	v_mov_b32_e32 v19, v24
	v_pk_mul_f32 v[20:21], v[196:197], v[20:21]
	v_mov_b32_e32 v112, v111
	v_add_f32_e32 v0, v0, v114
	v_pk_fma_f32 v[36:37], v[18:19], v[72:73], v[20:21] op_sel_hi:[1,0,1] neg_lo:[0,0,1] neg_hi:[0,0,1]
	v_mov_b32_e32 v24, v23
	v_pk_mul_f32 v[18:19], v[196:197], v[112:113]
	v_add_f32_e32 v0, v0, v137
	v_pk_mul_f32 v[116:117], v[36:37], v[36:37]
	v_pk_fma_f32 v[38:39], v[24:25], v[72:73], v[18:19] op_sel_hi:[1,0,1] neg_lo:[0,0,1] neg_hi:[0,0,1]
	v_add_f32_e32 v0, v0, v115
	v_pk_mul_f32 v[110:111], v[38:39], v[38:39]
	v_mov_b32_e32 v20, v106
	v_mov_b32_e32 v21, v108
	v_add_f32_e32 v0, v0, v116
	v_mov_b32_e32 v18, v26
	v_mov_b32_e32 v19, v28
	v_pk_mul_f32 v[20:21], v[196:197], v[20:21]
	v_mov_b32_e32 v108, v107
	v_add_f32_e32 v0, v0, v110
	v_pk_fma_f32 v[34:35], v[18:19], v[72:73], v[20:21] op_sel_hi:[1,0,1] neg_lo:[0,0,1] neg_hi:[0,0,1]
	v_mov_b32_e32 v28, v27
	v_pk_mul_f32 v[18:19], v[196:197], v[108:109]
	v_add_f32_e32 v0, v0, v117
	v_pk_mul_f32 v[112:113], v[34:35], v[34:35]
	v_pk_fma_f32 v[26:27], v[28:29], v[72:73], v[18:19] op_sel_hi:[1,0,1] neg_lo:[0,0,1] neg_hi:[0,0,1]
	v_add_f32_e32 v0, v0, v111
	v_pk_mul_f32 v[28:29], v[26:27], v[26:27]
	v_mov_b32_e32 v20, v102
	v_mov_b32_e32 v21, v104
	v_add_f32_e32 v0, v0, v112
	v_mov_b32_e32 v18, v30
	v_mov_b32_e32 v19, v32
	v_pk_mul_f32 v[20:21], v[196:197], v[20:21]
	v_mov_b32_e32 v104, v103
	v_add_f32_e32 v0, v0, v28
	v_pk_fma_f32 v[22:23], v[18:19], v[72:73], v[20:21] op_sel_hi:[1,0,1] neg_lo:[0,0,1] neg_hi:[0,0,1]
	v_mov_b32_e32 v32, v31
	v_pk_mul_f32 v[18:19], v[196:197], v[104:105]
	v_add_f32_e32 v0, v0, v113
	v_pk_mul_f32 v[106:107], v[22:23], v[22:23]
	v_pk_fma_f32 v[24:25], v[32:33], v[72:73], v[18:19] op_sel_hi:[1,0,1] neg_lo:[0,0,1] neg_hi:[0,0,1]
	v_add_f32_e32 v0, v0, v29
	v_pk_mul_f32 v[30:31], v[24:25], v[24:25]
	v_mov_b32_e32 v20, v98
	v_mov_b32_e32 v21, v100
	v_add_f32_e32 v0, v0, v106
	v_mov_b32_e32 v18, v2
	v_mov_b32_e32 v19, v4
	v_pk_mul_f32 v[20:21], v[196:197], v[20:21]
	v_mov_b32_e32 v100, v99
	v_add_f32_e32 v0, v0, v30
	v_pk_fma_f32 v[18:19], v[18:19], v[72:73], v[20:21] op_sel_hi:[1,0,1] neg_lo:[0,0,1] neg_hi:[0,0,1]
	v_mov_b32_e32 v4, v3
	v_pk_mul_f32 v[2:3], v[196:197], v[100:101]
	v_add_f32_e32 v0, v0, v107
	v_pk_mul_f32 v[32:33], v[18:19], v[18:19]
	v_pk_fma_f32 v[20:21], v[4:5], v[72:73], v[2:3] op_sel_hi:[1,0,1] neg_lo:[0,0,1] neg_hi:[0,0,1]
	v_add_f32_e32 v0, v0, v31
	v_pk_mul_f32 v[98:99], v[20:21], v[20:21]
	v_mov_b32_e32 v4, v94
	v_mov_b32_e32 v5, v96
	v_add_f32_e32 v0, v0, v32
	v_mov_b32_e32 v2, v6
	v_mov_b32_e32 v3, v8
	v_pk_mul_f32 v[4:5], v[196:197], v[4:5]
	v_mov_b32_e32 v96, v95
	v_add_f32_e32 v0, v0, v98
	v_pk_fma_f32 v[2:3], v[2:3], v[72:73], v[4:5] op_sel_hi:[1,0,1] neg_lo:[0,0,1] neg_hi:[0,0,1]
	v_mov_b32_e32 v8, v7
	v_pk_mul_f32 v[4:5], v[196:197], v[96:97]
	v_add_f32_e32 v0, v0, v33
	v_pk_mul_f32 v[100:101], v[2:3], v[2:3]
	v_pk_fma_f32 v[4:5], v[8:9], v[72:73], v[4:5] op_sel_hi:[1,0,1] neg_lo:[0,0,1] neg_hi:[0,0,1]
	v_add_f32_e32 v0, v0, v99
	v_pk_mul_f32 v[6:7], v[4:5], v[4:5]
	v_add_f32_e32 v0, v0, v100
	v_add_f32_e32 v0, v0, v6
	v_add_f32_e32 v0, v0, v101
	v_add_f32_e32 v0, v0, v7
	v_fmac_f32_e32 v0, v66, v66
	v_pk_mul_f32 v[88:89], v[70:71], v[70:71]
	v_fmac_f32_e32 v0, v68, v68
	v_add_f32_e32 v0, v0, v88
	v_pk_mul_f32 v[90:91], v[14:15], v[14:15]
	v_add_f32_e32 v0, v0, v89
	v_add_f32_e32 v0, v0, v90
	v_pk_mul_f32 v[92:93], v[16:17], v[16:17]
	v_add_f32_e32 v0, v0, v91
	v_add_f32_e32 v0, v0, v92
	v_add_f32_e32 v0, v0, v93
	v_mov_b32_e32 v8, v0
	s_nop 1
	v_permlane32_swap_b32_e32 v8, v0
	v_mov_b64_e32 v[6:7], s[12:13]
	v_mad_u64_u32 v[6:7], s[6:7], v206, s4, v[6:7]
	v_mad_i32_i24 v7, v207, s4, v7
	s_waitcnt lgkmcnt(0)
	v_add_f32_e32 v0, v0, v8
	v_fmamk_f32 v0, v0, 0x3c000000, v226
	v_mul_f32_e32 v8, 0x4f800000, v0
	v_cmp_gt_f32_e32 vcc, s89, v0
	v_lshl_add_u64 v[6:7], v[6:7], 0, s[96:97]
	v_lshl_add_u64 v[6:7], v[6:7], 0, v[204:205]
	v_cndmask_b32_e32 v0, v0, v8, vcc
	v_sqrt_f32_e32 v8, v0
	s_mov_b32 s4, 0x4c00000
	v_mov_b32_e32 v69, v71
	v_mov_b32_e32 v67, v70
	v_add_u32_e32 v9, -1, v8
	v_fma_f32 v28, -v9, v8, v0
	v_cmp_ge_f32_e64 s[38:39], 0, v28
	v_add_u32_e32 v28, 1, v8
	s_nop 0
	v_cndmask_b32_e64 v9, v8, v9, s[38:39]
	v_fma_f32 v8, -v28, v8, v0
	v_cmp_lt_f32_e64 s[38:39], 0, v8
	s_nop 1
	v_cndmask_b32_e64 v8, v9, v28, s[38:39]
	v_mul_f32_e32 v9, 0x37800000, v8
	v_cndmask_b32_e32 v8, v8, v9, vcc
	v_cmp_class_f32_e32 vcc, v0, v227
	s_waitcnt vmcnt(0)
	v_mov_b32_e32 v9, v12
	v_mov_b32_e32 v12, v11
	v_cndmask_b32_e32 v0, v8, v0, vcc
	v_div_scale_f32 v28, s[6:7], v0, v0, 1.0
	v_rcp_f32_e32 v29, v28
	v_mov_b32_e32 v8, v10
	s_mov_b64 s[6:7], 0x4c00800
	v_readlane_b32 s38, v255, 18
	v_fma_f32 v10, -v28, v29, 1.0
	v_fmac_f32_e32 v29, v10, v29
	v_div_scale_f32 v10, vcc, 1.0, v0, 1.0
	v_mul_f32_e32 v11, v10, v29
	v_fma_f32 v30, -v28, v11, v10
	v_fmac_f32_e32 v11, v30, v29
	v_fma_f32 v10, -v28, v11, v10
	v_div_fmas_f32 v10, v10, v29, v11
	v_div_fixup_f32 v0, v10, v0, 1.0
	v_mul_f32_e32 v0, v245, v0
	v_pk_mul_f32 v[10:11], v[84:85], v[0:1] op_sel_hi:[1,0]
	v_pk_mul_f32 v[26:27], v[26:27], v[0:1] op_sel_hi:[1,0]
	v_pk_mul_f32 v[8:9], v[8:9], v[10:11]
	v_pk_mul_f32 v[10:11], v[86:87], v[0:1] op_sel_hi:[1,0]
	v_pk_mul_f32 v[4:5], v[4:5], v[0:1] op_sel_hi:[1,0]
	v_pk_mul_f32 v[10:11], v[12:13], v[10:11]
	v_and_b32_sdwa v13, v8, v228 dst_sel:DWORD dst_unused:UNUSED_PAD src0_sel:WORD_1 src1_sel:DWORD
	v_and_b32_sdwa v12, v9, v228 dst_sel:DWORD dst_unused:UNUSED_PAD src0_sel:WORD_1 src1_sel:DWORD
	v_add3_u32 v8, v8, v13, s55
	v_and_b32_sdwa v13, v10, v228 dst_sel:DWORD dst_unused:UNUSED_PAD src0_sel:WORD_1 src1_sel:DWORD
	v_add3_u32 v9, v9, v12, s55
	v_and_b32_sdwa v12, v11, v228 dst_sel:DWORD dst_unused:UNUSED_PAD src0_sel:WORD_1 src1_sel:DWORD
	v_add3_u32 v10, v10, v13, s55
	v_add3_u32 v11, v11, v12, s55
	v_and_b32_e32 v10, 0xffff0000, v10
	v_and_b32_e32 v11, 0xffff0000, v11
	v_or_b32_sdwa v8, v10, v8 dst_sel:DWORD dst_unused:UNUSED_PAD src0_sel:DWORD src1_sel:WORD_1
	v_add_co_u32_e32 v10, vcc, s4, v6
	v_or_b32_sdwa v9, v11, v9 dst_sel:DWORD dst_unused:UNUSED_PAD src0_sel:DWORD src1_sel:WORD_1
	s_nop 0
	v_addc_co_u32_e32 v11, vcc, 0, v7, vcc
	global_store_dwordx2 v[10:11], v[8:9], off offset:2048
	global_load_dwordx4 v[8:11], v[186:187], off offset:32
	v_pk_mul_f32 v[12:13], v[80:81], v[0:1] op_sel_hi:[1,0]
	v_lshl_add_u64 v[6:7], v[6:7], 0, s[6:7]
	v_pk_mul_f32 v[2:3], v[2:3], v[0:1] op_sel_hi:[1,0]
	v_readlane_b32 s39, v255, 19
	s_waitcnt vmcnt(0)
	v_mov_b32_e32 v28, v8
	v_mov_b32_e32 v29, v10
	v_pk_mul_f32 v[12:13], v[28:29], v[12:13]
	v_pk_mul_f32 v[28:29], v[82:83], v[0:1] op_sel_hi:[1,0]
	v_mov_b32_e32 v10, v9
	v_pk_mul_f32 v[8:9], v[10:11], v[28:29]
	v_and_b32_sdwa v10, v13, v228 dst_sel:DWORD dst_unused:UNUSED_PAD src0_sel:WORD_1 src1_sel:DWORD
	v_and_b32_sdwa v11, v12, v228 dst_sel:DWORD dst_unused:UNUSED_PAD src0_sel:WORD_1 src1_sel:DWORD
	v_add3_u32 v11, v12, v11, s55
	v_add3_u32 v10, v13, v10, s55
	v_and_b32_sdwa v12, v9, v228 dst_sel:DWORD dst_unused:UNUSED_PAD src0_sel:WORD_1 src1_sel:DWORD
	v_and_b32_sdwa v13, v8, v228 dst_sel:DWORD dst_unused:UNUSED_PAD src0_sel:WORD_1 src1_sel:DWORD
	v_add3_u32 v9, v9, v12, s55
	v_add3_u32 v8, v8, v13, s55
	v_and_b32_e32 v9, 0xffff0000, v9
	v_and_b32_e32 v8, 0xffff0000, v8
	v_or_b32_sdwa v9, v9, v10 dst_sel:DWORD dst_unused:UNUSED_PAD src0_sel:DWORD src1_sel:WORD_1
	v_or_b32_sdwa v8, v8, v11 dst_sel:DWORD dst_unused:UNUSED_PAD src0_sel:DWORD src1_sel:WORD_1
	global_store_dwordx2 v[6:7], v[8:9], off offset:16
	global_load_dwordx4 v[8:11], v[186:187], off offset:64
	v_pk_mul_f32 v[12:13], v[76:77], v[0:1] op_sel_hi:[1,0]
	s_waitcnt vmcnt(0)
	v_mov_b32_e32 v28, v8
	v_mov_b32_e32 v29, v10
	v_pk_mul_f32 v[12:13], v[28:29], v[12:13]
	v_pk_mul_f32 v[28:29], v[78:79], v[0:1] op_sel_hi:[1,0]
	v_mov_b32_e32 v10, v9
	v_pk_mul_f32 v[8:9], v[10:11], v[28:29]
	v_and_b32_sdwa v10, v13, v228 dst_sel:DWORD dst_unused:UNUSED_PAD src0_sel:WORD_1 src1_sel:DWORD
	v_and_b32_sdwa v11, v12, v228 dst_sel:DWORD dst_unused:UNUSED_PAD src0_sel:WORD_1 src1_sel:DWORD
	v_add3_u32 v11, v12, v11, s55
	v_add3_u32 v10, v13, v10, s55
	v_and_b32_sdwa v12, v9, v228 dst_sel:DWORD dst_unused:UNUSED_PAD src0_sel:WORD_1 src1_sel:DWORD
	v_and_b32_sdwa v13, v8, v228 dst_sel:DWORD dst_unused:UNUSED_PAD src0_sel:WORD_1 src1_sel:DWORD
	v_add3_u32 v9, v9, v12, s55
	v_add3_u32 v8, v8, v13, s55
	v_and_b32_e32 v9, 0xffff0000, v9
	v_and_b32_e32 v8, 0xffff0000, v8
	v_or_b32_sdwa v9, v9, v10 dst_sel:DWORD dst_unused:UNUSED_PAD src0_sel:DWORD src1_sel:WORD_1
	v_or_b32_sdwa v8, v8, v11 dst_sel:DWORD dst_unused:UNUSED_PAD src0_sel:DWORD src1_sel:WORD_1
	global_store_dwordx2 v[6:7], v[8:9], off offset:32
	global_load_dwordx4 v[8:11], v[186:187], off offset:96
	v_pk_mul_f32 v[12:13], v[74:75], v[0:1] op_sel_hi:[1,0]
	s_waitcnt vmcnt(0)
	v_mov_b32_e32 v28, v8
	v_mov_b32_e32 v29, v10
	v_pk_mul_f32 v[12:13], v[28:29], v[12:13]
	v_pk_mul_f32 v[28:29], v[62:63], v[0:1] op_sel_hi:[1,0]
	v_mov_b32_e32 v10, v9
	v_pk_mul_f32 v[8:9], v[10:11], v[28:29]
	v_and_b32_sdwa v10, v13, v228 dst_sel:DWORD dst_unused:UNUSED_PAD src0_sel:WORD_1 src1_sel:DWORD
	v_and_b32_sdwa v11, v12, v228 dst_sel:DWORD dst_unused:UNUSED_PAD src0_sel:WORD_1 src1_sel:DWORD
	v_add3_u32 v11, v12, v11, s55
	v_add3_u32 v10, v13, v10, s55
	v_and_b32_sdwa v12, v9, v228 dst_sel:DWORD dst_unused:UNUSED_PAD src0_sel:WORD_1 src1_sel:DWORD
	v_and_b32_sdwa v13, v8, v228 dst_sel:DWORD dst_unused:UNUSED_PAD src0_sel:WORD_1 src1_sel:DWORD
	v_add3_u32 v9, v9, v12, s55
	v_add3_u32 v8, v8, v13, s55
	v_and_b32_e32 v9, 0xffff0000, v9
	v_and_b32_e32 v8, 0xffff0000, v8
	v_or_b32_sdwa v9, v9, v10 dst_sel:DWORD dst_unused:UNUSED_PAD src0_sel:DWORD src1_sel:WORD_1
	v_or_b32_sdwa v8, v8, v11 dst_sel:DWORD dst_unused:UNUSED_PAD src0_sel:DWORD src1_sel:WORD_1
	global_store_dwordx2 v[6:7], v[8:9], off offset:48
	global_load_dwordx4 v[8:11], v[186:187], off offset:128
	v_pk_mul_f32 v[28:29], v[60:61], v[0:1] op_sel_hi:[1,0]
	v_pk_mul_f32 v[12:13], v[58:59], v[0:1] op_sel_hi:[1,0]
	s_waitcnt vmcnt(0)
	v_mov_b32_e32 v31, v10
	v_mov_b32_e32 v10, v9
	v_mov_b32_e32 v30, v8
	v_pk_mul_f32 v[10:11], v[10:11], v[28:29]
	v_pk_mul_f32 v[8:9], v[30:31], v[12:13]
	v_and_b32_sdwa v28, v11, v228 dst_sel:DWORD dst_unused:UNUSED_PAD src0_sel:WORD_1 src1_sel:DWORD
	v_and_b32_sdwa v29, v10, v228 dst_sel:DWORD dst_unused:UNUSED_PAD src0_sel:WORD_1 src1_sel:DWORD
	v_and_b32_sdwa v12, v9, v228 dst_sel:DWORD dst_unused:UNUSED_PAD src0_sel:WORD_1 src1_sel:DWORD
	v_and_b32_sdwa v13, v8, v228 dst_sel:DWORD dst_unused:UNUSED_PAD src0_sel:WORD_1 src1_sel:DWORD
	v_add3_u32 v11, v11, v28, s55
	v_add3_u32 v10, v10, v29, s55
	v_add3_u32 v8, v8, v13, s55
	v_add3_u32 v9, v9, v12, s55
	v_and_b32_e32 v11, 0xffff0000, v11
	v_and_b32_e32 v10, 0xffff0000, v10
	v_or_b32_sdwa v9, v11, v9 dst_sel:DWORD dst_unused:UNUSED_PAD src0_sel:DWORD src1_sel:WORD_1
	v_or_b32_sdwa v8, v10, v8 dst_sel:DWORD dst_unused:UNUSED_PAD src0_sel:DWORD src1_sel:WORD_1
	global_store_dwordx2 v[6:7], v[8:9], off offset:64
	global_load_dwordx4 v[8:11], v[186:187], off offset:160
	v_pk_mul_f32 v[28:29], v[56:57], v[0:1] op_sel_hi:[1,0]
	v_pk_mul_f32 v[12:13], v[54:55], v[0:1] op_sel_hi:[1,0]
	s_waitcnt vmcnt(0)
	v_mov_b32_e32 v31, v10
	v_mov_b32_e32 v10, v9
	v_mov_b32_e32 v30, v8
	v_pk_mul_f32 v[10:11], v[28:29], v[10:11]
	v_pk_mul_f32 v[8:9], v[12:13], v[30:31]
	v_and_b32_sdwa v28, v11, v228 dst_sel:DWORD dst_unused:UNUSED_PAD src0_sel:WORD_1 src1_sel:DWORD
	v_and_b32_sdwa v29, v10, v228 dst_sel:DWORD dst_unused:UNUSED_PAD src0_sel:WORD_1 src1_sel:DWORD
	v_and_b32_sdwa v12, v9, v228 dst_sel:DWORD dst_unused:UNUSED_PAD src0_sel:WORD_1 src1_sel:DWORD
	v_and_b32_sdwa v13, v8, v228 dst_sel:DWORD dst_unused:UNUSED_PAD src0_sel:WORD_1 src1_sel:DWORD
	v_add3_u32 v11, v11, v28, s55
	v_add3_u32 v10, v10, v29, s55
	v_add3_u32 v8, v8, v13, s55
	v_add3_u32 v9, v9, v12, s55
	v_and_b32_e32 v11, 0xffff0000, v11
	v_and_b32_e32 v10, 0xffff0000, v10
	v_or_b32_sdwa v9, v11, v9 dst_sel:DWORD dst_unused:UNUSED_PAD src0_sel:DWORD src1_sel:WORD_1
	v_or_b32_sdwa v8, v10, v8 dst_sel:DWORD dst_unused:UNUSED_PAD src0_sel:DWORD src1_sel:WORD_1
	global_store_dwordx2 v[6:7], v[8:9], off offset:80
	global_load_dwordx4 v[8:11], v[186:187], off offset:192
	v_pk_mul_f32 v[28:29], v[52:53], v[0:1] op_sel_hi:[1,0]
	v_pk_mul_f32 v[12:13], v[50:51], v[0:1] op_sel_hi:[1,0]
	s_waitcnt vmcnt(0)
	v_mov_b32_e32 v31, v10
	v_mov_b32_e32 v10, v9
	v_mov_b32_e32 v30, v8
	v_pk_mul_f32 v[10:11], v[28:29], v[10:11]
	v_pk_mul_f32 v[8:9], v[12:13], v[30:31]
	v_and_b32_sdwa v28, v11, v228 dst_sel:DWORD dst_unused:UNUSED_PAD src0_sel:WORD_1 src1_sel:DWORD
	v_and_b32_sdwa v29, v10, v228 dst_sel:DWORD dst_unused:UNUSED_PAD src0_sel:WORD_1 src1_sel:DWORD
	v_and_b32_sdwa v12, v9, v228 dst_sel:DWORD dst_unused:UNUSED_PAD src0_sel:WORD_1 src1_sel:DWORD
	v_and_b32_sdwa v13, v8, v228 dst_sel:DWORD dst_unused:UNUSED_PAD src0_sel:WORD_1 src1_sel:DWORD
	v_add3_u32 v11, v11, v28, s55
	v_add3_u32 v10, v10, v29, s55
	v_add3_u32 v8, v8, v13, s55
	v_add3_u32 v9, v9, v12, s55
	v_and_b32_e32 v11, 0xffff0000, v11
	v_and_b32_e32 v10, 0xffff0000, v10
	v_or_b32_sdwa v9, v11, v9 dst_sel:DWORD dst_unused:UNUSED_PAD src0_sel:DWORD src1_sel:WORD_1
	v_or_b32_sdwa v8, v10, v8 dst_sel:DWORD dst_unused:UNUSED_PAD src0_sel:DWORD src1_sel:WORD_1
	global_store_dwordx2 v[6:7], v[8:9], off offset:96
	global_load_dwordx4 v[8:11], v[186:187], off offset:224
	v_pk_mul_f32 v[28:29], v[46:47], v[0:1] op_sel_hi:[1,0]
	v_pk_mul_f32 v[12:13], v[44:45], v[0:1] op_sel_hi:[1,0]
	s_waitcnt vmcnt(0)
	v_mov_b32_e32 v31, v10
	v_mov_b32_e32 v10, v9
	v_mov_b32_e32 v30, v8
	v_pk_mul_f32 v[10:11], v[28:29], v[10:11]
	v_pk_mul_f32 v[8:9], v[12:13], v[30:31]
	v_and_b32_sdwa v28, v11, v228 dst_sel:DWORD dst_unused:UNUSED_PAD src0_sel:WORD_1 src1_sel:DWORD
	v_and_b32_sdwa v29, v10, v228 dst_sel:DWORD dst_unused:UNUSED_PAD src0_sel:WORD_1 src1_sel:DWORD
	v_and_b32_sdwa v12, v9, v228 dst_sel:DWORD dst_unused:UNUSED_PAD src0_sel:WORD_1 src1_sel:DWORD
	v_and_b32_sdwa v13, v8, v228 dst_sel:DWORD dst_unused:UNUSED_PAD src0_sel:WORD_1 src1_sel:DWORD
	v_add3_u32 v11, v11, v28, s55
	v_add3_u32 v10, v10, v29, s55
	v_add3_u32 v8, v8, v13, s55
	v_add3_u32 v9, v9, v12, s55
	v_and_b32_e32 v11, 0xffff0000, v11
	v_and_b32_e32 v10, 0xffff0000, v10
	v_or_b32_sdwa v9, v11, v9 dst_sel:DWORD dst_unused:UNUSED_PAD src0_sel:DWORD src1_sel:WORD_1
	v_or_b32_sdwa v8, v10, v8 dst_sel:DWORD dst_unused:UNUSED_PAD src0_sel:DWORD src1_sel:WORD_1
	global_store_dwordx2 v[6:7], v[8:9], off offset:112
	global_load_dwordx4 v[8:11], v[186:187], off offset:256
	v_pk_mul_f32 v[28:29], v[42:43], v[0:1] op_sel_hi:[1,0]
	v_pk_mul_f32 v[12:13], v[40:41], v[0:1] op_sel_hi:[1,0]
	s_waitcnt vmcnt(0)
	v_mov_b32_e32 v31, v10
	v_mov_b32_e32 v10, v9
	v_mov_b32_e32 v30, v8
	v_pk_mul_f32 v[10:11], v[28:29], v[10:11]
	v_pk_mul_f32 v[8:9], v[12:13], v[30:31]
	v_and_b32_sdwa v28, v11, v228 dst_sel:DWORD dst_unused:UNUSED_PAD src0_sel:WORD_1 src1_sel:DWORD
	v_and_b32_sdwa v29, v10, v228 dst_sel:DWORD dst_unused:UNUSED_PAD src0_sel:WORD_1 src1_sel:DWORD
	v_and_b32_sdwa v12, v9, v228 dst_sel:DWORD dst_unused:UNUSED_PAD src0_sel:WORD_1 src1_sel:DWORD
	v_and_b32_sdwa v13, v8, v228 dst_sel:DWORD dst_unused:UNUSED_PAD src0_sel:WORD_1 src1_sel:DWORD
	v_add3_u32 v11, v11, v28, s55
	v_add3_u32 v10, v10, v29, s55
	v_add3_u32 v8, v8, v13, s55
	v_add3_u32 v9, v9, v12, s55
	v_and_b32_e32 v11, 0xffff0000, v11
	v_and_b32_e32 v10, 0xffff0000, v10
	v_or_b32_sdwa v9, v11, v9 dst_sel:DWORD dst_unused:UNUSED_PAD src0_sel:DWORD src1_sel:WORD_1
	v_or_b32_sdwa v8, v10, v8 dst_sel:DWORD dst_unused:UNUSED_PAD src0_sel:DWORD src1_sel:WORD_1
	global_store_dwordx2 v[6:7], v[8:9], off offset:128
	global_load_dwordx4 v[8:11], v[186:187], off offset:288
	v_pk_mul_f32 v[28:29], v[38:39], v[0:1] op_sel_hi:[1,0]
	v_pk_mul_f32 v[12:13], v[36:37], v[0:1] op_sel_hi:[1,0]
	s_waitcnt vmcnt(0)
	v_mov_b32_e32 v31, v10
	v_mov_b32_e32 v10, v9
	v_mov_b32_e32 v30, v8
	v_pk_mul_f32 v[10:11], v[28:29], v[10:11]
	v_pk_mul_f32 v[8:9], v[12:13], v[30:31]
	v_and_b32_sdwa v28, v11, v228 dst_sel:DWORD dst_unused:UNUSED_PAD src0_sel:WORD_1 src1_sel:DWORD
	v_and_b32_sdwa v29, v10, v228 dst_sel:DWORD dst_unused:UNUSED_PAD src0_sel:WORD_1 src1_sel:DWORD
	v_and_b32_sdwa v12, v9, v228 dst_sel:DWORD dst_unused:UNUSED_PAD src0_sel:WORD_1 src1_sel:DWORD
	v_and_b32_sdwa v13, v8, v228 dst_sel:DWORD dst_unused:UNUSED_PAD src0_sel:WORD_1 src1_sel:DWORD
	v_add3_u32 v11, v11, v28, s55
	v_add3_u32 v10, v10, v29, s55
	v_add3_u32 v8, v8, v13, s55
	v_add3_u32 v9, v9, v12, s55
	v_and_b32_e32 v11, 0xffff0000, v11
	v_and_b32_e32 v10, 0xffff0000, v10
	v_or_b32_sdwa v9, v11, v9 dst_sel:DWORD dst_unused:UNUSED_PAD src0_sel:DWORD src1_sel:WORD_1
	v_or_b32_sdwa v8, v10, v8 dst_sel:DWORD dst_unused:UNUSED_PAD src0_sel:DWORD src1_sel:WORD_1
	global_store_dwordx2 v[6:7], v[8:9], off offset:144
	global_load_dwordx4 v[8:11], v[186:187], off offset:320
	v_pk_mul_f32 v[12:13], v[34:35], v[0:1] op_sel_hi:[1,0]
	s_waitcnt vmcnt(0)
	v_mov_b32_e32 v29, v10
	v_mov_b32_e32 v10, v9
	v_mov_b32_e32 v28, v8
	v_pk_mul_f32 v[10:11], v[26:27], v[10:11]
	v_pk_mul_f32 v[8:9], v[12:13], v[28:29]
	v_and_b32_sdwa v26, v11, v228 dst_sel:DWORD dst_unused:UNUSED_PAD src0_sel:WORD_1 src1_sel:DWORD
	v_and_b32_sdwa v27, v10, v228 dst_sel:DWORD dst_unused:UNUSED_PAD src0_sel:WORD_1 src1_sel:DWORD
	v_and_b32_sdwa v12, v9, v228 dst_sel:DWORD dst_unused:UNUSED_PAD src0_sel:WORD_1 src1_sel:DWORD
	v_and_b32_sdwa v13, v8, v228 dst_sel:DWORD dst_unused:UNUSED_PAD src0_sel:WORD_1 src1_sel:DWORD
	v_add3_u32 v11, v11, v26, s55
	v_add3_u32 v10, v10, v27, s55
	v_add3_u32 v8, v8, v13, s55
	v_add3_u32 v9, v9, v12, s55
	v_and_b32_e32 v11, 0xffff0000, v11
	v_and_b32_e32 v10, 0xffff0000, v10
	v_or_b32_sdwa v9, v11, v9 dst_sel:DWORD dst_unused:UNUSED_PAD src0_sel:DWORD src1_sel:WORD_1
	v_or_b32_sdwa v8, v10, v8 dst_sel:DWORD dst_unused:UNUSED_PAD src0_sel:DWORD src1_sel:WORD_1
	global_store_dwordx2 v[6:7], v[8:9], off offset:160
	global_load_dwordx4 v[8:11], v[186:187], off offset:352
	v_pk_mul_f32 v[12:13], v[22:23], v[0:1] op_sel_hi:[1,0]
	v_pk_mul_f32 v[22:23], v[24:25], v[0:1] op_sel_hi:[1,0]
	s_waitcnt vmcnt(0)
	v_mov_b32_e32 v25, v10
	v_mov_b32_e32 v10, v9
	v_mov_b32_e32 v24, v8
	v_pk_mul_f32 v[10:11], v[22:23], v[10:11]
	v_pk_mul_f32 v[8:9], v[12:13], v[24:25]
	v_and_b32_sdwa v22, v11, v228 dst_sel:DWORD dst_unused:UNUSED_PAD src0_sel:WORD_1 src1_sel:DWORD
	v_and_b32_sdwa v23, v10, v228 dst_sel:DWORD dst_unused:UNUSED_PAD src0_sel:WORD_1 src1_sel:DWORD
	v_and_b32_sdwa v12, v9, v228 dst_sel:DWORD dst_unused:UNUSED_PAD src0_sel:WORD_1 src1_sel:DWORD
	v_and_b32_sdwa v13, v8, v228 dst_sel:DWORD dst_unused:UNUSED_PAD src0_sel:WORD_1 src1_sel:DWORD
	v_add3_u32 v11, v11, v22, s55
	v_add3_u32 v10, v10, v23, s55
	v_add3_u32 v8, v8, v13, s55
	v_add3_u32 v9, v9, v12, s55
	v_and_b32_e32 v11, 0xffff0000, v11
	v_and_b32_e32 v10, 0xffff0000, v10
	v_or_b32_sdwa v9, v11, v9 dst_sel:DWORD dst_unused:UNUSED_PAD src0_sel:DWORD src1_sel:WORD_1
	v_or_b32_sdwa v8, v10, v8 dst_sel:DWORD dst_unused:UNUSED_PAD src0_sel:DWORD src1_sel:WORD_1
	global_store_dwordx2 v[6:7], v[8:9], off offset:176
	global_load_dwordx4 v[8:11], v[186:187], off offset:384
	v_pk_mul_f32 v[12:13], v[18:19], v[0:1] op_sel_hi:[1,0]
	v_pk_mul_f32 v[18:19], v[20:21], v[0:1] op_sel_hi:[1,0]
	s_waitcnt vmcnt(0)
	v_mov_b32_e32 v21, v10
	v_mov_b32_e32 v10, v9
	v_mov_b32_e32 v20, v8
	v_pk_mul_f32 v[10:11], v[18:19], v[10:11]
	v_pk_mul_f32 v[8:9], v[12:13], v[20:21]
	v_and_b32_sdwa v18, v11, v228 dst_sel:DWORD dst_unused:UNUSED_PAD src0_sel:WORD_1 src1_sel:DWORD
	v_and_b32_sdwa v19, v10, v228 dst_sel:DWORD dst_unused:UNUSED_PAD src0_sel:WORD_1 src1_sel:DWORD
	v_and_b32_sdwa v12, v9, v228 dst_sel:DWORD dst_unused:UNUSED_PAD src0_sel:WORD_1 src1_sel:DWORD
	v_and_b32_sdwa v13, v8, v228 dst_sel:DWORD dst_unused:UNUSED_PAD src0_sel:WORD_1 src1_sel:DWORD
	v_add3_u32 v11, v11, v18, s55
	v_add3_u32 v10, v10, v19, s55
	v_add3_u32 v8, v8, v13, s55
	v_add3_u32 v9, v9, v12, s55
	v_and_b32_e32 v11, 0xffff0000, v11
	v_and_b32_e32 v10, 0xffff0000, v10
	v_or_b32_sdwa v9, v11, v9 dst_sel:DWORD dst_unused:UNUSED_PAD src0_sel:DWORD src1_sel:WORD_1
	v_or_b32_sdwa v8, v10, v8 dst_sel:DWORD dst_unused:UNUSED_PAD src0_sel:DWORD src1_sel:WORD_1
	global_store_dwordx2 v[6:7], v[8:9], off offset:192
	global_load_dwordx4 v[8:11], v[186:187], off offset:416
	s_waitcnt vmcnt(0)
	v_mov_b32_e32 v13, v10
	v_mov_b32_e32 v10, v9
	v_mov_b32_e32 v12, v8
	v_pk_mul_f32 v[4:5], v[4:5], v[10:11]
	v_pk_mul_f32 v[2:3], v[2:3], v[12:13]
	v_and_b32_sdwa v10, v5, v228 dst_sel:DWORD dst_unused:UNUSED_PAD src0_sel:WORD_1 src1_sel:DWORD
	v_and_b32_sdwa v11, v4, v228 dst_sel:DWORD dst_unused:UNUSED_PAD src0_sel:WORD_1 src1_sel:DWORD
	v_and_b32_sdwa v8, v3, v228 dst_sel:DWORD dst_unused:UNUSED_PAD src0_sel:WORD_1 src1_sel:DWORD
	v_and_b32_sdwa v9, v2, v228 dst_sel:DWORD dst_unused:UNUSED_PAD src0_sel:WORD_1 src1_sel:DWORD
	v_add3_u32 v5, v5, v10, s55
	v_add3_u32 v4, v4, v11, s55
	v_add3_u32 v2, v2, v9, s55
	v_add3_u32 v3, v3, v8, s55
	v_and_b32_e32 v5, 0xffff0000, v5
	v_and_b32_e32 v4, 0xffff0000, v4
	v_or_b32_sdwa v3, v5, v3 dst_sel:DWORD dst_unused:UNUSED_PAD src0_sel:DWORD src1_sel:WORD_1
	v_or_b32_sdwa v2, v4, v2 dst_sel:DWORD dst_unused:UNUSED_PAD src0_sel:DWORD src1_sel:WORD_1
	global_store_dwordx2 v[6:7], v[2:3], off offset:208
	global_load_dwordx4 v[2:5], v[186:187], off offset:448
	v_pk_mul_f32 v[10:11], v[68:69], v[0:1] op_sel_hi:[1,0]
	v_pk_mul_f32 v[8:9], v[66:67], v[0:1] op_sel_hi:[1,0]
	s_waitcnt vmcnt(0)
	v_mov_b32_e32 v13, v4
	v_mov_b32_e32 v4, v3
	v_mov_b32_e32 v12, v2
	v_pk_mul_f32 v[4:5], v[10:11], v[4:5]
	v_pk_mul_f32 v[2:3], v[8:9], v[12:13]
	v_and_b32_sdwa v10, v5, v228 dst_sel:DWORD dst_unused:UNUSED_PAD src0_sel:WORD_1 src1_sel:DWORD
	v_and_b32_sdwa v11, v4, v228 dst_sel:DWORD dst_unused:UNUSED_PAD src0_sel:WORD_1 src1_sel:DWORD
	v_and_b32_sdwa v8, v3, v228 dst_sel:DWORD dst_unused:UNUSED_PAD src0_sel:WORD_1 src1_sel:DWORD
	v_and_b32_sdwa v9, v2, v228 dst_sel:DWORD dst_unused:UNUSED_PAD src0_sel:WORD_1 src1_sel:DWORD
	v_add3_u32 v5, v5, v10, s55
	v_add3_u32 v4, v4, v11, s55
	v_add3_u32 v2, v2, v9, s55
	v_add3_u32 v3, v3, v8, s55
	v_and_b32_e32 v5, 0xffff0000, v5
	v_and_b32_e32 v4, 0xffff0000, v4
	v_or_b32_sdwa v3, v5, v3 dst_sel:DWORD dst_unused:UNUSED_PAD src0_sel:DWORD src1_sel:WORD_1
	v_or_b32_sdwa v2, v4, v2 dst_sel:DWORD dst_unused:UNUSED_PAD src0_sel:DWORD src1_sel:WORD_1
	global_store_dwordx2 v[6:7], v[2:3], off offset:224
	global_load_dwordx4 v[2:5], v[186:187], off offset:480
	v_mov_b32_e32 v8, v14
	v_mov_b32_e32 v9, v16
	v_mov_b32_e32 v16, v15
	v_pk_mul_f32 v[8:9], v[8:9], v[0:1] op_sel_hi:[1,0]
	v_pk_mul_f32 v[10:11], v[16:17], v[0:1] op_sel_hi:[1,0]
	s_waitcnt vmcnt(0)
	v_mov_b32_e32 v12, v2
	v_mov_b32_e32 v13, v4
	v_mov_b32_e32 v4, v3
	v_pk_mul_f32 v[2:3], v[8:9], v[12:13]
	v_pk_mul_f32 v[4:5], v[10:11], v[4:5]
	v_and_b32_sdwa v0, v3, v228 dst_sel:DWORD dst_unused:UNUSED_PAD src0_sel:WORD_1 src1_sel:DWORD
	v_and_b32_sdwa v9, v5, v228 dst_sel:DWORD dst_unused:UNUSED_PAD src0_sel:WORD_1 src1_sel:DWORD
	v_and_b32_sdwa v10, v4, v228 dst_sel:DWORD dst_unused:UNUSED_PAD src0_sel:WORD_1 src1_sel:DWORD
	v_and_b32_sdwa v8, v2, v228 dst_sel:DWORD dst_unused:UNUSED_PAD src0_sel:WORD_1 src1_sel:DWORD
	v_add3_u32 v0, v3, v0, s55
	v_add3_u32 v3, v5, v9, s55
	v_add3_u32 v4, v4, v10, s55
	v_add3_u32 v2, v2, v8, s55
	v_and_b32_e32 v3, 0xffff0000, v3
	v_and_b32_e32 v4, 0xffff0000, v4
	v_or_b32_sdwa v3, v3, v0 dst_sel:DWORD dst_unused:UNUSED_PAD src0_sel:DWORD src1_sel:WORD_1
	v_or_b32_sdwa v2, v4, v2 dst_sel:DWORD dst_unused:UNUSED_PAD src0_sel:DWORD src1_sel:WORD_1
	global_store_dwordx2 v[6:7], v[2:3], off offset:240
	s_branch .LBB0_1000

.LBB0_1533:
	s_lshl_b32 s4, s49, 5
	s_lshl_b32 s8, s16, 8
	v_lshrrev_b32_e32 v0, 1, v166
	s_or_b32 s4, s8, s4
	v_and_or_b32 v220, v0, 24, s4
	s_lshl_b32 s29, s47, 8
	v_add_u32_e32 v118, s29, v240
	v_ashrrev_i32_e32 v221, 31, v220
	v_lshl_add_u64 v[120:121], v[220:221], 1, s[6:7]
	s_mov_b64 s[6:7], 0x4000000
	v_ashrrev_i32_e32 v119, 31, v118
	v_lshl_add_u64 v[120:121], v[120:121], 0, s[6:7]
	v_lshlrev_b64 v[224:225], 11, v[118:119]
	v_lshl_add_u64 v[126:127], v[120:121], 0, v[224:225]
	s_barrier
	global_load_dwordx4 v[206:209], v[126:127], off
	global_load_dwordx4 v[202:205], v[126:127], off offset:256
	v_or_b32_e32 v126, 16, v118
	v_ashrrev_i32_e32 v127, 31, v126
	v_lshlrev_b64 v[126:127], 11, v[126:127]
	v_lshl_add_u64 v[126:127], v[120:121], 0, v[126:127]
	global_load_dwordx4 v[198:201], v[126:127], off
	global_load_dwordx4 v[194:197], v[126:127], off offset:256
	v_or_b32_e32 v126, 32, v118
	v_ashrrev_i32_e32 v127, 31, v126
	v_lshlrev_b64 v[126:127], 11, v[126:127]
	v_lshl_add_u64 v[126:127], v[120:121], 0, v[126:127]
	global_load_dwordx4 v[190:193], v[126:127], off
	global_load_dwordx4 v[186:189], v[126:127], off offset:256
	v_or_b32_e32 v126, 48, v118
	v_ashrrev_i32_e32 v127, 31, v126
	v_lshlrev_b64 v[126:127], 11, v[126:127]
	v_lshl_add_u64 v[126:127], v[120:121], 0, v[126:127]
	global_load_dwordx4 v[174:177], v[126:127], off
	global_load_dwordx4 v[162:165], v[126:127], off offset:256
	v_add_u32_e32 v126, 0x80, v118
	v_ashrrev_i32_e32 v127, 31, v126
	v_lshlrev_b64 v[126:127], 11, v[126:127]
	v_lshl_add_u64 v[126:127], v[120:121], 0, v[126:127]
	global_load_dwordx4 v[158:161], v[126:127], off
	global_load_dwordx4 v[154:157], v[126:127], off offset:256
	v_add_u32_e32 v126, 0x90, v118
	v_ashrrev_i32_e32 v127, 31, v126
	v_lshlrev_b64 v[126:127], 11, v[126:127]
	v_lshl_add_u64 v[126:127], v[120:121], 0, v[126:127]
	global_load_dwordx4 v[150:153], v[126:127], off
	global_load_dwordx4 v[146:149], v[126:127], off offset:256
	v_add_u32_e32 v126, 0xa0, v118
	v_add_u32_e32 v118, 0xb0, v118
	v_ashrrev_i32_e32 v127, 31, v126
	v_ashrrev_i32_e32 v119, 31, v118
	v_lshlrev_b64 v[126:127], 11, v[126:127]
	v_lshlrev_b64 v[118:119], 11, v[118:119]
	v_lshl_add_u64 v[126:127], v[120:121], 0, v[126:127]
	v_lshl_add_u64 v[118:119], v[120:121], 0, v[118:119]
	global_load_dwordx4 v[142:145], v[126:127], off
	global_load_dwordx4 v[138:141], v[126:127], off offset:256
	s_nop 0
	global_load_dwordx4 v[126:129], v[118:119], off
	s_nop 0
	global_load_dwordx4 v[118:121], v[118:119], off offset:256
	v_and_b32_e32 v168, 64, v231
	v_xor_b32_e32 v0, 16, v231
	v_add_u32_e32 v168, 64, v168
	v_cmp_lt_i32_e32 vcc, v0, v168
	v_mul_f32_e32 v169, v137, v137
	v_fmac_f32_e32 v169, v136, v136
	v_cndmask_b32_e32 v0, v231, v0, vcc
	v_lshlrev_b32_e32 v241, 2, v0
	v_mul_f32_e32 v0, v135, v135
	v_fmac_f32_e32 v0, v134, v134
	v_add_f32_e32 v0, v0, v169
	v_mul_f32_e32 v169, v131, v131
	v_mul_f32_e32 v170, v133, v133
	v_fmac_f32_e32 v169, v130, v130
	v_fmac_f32_e32 v170, v132, v132
	v_add_f32_e32 v169, v169, v170
	v_add_f32_e32 v0, v169, v0
	v_mul_f32_e32 v169, v123, v123
	v_mul_f32_e32 v170, v125, v125
	v_fmac_f32_e32 v169, v122, v122
	v_fmac_f32_e32 v170, v124, v124
	v_add_f32_e32 v169, v169, v170
	v_add_f32_e32 v0, v169, v0
	v_mul_f32_e32 v169, v115, v115
	v_mul_f32_e32 v170, v117, v117
	v_fmac_f32_e32 v169, v114, v114
	v_fmac_f32_e32 v170, v116, v116
	v_add_f32_e32 v169, v169, v170
	v_add_f32_e32 v0, v169, v0
	v_mov_b32_e32 v169, v0
	s_nop 1
	v_permlane16_swap_b32_e32 v169, v0
	v_xor_b32_e32 v170, 32, v231
	v_cmp_lt_i32_e32 vcc, v170, v168
	s_lshl_b32 s4, s49, 2
	s_add_i32 s28, s4, 0
	v_cndmask_b32_e32 v168, v231, v170, vcc
	v_lshlrev_b32_e32 v242, 2, v168
	s_waitcnt lgkmcnt(0)
	v_add_f32_e32 v168, v0, v169
	v_mov_b32_e32 v169, v168
	s_nop 1
	v_permlane32_swap_b32_e32 v169, v168
	v_and_b32_e32 v0, 63, v166
	v_cmp_gt_u32_e64 s[40:41], 16, v0
	s_and_saveexec_b64 s[6:7], s[40:41]
	v_readlane_b32 s64, v252, 3
	v_readlane_b32 s65, v255, 10
	v_readlane_b32 s68, v255, 11
	s_cbranch_execz .LBB0_1535
	s_lshl_b32 s4, s46, 10
	s_add_i32 s4, s28, s4
	s_waitcnt lgkmcnt(0)
	v_add_f32_e32 v168, v168, v169
	v_lshl_add_u32 v169, v167, 4, s4
	ds_write_b32 v169, v168
.LBB0_1535:
	s_or_b64 exec, exec, s[6:7]
	v_mul_f32_e32 v168, v111, v111
	s_waitcnt lgkmcnt(0)
	v_mul_f32_e32 v169, v113, v113
	v_fmac_f32_e32 v168, v110, v110
	v_fmac_f32_e32 v169, v112, v112
	v_add_f32_e32 v168, v168, v169
	v_mul_f32_e32 v169, v107, v107
	v_mul_f32_e32 v170, v109, v109
	v_fmac_f32_e32 v169, v106, v106
	v_fmac_f32_e32 v170, v108, v108
	v_add_f32_e32 v169, v169, v170
	v_add_f32_e32 v168, v169, v168
	v_mul_f32_e32 v169, v103, v103
	v_mul_f32_e32 v170, v105, v105
	v_fmac_f32_e32 v169, v102, v102
	v_fmac_f32_e32 v170, v104, v104
	v_add_f32_e32 v169, v169, v170
	v_add_f32_e32 v168, v169, v168
	v_mul_f32_e32 v169, v99, v99
	v_mul_f32_e32 v170, v101, v101
	v_fmac_f32_e32 v169, v98, v98
	v_fmac_f32_e32 v170, v100, v100
	v_add_f32_e32 v169, v169, v170
	v_add_f32_e32 v168, v169, v168
	v_mov_b32_e32 v169, v168
	s_nop 1
	v_permlane16_swap_b32_e32 v169, v168
	s_waitcnt lgkmcnt(0)
	v_add_f32_e32 v168, v168, v169
	v_mov_b32_e32 v169, v168
	s_nop 1
	v_permlane32_swap_b32_e32 v169, v168
	s_and_saveexec_b64 s[6:7], s[40:41]
	s_cbranch_execz .LBB0_1537
	s_lshl_b32 s4, s46, 10
	s_add_i32 s4, s28, s4
	s_waitcnt lgkmcnt(0)
	v_add_f32_e32 v168, v168, v169
	v_lshl_add_u32 v169, v167, 4, s4
	ds_write_b32 v169, v168 offset:256
.LBB0_1537:
	s_or_b64 exec, exec, s[6:7]
	v_mul_f32_e32 v168, v95, v95
	s_waitcnt lgkmcnt(0)
	v_mul_f32_e32 v169, v97, v97
	v_fmac_f32_e32 v168, v94, v94
	v_fmac_f32_e32 v169, v96, v96
	v_add_f32_e32 v168, v168, v169
	v_mul_f32_e32 v169, v91, v91
	v_mul_f32_e32 v170, v93, v93
	v_fmac_f32_e32 v169, v90, v90
	v_fmac_f32_e32 v170, v92, v92
	v_add_f32_e32 v169, v169, v170
	v_add_f32_e32 v168, v169, v168
	v_mul_f32_e32 v169, v87, v87
	v_mul_f32_e32 v170, v89, v89
	v_fmac_f32_e32 v169, v86, v86
	v_fmac_f32_e32 v170, v88, v88
	v_add_f32_e32 v169, v169, v170
	v_add_f32_e32 v168, v169, v168
	v_mul_f32_e32 v169, v83, v83
	v_mul_f32_e32 v170, v85, v85
	v_fmac_f32_e32 v169, v82, v82
	v_fmac_f32_e32 v170, v84, v84
	v_add_f32_e32 v169, v169, v170
	v_add_f32_e32 v168, v169, v168
	v_mov_b32_e32 v169, v168
	s_nop 1
	v_permlane16_swap_b32_e32 v169, v168
	s_waitcnt lgkmcnt(0)
	v_add_f32_e32 v168, v168, v169
	v_mov_b32_e32 v169, v168
	s_nop 1
	v_permlane32_swap_b32_e32 v169, v168
	s_and_saveexec_b64 s[6:7], s[40:41]
	s_cbranch_execz .LBB0_1539
	s_lshl_b32 s4, s46, 10
	s_add_i32 s4, s28, s4
	s_waitcnt lgkmcnt(0)
	v_add_f32_e32 v168, v168, v169
	v_lshl_add_u32 v169, v167, 4, s4
	ds_write_b32 v169, v168 offset:512
.LBB0_1539:
	s_or_b64 exec, exec, s[6:7]
	v_mul_f32_e32 v168, v79, v79
	s_waitcnt lgkmcnt(0)
	v_mul_f32_e32 v169, v81, v81
	v_fmac_f32_e32 v168, v78, v78
	v_fmac_f32_e32 v169, v80, v80
	v_add_f32_e32 v168, v168, v169
	v_mul_f32_e32 v169, v75, v75
	v_mul_f32_e32 v170, v77, v77
	v_fmac_f32_e32 v169, v74, v74
	v_fmac_f32_e32 v170, v76, v76
	v_add_f32_e32 v169, v169, v170
	v_add_f32_e32 v168, v169, v168
	v_mul_f32_e32 v169, v71, v71
	v_mul_f32_e32 v170, v73, v73
	v_fmac_f32_e32 v169, v70, v70
	v_fmac_f32_e32 v170, v72, v72
	v_add_f32_e32 v169, v169, v170
	v_add_f32_e32 v168, v169, v168
	v_mul_f32_e32 v169, v67, v67
	v_mul_f32_e32 v170, v69, v69
	v_fmac_f32_e32 v169, v66, v66
	v_fmac_f32_e32 v170, v68, v68
	v_add_f32_e32 v169, v169, v170
	v_add_f32_e32 v168, v169, v168
	v_mov_b32_e32 v169, v168
	s_nop 1
	v_permlane16_swap_b32_e32 v169, v168
	s_waitcnt lgkmcnt(0)
	v_add_f32_e32 v168, v168, v169
	v_mov_b32_e32 v169, v168
	s_nop 1
	v_permlane32_swap_b32_e32 v169, v168
	s_and_saveexec_b64 s[6:7], s[40:41]
	s_cbranch_execz .LBB0_1541
	s_lshl_b32 s4, s46, 10
	s_add_i32 s4, s28, s4
	s_waitcnt lgkmcnt(0)
	v_add_f32_e32 v168, v168, v169
	v_lshl_add_u32 v169, v167, 4, s4
	ds_write_b32 v169, v168 offset:768
.LBB0_1541:
	s_or_b64 exec, exec, s[6:7]
	v_mul_f32_e32 v168, v63, v63
	s_waitcnt lgkmcnt(0)
	v_mul_f32_e32 v169, v65, v65
	v_fmac_f32_e32 v168, v62, v62
	v_fmac_f32_e32 v169, v64, v64
	v_add_f32_e32 v168, v168, v169
	v_mul_f32_e32 v169, v59, v59
	v_mul_f32_e32 v170, v61, v61
	v_fmac_f32_e32 v169, v58, v58
	v_fmac_f32_e32 v170, v60, v60
	v_add_f32_e32 v169, v169, v170
	v_add_f32_e32 v168, v169, v168
	v_mul_f32_e32 v169, v55, v55
	v_mul_f32_e32 v170, v57, v57
	v_fmac_f32_e32 v169, v54, v54
	v_fmac_f32_e32 v170, v56, v56
	v_add_f32_e32 v169, v169, v170
	v_add_f32_e32 v168, v169, v168
	v_mul_f32_e32 v169, v51, v51
	v_mul_f32_e32 v170, v53, v53
	v_fmac_f32_e32 v169, v50, v50
	v_fmac_f32_e32 v170, v52, v52
	v_add_f32_e32 v169, v169, v170
	v_add_f32_e32 v168, v169, v168
	v_mov_b32_e32 v169, v168
	s_nop 1
	v_permlane16_swap_b32_e32 v169, v168
	s_waitcnt lgkmcnt(0)
	v_add_f32_e32 v168, v168, v169
	v_mov_b32_e32 v169, v168
	s_nop 1
	v_permlane32_swap_b32_e32 v169, v168
	s_and_saveexec_b64 s[6:7], s[40:41]
	s_cbranch_execz .LBB0_1543
	s_lshl_b32 s4, s46, 10
	s_add_i32 s4, s28, s4
	s_waitcnt lgkmcnt(0)
	v_add_f32_e32 v168, v168, v169
	v_lshl_add_u32 v169, v167, 4, s4
	ds_write_b32 v169, v168 offset:2048
.LBB0_1543:
	s_or_b64 exec, exec, s[6:7]
	v_mul_f32_e32 v168, v47, v47
	s_waitcnt lgkmcnt(0)
	v_mul_f32_e32 v169, v49, v49
	v_fmac_f32_e32 v168, v46, v46
	v_fmac_f32_e32 v169, v48, v48
	v_add_f32_e32 v168, v168, v169
	v_mul_f32_e32 v169, v43, v43
	v_mul_f32_e32 v170, v45, v45
	v_fmac_f32_e32 v169, v42, v42
	v_fmac_f32_e32 v170, v44, v44
	v_add_f32_e32 v169, v169, v170
	v_add_f32_e32 v168, v169, v168
	v_mul_f32_e32 v169, v39, v39
	v_mul_f32_e32 v170, v41, v41
	v_fmac_f32_e32 v169, v38, v38
	v_fmac_f32_e32 v170, v40, v40
	v_add_f32_e32 v169, v169, v170
	v_add_f32_e32 v168, v169, v168
	v_mul_f32_e32 v169, v35, v35
	v_mul_f32_e32 v170, v37, v37
	v_fmac_f32_e32 v169, v34, v34
	v_fmac_f32_e32 v170, v36, v36
	v_add_f32_e32 v169, v169, v170
	v_add_f32_e32 v168, v169, v168
	v_mov_b32_e32 v169, v168
	s_nop 1
	v_permlane16_swap_b32_e32 v169, v168
	s_waitcnt lgkmcnt(0)
	v_add_f32_e32 v168, v168, v169
	v_mov_b32_e32 v169, v168
	s_nop 1
	v_permlane32_swap_b32_e32 v169, v168
	s_and_saveexec_b64 s[6:7], s[40:41]
	s_cbranch_execz .LBB0_1545
	s_lshl_b32 s4, s46, 10
	s_add_i32 s4, s28, s4
	s_waitcnt lgkmcnt(0)
	v_add_f32_e32 v168, v168, v169
	v_lshl_add_u32 v169, v167, 4, s4
	ds_write_b32 v169, v168 offset:2304
.LBB0_1545:
	s_or_b64 exec, exec, s[6:7]
	v_mul_f32_e32 v168, v31, v31
	s_waitcnt lgkmcnt(0)
	v_mul_f32_e32 v169, v33, v33
	v_fmac_f32_e32 v168, v30, v30
	v_fmac_f32_e32 v169, v32, v32
	v_add_f32_e32 v168, v168, v169
	v_mul_f32_e32 v169, v27, v27
	v_mul_f32_e32 v170, v29, v29
	v_fmac_f32_e32 v169, v26, v26
	v_fmac_f32_e32 v170, v28, v28
	v_add_f32_e32 v169, v169, v170
	v_add_f32_e32 v168, v169, v168
	v_mul_f32_e32 v169, v23, v23
	v_mul_f32_e32 v170, v25, v25
	v_fmac_f32_e32 v169, v22, v22
	v_fmac_f32_e32 v170, v24, v24
	v_add_f32_e32 v169, v169, v170
	v_add_f32_e32 v168, v169, v168
	v_mul_f32_e32 v169, v19, v19
	v_mul_f32_e32 v170, v21, v21
	v_fmac_f32_e32 v169, v18, v18
	v_fmac_f32_e32 v170, v20, v20
	v_add_f32_e32 v169, v169, v170
	v_add_f32_e32 v168, v169, v168
	v_mov_b32_e32 v169, v168
	s_nop 1
	v_permlane16_swap_b32_e32 v169, v168
	s_waitcnt lgkmcnt(0)
	v_add_f32_e32 v168, v168, v169
	v_mov_b32_e32 v169, v168
	s_nop 1
	v_permlane32_swap_b32_e32 v169, v168
	s_and_saveexec_b64 s[6:7], s[40:41]
	s_cbranch_execz .LBB0_1547
	s_lshl_b32 s4, s46, 10
	s_add_i32 s4, s28, s4
	s_waitcnt lgkmcnt(0)
	v_add_f32_e32 v168, v168, v169
	v_lshl_add_u32 v169, v167, 4, s4
	ds_write_b32 v169, v168 offset:2560
.LBB0_1547:
	s_or_b64 exec, exec, s[6:7]
	v_mul_f32_e32 v168, v15, v15
	s_waitcnt lgkmcnt(0)
	v_mul_f32_e32 v169, v17, v17
	v_fmac_f32_e32 v168, v14, v14
	v_fmac_f32_e32 v169, v16, v16
	v_add_f32_e32 v168, v168, v169
	v_mul_f32_e32 v169, v11, v11
	v_mul_f32_e32 v170, v13, v13
	v_fmac_f32_e32 v169, v10, v10
	v_fmac_f32_e32 v170, v12, v12
	v_add_f32_e32 v169, v169, v170
	v_add_f32_e32 v168, v169, v168
	v_mul_f32_e32 v169, v7, v7
	v_mul_f32_e32 v170, v9, v9
	v_fmac_f32_e32 v169, v6, v6
	v_fmac_f32_e32 v170, v8, v8
	v_add_f32_e32 v169, v169, v170
	v_add_f32_e32 v168, v169, v168
	v_mul_f32_e32 v169, v3, v3
	v_mul_f32_e32 v170, v5, v5
	v_fmac_f32_e32 v169, v2, v2
	v_fmac_f32_e32 v170, v4, v4
	v_add_f32_e32 v169, v169, v170
	v_add_f32_e32 v168, v169, v168
	v_mov_b32_e32 v169, v168
	s_nop 1
	v_permlane16_swap_b32_e32 v169, v168
	s_waitcnt lgkmcnt(0)
	v_add_f32_e32 v168, v168, v169
	v_mov_b32_e32 v169, v168
	s_nop 1
	v_permlane32_swap_b32_e32 v169, v168
	s_and_saveexec_b64 s[6:7], s[40:41]
	s_cbranch_execz .LBB0_1549
	s_lshl_b32 s4, s46, 10
	s_add_i32 s4, s28, s4
	s_waitcnt lgkmcnt(0)
	v_add_f32_e32 v168, v168, v169
	v_lshl_add_u32 v167, v167, 4, s4
	ds_write_b32 v167, v168 offset:2816

.LBB0_1575:
	s_waitcnt vmcnt(0)
	v_lshlrev_b32_e32 v216, 16, v206
	v_and_b32_e32 v217, 0xffff0000, v206
	v_lshlrev_b32_e32 v206, 16, v207
	v_and_b32_e32 v207, 0xffff0000, v207
	s_waitcnt lgkmcnt(0)
	v_pk_mul_f32 v[136:137], v[136:137], v[0:1] op_sel_hi:[1,0]
	v_pk_mul_f32 v[134:135], v[134:135], v[0:1] op_sel_hi:[1,0]
	v_lshlrev_b32_e32 v218, 16, v208
	v_and_b32_e32 v219, 0xffff0000, v208
	v_lshlrev_b32_e32 v208, 16, v209
	v_and_b32_e32 v209, 0xffff0000, v209
	v_pk_fma_f32 v[136:137], v[184:185], v[136:137], v[206:207]
	v_pk_fma_f32 v[134:135], v[182:183], v[134:135], v[216:217]
	v_pk_mul_f32 v[132:133], v[132:133], v[0:1] op_sel_hi:[1,0]
	v_pk_mul_f32 v[130:131], v[130:131], v[0:1] op_sel_hi:[1,0]
	v_pk_fma_f32 v[206:207], v[180:181], v[132:133], v[208:209]
	v_pk_fma_f32 v[132:133], v[178:179], v[130:131], v[218:219]
	v_mul_f32_e32 v130, v135, v135
	v_mul_f32_e32 v131, v137, v137
	v_fmac_f32_e32 v130, v134, v134
	v_fmac_f32_e32 v131, v136, v136
	v_add_f32_e32 v130, v130, v131
	v_mul_f32_e32 v131, v133, v133
	v_mul_f32_e32 v208, v207, v207
	v_fmac_f32_e32 v131, v132, v132
	v_fmac_f32_e32 v208, v206, v206
	v_add_f32_e32 v131, v131, v208
	v_add_f32_e32 v208, v130, v131
	v_cvt_pk_bf16_f32 v130, v134, v135
	v_cvt_pk_bf16_f32 v131, v136, v137
	v_lshlrev_b32_e32 v134, 16, v202
	v_and_b32_e32 v135, 0xffff0000, v202
	v_lshlrev_b32_e32 v136, 16, v203
	v_and_b32_e32 v137, 0xffff0000, v203
	v_pk_mul_f32 v[124:125], v[124:125], v[0:1] op_sel_hi:[1,0]
	v_pk_mul_f32 v[122:123], v[122:123], v[0:1] op_sel_hi:[1,0]
	v_lshlrev_b32_e32 v202, 16, v204
	v_and_b32_e32 v203, 0xffff0000, v204
	v_pk_fma_f32 v[124:125], v[172:173], v[124:125], v[136:137]
	v_pk_fma_f32 v[122:123], v[170:171], v[122:123], v[134:135]
	v_pk_mul_f32 v[114:115], v[114:115], v[0:1] op_sel_hi:[1,0]
	v_lshlrev_b32_e32 v204, 16, v205
	v_and_b32_e32 v205, 0xffff0000, v205
	v_pk_mul_f32 v[116:117], v[116:117], v[0:1] op_sel_hi:[1,0]
	v_pk_fma_f32 v[134:135], v[166:167], v[114:115], v[202:203]
	v_mul_f32_e32 v0, v123, v123
	v_mul_f32_e32 v114, v125, v125
	v_pk_fma_f32 v[116:117], v[168:169], v[116:117], v[204:205]
	v_fmac_f32_e32 v0, v122, v122
	v_fmac_f32_e32 v114, v124, v124
	v_add_f32_e32 v0, v0, v114
	v_mul_f32_e32 v114, v135, v135
	v_mul_f32_e32 v115, v117, v117
	v_fmac_f32_e32 v114, v134, v134
	v_fmac_f32_e32 v115, v116, v116
	v_add_f32_e32 v114, v114, v115
	v_add_f32_e32 v0, v0, v114
	v_add_f32_e32 v0, v208, v0
	v_mov_b32_e32 v202, v0
	s_nop 1
	v_permlane16_swap_b32_e32 v202, v0
	s_add_u32 s6, s18, 0x4000000
	s_addc_u32 s7, s19, 0
	v_lshl_add_u64 v[114:115], s[6:7], 0, v[224:225]
	v_lshl_add_u64 v[136:137], v[220:221], 1, v[114:115]
	s_waitcnt lgkmcnt(0)
	v_add_f32_e32 v0, v0, v202
	v_mov_b32_e32 v114, v0
	s_nop 1
	v_permlane32_swap_b32_e32 v114, v0
	v_cvt_pk_bf16_f32 v132, v132, v133
	v_cvt_pk_bf16_f32 v133, v206, v207
	global_store_dwordx4 v[136:137], v[130:133], off
	v_cvt_pk_bf16_f32 v122, v122, v123
	v_cvt_pk_bf16_f32 v123, v124, v125
	v_cvt_pk_bf16_f32 v124, v134, v135
	v_cvt_pk_bf16_f32 v125, v116, v117
	global_store_dwordx4 v[136:137], v[122:125], off offset:256
	s_and_saveexec_b64 s[8:9], s[40:41]
	s_cbranch_execz .LBB0_1577
	v_lshl_add_u32 v115, v240, 4, s28
	s_waitcnt lgkmcnt(0)
	v_add_f32_e32 v0, v0, v114
	ds_write_b32 v115, v0 offset:6144

.LBB0_1579:
	v_lshlrev_b32_e32 v122, 16, v198
	v_and_b32_e32 v123, 0xffff0000, v198
	v_lshlrev_b32_e32 v124, 16, v199
	v_and_b32_e32 v125, 0xffff0000, v199
	s_waitcnt lgkmcnt(0)
	v_pk_mul_f32 v[112:113], v[112:113], v[0:1] op_sel_hi:[1,0]
	v_pk_mul_f32 v[110:111], v[110:111], v[0:1] op_sel_hi:[1,0]
	v_lshlrev_b32_e32 v130, 16, v200
	v_and_b32_e32 v131, 0xffff0000, v200
	v_lshlrev_b32_e32 v132, 16, v201
	v_and_b32_e32 v133, 0xffff0000, v201
	v_pk_fma_f32 v[112:113], v[184:185], v[112:113], v[124:125]
	v_pk_fma_f32 v[110:111], v[182:183], v[110:111], v[122:123]
	v_pk_mul_f32 v[108:109], v[108:109], v[0:1] op_sel_hi:[1,0]
	v_pk_mul_f32 v[106:107], v[106:107], v[0:1] op_sel_hi:[1,0]
	v_pk_fma_f32 v[122:123], v[180:181], v[108:109], v[132:133]
	v_pk_fma_f32 v[108:109], v[178:179], v[106:107], v[130:131]
	v_mul_f32_e32 v106, v111, v111
	v_mul_f32_e32 v107, v113, v113
	v_fmac_f32_e32 v106, v110, v110
	v_fmac_f32_e32 v107, v112, v112
	v_add_f32_e32 v106, v106, v107
	v_mul_f32_e32 v107, v109, v109
	v_mul_f32_e32 v115, v123, v123
	v_fmac_f32_e32 v107, v108, v108
	v_fmac_f32_e32 v115, v122, v122
	v_add_f32_e32 v107, v107, v115
	v_add_f32_e32 v115, v106, v107
	v_cvt_pk_bf16_f32 v106, v110, v111
	v_cvt_pk_bf16_f32 v107, v112, v113
	v_lshlrev_b32_e32 v110, 16, v194
	v_and_b32_e32 v111, 0xffff0000, v194
	v_lshlrev_b32_e32 v112, 16, v195
	v_and_b32_e32 v113, 0xffff0000, v195
	v_pk_mul_f32 v[104:105], v[104:105], v[0:1] op_sel_hi:[1,0]
	v_pk_mul_f32 v[102:103], v[102:103], v[0:1] op_sel_hi:[1,0]
	v_cvt_pk_bf16_f32 v108, v108, v109
	v_cvt_pk_bf16_f32 v109, v122, v123
	v_lshlrev_b32_e32 v122, 16, v196
	v_and_b32_e32 v123, 0xffff0000, v196
	v_pk_fma_f32 v[104:105], v[172:173], v[104:105], v[112:113]
	v_pk_fma_f32 v[102:103], v[170:171], v[102:103], v[110:111]
	v_pk_mul_f32 v[98:99], v[98:99], v[0:1] op_sel_hi:[1,0]
	v_lshlrev_b32_e32 v124, 16, v197
	v_and_b32_e32 v125, 0xffff0000, v197
	v_pk_mul_f32 v[100:101], v[100:101], v[0:1] op_sel_hi:[1,0]
	v_pk_fma_f32 v[112:113], v[166:167], v[98:99], v[122:123]
	v_mul_f32_e32 v0, v103, v103
	v_mul_f32_e32 v98, v105, v105
	v_pk_fma_f32 v[110:111], v[168:169], v[100:101], v[124:125]
	v_fmac_f32_e32 v0, v102, v102
	v_fmac_f32_e32 v98, v104, v104
	v_add_f32_e32 v0, v0, v98
	v_mul_f32_e32 v98, v113, v113
	v_mul_f32_e32 v99, v111, v111
	v_fmac_f32_e32 v98, v112, v112
	v_fmac_f32_e32 v99, v110, v110
	v_add_f32_e32 v98, v98, v99
	v_add_f32_e32 v0, v0, v98
	v_add_f32_e32 v0, v115, v0
	v_mov_b32_e32 v101, v0
	s_nop 1
	v_permlane16_swap_b32_e32 v101, v0
	v_or_b32_e32 v114, 16, v240
	v_add_u32_e32 v116, s29, v114
	v_ashrrev_i32_e32 v117, 31, v116
	v_lshlrev_b64 v[116:117], 11, v[116:117]
	v_lshl_add_u64 v[98:99], s[6:7], 0, v[116:117]
	s_waitcnt lgkmcnt(0)
	v_add_f32_e32 v0, v0, v101
	v_lshl_add_u64 v[116:117], v[220:221], 1, v[98:99]
	v_mov_b32_e32 v98, v0
	s_nop 1
	v_permlane32_swap_b32_e32 v98, v0
	global_store_dwordx4 v[116:117], v[106:109], off
	v_cvt_pk_bf16_f32 v100, v102, v103
	v_cvt_pk_bf16_f32 v101, v104, v105
	v_cvt_pk_bf16_f32 v102, v112, v113
	v_cvt_pk_bf16_f32 v103, v110, v111
	global_store_dwordx4 v[116:117], v[100:103], off offset:256
	s_and_saveexec_b64 s[8:9], s[40:41]
	s_cbranch_execz .LBB0_1581
	v_lshl_add_u32 v99, v114, 4, s28
	s_waitcnt lgkmcnt(0)
	v_add_f32_e32 v0, v0, v98
	ds_write_b32 v99, v0 offset:6144

.LBB0_1583:
	v_lshlrev_b32_e32 v102, 16, v190
	v_and_b32_e32 v103, 0xffff0000, v190
	v_lshlrev_b32_e32 v104, 16, v191
	v_and_b32_e32 v105, 0xffff0000, v191
	s_waitcnt lgkmcnt(0)
	v_pk_mul_f32 v[96:97], v[96:97], v[0:1] op_sel_hi:[1,0]
	v_pk_mul_f32 v[94:95], v[94:95], v[0:1] op_sel_hi:[1,0]
	v_lshlrev_b32_e32 v106, 16, v192
	v_and_b32_e32 v107, 0xffff0000, v192
	v_lshlrev_b32_e32 v108, 16, v193
	v_and_b32_e32 v109, 0xffff0000, v193
	v_pk_fma_f32 v[96:97], v[184:185], v[96:97], v[104:105]
	v_pk_fma_f32 v[94:95], v[182:183], v[94:95], v[102:103]
	v_pk_mul_f32 v[92:93], v[92:93], v[0:1] op_sel_hi:[1,0]
	v_pk_mul_f32 v[90:91], v[90:91], v[0:1] op_sel_hi:[1,0]
	v_pk_fma_f32 v[102:103], v[180:181], v[92:93], v[108:109]
	v_pk_fma_f32 v[92:93], v[178:179], v[90:91], v[106:107]
	v_mul_f32_e32 v90, v95, v95
	v_mul_f32_e32 v91, v97, v97
	v_fmac_f32_e32 v90, v94, v94
	v_fmac_f32_e32 v91, v96, v96
	v_add_f32_e32 v90, v90, v91
	v_mul_f32_e32 v91, v93, v93
	v_mul_f32_e32 v99, v103, v103
	v_fmac_f32_e32 v91, v92, v92
	v_fmac_f32_e32 v99, v102, v102
	v_add_f32_e32 v91, v91, v99
	v_add_f32_e32 v99, v90, v91
	v_cvt_pk_bf16_f32 v90, v94, v95
	v_cvt_pk_bf16_f32 v91, v96, v97
	v_lshlrev_b32_e32 v94, 16, v186
	v_and_b32_e32 v95, 0xffff0000, v186
	v_lshlrev_b32_e32 v96, 16, v187
	v_and_b32_e32 v97, 0xffff0000, v187
	v_pk_mul_f32 v[88:89], v[88:89], v[0:1] op_sel_hi:[1,0]
	v_pk_mul_f32 v[86:87], v[86:87], v[0:1] op_sel_hi:[1,0]
	v_cvt_pk_bf16_f32 v92, v92, v93
	v_cvt_pk_bf16_f32 v93, v102, v103
	v_lshlrev_b32_e32 v102, 16, v188
	v_and_b32_e32 v103, 0xffff0000, v188
	v_pk_fma_f32 v[88:89], v[172:173], v[88:89], v[96:97]
	v_pk_fma_f32 v[86:87], v[170:171], v[86:87], v[94:95]
	v_pk_mul_f32 v[82:83], v[82:83], v[0:1] op_sel_hi:[1,0]
	v_lshlrev_b32_e32 v104, 16, v189
	v_and_b32_e32 v105, 0xffff0000, v189
	v_pk_mul_f32 v[84:85], v[84:85], v[0:1] op_sel_hi:[1,0]
	v_pk_fma_f32 v[96:97], v[166:167], v[82:83], v[102:103]
	v_mul_f32_e32 v0, v87, v87
	v_mul_f32_e32 v82, v89, v89
	v_pk_fma_f32 v[94:95], v[168:169], v[84:85], v[104:105]
	v_fmac_f32_e32 v0, v86, v86
	v_fmac_f32_e32 v82, v88, v88
	v_add_f32_e32 v0, v0, v82
	v_mul_f32_e32 v82, v97, v97
	v_mul_f32_e32 v83, v95, v95
	v_fmac_f32_e32 v82, v96, v96
	v_fmac_f32_e32 v83, v94, v94
	v_add_f32_e32 v82, v82, v83
	v_add_f32_e32 v0, v0, v82
	v_add_f32_e32 v0, v99, v0
	v_mov_b32_e32 v85, v0
	s_nop 1
	v_permlane16_swap_b32_e32 v85, v0
	v_or_b32_e32 v98, 32, v240
	v_add_u32_e32 v100, s29, v98
	v_ashrrev_i32_e32 v101, 31, v100
	v_lshlrev_b64 v[100:101], 11, v[100:101]
	v_lshl_add_u64 v[82:83], s[6:7], 0, v[100:101]
	s_waitcnt lgkmcnt(0)
	v_add_f32_e32 v0, v0, v85
	v_lshl_add_u64 v[100:101], v[220:221], 1, v[82:83]
	v_mov_b32_e32 v82, v0
	s_nop 1
	v_permlane32_swap_b32_e32 v82, v0
	global_store_dwordx4 v[100:101], v[90:93], off
	v_cvt_pk_bf16_f32 v84, v86, v87
	v_cvt_pk_bf16_f32 v85, v88, v89
	v_cvt_pk_bf16_f32 v86, v96, v97
	v_cvt_pk_bf16_f32 v87, v94, v95
	global_store_dwordx4 v[100:101], v[84:87], off offset:256
	s_and_saveexec_b64 s[8:9], s[40:41]
	s_cbranch_execz .LBB0_1585
	v_lshl_add_u32 v83, v98, 4, s28
	s_waitcnt lgkmcnt(0)
	v_add_f32_e32 v0, v0, v82
	ds_write_b32 v83, v0 offset:6144

.LBB0_1587:
	v_lshlrev_b32_e32 v86, 16, v174
	v_and_b32_e32 v87, 0xffff0000, v174
	v_lshlrev_b32_e32 v88, 16, v175
	v_and_b32_e32 v89, 0xffff0000, v175
	s_waitcnt lgkmcnt(0)
	v_pk_mul_f32 v[80:81], v[80:81], v[0:1] op_sel_hi:[1,0]
	v_pk_mul_f32 v[78:79], v[78:79], v[0:1] op_sel_hi:[1,0]
	v_lshlrev_b32_e32 v90, 16, v176
	v_and_b32_e32 v91, 0xffff0000, v176
	v_lshlrev_b32_e32 v92, 16, v177
	v_and_b32_e32 v93, 0xffff0000, v177
	v_pk_fma_f32 v[80:81], v[184:185], v[80:81], v[88:89]
	v_pk_fma_f32 v[78:79], v[182:183], v[78:79], v[86:87]
	v_pk_mul_f32 v[76:77], v[76:77], v[0:1] op_sel_hi:[1,0]
	v_pk_mul_f32 v[74:75], v[74:75], v[0:1] op_sel_hi:[1,0]
	v_pk_fma_f32 v[86:87], v[180:181], v[76:77], v[92:93]
	v_pk_fma_f32 v[76:77], v[178:179], v[74:75], v[90:91]
	v_mul_f32_e32 v74, v79, v79
	v_mul_f32_e32 v75, v81, v81
	v_fmac_f32_e32 v74, v78, v78
	v_fmac_f32_e32 v75, v80, v80
	v_add_f32_e32 v74, v74, v75
	v_mul_f32_e32 v75, v77, v77
	v_mul_f32_e32 v83, v87, v87
	v_fmac_f32_e32 v75, v76, v76
	v_fmac_f32_e32 v83, v86, v86
	v_add_f32_e32 v75, v75, v83
	v_add_f32_e32 v83, v74, v75
	v_cvt_pk_bf16_f32 v74, v78, v79
	v_cvt_pk_bf16_f32 v75, v80, v81
	v_lshlrev_b32_e32 v78, 16, v162
	v_and_b32_e32 v79, 0xffff0000, v162
	v_lshlrev_b32_e32 v80, 16, v163
	v_and_b32_e32 v81, 0xffff0000, v163
	v_pk_mul_f32 v[72:73], v[72:73], v[0:1] op_sel_hi:[1,0]
	v_pk_mul_f32 v[70:71], v[70:71], v[0:1] op_sel_hi:[1,0]
	v_cvt_pk_bf16_f32 v76, v76, v77
	v_cvt_pk_bf16_f32 v77, v86, v87
	v_lshlrev_b32_e32 v86, 16, v164
	v_and_b32_e32 v87, 0xffff0000, v164
	v_pk_fma_f32 v[72:73], v[172:173], v[72:73], v[80:81]
	v_pk_fma_f32 v[70:71], v[170:171], v[70:71], v[78:79]
	v_pk_mul_f32 v[66:67], v[66:67], v[0:1] op_sel_hi:[1,0]
	v_lshlrev_b32_e32 v88, 16, v165
	v_and_b32_e32 v89, 0xffff0000, v165
	v_pk_mul_f32 v[68:69], v[68:69], v[0:1] op_sel_hi:[1,0]
	v_pk_fma_f32 v[80:81], v[166:167], v[66:67], v[86:87]
	v_mul_f32_e32 v0, v71, v71
	v_mul_f32_e32 v66, v73, v73
	v_pk_fma_f32 v[78:79], v[168:169], v[68:69], v[88:89]
	v_fmac_f32_e32 v0, v70, v70
	v_fmac_f32_e32 v66, v72, v72
	v_add_f32_e32 v0, v0, v66
	v_mul_f32_e32 v66, v81, v81
	v_mul_f32_e32 v67, v79, v79
	v_fmac_f32_e32 v66, v80, v80
	v_fmac_f32_e32 v67, v78, v78
	v_add_f32_e32 v66, v66, v67
	v_add_f32_e32 v0, v0, v66
	v_add_f32_e32 v0, v83, v0
	v_mov_b32_e32 v69, v0
	s_nop 1
	v_permlane16_swap_b32_e32 v69, v0
	v_or_b32_e32 v82, 48, v240
	v_add_u32_e32 v84, s29, v82
	v_ashrrev_i32_e32 v85, 31, v84
	v_lshlrev_b64 v[84:85], 11, v[84:85]
	v_lshl_add_u64 v[66:67], s[6:7], 0, v[84:85]
	s_waitcnt lgkmcnt(0)
	v_add_f32_e32 v0, v0, v69
	v_lshl_add_u64 v[84:85], v[220:221], 1, v[66:67]
	v_mov_b32_e32 v66, v0
	s_nop 1
	v_permlane32_swap_b32_e32 v66, v0
	global_store_dwordx4 v[84:85], v[74:77], off
	v_cvt_pk_bf16_f32 v68, v70, v71
	v_cvt_pk_bf16_f32 v69, v72, v73
	v_cvt_pk_bf16_f32 v70, v80, v81
	v_cvt_pk_bf16_f32 v71, v78, v79
	global_store_dwordx4 v[84:85], v[68:71], off offset:256
	s_and_saveexec_b64 s[8:9], s[40:41]
	s_cbranch_execz .LBB0_1589
	v_lshl_add_u32 v67, v82, 4, s28
	s_waitcnt lgkmcnt(0)
	v_add_f32_e32 v0, v0, v66
	ds_write_b32 v67, v0 offset:6144

.LBB0_1591:
	v_lshlrev_b32_e32 v70, 16, v158
	v_and_b32_e32 v71, 0xffff0000, v158
	v_lshlrev_b32_e32 v72, 16, v159
	v_and_b32_e32 v73, 0xffff0000, v159
	s_waitcnt lgkmcnt(0)
	v_pk_mul_f32 v[64:65], v[64:65], v[0:1] op_sel_hi:[1,0]
	v_pk_mul_f32 v[62:63], v[62:63], v[0:1] op_sel_hi:[1,0]
	v_lshlrev_b32_e32 v74, 16, v160
	v_and_b32_e32 v75, 0xffff0000, v160
	v_lshlrev_b32_e32 v76, 16, v161
	v_and_b32_e32 v77, 0xffff0000, v161
	v_pk_fma_f32 v[64:65], v[184:185], v[64:65], v[72:73]
	v_pk_fma_f32 v[62:63], v[182:183], v[62:63], v[70:71]
	v_pk_mul_f32 v[60:61], v[60:61], v[0:1] op_sel_hi:[1,0]
	v_pk_mul_f32 v[58:59], v[58:59], v[0:1] op_sel_hi:[1,0]
	v_pk_fma_f32 v[70:71], v[180:181], v[60:61], v[76:77]
	v_pk_fma_f32 v[60:61], v[178:179], v[58:59], v[74:75]
	v_mul_f32_e32 v58, v63, v63
	v_mul_f32_e32 v59, v65, v65
	v_fmac_f32_e32 v58, v62, v62
	v_fmac_f32_e32 v59, v64, v64
	v_add_f32_e32 v58, v58, v59
	v_mul_f32_e32 v59, v61, v61
	v_mul_f32_e32 v67, v71, v71
	v_fmac_f32_e32 v59, v60, v60
	v_fmac_f32_e32 v67, v70, v70
	v_add_f32_e32 v59, v59, v67
	v_add_f32_e32 v67, v58, v59
	v_cvt_pk_bf16_f32 v58, v62, v63
	v_cvt_pk_bf16_f32 v59, v64, v65
	v_lshlrev_b32_e32 v62, 16, v154
	v_and_b32_e32 v63, 0xffff0000, v154
	v_lshlrev_b32_e32 v64, 16, v155
	v_and_b32_e32 v65, 0xffff0000, v155
	v_pk_mul_f32 v[56:57], v[56:57], v[0:1] op_sel_hi:[1,0]
	v_pk_mul_f32 v[54:55], v[54:55], v[0:1] op_sel_hi:[1,0]
	v_cvt_pk_bf16_f32 v60, v60, v61
	v_cvt_pk_bf16_f32 v61, v70, v71
	v_lshlrev_b32_e32 v70, 16, v156
	v_and_b32_e32 v71, 0xffff0000, v156
	v_pk_fma_f32 v[56:57], v[172:173], v[56:57], v[64:65]
	v_pk_fma_f32 v[54:55], v[170:171], v[54:55], v[62:63]
	v_pk_mul_f32 v[50:51], v[50:51], v[0:1] op_sel_hi:[1,0]
	v_lshlrev_b32_e32 v72, 16, v157
	v_and_b32_e32 v73, 0xffff0000, v157
	v_pk_mul_f32 v[52:53], v[52:53], v[0:1] op_sel_hi:[1,0]
	v_pk_fma_f32 v[64:65], v[166:167], v[50:51], v[70:71]
	v_mul_f32_e32 v0, v55, v55
	v_mul_f32_e32 v50, v57, v57
	v_pk_fma_f32 v[62:63], v[168:169], v[52:53], v[72:73]
	v_fmac_f32_e32 v0, v54, v54
	v_fmac_f32_e32 v50, v56, v56
	v_add_f32_e32 v0, v0, v50
	v_mul_f32_e32 v50, v65, v65
	v_mul_f32_e32 v51, v63, v63
	v_fmac_f32_e32 v50, v64, v64
	v_fmac_f32_e32 v51, v62, v62
	v_add_f32_e32 v50, v50, v51
	v_add_f32_e32 v0, v0, v50
	v_add_f32_e32 v0, v67, v0
	v_mov_b32_e32 v53, v0
	s_nop 1
	v_permlane16_swap_b32_e32 v53, v0
	v_add_u32_e32 v66, 0x80, v240
	v_add_u32_e32 v68, s29, v66
	v_ashrrev_i32_e32 v69, 31, v68
	v_lshlrev_b64 v[68:69], 11, v[68:69]
	v_lshl_add_u64 v[50:51], s[6:7], 0, v[68:69]
	s_waitcnt lgkmcnt(0)
	v_add_f32_e32 v0, v0, v53
	v_lshl_add_u64 v[68:69], v[220:221], 1, v[50:51]
	v_mov_b32_e32 v50, v0
	s_nop 1
	v_permlane32_swap_b32_e32 v50, v0
	global_store_dwordx4 v[68:69], v[58:61], off
	v_cvt_pk_bf16_f32 v52, v54, v55
	v_cvt_pk_bf16_f32 v53, v56, v57
	v_cvt_pk_bf16_f32 v54, v64, v65
	v_cvt_pk_bf16_f32 v55, v62, v63
	global_store_dwordx4 v[68:69], v[52:55], off offset:256
	s_and_saveexec_b64 s[8:9], s[40:41]
	s_cbranch_execz .LBB0_1593
	v_lshl_add_u32 v51, v66, 4, s28
	s_waitcnt lgkmcnt(0)
	v_add_f32_e32 v0, v0, v50
	ds_write_b32 v51, v0 offset:6144

.LBB0_1595:
	v_lshlrev_b32_e32 v54, 16, v150
	v_and_b32_e32 v55, 0xffff0000, v150
	v_lshlrev_b32_e32 v56, 16, v151
	v_and_b32_e32 v57, 0xffff0000, v151
	s_waitcnt lgkmcnt(0)
	v_pk_mul_f32 v[48:49], v[48:49], v[0:1] op_sel_hi:[1,0]
	v_pk_mul_f32 v[46:47], v[46:47], v[0:1] op_sel_hi:[1,0]
	v_lshlrev_b32_e32 v58, 16, v152
	v_and_b32_e32 v59, 0xffff0000, v152
	v_lshlrev_b32_e32 v60, 16, v153
	v_and_b32_e32 v61, 0xffff0000, v153
	v_pk_fma_f32 v[48:49], v[184:185], v[48:49], v[56:57]
	v_pk_fma_f32 v[46:47], v[182:183], v[46:47], v[54:55]
	v_pk_mul_f32 v[44:45], v[44:45], v[0:1] op_sel_hi:[1,0]
	v_pk_mul_f32 v[42:43], v[42:43], v[0:1] op_sel_hi:[1,0]
	v_pk_fma_f32 v[54:55], v[180:181], v[44:45], v[60:61]
	v_pk_fma_f32 v[44:45], v[178:179], v[42:43], v[58:59]
	v_mul_f32_e32 v42, v47, v47
	v_mul_f32_e32 v43, v49, v49
	v_fmac_f32_e32 v42, v46, v46
	v_fmac_f32_e32 v43, v48, v48
	v_add_f32_e32 v42, v42, v43
	v_mul_f32_e32 v43, v45, v45
	v_mul_f32_e32 v51, v55, v55
	v_fmac_f32_e32 v43, v44, v44
	v_fmac_f32_e32 v51, v54, v54
	v_add_f32_e32 v43, v43, v51
	v_add_f32_e32 v51, v42, v43
	v_cvt_pk_bf16_f32 v42, v46, v47
	v_cvt_pk_bf16_f32 v43, v48, v49
	v_lshlrev_b32_e32 v46, 16, v146
	v_and_b32_e32 v47, 0xffff0000, v146
	v_lshlrev_b32_e32 v48, 16, v147
	v_and_b32_e32 v49, 0xffff0000, v147
	v_pk_mul_f32 v[40:41], v[40:41], v[0:1] op_sel_hi:[1,0]
	v_pk_mul_f32 v[38:39], v[38:39], v[0:1] op_sel_hi:[1,0]
	v_cvt_pk_bf16_f32 v44, v44, v45
	v_cvt_pk_bf16_f32 v45, v54, v55
	v_lshlrev_b32_e32 v54, 16, v148
	v_and_b32_e32 v55, 0xffff0000, v148
	v_pk_fma_f32 v[40:41], v[172:173], v[40:41], v[48:49]
	v_pk_fma_f32 v[38:39], v[170:171], v[38:39], v[46:47]
	v_pk_mul_f32 v[34:35], v[34:35], v[0:1] op_sel_hi:[1,0]
	v_lshlrev_b32_e32 v56, 16, v149
	v_and_b32_e32 v57, 0xffff0000, v149
	v_pk_mul_f32 v[36:37], v[36:37], v[0:1] op_sel_hi:[1,0]
	v_pk_fma_f32 v[48:49], v[166:167], v[34:35], v[54:55]
	v_mul_f32_e32 v0, v39, v39
	v_mul_f32_e32 v34, v41, v41
	v_pk_fma_f32 v[46:47], v[168:169], v[36:37], v[56:57]
	v_fmac_f32_e32 v0, v38, v38
	v_fmac_f32_e32 v34, v40, v40
	v_add_f32_e32 v0, v0, v34
	v_mul_f32_e32 v34, v49, v49
	v_mul_f32_e32 v35, v47, v47
	v_fmac_f32_e32 v34, v48, v48
	v_fmac_f32_e32 v35, v46, v46
	v_add_f32_e32 v34, v34, v35
	v_add_f32_e32 v0, v0, v34
	v_add_f32_e32 v0, v51, v0
	v_mov_b32_e32 v37, v0
	s_nop 1
	v_permlane16_swap_b32_e32 v37, v0
	v_add_u32_e32 v50, 0x90, v240
	v_add_u32_e32 v52, s29, v50
	v_ashrrev_i32_e32 v53, 31, v52
	v_lshlrev_b64 v[52:53], 11, v[52:53]
	v_lshl_add_u64 v[34:35], s[6:7], 0, v[52:53]
	s_waitcnt lgkmcnt(0)
	v_add_f32_e32 v0, v0, v37
	v_lshl_add_u64 v[52:53], v[220:221], 1, v[34:35]
	v_mov_b32_e32 v34, v0
	s_nop 1
	v_permlane32_swap_b32_e32 v34, v0
	global_store_dwordx4 v[52:53], v[42:45], off
	v_cvt_pk_bf16_f32 v36, v38, v39
	v_cvt_pk_bf16_f32 v37, v40, v41
	v_cvt_pk_bf16_f32 v38, v48, v49
	v_cvt_pk_bf16_f32 v39, v46, v47
	global_store_dwordx4 v[52:53], v[36:39], off offset:256
	s_and_saveexec_b64 s[8:9], s[40:41]
	s_cbranch_execz .LBB0_1597
	v_lshl_add_u32 v35, v50, 4, s28
	s_waitcnt lgkmcnt(0)
	v_add_f32_e32 v0, v0, v34
	ds_write_b32 v35, v0 offset:6144

.LBB0_1599:
	v_lshlrev_b32_e32 v38, 16, v142
	v_and_b32_e32 v39, 0xffff0000, v142
	v_lshlrev_b32_e32 v40, 16, v143
	v_and_b32_e32 v41, 0xffff0000, v143
	s_waitcnt lgkmcnt(0)
	v_pk_mul_f32 v[32:33], v[32:33], v[0:1] op_sel_hi:[1,0]
	v_pk_mul_f32 v[30:31], v[30:31], v[0:1] op_sel_hi:[1,0]
	v_lshlrev_b32_e32 v42, 16, v144
	v_and_b32_e32 v43, 0xffff0000, v144
	v_lshlrev_b32_e32 v44, 16, v145
	v_and_b32_e32 v45, 0xffff0000, v145
	v_pk_fma_f32 v[32:33], v[184:185], v[32:33], v[40:41]
	v_pk_fma_f32 v[30:31], v[182:183], v[30:31], v[38:39]
	v_pk_mul_f32 v[28:29], v[28:29], v[0:1] op_sel_hi:[1,0]
	v_pk_mul_f32 v[26:27], v[26:27], v[0:1] op_sel_hi:[1,0]
	v_pk_fma_f32 v[38:39], v[180:181], v[28:29], v[44:45]
	v_pk_fma_f32 v[28:29], v[178:179], v[26:27], v[42:43]
	v_mul_f32_e32 v26, v31, v31
	v_mul_f32_e32 v27, v33, v33
	v_fmac_f32_e32 v26, v30, v30
	v_fmac_f32_e32 v27, v32, v32
	v_add_f32_e32 v26, v26, v27
	v_mul_f32_e32 v27, v29, v29
	v_mul_f32_e32 v35, v39, v39
	v_fmac_f32_e32 v27, v28, v28
	v_fmac_f32_e32 v35, v38, v38
	v_add_f32_e32 v27, v27, v35
	v_add_f32_e32 v35, v26, v27
	v_cvt_pk_bf16_f32 v26, v30, v31
	v_cvt_pk_bf16_f32 v27, v32, v33
	v_lshlrev_b32_e32 v30, 16, v138
	v_and_b32_e32 v31, 0xffff0000, v138
	v_lshlrev_b32_e32 v32, 16, v139
	v_and_b32_e32 v33, 0xffff0000, v139
	v_pk_mul_f32 v[24:25], v[24:25], v[0:1] op_sel_hi:[1,0]
	v_pk_mul_f32 v[22:23], v[22:23], v[0:1] op_sel_hi:[1,0]
	v_cvt_pk_bf16_f32 v28, v28, v29
	v_cvt_pk_bf16_f32 v29, v38, v39
	v_lshlrev_b32_e32 v38, 16, v140
	v_and_b32_e32 v39, 0xffff0000, v140
	v_pk_fma_f32 v[24:25], v[172:173], v[24:25], v[32:33]
	v_pk_fma_f32 v[22:23], v[170:171], v[22:23], v[30:31]
	v_pk_mul_f32 v[18:19], v[18:19], v[0:1] op_sel_hi:[1,0]
	v_lshlrev_b32_e32 v40, 16, v141
	v_and_b32_e32 v41, 0xffff0000, v141
	v_pk_mul_f32 v[20:21], v[20:21], v[0:1] op_sel_hi:[1,0]
	v_pk_fma_f32 v[32:33], v[166:167], v[18:19], v[38:39]
	v_mul_f32_e32 v0, v23, v23
	v_mul_f32_e32 v18, v25, v25
	v_pk_fma_f32 v[30:31], v[168:169], v[20:21], v[40:41]
	v_fmac_f32_e32 v0, v22, v22
	v_fmac_f32_e32 v18, v24, v24
	v_add_f32_e32 v0, v0, v18
	v_mul_f32_e32 v18, v33, v33
	v_mul_f32_e32 v19, v31, v31
	v_fmac_f32_e32 v18, v32, v32
	v_fmac_f32_e32 v19, v30, v30
	v_add_f32_e32 v18, v18, v19
	v_add_f32_e32 v0, v0, v18
	v_add_f32_e32 v0, v35, v0
	v_mov_b32_e32 v21, v0
	s_nop 1
	v_permlane16_swap_b32_e32 v21, v0
	v_add_u32_e32 v34, 0xa0, v240
	v_add_u32_e32 v36, s29, v34
	v_ashrrev_i32_e32 v37, 31, v36
	v_lshlrev_b64 v[36:37], 11, v[36:37]
	v_lshl_add_u64 v[18:19], s[6:7], 0, v[36:37]
	s_waitcnt lgkmcnt(0)
	v_add_f32_e32 v0, v0, v21
	v_lshl_add_u64 v[36:37], v[220:221], 1, v[18:19]
	v_mov_b32_e32 v18, v0
	s_nop 1
	v_permlane32_swap_b32_e32 v18, v0
	global_store_dwordx4 v[36:37], v[26:29], off
	v_cvt_pk_bf16_f32 v20, v22, v23
	v_cvt_pk_bf16_f32 v21, v24, v25
	v_cvt_pk_bf16_f32 v22, v32, v33
	v_cvt_pk_bf16_f32 v23, v30, v31
	global_store_dwordx4 v[36:37], v[20:23], off offset:256
	s_and_saveexec_b64 s[8:9], s[40:41]
	s_cbranch_execz .LBB0_1601
	v_lshl_add_u32 v19, v34, 4, s28
	s_waitcnt lgkmcnt(0)
	v_add_f32_e32 v0, v0, v18
	ds_write_b32 v19, v0 offset:6144

.LBB0_1603:
	v_lshlrev_b32_e32 v22, 16, v126
	v_and_b32_e32 v23, 0xffff0000, v126
	v_lshlrev_b32_e32 v24, 16, v127
	v_and_b32_e32 v25, 0xffff0000, v127
	s_waitcnt lgkmcnt(0)
	v_pk_mul_f32 v[16:17], v[16:17], v[0:1] op_sel_hi:[1,0]
	v_pk_mul_f32 v[14:15], v[14:15], v[0:1] op_sel_hi:[1,0]
	v_lshlrev_b32_e32 v26, 16, v128
	v_and_b32_e32 v27, 0xffff0000, v128
	v_lshlrev_b32_e32 v28, 16, v129
	v_and_b32_e32 v29, 0xffff0000, v129
	v_pk_fma_f32 v[16:17], v[184:185], v[16:17], v[24:25]
	v_pk_fma_f32 v[14:15], v[182:183], v[14:15], v[22:23]
	v_pk_mul_f32 v[12:13], v[12:13], v[0:1] op_sel_hi:[1,0]
	v_pk_mul_f32 v[10:11], v[10:11], v[0:1] op_sel_hi:[1,0]
	v_pk_fma_f32 v[22:23], v[180:181], v[12:13], v[28:29]
	v_pk_fma_f32 v[12:13], v[178:179], v[10:11], v[26:27]
	v_mul_f32_e32 v10, v15, v15
	v_mul_f32_e32 v11, v17, v17
	v_fmac_f32_e32 v10, v14, v14
	v_fmac_f32_e32 v11, v16, v16
	v_add_f32_e32 v10, v10, v11
	v_mul_f32_e32 v11, v13, v13
	v_mul_f32_e32 v19, v23, v23
	v_fmac_f32_e32 v11, v12, v12
	v_fmac_f32_e32 v19, v22, v22
	v_add_f32_e32 v11, v11, v19
	v_add_f32_e32 v19, v10, v11
	v_cvt_pk_bf16_f32 v10, v14, v15
	v_cvt_pk_bf16_f32 v11, v16, v17
	v_lshlrev_b32_e32 v14, 16, v118
	v_and_b32_e32 v15, 0xffff0000, v118
	v_lshlrev_b32_e32 v16, 16, v119
	v_and_b32_e32 v17, 0xffff0000, v119
	v_pk_mul_f32 v[8:9], v[8:9], v[0:1] op_sel_hi:[1,0]
	v_pk_mul_f32 v[6:7], v[6:7], v[0:1] op_sel_hi:[1,0]
	v_cvt_pk_bf16_f32 v12, v12, v13
	v_cvt_pk_bf16_f32 v13, v22, v23
	v_lshlrev_b32_e32 v22, 16, v120
	v_and_b32_e32 v23, 0xffff0000, v120
	v_pk_fma_f32 v[8:9], v[172:173], v[8:9], v[16:17]
	v_pk_fma_f32 v[6:7], v[170:171], v[6:7], v[14:15]
	v_pk_mul_f32 v[2:3], v[2:3], v[0:1] op_sel_hi:[1,0]
	v_lshlrev_b32_e32 v24, 16, v121
	v_and_b32_e32 v25, 0xffff0000, v121
	v_pk_mul_f32 v[4:5], v[4:5], v[0:1] op_sel_hi:[1,0]
	v_pk_fma_f32 v[16:17], v[166:167], v[2:3], v[22:23]
	v_mul_f32_e32 v0, v7, v7
	v_mul_f32_e32 v2, v9, v9
	v_pk_fma_f32 v[14:15], v[168:169], v[4:5], v[24:25]
	v_fmac_f32_e32 v0, v6, v6
	v_fmac_f32_e32 v2, v8, v8
	v_add_f32_e32 v0, v0, v2
	v_mul_f32_e32 v2, v17, v17
	v_mul_f32_e32 v3, v15, v15
	v_fmac_f32_e32 v2, v16, v16
	v_fmac_f32_e32 v3, v14, v14
	v_add_f32_e32 v2, v2, v3
	v_add_f32_e32 v0, v0, v2
	v_add_f32_e32 v0, v19, v0
	v_mov_b32_e32 v5, v0
	s_nop 1
	v_permlane16_swap_b32_e32 v5, v0
	v_add_u32_e32 v18, 0xb0, v240
	v_add_u32_e32 v20, s29, v18
	v_ashrrev_i32_e32 v21, 31, v20
	v_lshlrev_b64 v[20:21], 11, v[20:21]
	v_lshl_add_u64 v[2:3], s[6:7], 0, v[20:21]
	s_waitcnt lgkmcnt(0)
	v_add_f32_e32 v0, v0, v5
	v_lshl_add_u64 v[20:21], v[220:221], 1, v[2:3]
	v_mov_b32_e32 v2, v0
	s_nop 1
	v_permlane32_swap_b32_e32 v2, v0
	global_store_dwordx4 v[20:21], v[10:13], off
	v_cvt_pk_bf16_f32 v4, v6, v7
	v_cvt_pk_bf16_f32 v5, v8, v9
	v_cvt_pk_bf16_f32 v6, v16, v17
	v_cvt_pk_bf16_f32 v7, v14, v15
	global_store_dwordx4 v[20:21], v[4:7], off offset:256
	s_and_saveexec_b64 s[6:7], s[40:41]
	s_cbranch_execz .LBB0_1605
	v_lshl_add_u32 v3, v18, 4, s28
	s_waitcnt lgkmcnt(0)
	v_add_f32_e32 v0, v0, v2
	ds_write_b32 v3, v0 offset:6144

.LBB0_1630:
	s_lshl_b32 s8, s45, 5
	s_lshl_b32 s9, s16, 8
	v_lshrrev_b32_e32 v0, 1, v239
	s_add_i32 s4, s76, 64
	s_or_b32 s8, s9, s8
	v_and_or_b32 v220, v0, 24, s8
	s_lshl_b32 s29, s4, 8
	v_add_u32_e32 v118, s29, v240
	v_ashrrev_i32_e32 v221, 31, v220
	v_lshl_add_u64 v[120:121], v[220:221], 1, s[6:7]
	s_mov_b64 s[6:7], 0x4000000
	v_ashrrev_i32_e32 v119, 31, v118
	v_lshl_add_u64 v[120:121], v[120:121], 0, s[6:7]
	v_lshlrev_b64 v[224:225], 11, v[118:119]
	v_lshl_add_u64 v[126:127], v[120:121], 0, v[224:225]
	s_barrier
	global_load_dwordx4 v[206:209], v[126:127], off
	global_load_dwordx4 v[202:205], v[126:127], off offset:256
	v_or_b32_e32 v126, 16, v118
	v_ashrrev_i32_e32 v127, 31, v126
	v_lshlrev_b64 v[126:127], 11, v[126:127]
	v_lshl_add_u64 v[126:127], v[120:121], 0, v[126:127]
	global_load_dwordx4 v[198:201], v[126:127], off
	global_load_dwordx4 v[194:197], v[126:127], off offset:256
	v_or_b32_e32 v126, 32, v118
	v_ashrrev_i32_e32 v127, 31, v126
	v_lshlrev_b64 v[126:127], 11, v[126:127]
	v_lshl_add_u64 v[126:127], v[120:121], 0, v[126:127]
	global_load_dwordx4 v[190:193], v[126:127], off
	global_load_dwordx4 v[186:189], v[126:127], off offset:256
	v_or_b32_e32 v126, 48, v118
	v_ashrrev_i32_e32 v127, 31, v126
	v_lshlrev_b64 v[126:127], 11, v[126:127]
	v_lshl_add_u64 v[126:127], v[120:121], 0, v[126:127]
	global_load_dwordx4 v[174:177], v[126:127], off
	global_load_dwordx4 v[162:165], v[126:127], off offset:256
	v_add_u32_e32 v126, 0x80, v118
	v_ashrrev_i32_e32 v127, 31, v126
	v_lshlrev_b64 v[126:127], 11, v[126:127]
	v_lshl_add_u64 v[126:127], v[120:121], 0, v[126:127]
	global_load_dwordx4 v[158:161], v[126:127], off
	global_load_dwordx4 v[154:157], v[126:127], off offset:256
	v_add_u32_e32 v126, 0x90, v118
	v_ashrrev_i32_e32 v127, 31, v126
	v_lshlrev_b64 v[126:127], 11, v[126:127]
	v_lshl_add_u64 v[126:127], v[120:121], 0, v[126:127]
	global_load_dwordx4 v[150:153], v[126:127], off
	global_load_dwordx4 v[146:149], v[126:127], off offset:256
	v_add_u32_e32 v126, 0xa0, v118
	v_add_u32_e32 v118, 0xb0, v118
	v_ashrrev_i32_e32 v127, 31, v126
	v_ashrrev_i32_e32 v119, 31, v118
	v_lshlrev_b64 v[126:127], 11, v[126:127]
	v_lshlrev_b64 v[118:119], 11, v[118:119]
	v_lshl_add_u64 v[126:127], v[120:121], 0, v[126:127]
	v_lshl_add_u64 v[118:119], v[120:121], 0, v[118:119]
	global_load_dwordx4 v[142:145], v[126:127], off
	global_load_dwordx4 v[138:141], v[126:127], off offset:256
	s_nop 0
	global_load_dwordx4 v[126:129], v[118:119], off
	s_nop 0
	global_load_dwordx4 v[118:121], v[118:119], off offset:256
	v_and_b32_e32 v167, 64, v231
	v_xor_b32_e32 v0, 16, v231
	v_add_u32_e32 v167, 64, v167
	v_cmp_lt_i32_e32 vcc, v0, v167
	v_mul_f32_e32 v168, v137, v137
	v_fmac_f32_e32 v168, v136, v136
	v_cndmask_b32_e32 v0, v231, v0, vcc
	v_lshlrev_b32_e32 v241, 2, v0
	v_mul_f32_e32 v0, v135, v135
	v_fmac_f32_e32 v0, v134, v134
	v_add_f32_e32 v0, v0, v168
	v_mul_f32_e32 v168, v131, v131
	v_mul_f32_e32 v169, v133, v133
	v_fmac_f32_e32 v168, v130, v130
	v_fmac_f32_e32 v169, v132, v132
	v_add_f32_e32 v168, v168, v169
	v_add_f32_e32 v0, v168, v0
	v_mul_f32_e32 v168, v123, v123
	v_mul_f32_e32 v169, v125, v125
	v_fmac_f32_e32 v168, v122, v122
	v_fmac_f32_e32 v169, v124, v124
	v_add_f32_e32 v168, v168, v169
	v_add_f32_e32 v0, v168, v0
	v_mul_f32_e32 v168, v115, v115
	v_mul_f32_e32 v169, v117, v117
	v_fmac_f32_e32 v168, v114, v114
	v_fmac_f32_e32 v169, v116, v116
	v_add_f32_e32 v168, v168, v169
	v_add_f32_e32 v0, v168, v0
	v_mov_b32_e32 v168, v0
	s_nop 1
	v_permlane16_swap_b32_e32 v168, v0
	v_xor_b32_e32 v169, 32, v231
	v_cmp_lt_i32_e32 vcc, v169, v167
	s_lshl_b32 s6, s45, 2
	s_add_i32 s28, s6, 0
	v_cndmask_b32_e32 v167, v231, v169, vcc
	v_lshlrev_b32_e32 v242, 2, v167
	s_waitcnt lgkmcnt(0)
	v_add_f32_e32 v167, v0, v168
	v_mov_b32_e32 v168, v167
	s_nop 1
	v_permlane32_swap_b32_e32 v168, v167
	v_and_b32_e32 v0, 63, v239
	v_cmp_gt_u32_e64 s[38:39], 16, v0
	s_and_saveexec_b64 s[6:7], s[38:39]
	v_readlane_b32 s64, v252, 3
	v_readlane_b32 s65, v255, 10
	v_readlane_b32 s68, v255, 11
	s_cbranch_execz .LBB0_1632
	s_lshl_b32 s8, s44, 10
	s_add_i32 s8, s28, s8
	s_waitcnt lgkmcnt(0)
	v_add_f32_e32 v167, v167, v168
	v_lshl_add_u32 v168, v166, 4, s8
	ds_write_b32 v168, v167
.LBB0_1632:
	s_or_b64 exec, exec, s[6:7]
	v_mul_f32_e32 v167, v111, v111
	s_waitcnt lgkmcnt(0)
	v_mul_f32_e32 v168, v113, v113
	v_fmac_f32_e32 v167, v110, v110
	v_fmac_f32_e32 v168, v112, v112
	v_add_f32_e32 v167, v167, v168
	v_mul_f32_e32 v168, v107, v107
	v_mul_f32_e32 v169, v109, v109
	v_fmac_f32_e32 v168, v106, v106
	v_fmac_f32_e32 v169, v108, v108
	v_add_f32_e32 v168, v168, v169
	v_add_f32_e32 v167, v168, v167
	v_mul_f32_e32 v168, v103, v103
	v_mul_f32_e32 v169, v105, v105
	v_fmac_f32_e32 v168, v102, v102
	v_fmac_f32_e32 v169, v104, v104
	v_add_f32_e32 v168, v168, v169
	v_add_f32_e32 v167, v168, v167
	v_mul_f32_e32 v168, v99, v99
	v_mul_f32_e32 v169, v101, v101
	v_fmac_f32_e32 v168, v98, v98
	v_fmac_f32_e32 v169, v100, v100
	v_add_f32_e32 v168, v168, v169
	v_add_f32_e32 v167, v168, v167
	v_mov_b32_e32 v168, v167
	s_nop 1
	v_permlane16_swap_b32_e32 v168, v167
	s_waitcnt lgkmcnt(0)
	v_add_f32_e32 v167, v167, v168
	v_mov_b32_e32 v168, v167
	s_nop 1
	v_permlane32_swap_b32_e32 v168, v167
	s_and_saveexec_b64 s[6:7], s[38:39]
	s_cbranch_execz .LBB0_1634
	s_lshl_b32 s8, s44, 10
	s_add_i32 s8, s28, s8
	s_waitcnt lgkmcnt(0)
	v_add_f32_e32 v167, v167, v168
	v_lshl_add_u32 v168, v166, 4, s8
	ds_write_b32 v168, v167 offset:256
.LBB0_1634:
	s_or_b64 exec, exec, s[6:7]
	v_mul_f32_e32 v167, v95, v95
	s_waitcnt lgkmcnt(0)
	v_mul_f32_e32 v168, v97, v97
	v_fmac_f32_e32 v167, v94, v94
	v_fmac_f32_e32 v168, v96, v96
	v_add_f32_e32 v167, v167, v168
	v_mul_f32_e32 v168, v91, v91
	v_mul_f32_e32 v169, v93, v93
	v_fmac_f32_e32 v168, v90, v90
	v_fmac_f32_e32 v169, v92, v92
	v_add_f32_e32 v168, v168, v169
	v_add_f32_e32 v167, v168, v167
	v_mul_f32_e32 v168, v87, v87
	v_mul_f32_e32 v169, v89, v89
	v_fmac_f32_e32 v168, v86, v86
	v_fmac_f32_e32 v169, v88, v88
	v_add_f32_e32 v168, v168, v169
	v_add_f32_e32 v167, v168, v167
	v_mul_f32_e32 v168, v83, v83
	v_mul_f32_e32 v169, v85, v85
	v_fmac_f32_e32 v168, v82, v82
	v_fmac_f32_e32 v169, v84, v84
	v_add_f32_e32 v168, v168, v169
	v_add_f32_e32 v167, v168, v167
	v_mov_b32_e32 v168, v167
	s_nop 1
	v_permlane16_swap_b32_e32 v168, v167
	s_waitcnt lgkmcnt(0)
	v_add_f32_e32 v167, v167, v168
	v_mov_b32_e32 v168, v167
	s_nop 1
	v_permlane32_swap_b32_e32 v168, v167
	s_and_saveexec_b64 s[6:7], s[38:39]
	s_cbranch_execz .LBB0_1636
	s_lshl_b32 s8, s44, 10
	s_add_i32 s8, s28, s8
	s_waitcnt lgkmcnt(0)
	v_add_f32_e32 v167, v167, v168
	v_lshl_add_u32 v168, v166, 4, s8
	ds_write_b32 v168, v167 offset:512
.LBB0_1636:
	s_or_b64 exec, exec, s[6:7]
	v_mul_f32_e32 v167, v79, v79
	s_waitcnt lgkmcnt(0)
	v_mul_f32_e32 v168, v81, v81
	v_fmac_f32_e32 v167, v78, v78
	v_fmac_f32_e32 v168, v80, v80
	v_add_f32_e32 v167, v167, v168
	v_mul_f32_e32 v168, v75, v75
	v_mul_f32_e32 v169, v77, v77
	v_fmac_f32_e32 v168, v74, v74
	v_fmac_f32_e32 v169, v76, v76
	v_add_f32_e32 v168, v168, v169
	v_add_f32_e32 v167, v168, v167
	v_mul_f32_e32 v168, v71, v71
	v_mul_f32_e32 v169, v73, v73
	v_fmac_f32_e32 v168, v70, v70
	v_fmac_f32_e32 v169, v72, v72
	v_add_f32_e32 v168, v168, v169
	v_add_f32_e32 v167, v168, v167
	v_mul_f32_e32 v168, v67, v67
	v_mul_f32_e32 v169, v69, v69
	v_fmac_f32_e32 v168, v66, v66
	v_fmac_f32_e32 v169, v68, v68
	v_add_f32_e32 v168, v168, v169
	v_add_f32_e32 v167, v168, v167
	v_mov_b32_e32 v168, v167
	s_nop 1
	v_permlane16_swap_b32_e32 v168, v167
	s_waitcnt lgkmcnt(0)
	v_add_f32_e32 v167, v167, v168
	v_mov_b32_e32 v168, v167
	s_nop 1
	v_permlane32_swap_b32_e32 v168, v167
	s_and_saveexec_b64 s[6:7], s[38:39]
	s_cbranch_execz .LBB0_1638
	s_lshl_b32 s8, s44, 10
	s_add_i32 s8, s28, s8
	s_waitcnt lgkmcnt(0)
	v_add_f32_e32 v167, v167, v168
	v_lshl_add_u32 v168, v166, 4, s8
	ds_write_b32 v168, v167 offset:768
.LBB0_1638:
	s_or_b64 exec, exec, s[6:7]
	v_mul_f32_e32 v167, v63, v63
	s_waitcnt lgkmcnt(0)
	v_mul_f32_e32 v168, v65, v65
	v_fmac_f32_e32 v167, v62, v62
	v_fmac_f32_e32 v168, v64, v64
	v_add_f32_e32 v167, v167, v168
	v_mul_f32_e32 v168, v59, v59
	v_mul_f32_e32 v169, v61, v61
	v_fmac_f32_e32 v168, v58, v58
	v_fmac_f32_e32 v169, v60, v60
	v_add_f32_e32 v168, v168, v169
	v_add_f32_e32 v167, v168, v167
	v_mul_f32_e32 v168, v55, v55
	v_mul_f32_e32 v169, v57, v57
	v_fmac_f32_e32 v168, v54, v54
	v_fmac_f32_e32 v169, v56, v56
	v_add_f32_e32 v168, v168, v169
	v_add_f32_e32 v167, v168, v167
	v_mul_f32_e32 v168, v51, v51
	v_mul_f32_e32 v169, v53, v53
	v_fmac_f32_e32 v168, v50, v50
	v_fmac_f32_e32 v169, v52, v52
	v_add_f32_e32 v168, v168, v169
	v_add_f32_e32 v167, v168, v167
	v_mov_b32_e32 v168, v167
	s_nop 1
	v_permlane16_swap_b32_e32 v168, v167
	s_waitcnt lgkmcnt(0)
	v_add_f32_e32 v167, v167, v168
	v_mov_b32_e32 v168, v167
	s_nop 1
	v_permlane32_swap_b32_e32 v168, v167
	s_and_saveexec_b64 s[6:7], s[38:39]
	s_cbranch_execz .LBB0_1640
	s_lshl_b32 s8, s44, 10
	s_add_i32 s8, s28, s8
	s_waitcnt lgkmcnt(0)
	v_add_f32_e32 v167, v167, v168
	v_lshl_add_u32 v168, v166, 4, s8
	ds_write_b32 v168, v167 offset:2048
.LBB0_1640:
	s_or_b64 exec, exec, s[6:7]
	v_mul_f32_e32 v167, v47, v47
	s_waitcnt lgkmcnt(0)
	v_mul_f32_e32 v168, v49, v49
	v_fmac_f32_e32 v167, v46, v46
	v_fmac_f32_e32 v168, v48, v48
	v_add_f32_e32 v167, v167, v168
	v_mul_f32_e32 v168, v43, v43
	v_mul_f32_e32 v169, v45, v45
	v_fmac_f32_e32 v168, v42, v42
	v_fmac_f32_e32 v169, v44, v44
	v_add_f32_e32 v168, v168, v169
	v_add_f32_e32 v167, v168, v167
	v_mul_f32_e32 v168, v39, v39
	v_mul_f32_e32 v169, v41, v41
	v_fmac_f32_e32 v168, v38, v38
	v_fmac_f32_e32 v169, v40, v40
	v_add_f32_e32 v168, v168, v169
	v_add_f32_e32 v167, v168, v167
	v_mul_f32_e32 v168, v35, v35
	v_mul_f32_e32 v169, v37, v37
	v_fmac_f32_e32 v168, v34, v34
	v_fmac_f32_e32 v169, v36, v36
	v_add_f32_e32 v168, v168, v169
	v_add_f32_e32 v167, v168, v167
	v_mov_b32_e32 v168, v167
	s_nop 1
	v_permlane16_swap_b32_e32 v168, v167
	s_waitcnt lgkmcnt(0)
	v_add_f32_e32 v167, v167, v168
	v_mov_b32_e32 v168, v167
	s_nop 1
	v_permlane32_swap_b32_e32 v168, v167
	s_and_saveexec_b64 s[6:7], s[38:39]
	s_cbranch_execz .LBB0_1642
	s_lshl_b32 s8, s44, 10
	s_add_i32 s8, s28, s8
	s_waitcnt lgkmcnt(0)
	v_add_f32_e32 v167, v167, v168
	v_lshl_add_u32 v168, v166, 4, s8
	ds_write_b32 v168, v167 offset:2304
.LBB0_1642:
	s_or_b64 exec, exec, s[6:7]
	v_mul_f32_e32 v167, v31, v31
	s_waitcnt lgkmcnt(0)
	v_mul_f32_e32 v168, v33, v33
	v_fmac_f32_e32 v167, v30, v30
	v_fmac_f32_e32 v168, v32, v32
	v_add_f32_e32 v167, v167, v168
	v_mul_f32_e32 v168, v27, v27
	v_mul_f32_e32 v169, v29, v29
	v_fmac_f32_e32 v168, v26, v26
	v_fmac_f32_e32 v169, v28, v28
	v_add_f32_e32 v168, v168, v169
	v_add_f32_e32 v167, v168, v167
	v_mul_f32_e32 v168, v23, v23
	v_mul_f32_e32 v169, v25, v25
	v_fmac_f32_e32 v168, v22, v22
	v_fmac_f32_e32 v169, v24, v24
	v_add_f32_e32 v168, v168, v169
	v_add_f32_e32 v167, v168, v167
	v_mul_f32_e32 v168, v19, v19
	v_mul_f32_e32 v169, v21, v21
	v_fmac_f32_e32 v168, v18, v18
	v_fmac_f32_e32 v169, v20, v20
	v_add_f32_e32 v168, v168, v169
	v_add_f32_e32 v167, v168, v167
	v_mov_b32_e32 v168, v167
	s_nop 1
	v_permlane16_swap_b32_e32 v168, v167
	s_waitcnt lgkmcnt(0)
	v_add_f32_e32 v167, v167, v168
	v_mov_b32_e32 v168, v167
	s_nop 1
	v_permlane32_swap_b32_e32 v168, v167
	s_and_saveexec_b64 s[6:7], s[38:39]
	s_cbranch_execz .LBB0_1644
	s_lshl_b32 s8, s44, 10
	s_add_i32 s8, s28, s8
	s_waitcnt lgkmcnt(0)
	v_add_f32_e32 v167, v167, v168
	v_lshl_add_u32 v168, v166, 4, s8
	ds_write_b32 v168, v167 offset:2560
.LBB0_1644:
	s_or_b64 exec, exec, s[6:7]
	v_mul_f32_e32 v167, v15, v15
	s_waitcnt lgkmcnt(0)
	v_mul_f32_e32 v168, v17, v17
	v_fmac_f32_e32 v167, v14, v14
	v_fmac_f32_e32 v168, v16, v16
	v_add_f32_e32 v167, v167, v168
	v_mul_f32_e32 v168, v11, v11
	v_mul_f32_e32 v169, v13, v13
	v_fmac_f32_e32 v168, v10, v10
	v_fmac_f32_e32 v169, v12, v12
	v_add_f32_e32 v168, v168, v169
	v_add_f32_e32 v167, v168, v167
	v_mul_f32_e32 v168, v7, v7
	v_mul_f32_e32 v169, v9, v9
	v_fmac_f32_e32 v168, v6, v6
	v_fmac_f32_e32 v169, v8, v8
	v_add_f32_e32 v168, v168, v169
	v_add_f32_e32 v167, v168, v167
	v_mul_f32_e32 v168, v3, v3
	v_mul_f32_e32 v169, v5, v5
	v_fmac_f32_e32 v168, v2, v2
	v_fmac_f32_e32 v169, v4, v4
	v_add_f32_e32 v168, v168, v169
	v_add_f32_e32 v167, v168, v167
	v_mov_b32_e32 v168, v167
	s_nop 1
	v_permlane16_swap_b32_e32 v168, v167
	s_waitcnt lgkmcnt(0)
	v_add_f32_e32 v167, v167, v168
	v_mov_b32_e32 v168, v167
	s_nop 1
	v_permlane32_swap_b32_e32 v168, v167
	s_and_saveexec_b64 s[6:7], s[38:39]
	s_cbranch_execz .LBB0_1646
	s_lshl_b32 s8, s44, 10
	s_add_i32 s8, s28, s8
	s_waitcnt lgkmcnt(0)
	v_add_f32_e32 v167, v167, v168
	v_lshl_add_u32 v166, v166, 4, s8
	ds_write_b32 v166, v167 offset:2816

.LBB0_1672:
	s_waitcnt vmcnt(0)
	v_lshlrev_b32_e32 v216, 16, v206
	v_and_b32_e32 v217, 0xffff0000, v206
	v_lshlrev_b32_e32 v206, 16, v207
	v_and_b32_e32 v207, 0xffff0000, v207
	s_waitcnt lgkmcnt(0)
	v_pk_mul_f32 v[136:137], v[136:137], v[0:1] op_sel_hi:[1,0]
	v_pk_mul_f32 v[134:135], v[134:135], v[0:1] op_sel_hi:[1,0]
	v_lshlrev_b32_e32 v218, 16, v208
	v_and_b32_e32 v219, 0xffff0000, v208
	v_lshlrev_b32_e32 v208, 16, v209
	v_and_b32_e32 v209, 0xffff0000, v209
	v_pk_fma_f32 v[136:137], v[184:185], v[136:137], v[206:207]
	v_pk_fma_f32 v[134:135], v[182:183], v[134:135], v[216:217]
	v_pk_mul_f32 v[132:133], v[132:133], v[0:1] op_sel_hi:[1,0]
	v_pk_mul_f32 v[130:131], v[130:131], v[0:1] op_sel_hi:[1,0]
	v_pk_fma_f32 v[206:207], v[180:181], v[132:133], v[208:209]
	v_pk_fma_f32 v[132:133], v[178:179], v[130:131], v[218:219]
	v_mul_f32_e32 v130, v135, v135
	v_mul_f32_e32 v131, v137, v137
	v_fmac_f32_e32 v130, v134, v134
	v_fmac_f32_e32 v131, v136, v136
	v_add_f32_e32 v130, v130, v131
	v_mul_f32_e32 v131, v133, v133
	v_mul_f32_e32 v208, v207, v207
	v_fmac_f32_e32 v131, v132, v132
	v_fmac_f32_e32 v208, v206, v206
	v_add_f32_e32 v131, v131, v208
	v_add_f32_e32 v208, v130, v131
	v_cvt_pk_bf16_f32 v130, v134, v135
	v_cvt_pk_bf16_f32 v131, v136, v137
	v_lshlrev_b32_e32 v134, 16, v202
	v_and_b32_e32 v135, 0xffff0000, v202
	v_lshlrev_b32_e32 v136, 16, v203
	v_and_b32_e32 v137, 0xffff0000, v203
	v_pk_mul_f32 v[124:125], v[124:125], v[0:1] op_sel_hi:[1,0]
	v_pk_mul_f32 v[122:123], v[122:123], v[0:1] op_sel_hi:[1,0]
	v_lshlrev_b32_e32 v202, 16, v204
	v_and_b32_e32 v203, 0xffff0000, v204
	v_pk_fma_f32 v[124:125], v[172:173], v[124:125], v[136:137]
	v_pk_fma_f32 v[122:123], v[170:171], v[122:123], v[134:135]
	v_pk_mul_f32 v[114:115], v[114:115], v[0:1] op_sel_hi:[1,0]
	v_lshlrev_b32_e32 v204, 16, v205
	v_and_b32_e32 v205, 0xffff0000, v205
	v_pk_mul_f32 v[116:117], v[116:117], v[0:1] op_sel_hi:[1,0]
	v_pk_fma_f32 v[134:135], v[166:167], v[114:115], v[202:203]
	v_mul_f32_e32 v0, v123, v123
	v_mul_f32_e32 v114, v125, v125
	v_pk_fma_f32 v[116:117], v[168:169], v[116:117], v[204:205]
	v_fmac_f32_e32 v0, v122, v122
	v_fmac_f32_e32 v114, v124, v124
	v_add_f32_e32 v0, v0, v114
	v_mul_f32_e32 v114, v135, v135
	v_mul_f32_e32 v115, v117, v117
	v_fmac_f32_e32 v114, v134, v134
	v_fmac_f32_e32 v115, v116, v116
	v_add_f32_e32 v114, v114, v115
	v_add_f32_e32 v0, v0, v114
	v_add_f32_e32 v0, v208, v0
	v_mov_b32_e32 v202, v0
	s_nop 1
	v_permlane16_swap_b32_e32 v202, v0
	s_add_u32 s6, s18, 0x4000000
	s_addc_u32 s7, s19, 0
	v_lshl_add_u64 v[114:115], s[6:7], 0, v[224:225]
	v_lshl_add_u64 v[136:137], v[220:221], 1, v[114:115]
	s_waitcnt lgkmcnt(0)
	v_add_f32_e32 v0, v0, v202
	v_mov_b32_e32 v114, v0
	s_nop 1
	v_permlane32_swap_b32_e32 v114, v0
	v_cvt_pk_bf16_f32 v132, v132, v133
	v_cvt_pk_bf16_f32 v133, v206, v207
	global_store_dwordx4 v[136:137], v[130:133], off
	v_cvt_pk_bf16_f32 v122, v122, v123
	v_cvt_pk_bf16_f32 v123, v124, v125
	v_cvt_pk_bf16_f32 v124, v134, v135
	v_cvt_pk_bf16_f32 v125, v116, v117
	global_store_dwordx4 v[136:137], v[122:125], off offset:256
	s_and_saveexec_b64 s[8:9], s[38:39]
	s_cbranch_execz .LBB0_1674
	v_lshl_add_u32 v115, v240, 4, s28
	s_waitcnt lgkmcnt(0)
	v_add_f32_e32 v0, v0, v114
	ds_write_b32 v115, v0 offset:6144

.LBB0_1676:
	v_lshlrev_b32_e32 v122, 16, v198
	v_and_b32_e32 v123, 0xffff0000, v198
	v_lshlrev_b32_e32 v124, 16, v199
	v_and_b32_e32 v125, 0xffff0000, v199
	s_waitcnt lgkmcnt(0)
	v_pk_mul_f32 v[112:113], v[112:113], v[0:1] op_sel_hi:[1,0]
	v_pk_mul_f32 v[110:111], v[110:111], v[0:1] op_sel_hi:[1,0]
	v_lshlrev_b32_e32 v130, 16, v200
	v_and_b32_e32 v131, 0xffff0000, v200
	v_lshlrev_b32_e32 v132, 16, v201
	v_and_b32_e32 v133, 0xffff0000, v201
	v_pk_fma_f32 v[112:113], v[184:185], v[112:113], v[124:125]
	v_pk_fma_f32 v[110:111], v[182:183], v[110:111], v[122:123]
	v_pk_mul_f32 v[108:109], v[108:109], v[0:1] op_sel_hi:[1,0]
	v_pk_mul_f32 v[106:107], v[106:107], v[0:1] op_sel_hi:[1,0]
	v_pk_fma_f32 v[122:123], v[180:181], v[108:109], v[132:133]
	v_pk_fma_f32 v[108:109], v[178:179], v[106:107], v[130:131]
	v_mul_f32_e32 v106, v111, v111
	v_mul_f32_e32 v107, v113, v113
	v_fmac_f32_e32 v106, v110, v110
	v_fmac_f32_e32 v107, v112, v112
	v_add_f32_e32 v106, v106, v107
	v_mul_f32_e32 v107, v109, v109
	v_mul_f32_e32 v115, v123, v123
	v_fmac_f32_e32 v107, v108, v108
	v_fmac_f32_e32 v115, v122, v122
	v_add_f32_e32 v107, v107, v115
	v_add_f32_e32 v115, v106, v107
	v_cvt_pk_bf16_f32 v106, v110, v111
	v_cvt_pk_bf16_f32 v107, v112, v113
	v_lshlrev_b32_e32 v110, 16, v194
	v_and_b32_e32 v111, 0xffff0000, v194
	v_lshlrev_b32_e32 v112, 16, v195
	v_and_b32_e32 v113, 0xffff0000, v195
	v_pk_mul_f32 v[104:105], v[104:105], v[0:1] op_sel_hi:[1,0]
	v_pk_mul_f32 v[102:103], v[102:103], v[0:1] op_sel_hi:[1,0]
	v_cvt_pk_bf16_f32 v108, v108, v109
	v_cvt_pk_bf16_f32 v109, v122, v123
	v_lshlrev_b32_e32 v122, 16, v196
	v_and_b32_e32 v123, 0xffff0000, v196
	v_pk_fma_f32 v[104:105], v[172:173], v[104:105], v[112:113]
	v_pk_fma_f32 v[102:103], v[170:171], v[102:103], v[110:111]
	v_pk_mul_f32 v[98:99], v[98:99], v[0:1] op_sel_hi:[1,0]
	v_lshlrev_b32_e32 v124, 16, v197
	v_and_b32_e32 v125, 0xffff0000, v197
	v_pk_mul_f32 v[100:101], v[100:101], v[0:1] op_sel_hi:[1,0]
	v_pk_fma_f32 v[112:113], v[166:167], v[98:99], v[122:123]
	v_mul_f32_e32 v0, v103, v103
	v_mul_f32_e32 v98, v105, v105
	v_pk_fma_f32 v[110:111], v[168:169], v[100:101], v[124:125]
	v_fmac_f32_e32 v0, v102, v102
	v_fmac_f32_e32 v98, v104, v104
	v_add_f32_e32 v0, v0, v98
	v_mul_f32_e32 v98, v113, v113
	v_mul_f32_e32 v99, v111, v111
	v_fmac_f32_e32 v98, v112, v112
	v_fmac_f32_e32 v99, v110, v110
	v_add_f32_e32 v98, v98, v99
	v_add_f32_e32 v0, v0, v98
	v_add_f32_e32 v0, v115, v0
	v_mov_b32_e32 v101, v0
	s_nop 1
	v_permlane16_swap_b32_e32 v101, v0
	v_or_b32_e32 v114, 16, v240
	v_add_u32_e32 v116, s29, v114
	v_ashrrev_i32_e32 v117, 31, v116
	v_lshlrev_b64 v[116:117], 11, v[116:117]
	v_lshl_add_u64 v[98:99], s[6:7], 0, v[116:117]
	s_waitcnt lgkmcnt(0)
	v_add_f32_e32 v0, v0, v101
	v_lshl_add_u64 v[116:117], v[220:221], 1, v[98:99]
	v_mov_b32_e32 v98, v0
	s_nop 1
	v_permlane32_swap_b32_e32 v98, v0
	global_store_dwordx4 v[116:117], v[106:109], off
	v_cvt_pk_bf16_f32 v100, v102, v103
	v_cvt_pk_bf16_f32 v101, v104, v105
	v_cvt_pk_bf16_f32 v102, v112, v113
	v_cvt_pk_bf16_f32 v103, v110, v111
	global_store_dwordx4 v[116:117], v[100:103], off offset:256
	s_and_saveexec_b64 s[8:9], s[38:39]
	s_cbranch_execz .LBB0_1678
	v_lshl_add_u32 v99, v114, 4, s28
	s_waitcnt lgkmcnt(0)
	v_add_f32_e32 v0, v0, v98
	ds_write_b32 v99, v0 offset:6144

.LBB0_1680:
	v_lshlrev_b32_e32 v102, 16, v190
	v_and_b32_e32 v103, 0xffff0000, v190
	v_lshlrev_b32_e32 v104, 16, v191
	v_and_b32_e32 v105, 0xffff0000, v191
	s_waitcnt lgkmcnt(0)
	v_pk_mul_f32 v[96:97], v[96:97], v[0:1] op_sel_hi:[1,0]
	v_pk_mul_f32 v[94:95], v[94:95], v[0:1] op_sel_hi:[1,0]
	v_lshlrev_b32_e32 v106, 16, v192
	v_and_b32_e32 v107, 0xffff0000, v192
	v_lshlrev_b32_e32 v108, 16, v193
	v_and_b32_e32 v109, 0xffff0000, v193
	v_pk_fma_f32 v[96:97], v[184:185], v[96:97], v[104:105]
	v_pk_fma_f32 v[94:95], v[182:183], v[94:95], v[102:103]
	v_pk_mul_f32 v[92:93], v[92:93], v[0:1] op_sel_hi:[1,0]
	v_pk_mul_f32 v[90:91], v[90:91], v[0:1] op_sel_hi:[1,0]
	v_pk_fma_f32 v[102:103], v[180:181], v[92:93], v[108:109]
	v_pk_fma_f32 v[92:93], v[178:179], v[90:91], v[106:107]
	v_mul_f32_e32 v90, v95, v95
	v_mul_f32_e32 v91, v97, v97
	v_fmac_f32_e32 v90, v94, v94
	v_fmac_f32_e32 v91, v96, v96
	v_add_f32_e32 v90, v90, v91
	v_mul_f32_e32 v91, v93, v93
	v_mul_f32_e32 v99, v103, v103
	v_fmac_f32_e32 v91, v92, v92
	v_fmac_f32_e32 v99, v102, v102
	v_add_f32_e32 v91, v91, v99
	v_add_f32_e32 v99, v90, v91
	v_cvt_pk_bf16_f32 v90, v94, v95
	v_cvt_pk_bf16_f32 v91, v96, v97
	v_lshlrev_b32_e32 v94, 16, v186
	v_and_b32_e32 v95, 0xffff0000, v186
	v_lshlrev_b32_e32 v96, 16, v187
	v_and_b32_e32 v97, 0xffff0000, v187
	v_pk_mul_f32 v[88:89], v[88:89], v[0:1] op_sel_hi:[1,0]
	v_pk_mul_f32 v[86:87], v[86:87], v[0:1] op_sel_hi:[1,0]
	v_cvt_pk_bf16_f32 v92, v92, v93
	v_cvt_pk_bf16_f32 v93, v102, v103
	v_lshlrev_b32_e32 v102, 16, v188
	v_and_b32_e32 v103, 0xffff0000, v188
	v_pk_fma_f32 v[88:89], v[172:173], v[88:89], v[96:97]
	v_pk_fma_f32 v[86:87], v[170:171], v[86:87], v[94:95]
	v_pk_mul_f32 v[82:83], v[82:83], v[0:1] op_sel_hi:[1,0]
	v_lshlrev_b32_e32 v104, 16, v189
	v_and_b32_e32 v105, 0xffff0000, v189
	v_pk_mul_f32 v[84:85], v[84:85], v[0:1] op_sel_hi:[1,0]
	v_pk_fma_f32 v[96:97], v[166:167], v[82:83], v[102:103]
	v_mul_f32_e32 v0, v87, v87
	v_mul_f32_e32 v82, v89, v89
	v_pk_fma_f32 v[94:95], v[168:169], v[84:85], v[104:105]
	v_fmac_f32_e32 v0, v86, v86
	v_fmac_f32_e32 v82, v88, v88
	v_add_f32_e32 v0, v0, v82
	v_mul_f32_e32 v82, v97, v97
	v_mul_f32_e32 v83, v95, v95
	v_fmac_f32_e32 v82, v96, v96
	v_fmac_f32_e32 v83, v94, v94
	v_add_f32_e32 v82, v82, v83
	v_add_f32_e32 v0, v0, v82
	v_add_f32_e32 v0, v99, v0
	v_mov_b32_e32 v85, v0
	s_nop 1
	v_permlane16_swap_b32_e32 v85, v0
	v_or_b32_e32 v98, 32, v240
	v_add_u32_e32 v100, s29, v98
	v_ashrrev_i32_e32 v101, 31, v100
	v_lshlrev_b64 v[100:101], 11, v[100:101]
	v_lshl_add_u64 v[82:83], s[6:7], 0, v[100:101]
	s_waitcnt lgkmcnt(0)
	v_add_f32_e32 v0, v0, v85
	v_lshl_add_u64 v[100:101], v[220:221], 1, v[82:83]
	v_mov_b32_e32 v82, v0
	s_nop 1
	v_permlane32_swap_b32_e32 v82, v0
	global_store_dwordx4 v[100:101], v[90:93], off
	v_cvt_pk_bf16_f32 v84, v86, v87
	v_cvt_pk_bf16_f32 v85, v88, v89
	v_cvt_pk_bf16_f32 v86, v96, v97
	v_cvt_pk_bf16_f32 v87, v94, v95
	global_store_dwordx4 v[100:101], v[84:87], off offset:256
	s_and_saveexec_b64 s[8:9], s[38:39]
	s_cbranch_execz .LBB0_1682
	v_lshl_add_u32 v83, v98, 4, s28
	s_waitcnt lgkmcnt(0)
	v_add_f32_e32 v0, v0, v82
	ds_write_b32 v83, v0 offset:6144

.LBB0_1684:
	v_lshlrev_b32_e32 v86, 16, v174
	v_and_b32_e32 v87, 0xffff0000, v174
	v_lshlrev_b32_e32 v88, 16, v175
	v_and_b32_e32 v89, 0xffff0000, v175
	s_waitcnt lgkmcnt(0)
	v_pk_mul_f32 v[80:81], v[80:81], v[0:1] op_sel_hi:[1,0]
	v_pk_mul_f32 v[78:79], v[78:79], v[0:1] op_sel_hi:[1,0]
	v_lshlrev_b32_e32 v90, 16, v176
	v_and_b32_e32 v91, 0xffff0000, v176
	v_lshlrev_b32_e32 v92, 16, v177
	v_and_b32_e32 v93, 0xffff0000, v177
	v_pk_fma_f32 v[80:81], v[184:185], v[80:81], v[88:89]
	v_pk_fma_f32 v[78:79], v[182:183], v[78:79], v[86:87]
	v_pk_mul_f32 v[76:77], v[76:77], v[0:1] op_sel_hi:[1,0]
	v_pk_mul_f32 v[74:75], v[74:75], v[0:1] op_sel_hi:[1,0]
	v_pk_fma_f32 v[86:87], v[180:181], v[76:77], v[92:93]
	v_pk_fma_f32 v[76:77], v[178:179], v[74:75], v[90:91]
	v_mul_f32_e32 v74, v79, v79
	v_mul_f32_e32 v75, v81, v81
	v_fmac_f32_e32 v74, v78, v78
	v_fmac_f32_e32 v75, v80, v80
	v_add_f32_e32 v74, v74, v75
	v_mul_f32_e32 v75, v77, v77
	v_mul_f32_e32 v83, v87, v87
	v_fmac_f32_e32 v75, v76, v76
	v_fmac_f32_e32 v83, v86, v86
	v_add_f32_e32 v75, v75, v83
	v_add_f32_e32 v83, v74, v75
	v_cvt_pk_bf16_f32 v74, v78, v79
	v_cvt_pk_bf16_f32 v75, v80, v81
	v_lshlrev_b32_e32 v78, 16, v162
	v_and_b32_e32 v79, 0xffff0000, v162
	v_lshlrev_b32_e32 v80, 16, v163
	v_and_b32_e32 v81, 0xffff0000, v163
	v_pk_mul_f32 v[72:73], v[72:73], v[0:1] op_sel_hi:[1,0]
	v_pk_mul_f32 v[70:71], v[70:71], v[0:1] op_sel_hi:[1,0]
	v_cvt_pk_bf16_f32 v76, v76, v77
	v_cvt_pk_bf16_f32 v77, v86, v87
	v_lshlrev_b32_e32 v86, 16, v164
	v_and_b32_e32 v87, 0xffff0000, v164
	v_pk_fma_f32 v[72:73], v[172:173], v[72:73], v[80:81]
	v_pk_fma_f32 v[70:71], v[170:171], v[70:71], v[78:79]
	v_pk_mul_f32 v[66:67], v[66:67], v[0:1] op_sel_hi:[1,0]
	v_lshlrev_b32_e32 v88, 16, v165
	v_and_b32_e32 v89, 0xffff0000, v165
	v_pk_mul_f32 v[68:69], v[68:69], v[0:1] op_sel_hi:[1,0]
	v_pk_fma_f32 v[80:81], v[166:167], v[66:67], v[86:87]
	v_mul_f32_e32 v0, v71, v71
	v_mul_f32_e32 v66, v73, v73
	v_pk_fma_f32 v[78:79], v[168:169], v[68:69], v[88:89]
	v_fmac_f32_e32 v0, v70, v70
	v_fmac_f32_e32 v66, v72, v72
	v_add_f32_e32 v0, v0, v66
	v_mul_f32_e32 v66, v81, v81
	v_mul_f32_e32 v67, v79, v79
	v_fmac_f32_e32 v66, v80, v80
	v_fmac_f32_e32 v67, v78, v78
	v_add_f32_e32 v66, v66, v67
	v_add_f32_e32 v0, v0, v66
	v_add_f32_e32 v0, v83, v0
	v_mov_b32_e32 v69, v0
	s_nop 1
	v_permlane16_swap_b32_e32 v69, v0
	v_or_b32_e32 v82, 48, v240
	v_add_u32_e32 v84, s29, v82
	v_ashrrev_i32_e32 v85, 31, v84
	v_lshlrev_b64 v[84:85], 11, v[84:85]
	v_lshl_add_u64 v[66:67], s[6:7], 0, v[84:85]
	s_waitcnt lgkmcnt(0)
	v_add_f32_e32 v0, v0, v69
	v_lshl_add_u64 v[84:85], v[220:221], 1, v[66:67]
	v_mov_b32_e32 v66, v0
	s_nop 1
	v_permlane32_swap_b32_e32 v66, v0
	global_store_dwordx4 v[84:85], v[74:77], off
	v_cvt_pk_bf16_f32 v68, v70, v71
	v_cvt_pk_bf16_f32 v69, v72, v73
	v_cvt_pk_bf16_f32 v70, v80, v81
	v_cvt_pk_bf16_f32 v71, v78, v79
	global_store_dwordx4 v[84:85], v[68:71], off offset:256
	s_and_saveexec_b64 s[8:9], s[38:39]
	s_cbranch_execz .LBB0_1686
	v_lshl_add_u32 v67, v82, 4, s28
	s_waitcnt lgkmcnt(0)
	v_add_f32_e32 v0, v0, v66
	ds_write_b32 v67, v0 offset:6144

.LBB0_1688:
	v_lshlrev_b32_e32 v70, 16, v158
	v_and_b32_e32 v71, 0xffff0000, v158
	v_lshlrev_b32_e32 v72, 16, v159
	v_and_b32_e32 v73, 0xffff0000, v159
	s_waitcnt lgkmcnt(0)
	v_pk_mul_f32 v[64:65], v[64:65], v[0:1] op_sel_hi:[1,0]
	v_pk_mul_f32 v[62:63], v[62:63], v[0:1] op_sel_hi:[1,0]
	v_lshlrev_b32_e32 v74, 16, v160
	v_and_b32_e32 v75, 0xffff0000, v160
	v_lshlrev_b32_e32 v76, 16, v161
	v_and_b32_e32 v77, 0xffff0000, v161
	v_pk_fma_f32 v[64:65], v[184:185], v[64:65], v[72:73]
	v_pk_fma_f32 v[62:63], v[182:183], v[62:63], v[70:71]
	v_pk_mul_f32 v[60:61], v[60:61], v[0:1] op_sel_hi:[1,0]
	v_pk_mul_f32 v[58:59], v[58:59], v[0:1] op_sel_hi:[1,0]
	v_pk_fma_f32 v[70:71], v[180:181], v[60:61], v[76:77]
	v_pk_fma_f32 v[60:61], v[178:179], v[58:59], v[74:75]
	v_mul_f32_e32 v58, v63, v63
	v_mul_f32_e32 v59, v65, v65
	v_fmac_f32_e32 v58, v62, v62
	v_fmac_f32_e32 v59, v64, v64
	v_add_f32_e32 v58, v58, v59
	v_mul_f32_e32 v59, v61, v61
	v_mul_f32_e32 v67, v71, v71
	v_fmac_f32_e32 v59, v60, v60
	v_fmac_f32_e32 v67, v70, v70
	v_add_f32_e32 v59, v59, v67
	v_add_f32_e32 v67, v58, v59
	v_cvt_pk_bf16_f32 v58, v62, v63
	v_cvt_pk_bf16_f32 v59, v64, v65
	v_lshlrev_b32_e32 v62, 16, v154
	v_and_b32_e32 v63, 0xffff0000, v154
	v_lshlrev_b32_e32 v64, 16, v155
	v_and_b32_e32 v65, 0xffff0000, v155
	v_pk_mul_f32 v[56:57], v[56:57], v[0:1] op_sel_hi:[1,0]
	v_pk_mul_f32 v[54:55], v[54:55], v[0:1] op_sel_hi:[1,0]
	v_cvt_pk_bf16_f32 v60, v60, v61
	v_cvt_pk_bf16_f32 v61, v70, v71
	v_lshlrev_b32_e32 v70, 16, v156
	v_and_b32_e32 v71, 0xffff0000, v156
	v_pk_fma_f32 v[56:57], v[172:173], v[56:57], v[64:65]
	v_pk_fma_f32 v[54:55], v[170:171], v[54:55], v[62:63]
	v_pk_mul_f32 v[50:51], v[50:51], v[0:1] op_sel_hi:[1,0]
	v_lshlrev_b32_e32 v72, 16, v157
	v_and_b32_e32 v73, 0xffff0000, v157
	v_pk_mul_f32 v[52:53], v[52:53], v[0:1] op_sel_hi:[1,0]
	v_pk_fma_f32 v[64:65], v[166:167], v[50:51], v[70:71]
	v_mul_f32_e32 v0, v55, v55
	v_mul_f32_e32 v50, v57, v57
	v_pk_fma_f32 v[62:63], v[168:169], v[52:53], v[72:73]
	v_fmac_f32_e32 v0, v54, v54
	v_fmac_f32_e32 v50, v56, v56
	v_add_f32_e32 v0, v0, v50
	v_mul_f32_e32 v50, v65, v65
	v_mul_f32_e32 v51, v63, v63
	v_fmac_f32_e32 v50, v64, v64
	v_fmac_f32_e32 v51, v62, v62
	v_add_f32_e32 v50, v50, v51
	v_add_f32_e32 v0, v0, v50
	v_add_f32_e32 v0, v67, v0
	v_mov_b32_e32 v53, v0
	s_nop 1
	v_permlane16_swap_b32_e32 v53, v0
	v_add_u32_e32 v66, 0x80, v240
	v_add_u32_e32 v68, s29, v66
	v_ashrrev_i32_e32 v69, 31, v68
	v_lshlrev_b64 v[68:69], 11, v[68:69]
	v_lshl_add_u64 v[50:51], s[6:7], 0, v[68:69]
	s_waitcnt lgkmcnt(0)
	v_add_f32_e32 v0, v0, v53
	v_lshl_add_u64 v[68:69], v[220:221], 1, v[50:51]
	v_mov_b32_e32 v50, v0
	s_nop 1
	v_permlane32_swap_b32_e32 v50, v0
	global_store_dwordx4 v[68:69], v[58:61], off
	v_cvt_pk_bf16_f32 v52, v54, v55
	v_cvt_pk_bf16_f32 v53, v56, v57
	v_cvt_pk_bf16_f32 v54, v64, v65
	v_cvt_pk_bf16_f32 v55, v62, v63
	global_store_dwordx4 v[68:69], v[52:55], off offset:256
	s_and_saveexec_b64 s[8:9], s[38:39]
	s_cbranch_execz .LBB0_1690
	v_lshl_add_u32 v51, v66, 4, s28
	s_waitcnt lgkmcnt(0)
	v_add_f32_e32 v0, v0, v50
	ds_write_b32 v51, v0 offset:6144

.LBB0_1692:
	v_lshlrev_b32_e32 v54, 16, v150
	v_and_b32_e32 v55, 0xffff0000, v150
	v_lshlrev_b32_e32 v56, 16, v151
	v_and_b32_e32 v57, 0xffff0000, v151
	s_waitcnt lgkmcnt(0)
	v_pk_mul_f32 v[48:49], v[48:49], v[0:1] op_sel_hi:[1,0]
	v_pk_mul_f32 v[46:47], v[46:47], v[0:1] op_sel_hi:[1,0]
	v_lshlrev_b32_e32 v58, 16, v152
	v_and_b32_e32 v59, 0xffff0000, v152
	v_lshlrev_b32_e32 v60, 16, v153
	v_and_b32_e32 v61, 0xffff0000, v153
	v_pk_fma_f32 v[48:49], v[184:185], v[48:49], v[56:57]
	v_pk_fma_f32 v[46:47], v[182:183], v[46:47], v[54:55]
	v_pk_mul_f32 v[44:45], v[44:45], v[0:1] op_sel_hi:[1,0]
	v_pk_mul_f32 v[42:43], v[42:43], v[0:1] op_sel_hi:[1,0]
	v_pk_fma_f32 v[54:55], v[180:181], v[44:45], v[60:61]
	v_pk_fma_f32 v[44:45], v[178:179], v[42:43], v[58:59]
	v_mul_f32_e32 v42, v47, v47
	v_mul_f32_e32 v43, v49, v49
	v_fmac_f32_e32 v42, v46, v46
	v_fmac_f32_e32 v43, v48, v48
	v_add_f32_e32 v42, v42, v43
	v_mul_f32_e32 v43, v45, v45
	v_mul_f32_e32 v51, v55, v55
	v_fmac_f32_e32 v43, v44, v44
	v_fmac_f32_e32 v51, v54, v54
	v_add_f32_e32 v43, v43, v51
	v_add_f32_e32 v51, v42, v43
	v_cvt_pk_bf16_f32 v42, v46, v47
	v_cvt_pk_bf16_f32 v43, v48, v49
	v_lshlrev_b32_e32 v46, 16, v146
	v_and_b32_e32 v47, 0xffff0000, v146
	v_lshlrev_b32_e32 v48, 16, v147
	v_and_b32_e32 v49, 0xffff0000, v147
	v_pk_mul_f32 v[40:41], v[40:41], v[0:1] op_sel_hi:[1,0]
	v_pk_mul_f32 v[38:39], v[38:39], v[0:1] op_sel_hi:[1,0]
	v_cvt_pk_bf16_f32 v44, v44, v45
	v_cvt_pk_bf16_f32 v45, v54, v55
	v_lshlrev_b32_e32 v54, 16, v148
	v_and_b32_e32 v55, 0xffff0000, v148
	v_pk_fma_f32 v[40:41], v[172:173], v[40:41], v[48:49]
	v_pk_fma_f32 v[38:39], v[170:171], v[38:39], v[46:47]
	v_pk_mul_f32 v[34:35], v[34:35], v[0:1] op_sel_hi:[1,0]
	v_lshlrev_b32_e32 v56, 16, v149
	v_and_b32_e32 v57, 0xffff0000, v149
	v_pk_mul_f32 v[36:37], v[36:37], v[0:1] op_sel_hi:[1,0]
	v_pk_fma_f32 v[48:49], v[166:167], v[34:35], v[54:55]
	v_mul_f32_e32 v0, v39, v39
	v_mul_f32_e32 v34, v41, v41
	v_pk_fma_f32 v[46:47], v[168:169], v[36:37], v[56:57]
	v_fmac_f32_e32 v0, v38, v38
	v_fmac_f32_e32 v34, v40, v40
	v_add_f32_e32 v0, v0, v34
	v_mul_f32_e32 v34, v49, v49
	v_mul_f32_e32 v35, v47, v47
	v_fmac_f32_e32 v34, v48, v48
	v_fmac_f32_e32 v35, v46, v46
	v_add_f32_e32 v34, v34, v35
	v_add_f32_e32 v0, v0, v34
	v_add_f32_e32 v0, v51, v0
	v_mov_b32_e32 v37, v0
	s_nop 1
	v_permlane16_swap_b32_e32 v37, v0
	v_add_u32_e32 v50, 0x90, v240
	v_add_u32_e32 v52, s29, v50
	v_ashrrev_i32_e32 v53, 31, v52
	v_lshlrev_b64 v[52:53], 11, v[52:53]
	v_lshl_add_u64 v[34:35], s[6:7], 0, v[52:53]
	s_waitcnt lgkmcnt(0)
	v_add_f32_e32 v0, v0, v37
	v_lshl_add_u64 v[52:53], v[220:221], 1, v[34:35]
	v_mov_b32_e32 v34, v0
	s_nop 1
	v_permlane32_swap_b32_e32 v34, v0
	global_store_dwordx4 v[52:53], v[42:45], off
	v_cvt_pk_bf16_f32 v36, v38, v39
	v_cvt_pk_bf16_f32 v37, v40, v41
	v_cvt_pk_bf16_f32 v38, v48, v49
	v_cvt_pk_bf16_f32 v39, v46, v47
	global_store_dwordx4 v[52:53], v[36:39], off offset:256
	s_and_saveexec_b64 s[8:9], s[38:39]
	s_cbranch_execz .LBB0_1694
	v_lshl_add_u32 v35, v50, 4, s28
	s_waitcnt lgkmcnt(0)
	v_add_f32_e32 v0, v0, v34
	ds_write_b32 v35, v0 offset:6144

.LBB0_1696:
	v_lshlrev_b32_e32 v38, 16, v142
	v_and_b32_e32 v39, 0xffff0000, v142
	v_lshlrev_b32_e32 v40, 16, v143
	v_and_b32_e32 v41, 0xffff0000, v143
	s_waitcnt lgkmcnt(0)
	v_pk_mul_f32 v[32:33], v[32:33], v[0:1] op_sel_hi:[1,0]
	v_pk_mul_f32 v[30:31], v[30:31], v[0:1] op_sel_hi:[1,0]
	v_lshlrev_b32_e32 v42, 16, v144
	v_and_b32_e32 v43, 0xffff0000, v144
	v_lshlrev_b32_e32 v44, 16, v145
	v_and_b32_e32 v45, 0xffff0000, v145
	v_pk_fma_f32 v[32:33], v[184:185], v[32:33], v[40:41]
	v_pk_fma_f32 v[30:31], v[182:183], v[30:31], v[38:39]
	v_pk_mul_f32 v[28:29], v[28:29], v[0:1] op_sel_hi:[1,0]
	v_pk_mul_f32 v[26:27], v[26:27], v[0:1] op_sel_hi:[1,0]
	v_pk_fma_f32 v[38:39], v[180:181], v[28:29], v[44:45]
	v_pk_fma_f32 v[28:29], v[178:179], v[26:27], v[42:43]
	v_mul_f32_e32 v26, v31, v31
	v_mul_f32_e32 v27, v33, v33
	v_fmac_f32_e32 v26, v30, v30
	v_fmac_f32_e32 v27, v32, v32
	v_add_f32_e32 v26, v26, v27
	v_mul_f32_e32 v27, v29, v29
	v_mul_f32_e32 v35, v39, v39
	v_fmac_f32_e32 v27, v28, v28
	v_fmac_f32_e32 v35, v38, v38
	v_add_f32_e32 v27, v27, v35
	v_add_f32_e32 v35, v26, v27
	v_cvt_pk_bf16_f32 v26, v30, v31
	v_cvt_pk_bf16_f32 v27, v32, v33
	v_lshlrev_b32_e32 v30, 16, v138
	v_and_b32_e32 v31, 0xffff0000, v138
	v_lshlrev_b32_e32 v32, 16, v139
	v_and_b32_e32 v33, 0xffff0000, v139
	v_pk_mul_f32 v[24:25], v[24:25], v[0:1] op_sel_hi:[1,0]
	v_pk_mul_f32 v[22:23], v[22:23], v[0:1] op_sel_hi:[1,0]
	v_cvt_pk_bf16_f32 v28, v28, v29
	v_cvt_pk_bf16_f32 v29, v38, v39
	v_lshlrev_b32_e32 v38, 16, v140
	v_and_b32_e32 v39, 0xffff0000, v140
	v_pk_fma_f32 v[24:25], v[172:173], v[24:25], v[32:33]
	v_pk_fma_f32 v[22:23], v[170:171], v[22:23], v[30:31]
	v_pk_mul_f32 v[18:19], v[18:19], v[0:1] op_sel_hi:[1,0]
	v_lshlrev_b32_e32 v40, 16, v141
	v_and_b32_e32 v41, 0xffff0000, v141
	v_pk_mul_f32 v[20:21], v[20:21], v[0:1] op_sel_hi:[1,0]
	v_pk_fma_f32 v[32:33], v[166:167], v[18:19], v[38:39]
	v_mul_f32_e32 v0, v23, v23
	v_mul_f32_e32 v18, v25, v25
	v_pk_fma_f32 v[30:31], v[168:169], v[20:21], v[40:41]
	v_fmac_f32_e32 v0, v22, v22
	v_fmac_f32_e32 v18, v24, v24
	v_add_f32_e32 v0, v0, v18
	v_mul_f32_e32 v18, v33, v33
	v_mul_f32_e32 v19, v31, v31
	v_fmac_f32_e32 v18, v32, v32
	v_fmac_f32_e32 v19, v30, v30
	v_add_f32_e32 v18, v18, v19
	v_add_f32_e32 v0, v0, v18
	v_add_f32_e32 v0, v35, v0
	v_mov_b32_e32 v21, v0
	s_nop 1
	v_permlane16_swap_b32_e32 v21, v0
	v_add_u32_e32 v34, 0xa0, v240
	v_add_u32_e32 v36, s29, v34
	v_ashrrev_i32_e32 v37, 31, v36
	v_lshlrev_b64 v[36:37], 11, v[36:37]
	v_lshl_add_u64 v[18:19], s[6:7], 0, v[36:37]
	s_waitcnt lgkmcnt(0)
	v_add_f32_e32 v0, v0, v21
	v_lshl_add_u64 v[36:37], v[220:221], 1, v[18:19]
	v_mov_b32_e32 v18, v0
	s_nop 1
	v_permlane32_swap_b32_e32 v18, v0
	global_store_dwordx4 v[36:37], v[26:29], off
	v_cvt_pk_bf16_f32 v20, v22, v23
	v_cvt_pk_bf16_f32 v21, v24, v25
	v_cvt_pk_bf16_f32 v22, v32, v33
	v_cvt_pk_bf16_f32 v23, v30, v31
	global_store_dwordx4 v[36:37], v[20:23], off offset:256
	s_and_saveexec_b64 s[8:9], s[38:39]
	s_cbranch_execz .LBB0_1698
	v_lshl_add_u32 v19, v34, 4, s28
	s_waitcnt lgkmcnt(0)
	v_add_f32_e32 v0, v0, v18
	ds_write_b32 v19, v0 offset:6144

.LBB0_1700:
	v_lshlrev_b32_e32 v22, 16, v126
	v_and_b32_e32 v23, 0xffff0000, v126
	v_lshlrev_b32_e32 v24, 16, v127
	v_and_b32_e32 v25, 0xffff0000, v127
	s_waitcnt lgkmcnt(0)
	v_pk_mul_f32 v[16:17], v[16:17], v[0:1] op_sel_hi:[1,0]
	v_pk_mul_f32 v[14:15], v[14:15], v[0:1] op_sel_hi:[1,0]
	v_lshlrev_b32_e32 v26, 16, v128
	v_and_b32_e32 v27, 0xffff0000, v128
	v_lshlrev_b32_e32 v28, 16, v129
	v_and_b32_e32 v29, 0xffff0000, v129
	v_pk_fma_f32 v[16:17], v[184:185], v[16:17], v[24:25]
	v_pk_fma_f32 v[14:15], v[182:183], v[14:15], v[22:23]
	v_pk_mul_f32 v[12:13], v[12:13], v[0:1] op_sel_hi:[1,0]
	v_pk_mul_f32 v[10:11], v[10:11], v[0:1] op_sel_hi:[1,0]
	v_pk_fma_f32 v[22:23], v[180:181], v[12:13], v[28:29]
	v_pk_fma_f32 v[12:13], v[178:179], v[10:11], v[26:27]
	v_mul_f32_e32 v10, v15, v15
	v_mul_f32_e32 v11, v17, v17
	v_fmac_f32_e32 v10, v14, v14
	v_fmac_f32_e32 v11, v16, v16
	v_add_f32_e32 v10, v10, v11
	v_mul_f32_e32 v11, v13, v13
	v_mul_f32_e32 v19, v23, v23
	v_fmac_f32_e32 v11, v12, v12
	v_fmac_f32_e32 v19, v22, v22
	v_add_f32_e32 v11, v11, v19
	v_add_f32_e32 v19, v10, v11
	v_cvt_pk_bf16_f32 v10, v14, v15
	v_cvt_pk_bf16_f32 v11, v16, v17
	v_lshlrev_b32_e32 v14, 16, v118
	v_and_b32_e32 v15, 0xffff0000, v118
	v_lshlrev_b32_e32 v16, 16, v119
	v_and_b32_e32 v17, 0xffff0000, v119
	v_pk_mul_f32 v[8:9], v[8:9], v[0:1] op_sel_hi:[1,0]
	v_pk_mul_f32 v[6:7], v[6:7], v[0:1] op_sel_hi:[1,0]
	v_cvt_pk_bf16_f32 v12, v12, v13
	v_cvt_pk_bf16_f32 v13, v22, v23
	v_lshlrev_b32_e32 v22, 16, v120
	v_and_b32_e32 v23, 0xffff0000, v120
	v_pk_fma_f32 v[8:9], v[172:173], v[8:9], v[16:17]
	v_pk_fma_f32 v[6:7], v[170:171], v[6:7], v[14:15]
	v_pk_mul_f32 v[2:3], v[2:3], v[0:1] op_sel_hi:[1,0]
	v_lshlrev_b32_e32 v24, 16, v121
	v_and_b32_e32 v25, 0xffff0000, v121
	v_pk_mul_f32 v[4:5], v[4:5], v[0:1] op_sel_hi:[1,0]
	v_pk_fma_f32 v[16:17], v[166:167], v[2:3], v[22:23]
	v_mul_f32_e32 v0, v7, v7
	v_mul_f32_e32 v2, v9, v9
	v_pk_fma_f32 v[14:15], v[168:169], v[4:5], v[24:25]
	v_fmac_f32_e32 v0, v6, v6
	v_fmac_f32_e32 v2, v8, v8
	v_add_f32_e32 v0, v0, v2
	v_mul_f32_e32 v2, v17, v17
	v_mul_f32_e32 v3, v15, v15
	v_fmac_f32_e32 v2, v16, v16
	v_fmac_f32_e32 v3, v14, v14
	v_add_f32_e32 v2, v2, v3
	v_add_f32_e32 v0, v0, v2
	v_add_f32_e32 v0, v19, v0
	v_mov_b32_e32 v5, v0
	s_nop 1
	v_permlane16_swap_b32_e32 v5, v0
	v_add_u32_e32 v18, 0xb0, v240
	v_add_u32_e32 v20, s29, v18
	v_ashrrev_i32_e32 v21, 31, v20
	v_lshlrev_b64 v[20:21], 11, v[20:21]
	v_lshl_add_u64 v[2:3], s[6:7], 0, v[20:21]
	s_waitcnt lgkmcnt(0)
	v_add_f32_e32 v0, v0, v5
	v_lshl_add_u64 v[20:21], v[220:221], 1, v[2:3]
	v_mov_b32_e32 v2, v0
	s_nop 1
	v_permlane32_swap_b32_e32 v2, v0
	global_store_dwordx4 v[20:21], v[10:13], off
	v_cvt_pk_bf16_f32 v4, v6, v7
	v_cvt_pk_bf16_f32 v5, v8, v9
	v_cvt_pk_bf16_f32 v6, v16, v17
	v_cvt_pk_bf16_f32 v7, v14, v15
	global_store_dwordx4 v[20:21], v[4:7], off offset:256
	s_and_saveexec_b64 s[6:7], s[38:39]
	s_cbranch_execz .LBB0_1702
	v_lshl_add_u32 v3, v18, 4, s28
	s_waitcnt lgkmcnt(0)
	v_add_f32_e32 v0, v0, v2
	ds_write_b32 v3, v0 offset:6144

.LBB0_2281:
	v_mov_b32_e32 v0, v123
	s_nop 1
	v_permlane32_swap_b32_e32 v0, v123
	v_lshl_add_u64 v[34:35], s[10:11], 0, v[128:129]
	s_lshl_b32 s96, s21, 1
	v_lshl_add_u64 v[34:35], v[34:35], 0, s[96:97]
	v_mov_b32_e32 v127, v1
	s_waitcnt lgkmcnt(0)
	v_add_f32_e32 v0, v123, v0
	v_div_scale_f32 v36, s[14:15], v0, v0, 1.0
	v_rcp_f32_e32 v37, v36
	v_div_scale_f32 v38, vcc, 1.0, v0, 1.0
	v_lshl_add_u64 v[34:35], v[34:35], 0, v[126:127]
	v_fma_f32 v39, -v36, v37, 1.0
	v_fmac_f32_e32 v37, v39, v37
	v_mul_f32_e32 v39, v38, v37
	v_fma_f32 v40, -v36, v39, v38
	v_fmac_f32_e32 v39, v40, v37
	v_fma_f32 v36, -v36, v39, v38
	v_div_fmas_f32 v36, v36, v37, v39
	v_div_fixup_f32 v0, v36, v0, 1.0
	v_mov_b32_e32 v36, v2
	v_mov_b32_e32 v37, v4
	v_pk_mul_f32 v[36:37], v[36:37], v[0:1] op_sel_hi:[1,0]
	v_mov_b32_e32 v4, v3
	v_pk_mul_f32 v[2:3], v[4:5], v[0:1] op_sel_hi:[1,0]
	v_and_b32_sdwa v4, v37, v228 dst_sel:DWORD dst_unused:UNUSED_PAD src0_sel:WORD_1 src1_sel:DWORD
	v_and_b32_sdwa v5, v36, v228 dst_sel:DWORD dst_unused:UNUSED_PAD src0_sel:WORD_1 src1_sel:DWORD
	v_add3_u32 v5, v36, v5, s55
	v_add3_u32 v4, v37, v4, s55
	v_and_b32_sdwa v36, v3, v228 dst_sel:DWORD dst_unused:UNUSED_PAD src0_sel:WORD_1 src1_sel:DWORD
	v_and_b32_sdwa v37, v2, v228 dst_sel:DWORD dst_unused:UNUSED_PAD src0_sel:WORD_1 src1_sel:DWORD
	v_add3_u32 v3, v3, v36, s55
	v_add3_u32 v2, v2, v37, s55
	v_and_b32_e32 v3, 0xffff0000, v3
	v_and_b32_e32 v2, 0xffff0000, v2
	v_or_b32_sdwa v3, v3, v4 dst_sel:DWORD dst_unused:UNUSED_PAD src0_sel:DWORD src1_sel:WORD_1
	v_or_b32_sdwa v2, v2, v5 dst_sel:DWORD dst_unused:UNUSED_PAD src0_sel:DWORD src1_sel:WORD_1
	global_store_dwordx2 v[34:35], v[2:3], off
	v_mov_b32_e32 v2, v6
	v_mov_b32_e32 v3, v8
	v_pk_mul_f32 v[2:3], v[2:3], v[0:1] op_sel_hi:[1,0]
	v_mov_b32_e32 v8, v7
	v_pk_mul_f32 v[4:5], v[8:9], v[0:1] op_sel_hi:[1,0]
	v_and_b32_sdwa v6, v3, v228 dst_sel:DWORD dst_unused:UNUSED_PAD src0_sel:WORD_1 src1_sel:DWORD
	v_and_b32_sdwa v7, v2, v228 dst_sel:DWORD dst_unused:UNUSED_PAD src0_sel:WORD_1 src1_sel:DWORD
	v_add3_u32 v2, v2, v7, s55
	v_add3_u32 v3, v3, v6, s55
	v_and_b32_sdwa v6, v5, v228 dst_sel:DWORD dst_unused:UNUSED_PAD src0_sel:WORD_1 src1_sel:DWORD
	v_and_b32_sdwa v7, v4, v228 dst_sel:DWORD dst_unused:UNUSED_PAD src0_sel:WORD_1 src1_sel:DWORD
	v_add3_u32 v5, v5, v6, s55
	v_add3_u32 v4, v4, v7, s55
	v_and_b32_e32 v5, 0xffff0000, v5
	v_and_b32_e32 v4, 0xffff0000, v4
	v_or_b32_sdwa v3, v5, v3 dst_sel:DWORD dst_unused:UNUSED_PAD src0_sel:DWORD src1_sel:WORD_1
	v_or_b32_sdwa v2, v4, v2 dst_sel:DWORD dst_unused:UNUSED_PAD src0_sel:DWORD src1_sel:WORD_1
	global_store_dwordx2 v[34:35], v[2:3], off offset:16
	v_mov_b32_e32 v2, v10
	v_mov_b32_e32 v3, v12
	v_pk_mul_f32 v[2:3], v[2:3], v[0:1] op_sel_hi:[1,0]
	v_mov_b32_e32 v12, v11
	v_pk_mul_f32 v[4:5], v[12:13], v[0:1] op_sel_hi:[1,0]
	v_and_b32_sdwa v6, v3, v228 dst_sel:DWORD dst_unused:UNUSED_PAD src0_sel:WORD_1 src1_sel:DWORD
	v_and_b32_sdwa v7, v2, v228 dst_sel:DWORD dst_unused:UNUSED_PAD src0_sel:WORD_1 src1_sel:DWORD
	v_add3_u32 v2, v2, v7, s55
	v_add3_u32 v3, v3, v6, s55
	v_and_b32_sdwa v6, v5, v228 dst_sel:DWORD dst_unused:UNUSED_PAD src0_sel:WORD_1 src1_sel:DWORD
	v_and_b32_sdwa v7, v4, v228 dst_sel:DWORD dst_unused:UNUSED_PAD src0_sel:WORD_1 src1_sel:DWORD
	v_add3_u32 v5, v5, v6, s55
	v_add3_u32 v4, v4, v7, s55
	v_and_b32_e32 v5, 0xffff0000, v5
	v_and_b32_e32 v4, 0xffff0000, v4
	v_or_b32_sdwa v3, v5, v3 dst_sel:DWORD dst_unused:UNUSED_PAD src0_sel:DWORD src1_sel:WORD_1
	v_or_b32_sdwa v2, v4, v2 dst_sel:DWORD dst_unused:UNUSED_PAD src0_sel:DWORD src1_sel:WORD_1
	global_store_dwordx2 v[34:35], v[2:3], off offset:32
	v_mov_b32_e32 v2, v14
	v_mov_b32_e32 v3, v16
	v_pk_mul_f32 v[2:3], v[2:3], v[0:1] op_sel_hi:[1,0]
	v_mov_b32_e32 v16, v15
	v_pk_mul_f32 v[4:5], v[16:17], v[0:1] op_sel_hi:[1,0]
	v_and_b32_sdwa v6, v3, v228 dst_sel:DWORD dst_unused:UNUSED_PAD src0_sel:WORD_1 src1_sel:DWORD
	v_and_b32_sdwa v7, v2, v228 dst_sel:DWORD dst_unused:UNUSED_PAD src0_sel:WORD_1 src1_sel:DWORD
	v_add3_u32 v2, v2, v7, s55
	v_add3_u32 v3, v3, v6, s55
	v_and_b32_sdwa v6, v5, v228 dst_sel:DWORD dst_unused:UNUSED_PAD src0_sel:WORD_1 src1_sel:DWORD
	v_and_b32_sdwa v7, v4, v228 dst_sel:DWORD dst_unused:UNUSED_PAD src0_sel:WORD_1 src1_sel:DWORD
	v_add3_u32 v5, v5, v6, s55
	v_add3_u32 v4, v4, v7, s55
	v_and_b32_e32 v5, 0xffff0000, v5
	v_and_b32_e32 v4, 0xffff0000, v4
	v_or_b32_sdwa v3, v5, v3 dst_sel:DWORD dst_unused:UNUSED_PAD src0_sel:DWORD src1_sel:WORD_1
	v_or_b32_sdwa v2, v4, v2 dst_sel:DWORD dst_unused:UNUSED_PAD src0_sel:DWORD src1_sel:WORD_1
	global_store_dwordx2 v[34:35], v[2:3], off offset:48
	v_mov_b32_e32 v2, v18
	v_mov_b32_e32 v3, v20
	v_pk_mul_f32 v[2:3], v[2:3], v[0:1] op_sel_hi:[1,0]
	v_mov_b32_e32 v20, v19
	v_pk_mul_f32 v[4:5], v[20:21], v[0:1] op_sel_hi:[1,0]
	v_and_b32_sdwa v6, v3, v228 dst_sel:DWORD dst_unused:UNUSED_PAD src0_sel:WORD_1 src1_sel:DWORD
	v_and_b32_sdwa v7, v2, v228 dst_sel:DWORD dst_unused:UNUSED_PAD src0_sel:WORD_1 src1_sel:DWORD
	v_add3_u32 v2, v2, v7, s55
	v_add3_u32 v3, v3, v6, s55
	v_and_b32_sdwa v6, v5, v228 dst_sel:DWORD dst_unused:UNUSED_PAD src0_sel:WORD_1 src1_sel:DWORD
	v_and_b32_sdwa v7, v4, v228 dst_sel:DWORD dst_unused:UNUSED_PAD src0_sel:WORD_1 src1_sel:DWORD
	v_add3_u32 v5, v5, v6, s55
	v_add3_u32 v4, v4, v7, s55
	v_and_b32_e32 v5, 0xffff0000, v5
	v_and_b32_e32 v4, 0xffff0000, v4
	v_or_b32_sdwa v3, v5, v3 dst_sel:DWORD dst_unused:UNUSED_PAD src0_sel:DWORD src1_sel:WORD_1
	v_or_b32_sdwa v2, v4, v2 dst_sel:DWORD dst_unused:UNUSED_PAD src0_sel:DWORD src1_sel:WORD_1
	global_store_dwordx2 v[34:35], v[2:3], off offset:64
	v_mov_b32_e32 v2, v22
	v_mov_b32_e32 v3, v24
	v_pk_mul_f32 v[2:3], v[2:3], v[0:1] op_sel_hi:[1,0]
	v_mov_b32_e32 v24, v23
	v_pk_mul_f32 v[4:5], v[24:25], v[0:1] op_sel_hi:[1,0]
	v_and_b32_sdwa v6, v3, v228 dst_sel:DWORD dst_unused:UNUSED_PAD src0_sel:WORD_1 src1_sel:DWORD
	v_and_b32_sdwa v7, v2, v228 dst_sel:DWORD dst_unused:UNUSED_PAD src0_sel:WORD_1 src1_sel:DWORD
	v_add3_u32 v2, v2, v7, s55
	v_add3_u32 v3, v3, v6, s55
	v_and_b32_sdwa v6, v5, v228 dst_sel:DWORD dst_unused:UNUSED_PAD src0_sel:WORD_1 src1_sel:DWORD
	v_and_b32_sdwa v7, v4, v228 dst_sel:DWORD dst_unused:UNUSED_PAD src0_sel:WORD_1 src1_sel:DWORD
	v_add3_u32 v5, v5, v6, s55
	v_add3_u32 v4, v4, v7, s55
	v_and_b32_e32 v5, 0xffff0000, v5
	v_and_b32_e32 v4, 0xffff0000, v4
	v_or_b32_sdwa v3, v5, v3 dst_sel:DWORD dst_unused:UNUSED_PAD src0_sel:DWORD src1_sel:WORD_1
	v_or_b32_sdwa v2, v4, v2 dst_sel:DWORD dst_unused:UNUSED_PAD src0_sel:DWORD src1_sel:WORD_1
	global_store_dwordx2 v[34:35], v[2:3], off offset:80
	v_mov_b32_e32 v2, v26
	v_mov_b32_e32 v3, v28
	v_pk_mul_f32 v[2:3], v[2:3], v[0:1] op_sel_hi:[1,0]
	v_mov_b32_e32 v28, v27
	v_pk_mul_f32 v[4:5], v[28:29], v[0:1] op_sel_hi:[1,0]
	v_and_b32_sdwa v6, v3, v228 dst_sel:DWORD dst_unused:UNUSED_PAD src0_sel:WORD_1 src1_sel:DWORD
	v_and_b32_sdwa v7, v2, v228 dst_sel:DWORD dst_unused:UNUSED_PAD src0_sel:WORD_1 src1_sel:DWORD
	v_add3_u32 v2, v2, v7, s55
	v_add3_u32 v3, v3, v6, s55
	v_and_b32_sdwa v6, v5, v228 dst_sel:DWORD dst_unused:UNUSED_PAD src0_sel:WORD_1 src1_sel:DWORD
	v_and_b32_sdwa v7, v4, v228 dst_sel:DWORD dst_unused:UNUSED_PAD src0_sel:WORD_1 src1_sel:DWORD
	v_add3_u32 v5, v5, v6, s55
	v_add3_u32 v4, v4, v7, s55
	v_and_b32_e32 v5, 0xffff0000, v5
	v_and_b32_e32 v4, 0xffff0000, v4
	v_or_b32_sdwa v3, v5, v3 dst_sel:DWORD dst_unused:UNUSED_PAD src0_sel:DWORD src1_sel:WORD_1
	v_or_b32_sdwa v2, v4, v2 dst_sel:DWORD dst_unused:UNUSED_PAD src0_sel:DWORD src1_sel:WORD_1
	global_store_dwordx2 v[34:35], v[2:3], off offset:96
	v_mov_b32_e32 v2, v30
	v_mov_b32_e32 v3, v32
	v_pk_mul_f32 v[2:3], v[2:3], v[0:1] op_sel_hi:[1,0]
	v_mov_b32_e32 v32, v31
	v_pk_mul_f32 v[4:5], v[32:33], v[0:1] op_sel_hi:[1,0]
	v_and_b32_sdwa v0, v3, v228 dst_sel:DWORD dst_unused:UNUSED_PAD src0_sel:WORD_1 src1_sel:DWORD
	v_and_b32_sdwa v6, v2, v228 dst_sel:DWORD dst_unused:UNUSED_PAD src0_sel:WORD_1 src1_sel:DWORD
	v_add3_u32 v2, v2, v6, s55
	v_add3_u32 v0, v3, v0, s55
	v_and_b32_sdwa v3, v5, v228 dst_sel:DWORD dst_unused:UNUSED_PAD src0_sel:WORD_1 src1_sel:DWORD
	v_and_b32_sdwa v6, v4, v228 dst_sel:DWORD dst_unused:UNUSED_PAD src0_sel:WORD_1 src1_sel:DWORD
	v_add3_u32 v3, v5, v3, s55
	v_add3_u32 v4, v4, v6, s55
	v_and_b32_e32 v3, 0xffff0000, v3
	v_and_b32_e32 v4, 0xffff0000, v4
	v_or_b32_sdwa v3, v3, v0 dst_sel:DWORD dst_unused:UNUSED_PAD src0_sel:DWORD src1_sel:WORD_1
	v_or_b32_sdwa v2, v4, v2 dst_sel:DWORD dst_unused:UNUSED_PAD src0_sel:DWORD src1_sel:WORD_1
	s_and_b64 vcc, exec, s[12:13]
	s_mov_b32 s14, s20
	global_store_dwordx2 v[34:35], v[2:3], off offset:112
	s_cbranch_vccnz .LBB0_2292

.LBB0_2375:
	s_lshl_b32 s4, s17, 5
	s_add_u32 s6, s6, s28
	s_addc_u32 s7, s7, s29
	s_lshl_b32 s8, s16, 8
	v_lshrrev_b32_e32 v122, 1, v0
	s_or_b32 s4, s8, s4
	s_lshl_b32 s35, s94, 8
	v_and_or_b32 v220, v122, 24, s4
	v_add_u32_e32 v122, s35, v240
	v_ashrrev_i32_e32 v221, 31, v220
	v_ashrrev_i32_e32 v123, 31, v122
	v_lshl_add_u64 v[124:125], v[220:221], 1, s[6:7]
	v_lshlrev_b64 v[224:225], 11, v[122:123]
	v_lshl_add_u64 v[126:127], v[124:125], 0, v[224:225]
	s_barrier
	global_load_dwordx4 v[206:209], v[126:127], off
	global_load_dwordx4 v[202:205], v[126:127], off offset:256
	v_or_b32_e32 v126, 16, v122
	v_ashrrev_i32_e32 v127, 31, v126
	v_lshlrev_b64 v[126:127], 11, v[126:127]
	v_lshl_add_u64 v[126:127], v[124:125], 0, v[126:127]
	global_load_dwordx4 v[198:201], v[126:127], off
	global_load_dwordx4 v[194:197], v[126:127], off offset:256
	v_or_b32_e32 v126, 32, v122
	v_ashrrev_i32_e32 v127, 31, v126
	v_lshlrev_b64 v[126:127], 11, v[126:127]
	v_lshl_add_u64 v[126:127], v[124:125], 0, v[126:127]
	global_load_dwordx4 v[190:193], v[126:127], off
	global_load_dwordx4 v[186:189], v[126:127], off offset:256
	v_or_b32_e32 v126, 48, v122
	v_ashrrev_i32_e32 v127, 31, v126
	v_lshlrev_b64 v[126:127], 11, v[126:127]
	v_lshl_add_u64 v[126:127], v[124:125], 0, v[126:127]
	global_load_dwordx4 v[174:177], v[126:127], off
	global_load_dwordx4 v[162:165], v[126:127], off offset:256
	v_add_u32_e32 v126, 0x80, v122
	v_ashrrev_i32_e32 v127, 31, v126
	v_lshlrev_b64 v[126:127], 11, v[126:127]
	v_lshl_add_u64 v[126:127], v[124:125], 0, v[126:127]
	global_load_dwordx4 v[158:161], v[126:127], off
	global_load_dwordx4 v[154:157], v[126:127], off offset:256
	v_add_u32_e32 v126, 0x90, v122
	v_ashrrev_i32_e32 v127, 31, v126
	v_lshlrev_b64 v[126:127], 11, v[126:127]
	v_lshl_add_u64 v[126:127], v[124:125], 0, v[126:127]
	global_load_dwordx4 v[150:153], v[126:127], off
	global_load_dwordx4 v[146:149], v[126:127], off offset:256
	v_add_u32_e32 v126, 0xa0, v122
	v_add_u32_e32 v122, 0xb0, v122
	v_ashrrev_i32_e32 v127, 31, v126
	v_ashrrev_i32_e32 v123, 31, v122
	v_lshlrev_b64 v[126:127], 11, v[126:127]
	v_lshlrev_b64 v[122:123], 11, v[122:123]
	v_lshl_add_u64 v[126:127], v[124:125], 0, v[126:127]
	v_lshl_add_u64 v[122:123], v[124:125], 0, v[122:123]
	global_load_dwordx4 v[142:145], v[126:127], off
	global_load_dwordx4 v[138:141], v[126:127], off offset:256
	s_nop 0
	global_load_dwordx4 v[126:129], v[122:123], off
	s_nop 0
	global_load_dwordx4 v[122:125], v[122:123], off offset:256
	v_and_b32_e32 v168, 64, v231
	v_xor_b32_e32 v167, 16, v231
	v_add_u32_e32 v168, 64, v168
	v_cmp_lt_i32_e32 vcc, v167, v168
	v_mul_f32_e32 v169, v137, v137
	v_fmac_f32_e32 v169, v136, v136
	v_cndmask_b32_e32 v167, v231, v167, vcc
	v_lshlrev_b32_e32 v241, 2, v167
	v_mul_f32_e32 v167, v135, v135
	v_fmac_f32_e32 v167, v134, v134
	v_add_f32_e32 v167, v167, v169
	v_mul_f32_e32 v169, v131, v131
	v_mul_f32_e32 v170, v133, v133
	v_fmac_f32_e32 v169, v130, v130
	v_fmac_f32_e32 v170, v132, v132
	v_add_f32_e32 v169, v169, v170
	v_add_f32_e32 v167, v169, v167
	v_mul_f32_e32 v169, v119, v119
	v_mul_f32_e32 v170, v121, v121
	v_fmac_f32_e32 v169, v118, v118
	v_fmac_f32_e32 v170, v120, v120
	v_add_f32_e32 v169, v169, v170
	v_add_f32_e32 v167, v169, v167
	v_mul_f32_e32 v169, v115, v115
	v_mul_f32_e32 v170, v117, v117
	v_fmac_f32_e32 v169, v114, v114
	v_fmac_f32_e32 v170, v116, v116
	v_add_f32_e32 v169, v169, v170
	v_add_f32_e32 v167, v169, v167
	v_mov_b32_e32 v169, v167
	s_nop 1
	v_permlane16_swap_b32_e32 v169, v167
	v_xor_b32_e32 v170, 32, v231
	v_cmp_lt_i32_e32 vcc, v170, v168
	s_lshl_b32 s4, s17, 2
	s_add_i32 s34, s4, 0
	v_cndmask_b32_e32 v168, v231, v170, vcc
	v_lshlrev_b32_e32 v242, 2, v168
	s_waitcnt lgkmcnt(0)
	v_add_f32_e32 v168, v167, v169
	v_mov_b32_e32 v169, v168
	s_nop 1
	v_permlane32_swap_b32_e32 v169, v168
	v_and_b32_e32 v167, 63, v0
	v_cmp_gt_u32_e64 s[40:41], 16, v167
	s_and_saveexec_b64 s[6:7], s[40:41]
	s_load_dwordx2 s[90:91], s[0:1], 0xb0
	v_readlane_b32 s36, v255, 32
	v_readlane_b32 s64, v252, 3
	v_readlane_b32 s65, v255, 10
	v_readlane_b32 s68, v255, 11
	v_readlane_b32 s74, v255, 12
	v_readlane_b32 s95, v255, 13
	s_movk_i32 s92, 0x2b20
	v_readlane_b32 s33, v255, 22
	v_readlane_b32 s37, v255, 33
	s_cbranch_execz .LBB0_2377
	s_lshl_b32 s4, s93, 10
	s_add_i32 s4, s34, s4
	s_waitcnt lgkmcnt(0)
	v_add_f32_e32 v168, v168, v169
	v_lshl_add_u32 v169, v166, 4, s4
	ds_write_b32 v169, v168
.LBB0_2377:
	s_or_b64 exec, exec, s[6:7]
	v_mul_f32_e32 v168, v111, v111
	s_waitcnt lgkmcnt(0)
	v_mul_f32_e32 v169, v113, v113
	v_fmac_f32_e32 v168, v110, v110
	v_fmac_f32_e32 v169, v112, v112
	v_add_f32_e32 v168, v168, v169
	v_mul_f32_e32 v169, v107, v107
	v_mul_f32_e32 v170, v109, v109
	v_fmac_f32_e32 v169, v106, v106
	v_fmac_f32_e32 v170, v108, v108
	v_add_f32_e32 v169, v169, v170
	v_add_f32_e32 v168, v169, v168
	v_mul_f32_e32 v169, v103, v103
	v_mul_f32_e32 v170, v105, v105
	v_fmac_f32_e32 v169, v102, v102
	v_fmac_f32_e32 v170, v104, v104
	v_add_f32_e32 v169, v169, v170
	v_add_f32_e32 v168, v169, v168
	v_mul_f32_e32 v169, v99, v99
	v_mul_f32_e32 v170, v101, v101
	v_fmac_f32_e32 v169, v98, v98
	v_fmac_f32_e32 v170, v100, v100
	v_add_f32_e32 v169, v169, v170
	v_add_f32_e32 v168, v169, v168
	v_mov_b32_e32 v169, v168
	s_nop 1
	v_permlane16_swap_b32_e32 v169, v168
	s_waitcnt lgkmcnt(0)
	v_add_f32_e32 v168, v168, v169
	v_mov_b32_e32 v169, v168
	s_nop 1
	v_permlane32_swap_b32_e32 v169, v168
	s_and_saveexec_b64 s[6:7], s[40:41]
	s_cbranch_execz .LBB0_2379
	s_lshl_b32 s4, s93, 10
	s_add_i32 s4, s34, s4
	s_waitcnt lgkmcnt(0)
	v_add_f32_e32 v168, v168, v169
	v_lshl_add_u32 v169, v166, 4, s4
	ds_write_b32 v169, v168 offset:256
.LBB0_2379:
	s_or_b64 exec, exec, s[6:7]
	v_mul_f32_e32 v168, v95, v95
	s_waitcnt lgkmcnt(0)
	v_mul_f32_e32 v169, v97, v97
	v_fmac_f32_e32 v168, v94, v94
	v_fmac_f32_e32 v169, v96, v96
	v_add_f32_e32 v168, v168, v169
	v_mul_f32_e32 v169, v91, v91
	v_mul_f32_e32 v170, v93, v93
	v_fmac_f32_e32 v169, v90, v90
	v_fmac_f32_e32 v170, v92, v92
	v_add_f32_e32 v169, v169, v170
	v_add_f32_e32 v168, v169, v168
	v_mul_f32_e32 v169, v87, v87
	v_mul_f32_e32 v170, v89, v89
	v_fmac_f32_e32 v169, v86, v86
	v_fmac_f32_e32 v170, v88, v88
	v_add_f32_e32 v169, v169, v170
	v_add_f32_e32 v168, v169, v168
	v_mul_f32_e32 v169, v83, v83
	v_mul_f32_e32 v170, v85, v85
	v_fmac_f32_e32 v169, v82, v82
	v_fmac_f32_e32 v170, v84, v84
	v_add_f32_e32 v169, v169, v170
	v_add_f32_e32 v168, v169, v168
	v_mov_b32_e32 v169, v168
	s_nop 1
	v_permlane16_swap_b32_e32 v169, v168
	s_waitcnt lgkmcnt(0)
	v_add_f32_e32 v168, v168, v169
	v_mov_b32_e32 v169, v168
	s_nop 1
	v_permlane32_swap_b32_e32 v169, v168
	s_and_saveexec_b64 s[6:7], s[40:41]
	s_cbranch_execz .LBB0_2381
	s_lshl_b32 s4, s93, 10
	s_add_i32 s4, s34, s4
	s_waitcnt lgkmcnt(0)
	v_add_f32_e32 v168, v168, v169
	v_lshl_add_u32 v169, v166, 4, s4
	ds_write_b32 v169, v168 offset:512
.LBB0_2381:
	s_or_b64 exec, exec, s[6:7]
	v_mul_f32_e32 v168, v79, v79
	s_waitcnt lgkmcnt(0)
	v_mul_f32_e32 v169, v81, v81
	v_fmac_f32_e32 v168, v78, v78
	v_fmac_f32_e32 v169, v80, v80
	v_add_f32_e32 v168, v168, v169
	v_mul_f32_e32 v169, v75, v75
	v_mul_f32_e32 v170, v77, v77
	v_fmac_f32_e32 v169, v74, v74
	v_fmac_f32_e32 v170, v76, v76
	v_add_f32_e32 v169, v169, v170
	v_add_f32_e32 v168, v169, v168
	v_mul_f32_e32 v169, v71, v71
	v_mul_f32_e32 v170, v73, v73
	v_fmac_f32_e32 v169, v70, v70
	v_fmac_f32_e32 v170, v72, v72
	v_add_f32_e32 v169, v169, v170
	v_add_f32_e32 v168, v169, v168
	v_mul_f32_e32 v169, v67, v67
	v_mul_f32_e32 v170, v69, v69
	v_fmac_f32_e32 v169, v66, v66
	v_fmac_f32_e32 v170, v68, v68
	v_add_f32_e32 v169, v169, v170
	v_add_f32_e32 v168, v169, v168
	v_mov_b32_e32 v169, v168
	s_nop 1
	v_permlane16_swap_b32_e32 v169, v168
	s_waitcnt lgkmcnt(0)
	v_add_f32_e32 v168, v168, v169
	v_mov_b32_e32 v169, v168
	s_nop 1
	v_permlane32_swap_b32_e32 v169, v168
	s_and_saveexec_b64 s[6:7], s[40:41]
	s_cbranch_execz .LBB0_2383
	s_lshl_b32 s4, s93, 10
	s_add_i32 s4, s34, s4
	s_waitcnt lgkmcnt(0)
	v_add_f32_e32 v168, v168, v169
	v_lshl_add_u32 v169, v166, 4, s4
	ds_write_b32 v169, v168 offset:768
.LBB0_2383:
	s_or_b64 exec, exec, s[6:7]
	v_mul_f32_e32 v168, v63, v63
	s_waitcnt lgkmcnt(0)
	v_mul_f32_e32 v169, v65, v65
	v_fmac_f32_e32 v168, v62, v62
	v_fmac_f32_e32 v169, v64, v64
	v_add_f32_e32 v168, v168, v169
	v_mul_f32_e32 v169, v59, v59
	v_mul_f32_e32 v170, v61, v61
	v_fmac_f32_e32 v169, v58, v58
	v_fmac_f32_e32 v170, v60, v60
	v_add_f32_e32 v169, v169, v170
	v_add_f32_e32 v168, v169, v168
	v_mul_f32_e32 v169, v55, v55
	v_mul_f32_e32 v170, v57, v57
	v_fmac_f32_e32 v169, v54, v54
	v_fmac_f32_e32 v170, v56, v56
	v_add_f32_e32 v169, v169, v170
	v_add_f32_e32 v168, v169, v168
	v_mul_f32_e32 v169, v51, v51
	v_mul_f32_e32 v170, v53, v53
	v_fmac_f32_e32 v169, v50, v50
	v_fmac_f32_e32 v170, v52, v52
	v_add_f32_e32 v169, v169, v170
	v_add_f32_e32 v168, v169, v168
	v_mov_b32_e32 v169, v168
	s_nop 1
	v_permlane16_swap_b32_e32 v169, v168
	s_waitcnt lgkmcnt(0)
	v_add_f32_e32 v168, v168, v169
	v_mov_b32_e32 v169, v168
	s_nop 1
	v_permlane32_swap_b32_e32 v169, v168
	s_and_saveexec_b64 s[6:7], s[40:41]
	s_cbranch_execz .LBB0_2385
	s_lshl_b32 s4, s93, 10
	s_add_i32 s4, s34, s4
	s_waitcnt lgkmcnt(0)
	v_add_f32_e32 v168, v168, v169
	v_lshl_add_u32 v169, v166, 4, s4
	ds_write_b32 v169, v168 offset:2048
.LBB0_2385:
	s_or_b64 exec, exec, s[6:7]
	v_mul_f32_e32 v168, v47, v47
	s_waitcnt lgkmcnt(0)
	v_mul_f32_e32 v169, v49, v49
	v_fmac_f32_e32 v168, v46, v46
	v_fmac_f32_e32 v169, v48, v48
	v_add_f32_e32 v168, v168, v169
	v_mul_f32_e32 v169, v43, v43
	v_mul_f32_e32 v170, v45, v45
	v_fmac_f32_e32 v169, v42, v42
	v_fmac_f32_e32 v170, v44, v44
	v_add_f32_e32 v169, v169, v170
	v_add_f32_e32 v168, v169, v168
	v_mul_f32_e32 v169, v39, v39
	v_mul_f32_e32 v170, v41, v41
	v_fmac_f32_e32 v169, v38, v38
	v_fmac_f32_e32 v170, v40, v40
	v_add_f32_e32 v169, v169, v170
	v_add_f32_e32 v168, v169, v168
	v_mul_f32_e32 v169, v35, v35
	v_mul_f32_e32 v170, v37, v37
	v_fmac_f32_e32 v169, v34, v34
	v_fmac_f32_e32 v170, v36, v36
	v_add_f32_e32 v169, v169, v170
	v_add_f32_e32 v168, v169, v168
	v_mov_b32_e32 v169, v168
	s_nop 1
	v_permlane16_swap_b32_e32 v169, v168
	s_waitcnt lgkmcnt(0)
	v_add_f32_e32 v168, v168, v169
	v_mov_b32_e32 v169, v168
	s_nop 1
	v_permlane32_swap_b32_e32 v169, v168
	s_and_saveexec_b64 s[6:7], s[40:41]
	s_cbranch_execz .LBB0_2387
	s_lshl_b32 s4, s93, 10
	s_add_i32 s4, s34, s4
	s_waitcnt lgkmcnt(0)
	v_add_f32_e32 v168, v168, v169
	v_lshl_add_u32 v169, v166, 4, s4
	ds_write_b32 v169, v168 offset:2304
.LBB0_2387:
	s_or_b64 exec, exec, s[6:7]
	v_mul_f32_e32 v168, v31, v31
	s_waitcnt lgkmcnt(0)
	v_mul_f32_e32 v169, v33, v33
	v_fmac_f32_e32 v168, v30, v30
	v_fmac_f32_e32 v169, v32, v32
	v_add_f32_e32 v168, v168, v169
	v_mul_f32_e32 v169, v27, v27
	v_mul_f32_e32 v170, v29, v29
	v_fmac_f32_e32 v169, v26, v26
	v_fmac_f32_e32 v170, v28, v28
	v_add_f32_e32 v169, v169, v170
	v_add_f32_e32 v168, v169, v168
	v_mul_f32_e32 v169, v23, v23
	v_mul_f32_e32 v170, v25, v25
	v_fmac_f32_e32 v169, v22, v22
	v_fmac_f32_e32 v170, v24, v24
	v_add_f32_e32 v169, v169, v170
	v_add_f32_e32 v168, v169, v168
	v_mul_f32_e32 v169, v19, v19
	v_mul_f32_e32 v170, v21, v21
	v_fmac_f32_e32 v169, v18, v18
	v_fmac_f32_e32 v170, v20, v20
	v_add_f32_e32 v169, v169, v170
	v_add_f32_e32 v168, v169, v168
	v_mov_b32_e32 v169, v168
	s_nop 1
	v_permlane16_swap_b32_e32 v169, v168
	s_waitcnt lgkmcnt(0)
	v_add_f32_e32 v168, v168, v169
	v_mov_b32_e32 v169, v168
	s_nop 1
	v_permlane32_swap_b32_e32 v169, v168
	s_and_saveexec_b64 s[6:7], s[40:41]
	s_cbranch_execz .LBB0_2389
	s_lshl_b32 s4, s93, 10
	s_add_i32 s4, s34, s4
	s_waitcnt lgkmcnt(0)
	v_add_f32_e32 v168, v168, v169
	v_lshl_add_u32 v169, v166, 4, s4
	ds_write_b32 v169, v168 offset:2560
.LBB0_2389:
	s_or_b64 exec, exec, s[6:7]
	v_mul_f32_e32 v168, v15, v15
	s_waitcnt lgkmcnt(0)
	v_mul_f32_e32 v169, v17, v17
	v_fmac_f32_e32 v168, v14, v14
	v_fmac_f32_e32 v169, v16, v16
	v_add_f32_e32 v168, v168, v169
	v_mul_f32_e32 v169, v11, v11
	v_mul_f32_e32 v170, v13, v13
	v_fmac_f32_e32 v169, v10, v10
	v_fmac_f32_e32 v170, v12, v12
	v_add_f32_e32 v169, v169, v170
	v_add_f32_e32 v168, v169, v168
	v_mul_f32_e32 v169, v7, v7
	v_mul_f32_e32 v170, v9, v9
	v_fmac_f32_e32 v169, v6, v6
	v_fmac_f32_e32 v170, v8, v8
	v_add_f32_e32 v169, v169, v170
	v_add_f32_e32 v168, v169, v168
	v_mul_f32_e32 v169, v3, v3
	v_mul_f32_e32 v170, v5, v5
	v_fmac_f32_e32 v169, v2, v2
	v_fmac_f32_e32 v170, v4, v4
	v_add_f32_e32 v169, v169, v170
	v_add_f32_e32 v168, v169, v168
	v_mov_b32_e32 v169, v168
	s_nop 1
	v_permlane16_swap_b32_e32 v169, v168
	s_waitcnt lgkmcnt(0)
	v_add_f32_e32 v168, v168, v169
	v_mov_b32_e32 v169, v168
	s_nop 1
	v_permlane32_swap_b32_e32 v169, v168
	s_and_saveexec_b64 s[6:7], s[40:41]
	s_cbranch_execz .LBB0_2391
	s_lshl_b32 s4, s93, 10
	s_add_i32 s4, s34, s4
	s_waitcnt lgkmcnt(0)
	v_add_f32_e32 v168, v168, v169
	v_lshl_add_u32 v166, v166, 4, s4
	ds_write_b32 v166, v168 offset:2816

.LBB0_2417:
	s_waitcnt vmcnt(0)
	v_lshlrev_b32_e32 v216, 16, v206
	v_and_b32_e32 v217, 0xffff0000, v206
	v_lshlrev_b32_e32 v206, 16, v207
	v_and_b32_e32 v207, 0xffff0000, v207
	s_waitcnt lgkmcnt(0)
	v_pk_mul_f32 v[136:137], v[136:137], v[0:1] op_sel_hi:[1,0]
	v_pk_mul_f32 v[134:135], v[134:135], v[0:1] op_sel_hi:[1,0]
	v_lshlrev_b32_e32 v218, 16, v208
	v_and_b32_e32 v219, 0xffff0000, v208
	v_lshlrev_b32_e32 v208, 16, v209
	v_and_b32_e32 v209, 0xffff0000, v209
	v_pk_fma_f32 v[136:137], v[184:185], v[136:137], v[206:207]
	v_pk_fma_f32 v[134:135], v[182:183], v[134:135], v[216:217]
	v_pk_mul_f32 v[132:133], v[132:133], v[0:1] op_sel_hi:[1,0]
	v_pk_mul_f32 v[130:131], v[130:131], v[0:1] op_sel_hi:[1,0]
	v_pk_fma_f32 v[206:207], v[180:181], v[132:133], v[208:209]
	v_pk_fma_f32 v[132:133], v[178:179], v[130:131], v[218:219]
	v_mul_f32_e32 v130, v135, v135
	v_mul_f32_e32 v131, v137, v137
	v_fmac_f32_e32 v130, v134, v134
	v_fmac_f32_e32 v131, v136, v136
	v_add_f32_e32 v130, v130, v131
	v_mul_f32_e32 v131, v133, v133
	v_mul_f32_e32 v208, v207, v207
	v_fmac_f32_e32 v131, v132, v132
	v_fmac_f32_e32 v208, v206, v206
	v_add_f32_e32 v131, v131, v208
	v_add_f32_e32 v208, v130, v131
	v_cvt_pk_bf16_f32 v130, v134, v135
	v_cvt_pk_bf16_f32 v131, v136, v137
	v_lshlrev_b32_e32 v134, 16, v202
	v_and_b32_e32 v135, 0xffff0000, v202
	v_lshlrev_b32_e32 v136, 16, v203
	v_and_b32_e32 v137, 0xffff0000, v203
	v_pk_mul_f32 v[120:121], v[120:121], v[0:1] op_sel_hi:[1,0]
	v_pk_mul_f32 v[118:119], v[118:119], v[0:1] op_sel_hi:[1,0]
	v_lshlrev_b32_e32 v202, 16, v204
	v_and_b32_e32 v203, 0xffff0000, v204
	v_pk_fma_f32 v[120:121], v[172:173], v[120:121], v[136:137]
	v_pk_fma_f32 v[118:119], v[170:171], v[118:119], v[134:135]
	v_pk_mul_f32 v[114:115], v[114:115], v[0:1] op_sel_hi:[1,0]
	v_lshlrev_b32_e32 v204, 16, v205
	v_and_b32_e32 v205, 0xffff0000, v205
	v_pk_mul_f32 v[116:117], v[116:117], v[0:1] op_sel_hi:[1,0]
	v_pk_fma_f32 v[136:137], v[166:167], v[114:115], v[202:203]
	v_mul_f32_e32 v0, v119, v119
	v_mul_f32_e32 v114, v121, v121
	v_pk_fma_f32 v[134:135], v[168:169], v[116:117], v[204:205]
	v_fmac_f32_e32 v0, v118, v118
	v_fmac_f32_e32 v114, v120, v120
	v_add_f32_e32 v0, v0, v114
	v_mul_f32_e32 v114, v137, v137
	v_mul_f32_e32 v115, v135, v135
	v_fmac_f32_e32 v114, v136, v136
	v_fmac_f32_e32 v115, v134, v134
	v_add_f32_e32 v114, v114, v115
	v_add_f32_e32 v0, v0, v114
	v_add_f32_e32 v0, v208, v0
	v_mov_b32_e32 v117, v0
	s_nop 1
	v_permlane16_swap_b32_e32 v117, v0
	s_add_u32 s6, s18, s20
	s_addc_u32 s7, s19, s21
	v_lshl_add_u64 v[114:115], s[6:7], 0, v[224:225]
	v_lshl_add_u64 v[202:203], v[220:221], 1, v[114:115]
	s_waitcnt lgkmcnt(0)
	v_add_f32_e32 v0, v0, v117
	v_mov_b32_e32 v114, v0
	s_nop 1
	v_permlane32_swap_b32_e32 v114, v0
	v_cvt_pk_bf16_f32 v132, v132, v133
	v_cvt_pk_bf16_f32 v133, v206, v207
	global_store_dwordx4 v[202:203], v[130:133], off
	v_cvt_pk_bf16_f32 v116, v118, v119
	v_cvt_pk_bf16_f32 v117, v120, v121
	v_cvt_pk_bf16_f32 v118, v136, v137
	v_cvt_pk_bf16_f32 v119, v134, v135
	global_store_dwordx4 v[202:203], v[116:119], off offset:256
	s_and_saveexec_b64 s[18:19], s[40:41]
	s_cbranch_execz .LBB0_2419
	v_lshl_add_u32 v115, v240, 4, s34
	s_waitcnt lgkmcnt(0)
	v_add_f32_e32 v0, v0, v114
	ds_write_b32 v115, v0 offset:6144

.LBB0_2421:
	v_lshlrev_b32_e32 v118, 16, v198
	v_and_b32_e32 v119, 0xffff0000, v198
	v_lshlrev_b32_e32 v120, 16, v199
	v_and_b32_e32 v121, 0xffff0000, v199
	s_waitcnt lgkmcnt(0)
	v_pk_mul_f32 v[112:113], v[112:113], v[0:1] op_sel_hi:[1,0]
	v_pk_mul_f32 v[110:111], v[110:111], v[0:1] op_sel_hi:[1,0]
	v_lshlrev_b32_e32 v130, 16, v200
	v_and_b32_e32 v131, 0xffff0000, v200
	v_lshlrev_b32_e32 v132, 16, v201
	v_and_b32_e32 v133, 0xffff0000, v201
	v_pk_fma_f32 v[112:113], v[184:185], v[112:113], v[120:121]
	v_pk_fma_f32 v[110:111], v[182:183], v[110:111], v[118:119]
	v_pk_mul_f32 v[108:109], v[108:109], v[0:1] op_sel_hi:[1,0]
	v_pk_mul_f32 v[106:107], v[106:107], v[0:1] op_sel_hi:[1,0]
	v_pk_fma_f32 v[118:119], v[180:181], v[108:109], v[132:133]
	v_pk_fma_f32 v[108:109], v[178:179], v[106:107], v[130:131]
	v_mul_f32_e32 v106, v111, v111
	v_mul_f32_e32 v107, v113, v113
	v_fmac_f32_e32 v106, v110, v110
	v_fmac_f32_e32 v107, v112, v112
	v_add_f32_e32 v106, v106, v107
	v_mul_f32_e32 v107, v109, v109
	v_mul_f32_e32 v115, v119, v119
	v_fmac_f32_e32 v107, v108, v108
	v_fmac_f32_e32 v115, v118, v118
	v_add_f32_e32 v107, v107, v115
	v_add_f32_e32 v115, v106, v107
	v_cvt_pk_bf16_f32 v106, v110, v111
	v_cvt_pk_bf16_f32 v107, v112, v113
	v_lshlrev_b32_e32 v110, 16, v194
	v_and_b32_e32 v111, 0xffff0000, v194
	v_lshlrev_b32_e32 v112, 16, v195
	v_and_b32_e32 v113, 0xffff0000, v195
	v_pk_mul_f32 v[104:105], v[104:105], v[0:1] op_sel_hi:[1,0]
	v_pk_mul_f32 v[102:103], v[102:103], v[0:1] op_sel_hi:[1,0]
	v_cvt_pk_bf16_f32 v108, v108, v109
	v_cvt_pk_bf16_f32 v109, v118, v119
	v_lshlrev_b32_e32 v118, 16, v196
	v_and_b32_e32 v119, 0xffff0000, v196
	v_pk_fma_f32 v[104:105], v[172:173], v[104:105], v[112:113]
	v_pk_fma_f32 v[102:103], v[170:171], v[102:103], v[110:111]
	v_pk_mul_f32 v[98:99], v[98:99], v[0:1] op_sel_hi:[1,0]
	v_lshlrev_b32_e32 v120, 16, v197
	v_and_b32_e32 v121, 0xffff0000, v197
	v_pk_mul_f32 v[100:101], v[100:101], v[0:1] op_sel_hi:[1,0]
	v_pk_fma_f32 v[112:113], v[166:167], v[98:99], v[118:119]
	v_mul_f32_e32 v0, v103, v103
	v_mul_f32_e32 v98, v105, v105
	v_pk_fma_f32 v[110:111], v[168:169], v[100:101], v[120:121]
	v_fmac_f32_e32 v0, v102, v102
	v_fmac_f32_e32 v98, v104, v104
	v_add_f32_e32 v0, v0, v98
	v_mul_f32_e32 v98, v113, v113
	v_mul_f32_e32 v99, v111, v111
	v_fmac_f32_e32 v98, v112, v112
	v_fmac_f32_e32 v99, v110, v110
	v_add_f32_e32 v98, v98, v99
	v_add_f32_e32 v0, v0, v98
	v_add_f32_e32 v0, v115, v0
	v_mov_b32_e32 v101, v0
	s_nop 1
	v_permlane16_swap_b32_e32 v101, v0
	v_or_b32_e32 v114, 16, v240
	v_add_u32_e32 v116, s35, v114
	v_ashrrev_i32_e32 v117, 31, v116
	v_lshlrev_b64 v[116:117], 11, v[116:117]
	v_lshl_add_u64 v[98:99], s[6:7], 0, v[116:117]
	s_waitcnt lgkmcnt(0)
	v_add_f32_e32 v0, v0, v101
	v_lshl_add_u64 v[116:117], v[220:221], 1, v[98:99]
	v_mov_b32_e32 v98, v0
	s_nop 1
	v_permlane32_swap_b32_e32 v98, v0
	global_store_dwordx4 v[116:117], v[106:109], off
	v_cvt_pk_bf16_f32 v100, v102, v103
	v_cvt_pk_bf16_f32 v101, v104, v105
	v_cvt_pk_bf16_f32 v102, v112, v113
	v_cvt_pk_bf16_f32 v103, v110, v111
	global_store_dwordx4 v[116:117], v[100:103], off offset:256
	s_and_saveexec_b64 s[18:19], s[40:41]
	s_cbranch_execz .LBB0_2423
	v_lshl_add_u32 v99, v114, 4, s34
	s_waitcnt lgkmcnt(0)
	v_add_f32_e32 v0, v0, v98
	ds_write_b32 v99, v0 offset:6144

.LBB0_2425:
	v_lshlrev_b32_e32 v102, 16, v190
	v_and_b32_e32 v103, 0xffff0000, v190
	v_lshlrev_b32_e32 v104, 16, v191
	v_and_b32_e32 v105, 0xffff0000, v191
	s_waitcnt lgkmcnt(0)
	v_pk_mul_f32 v[96:97], v[96:97], v[0:1] op_sel_hi:[1,0]
	v_pk_mul_f32 v[94:95], v[94:95], v[0:1] op_sel_hi:[1,0]
	v_lshlrev_b32_e32 v106, 16, v192
	v_and_b32_e32 v107, 0xffff0000, v192
	v_lshlrev_b32_e32 v108, 16, v193
	v_and_b32_e32 v109, 0xffff0000, v193
	v_pk_fma_f32 v[96:97], v[184:185], v[96:97], v[104:105]
	v_pk_fma_f32 v[94:95], v[182:183], v[94:95], v[102:103]
	v_pk_mul_f32 v[92:93], v[92:93], v[0:1] op_sel_hi:[1,0]
	v_pk_mul_f32 v[90:91], v[90:91], v[0:1] op_sel_hi:[1,0]
	v_pk_fma_f32 v[102:103], v[180:181], v[92:93], v[108:109]
	v_pk_fma_f32 v[92:93], v[178:179], v[90:91], v[106:107]
	v_mul_f32_e32 v90, v95, v95
	v_mul_f32_e32 v91, v97, v97
	v_fmac_f32_e32 v90, v94, v94
	v_fmac_f32_e32 v91, v96, v96
	v_add_f32_e32 v90, v90, v91
	v_mul_f32_e32 v91, v93, v93
	v_mul_f32_e32 v99, v103, v103
	v_fmac_f32_e32 v91, v92, v92
	v_fmac_f32_e32 v99, v102, v102
	v_add_f32_e32 v91, v91, v99
	v_add_f32_e32 v99, v90, v91
	v_cvt_pk_bf16_f32 v90, v94, v95
	v_cvt_pk_bf16_f32 v91, v96, v97
	v_lshlrev_b32_e32 v94, 16, v186
	v_and_b32_e32 v95, 0xffff0000, v186
	v_lshlrev_b32_e32 v96, 16, v187
	v_and_b32_e32 v97, 0xffff0000, v187
	v_pk_mul_f32 v[88:89], v[88:89], v[0:1] op_sel_hi:[1,0]
	v_pk_mul_f32 v[86:87], v[86:87], v[0:1] op_sel_hi:[1,0]
	v_cvt_pk_bf16_f32 v92, v92, v93
	v_cvt_pk_bf16_f32 v93, v102, v103
	v_lshlrev_b32_e32 v102, 16, v188
	v_and_b32_e32 v103, 0xffff0000, v188
	v_pk_fma_f32 v[88:89], v[172:173], v[88:89], v[96:97]
	v_pk_fma_f32 v[86:87], v[170:171], v[86:87], v[94:95]
	v_pk_mul_f32 v[82:83], v[82:83], v[0:1] op_sel_hi:[1,0]
	v_lshlrev_b32_e32 v104, 16, v189
	v_and_b32_e32 v105, 0xffff0000, v189
	v_pk_mul_f32 v[84:85], v[84:85], v[0:1] op_sel_hi:[1,0]
	v_pk_fma_f32 v[96:97], v[166:167], v[82:83], v[102:103]
	v_mul_f32_e32 v0, v87, v87
	v_mul_f32_e32 v82, v89, v89
	v_pk_fma_f32 v[94:95], v[168:169], v[84:85], v[104:105]
	v_fmac_f32_e32 v0, v86, v86
	v_fmac_f32_e32 v82, v88, v88
	v_add_f32_e32 v0, v0, v82
	v_mul_f32_e32 v82, v97, v97
	v_mul_f32_e32 v83, v95, v95
	v_fmac_f32_e32 v82, v96, v96
	v_fmac_f32_e32 v83, v94, v94
	v_add_f32_e32 v82, v82, v83
	v_add_f32_e32 v0, v0, v82
	v_add_f32_e32 v0, v99, v0
	v_mov_b32_e32 v85, v0
	s_nop 1
	v_permlane16_swap_b32_e32 v85, v0
	v_or_b32_e32 v98, 32, v240
	v_add_u32_e32 v100, s35, v98
	v_ashrrev_i32_e32 v101, 31, v100
	v_lshlrev_b64 v[100:101], 11, v[100:101]
	v_lshl_add_u64 v[82:83], s[6:7], 0, v[100:101]
	s_waitcnt lgkmcnt(0)
	v_add_f32_e32 v0, v0, v85
	v_lshl_add_u64 v[100:101], v[220:221], 1, v[82:83]
	v_mov_b32_e32 v82, v0
	s_nop 1
	v_permlane32_swap_b32_e32 v82, v0
	global_store_dwordx4 v[100:101], v[90:93], off
	v_cvt_pk_bf16_f32 v84, v86, v87
	v_cvt_pk_bf16_f32 v85, v88, v89
	v_cvt_pk_bf16_f32 v86, v96, v97
	v_cvt_pk_bf16_f32 v87, v94, v95
	global_store_dwordx4 v[100:101], v[84:87], off offset:256
	s_and_saveexec_b64 s[18:19], s[40:41]
	s_cbranch_execz .LBB0_2427
	v_lshl_add_u32 v83, v98, 4, s34
	s_waitcnt lgkmcnt(0)
	v_add_f32_e32 v0, v0, v82
	ds_write_b32 v83, v0 offset:6144

.LBB0_2429:
	v_lshlrev_b32_e32 v86, 16, v174
	v_and_b32_e32 v87, 0xffff0000, v174
	v_lshlrev_b32_e32 v88, 16, v175
	v_and_b32_e32 v89, 0xffff0000, v175
	s_waitcnt lgkmcnt(0)
	v_pk_mul_f32 v[80:81], v[80:81], v[0:1] op_sel_hi:[1,0]
	v_pk_mul_f32 v[78:79], v[78:79], v[0:1] op_sel_hi:[1,0]
	v_lshlrev_b32_e32 v90, 16, v176
	v_and_b32_e32 v91, 0xffff0000, v176
	v_lshlrev_b32_e32 v92, 16, v177
	v_and_b32_e32 v93, 0xffff0000, v177
	v_pk_fma_f32 v[80:81], v[184:185], v[80:81], v[88:89]
	v_pk_fma_f32 v[78:79], v[182:183], v[78:79], v[86:87]
	v_pk_mul_f32 v[76:77], v[76:77], v[0:1] op_sel_hi:[1,0]
	v_pk_mul_f32 v[74:75], v[74:75], v[0:1] op_sel_hi:[1,0]
	v_pk_fma_f32 v[86:87], v[180:181], v[76:77], v[92:93]
	v_pk_fma_f32 v[76:77], v[178:179], v[74:75], v[90:91]
	v_mul_f32_e32 v74, v79, v79
	v_mul_f32_e32 v75, v81, v81
	v_fmac_f32_e32 v74, v78, v78
	v_fmac_f32_e32 v75, v80, v80
	v_add_f32_e32 v74, v74, v75
	v_mul_f32_e32 v75, v77, v77
	v_mul_f32_e32 v83, v87, v87
	v_fmac_f32_e32 v75, v76, v76
	v_fmac_f32_e32 v83, v86, v86
	v_add_f32_e32 v75, v75, v83
	v_add_f32_e32 v83, v74, v75
	v_cvt_pk_bf16_f32 v74, v78, v79
	v_cvt_pk_bf16_f32 v75, v80, v81
	v_lshlrev_b32_e32 v78, 16, v162
	v_and_b32_e32 v79, 0xffff0000, v162
	v_lshlrev_b32_e32 v80, 16, v163
	v_and_b32_e32 v81, 0xffff0000, v163
	v_pk_mul_f32 v[72:73], v[72:73], v[0:1] op_sel_hi:[1,0]
	v_pk_mul_f32 v[70:71], v[70:71], v[0:1] op_sel_hi:[1,0]
	v_cvt_pk_bf16_f32 v76, v76, v77
	v_cvt_pk_bf16_f32 v77, v86, v87
	v_lshlrev_b32_e32 v86, 16, v164
	v_and_b32_e32 v87, 0xffff0000, v164
	v_pk_fma_f32 v[72:73], v[172:173], v[72:73], v[80:81]
	v_pk_fma_f32 v[70:71], v[170:171], v[70:71], v[78:79]
	v_pk_mul_f32 v[66:67], v[66:67], v[0:1] op_sel_hi:[1,0]
	v_lshlrev_b32_e32 v88, 16, v165
	v_and_b32_e32 v89, 0xffff0000, v165
	v_pk_mul_f32 v[68:69], v[68:69], v[0:1] op_sel_hi:[1,0]
	v_pk_fma_f32 v[80:81], v[166:167], v[66:67], v[86:87]
	v_mul_f32_e32 v0, v71, v71
	v_mul_f32_e32 v66, v73, v73
	v_pk_fma_f32 v[78:79], v[168:169], v[68:69], v[88:89]
	v_fmac_f32_e32 v0, v70, v70
	v_fmac_f32_e32 v66, v72, v72
	v_add_f32_e32 v0, v0, v66
	v_mul_f32_e32 v66, v81, v81
	v_mul_f32_e32 v67, v79, v79
	v_fmac_f32_e32 v66, v80, v80
	v_fmac_f32_e32 v67, v78, v78
	v_add_f32_e32 v66, v66, v67
	v_add_f32_e32 v0, v0, v66
	v_add_f32_e32 v0, v83, v0
	v_mov_b32_e32 v69, v0
	s_nop 1
	v_permlane16_swap_b32_e32 v69, v0
	v_or_b32_e32 v82, 48, v240
	v_add_u32_e32 v84, s35, v82
	v_ashrrev_i32_e32 v85, 31, v84
	v_lshlrev_b64 v[84:85], 11, v[84:85]
	v_lshl_add_u64 v[66:67], s[6:7], 0, v[84:85]
	s_waitcnt lgkmcnt(0)
	v_add_f32_e32 v0, v0, v69
	v_lshl_add_u64 v[84:85], v[220:221], 1, v[66:67]
	v_mov_b32_e32 v66, v0
	s_nop 1
	v_permlane32_swap_b32_e32 v66, v0
	global_store_dwordx4 v[84:85], v[74:77], off
	v_cvt_pk_bf16_f32 v68, v70, v71
	v_cvt_pk_bf16_f32 v69, v72, v73
	v_cvt_pk_bf16_f32 v70, v80, v81
	v_cvt_pk_bf16_f32 v71, v78, v79
	global_store_dwordx4 v[84:85], v[68:71], off offset:256
	s_and_saveexec_b64 s[18:19], s[40:41]
	s_cbranch_execz .LBB0_2431
	v_lshl_add_u32 v67, v82, 4, s34
	s_waitcnt lgkmcnt(0)
	v_add_f32_e32 v0, v0, v66
	ds_write_b32 v67, v0 offset:6144

.LBB0_2433:
	v_lshlrev_b32_e32 v70, 16, v158
	v_and_b32_e32 v71, 0xffff0000, v158
	v_lshlrev_b32_e32 v72, 16, v159
	v_and_b32_e32 v73, 0xffff0000, v159
	s_waitcnt lgkmcnt(0)
	v_pk_mul_f32 v[64:65], v[64:65], v[0:1] op_sel_hi:[1,0]
	v_pk_mul_f32 v[62:63], v[62:63], v[0:1] op_sel_hi:[1,0]
	v_lshlrev_b32_e32 v74, 16, v160
	v_and_b32_e32 v75, 0xffff0000, v160
	v_lshlrev_b32_e32 v76, 16, v161
	v_and_b32_e32 v77, 0xffff0000, v161
	v_pk_fma_f32 v[64:65], v[184:185], v[64:65], v[72:73]
	v_pk_fma_f32 v[62:63], v[182:183], v[62:63], v[70:71]
	v_pk_mul_f32 v[60:61], v[60:61], v[0:1] op_sel_hi:[1,0]
	v_pk_mul_f32 v[58:59], v[58:59], v[0:1] op_sel_hi:[1,0]
	v_pk_fma_f32 v[70:71], v[180:181], v[60:61], v[76:77]
	v_pk_fma_f32 v[60:61], v[178:179], v[58:59], v[74:75]
	v_mul_f32_e32 v58, v63, v63
	v_mul_f32_e32 v59, v65, v65
	v_fmac_f32_e32 v58, v62, v62
	v_fmac_f32_e32 v59, v64, v64
	v_add_f32_e32 v58, v58, v59
	v_mul_f32_e32 v59, v61, v61
	v_mul_f32_e32 v67, v71, v71
	v_fmac_f32_e32 v59, v60, v60
	v_fmac_f32_e32 v67, v70, v70
	v_add_f32_e32 v59, v59, v67
	v_add_f32_e32 v67, v58, v59
	v_cvt_pk_bf16_f32 v58, v62, v63
	v_cvt_pk_bf16_f32 v59, v64, v65
	v_lshlrev_b32_e32 v62, 16, v154
	v_and_b32_e32 v63, 0xffff0000, v154
	v_lshlrev_b32_e32 v64, 16, v155
	v_and_b32_e32 v65, 0xffff0000, v155
	v_pk_mul_f32 v[56:57], v[56:57], v[0:1] op_sel_hi:[1,0]
	v_pk_mul_f32 v[54:55], v[54:55], v[0:1] op_sel_hi:[1,0]
	v_cvt_pk_bf16_f32 v60, v60, v61
	v_cvt_pk_bf16_f32 v61, v70, v71
	v_lshlrev_b32_e32 v70, 16, v156
	v_and_b32_e32 v71, 0xffff0000, v156
	v_pk_fma_f32 v[56:57], v[172:173], v[56:57], v[64:65]
	v_pk_fma_f32 v[54:55], v[170:171], v[54:55], v[62:63]
	v_pk_mul_f32 v[50:51], v[50:51], v[0:1] op_sel_hi:[1,0]
	v_lshlrev_b32_e32 v72, 16, v157
	v_and_b32_e32 v73, 0xffff0000, v157
	v_pk_mul_f32 v[52:53], v[52:53], v[0:1] op_sel_hi:[1,0]
	v_pk_fma_f32 v[64:65], v[166:167], v[50:51], v[70:71]
	v_mul_f32_e32 v0, v55, v55
	v_mul_f32_e32 v50, v57, v57
	v_pk_fma_f32 v[62:63], v[168:169], v[52:53], v[72:73]
	v_fmac_f32_e32 v0, v54, v54
	v_fmac_f32_e32 v50, v56, v56
	v_add_f32_e32 v0, v0, v50
	v_mul_f32_e32 v50, v65, v65
	v_mul_f32_e32 v51, v63, v63
	v_fmac_f32_e32 v50, v64, v64
	v_fmac_f32_e32 v51, v62, v62
	v_add_f32_e32 v50, v50, v51
	v_add_f32_e32 v0, v0, v50
	v_add_f32_e32 v0, v67, v0
	v_mov_b32_e32 v53, v0
	s_nop 1
	v_permlane16_swap_b32_e32 v53, v0
	v_add_u32_e32 v66, 0x80, v240
	v_add_u32_e32 v68, s35, v66
	v_ashrrev_i32_e32 v69, 31, v68
	v_lshlrev_b64 v[68:69], 11, v[68:69]
	v_lshl_add_u64 v[50:51], s[6:7], 0, v[68:69]
	s_waitcnt lgkmcnt(0)
	v_add_f32_e32 v0, v0, v53
	v_lshl_add_u64 v[68:69], v[220:221], 1, v[50:51]
	v_mov_b32_e32 v50, v0
	s_nop 1
	v_permlane32_swap_b32_e32 v50, v0
	global_store_dwordx4 v[68:69], v[58:61], off
	v_cvt_pk_bf16_f32 v52, v54, v55
	v_cvt_pk_bf16_f32 v53, v56, v57
	v_cvt_pk_bf16_f32 v54, v64, v65
	v_cvt_pk_bf16_f32 v55, v62, v63
	global_store_dwordx4 v[68:69], v[52:55], off offset:256
	s_and_saveexec_b64 s[18:19], s[40:41]
	s_cbranch_execz .LBB0_2435
	v_lshl_add_u32 v51, v66, 4, s34
	s_waitcnt lgkmcnt(0)
	v_add_f32_e32 v0, v0, v50
	ds_write_b32 v51, v0 offset:6144

.LBB0_2437:
	v_lshlrev_b32_e32 v54, 16, v150
	v_and_b32_e32 v55, 0xffff0000, v150
	v_lshlrev_b32_e32 v56, 16, v151
	v_and_b32_e32 v57, 0xffff0000, v151
	s_waitcnt lgkmcnt(0)
	v_pk_mul_f32 v[48:49], v[48:49], v[0:1] op_sel_hi:[1,0]
	v_pk_mul_f32 v[46:47], v[46:47], v[0:1] op_sel_hi:[1,0]
	v_lshlrev_b32_e32 v58, 16, v152
	v_and_b32_e32 v59, 0xffff0000, v152
	v_lshlrev_b32_e32 v60, 16, v153
	v_and_b32_e32 v61, 0xffff0000, v153
	v_pk_fma_f32 v[48:49], v[184:185], v[48:49], v[56:57]
	v_pk_fma_f32 v[46:47], v[182:183], v[46:47], v[54:55]
	v_pk_mul_f32 v[44:45], v[44:45], v[0:1] op_sel_hi:[1,0]
	v_pk_mul_f32 v[42:43], v[42:43], v[0:1] op_sel_hi:[1,0]
	v_pk_fma_f32 v[54:55], v[180:181], v[44:45], v[60:61]
	v_pk_fma_f32 v[44:45], v[178:179], v[42:43], v[58:59]
	v_mul_f32_e32 v42, v47, v47
	v_mul_f32_e32 v43, v49, v49
	v_fmac_f32_e32 v42, v46, v46
	v_fmac_f32_e32 v43, v48, v48
	v_add_f32_e32 v42, v42, v43
	v_mul_f32_e32 v43, v45, v45
	v_mul_f32_e32 v51, v55, v55
	v_fmac_f32_e32 v43, v44, v44
	v_fmac_f32_e32 v51, v54, v54
	v_add_f32_e32 v43, v43, v51
	v_add_f32_e32 v51, v42, v43
	v_cvt_pk_bf16_f32 v42, v46, v47
	v_cvt_pk_bf16_f32 v43, v48, v49
	v_lshlrev_b32_e32 v46, 16, v146
	v_and_b32_e32 v47, 0xffff0000, v146
	v_lshlrev_b32_e32 v48, 16, v147
	v_and_b32_e32 v49, 0xffff0000, v147
	v_pk_mul_f32 v[40:41], v[40:41], v[0:1] op_sel_hi:[1,0]
	v_pk_mul_f32 v[38:39], v[38:39], v[0:1] op_sel_hi:[1,0]
	v_cvt_pk_bf16_f32 v44, v44, v45
	v_cvt_pk_bf16_f32 v45, v54, v55
	v_lshlrev_b32_e32 v54, 16, v148
	v_and_b32_e32 v55, 0xffff0000, v148
	v_pk_fma_f32 v[40:41], v[172:173], v[40:41], v[48:49]
	v_pk_fma_f32 v[38:39], v[170:171], v[38:39], v[46:47]
	v_pk_mul_f32 v[34:35], v[34:35], v[0:1] op_sel_hi:[1,0]
	v_lshlrev_b32_e32 v56, 16, v149
	v_and_b32_e32 v57, 0xffff0000, v149
	v_pk_mul_f32 v[36:37], v[36:37], v[0:1] op_sel_hi:[1,0]
	v_pk_fma_f32 v[48:49], v[166:167], v[34:35], v[54:55]
	v_mul_f32_e32 v0, v39, v39
	v_mul_f32_e32 v34, v41, v41
	v_pk_fma_f32 v[46:47], v[168:169], v[36:37], v[56:57]
	v_fmac_f32_e32 v0, v38, v38
	v_fmac_f32_e32 v34, v40, v40
	v_add_f32_e32 v0, v0, v34
	v_mul_f32_e32 v34, v49, v49
	v_mul_f32_e32 v35, v47, v47
	v_fmac_f32_e32 v34, v48, v48
	v_fmac_f32_e32 v35, v46, v46
	v_add_f32_e32 v34, v34, v35
	v_add_f32_e32 v0, v0, v34
	v_add_f32_e32 v0, v51, v0
	v_mov_b32_e32 v37, v0
	s_nop 1
	v_permlane16_swap_b32_e32 v37, v0
	v_add_u32_e32 v50, 0x90, v240
	v_add_u32_e32 v52, s35, v50
	v_ashrrev_i32_e32 v53, 31, v52
	v_lshlrev_b64 v[52:53], 11, v[52:53]
	v_lshl_add_u64 v[34:35], s[6:7], 0, v[52:53]
	s_waitcnt lgkmcnt(0)
	v_add_f32_e32 v0, v0, v37
	v_lshl_add_u64 v[52:53], v[220:221], 1, v[34:35]
	v_mov_b32_e32 v34, v0
	s_nop 1
	v_permlane32_swap_b32_e32 v34, v0
	global_store_dwordx4 v[52:53], v[42:45], off
	v_cvt_pk_bf16_f32 v36, v38, v39
	v_cvt_pk_bf16_f32 v37, v40, v41
	v_cvt_pk_bf16_f32 v38, v48, v49
	v_cvt_pk_bf16_f32 v39, v46, v47
	global_store_dwordx4 v[52:53], v[36:39], off offset:256
	s_and_saveexec_b64 s[18:19], s[40:41]
	s_cbranch_execz .LBB0_2439
	v_lshl_add_u32 v35, v50, 4, s34
	s_waitcnt lgkmcnt(0)
	v_add_f32_e32 v0, v0, v34
	ds_write_b32 v35, v0 offset:6144

.LBB0_2441:
	v_lshlrev_b32_e32 v38, 16, v142
	v_and_b32_e32 v39, 0xffff0000, v142
	v_lshlrev_b32_e32 v40, 16, v143
	v_and_b32_e32 v41, 0xffff0000, v143
	s_waitcnt lgkmcnt(0)
	v_pk_mul_f32 v[32:33], v[32:33], v[0:1] op_sel_hi:[1,0]
	v_pk_mul_f32 v[30:31], v[30:31], v[0:1] op_sel_hi:[1,0]
	v_lshlrev_b32_e32 v42, 16, v144
	v_and_b32_e32 v43, 0xffff0000, v144
	v_lshlrev_b32_e32 v44, 16, v145
	v_and_b32_e32 v45, 0xffff0000, v145
	v_pk_fma_f32 v[32:33], v[184:185], v[32:33], v[40:41]
	v_pk_fma_f32 v[30:31], v[182:183], v[30:31], v[38:39]
	v_pk_mul_f32 v[28:29], v[28:29], v[0:1] op_sel_hi:[1,0]
	v_pk_mul_f32 v[26:27], v[26:27], v[0:1] op_sel_hi:[1,0]
	v_pk_fma_f32 v[38:39], v[180:181], v[28:29], v[44:45]
	v_pk_fma_f32 v[28:29], v[178:179], v[26:27], v[42:43]
	v_mul_f32_e32 v26, v31, v31
	v_mul_f32_e32 v27, v33, v33
	v_fmac_f32_e32 v26, v30, v30
	v_fmac_f32_e32 v27, v32, v32
	v_add_f32_e32 v26, v26, v27
	v_mul_f32_e32 v27, v29, v29
	v_mul_f32_e32 v35, v39, v39
	v_fmac_f32_e32 v27, v28, v28
	v_fmac_f32_e32 v35, v38, v38
	v_add_f32_e32 v27, v27, v35
	v_add_f32_e32 v35, v26, v27
	v_cvt_pk_bf16_f32 v26, v30, v31
	v_cvt_pk_bf16_f32 v27, v32, v33
	v_lshlrev_b32_e32 v30, 16, v138
	v_and_b32_e32 v31, 0xffff0000, v138
	v_lshlrev_b32_e32 v32, 16, v139
	v_and_b32_e32 v33, 0xffff0000, v139
	v_pk_mul_f32 v[24:25], v[24:25], v[0:1] op_sel_hi:[1,0]
	v_pk_mul_f32 v[22:23], v[22:23], v[0:1] op_sel_hi:[1,0]
	v_cvt_pk_bf16_f32 v28, v28, v29
	v_cvt_pk_bf16_f32 v29, v38, v39
	v_lshlrev_b32_e32 v38, 16, v140
	v_and_b32_e32 v39, 0xffff0000, v140
	v_pk_fma_f32 v[24:25], v[172:173], v[24:25], v[32:33]
	v_pk_fma_f32 v[22:23], v[170:171], v[22:23], v[30:31]
	v_pk_mul_f32 v[18:19], v[18:19], v[0:1] op_sel_hi:[1,0]
	v_lshlrev_b32_e32 v40, 16, v141
	v_and_b32_e32 v41, 0xffff0000, v141
	v_pk_mul_f32 v[20:21], v[20:21], v[0:1] op_sel_hi:[1,0]
	v_pk_fma_f32 v[32:33], v[166:167], v[18:19], v[38:39]
	v_mul_f32_e32 v0, v23, v23
	v_mul_f32_e32 v18, v25, v25
	v_pk_fma_f32 v[30:31], v[168:169], v[20:21], v[40:41]
	v_fmac_f32_e32 v0, v22, v22
	v_fmac_f32_e32 v18, v24, v24
	v_add_f32_e32 v0, v0, v18
	v_mul_f32_e32 v18, v33, v33
	v_mul_f32_e32 v19, v31, v31
	v_fmac_f32_e32 v18, v32, v32
	v_fmac_f32_e32 v19, v30, v30
	v_add_f32_e32 v18, v18, v19
	v_add_f32_e32 v0, v0, v18
	v_add_f32_e32 v0, v35, v0
	v_mov_b32_e32 v21, v0
	s_nop 1
	v_permlane16_swap_b32_e32 v21, v0
	v_add_u32_e32 v34, 0xa0, v240
	v_add_u32_e32 v36, s35, v34
	v_ashrrev_i32_e32 v37, 31, v36
	v_lshlrev_b64 v[36:37], 11, v[36:37]
	v_lshl_add_u64 v[18:19], s[6:7], 0, v[36:37]
	s_waitcnt lgkmcnt(0)
	v_add_f32_e32 v0, v0, v21
	v_lshl_add_u64 v[36:37], v[220:221], 1, v[18:19]
	v_mov_b32_e32 v18, v0
	s_nop 1
	v_permlane32_swap_b32_e32 v18, v0
	global_store_dwordx4 v[36:37], v[26:29], off
	v_cvt_pk_bf16_f32 v20, v22, v23
	v_cvt_pk_bf16_f32 v21, v24, v25
	v_cvt_pk_bf16_f32 v22, v32, v33
	v_cvt_pk_bf16_f32 v23, v30, v31
	global_store_dwordx4 v[36:37], v[20:23], off offset:256
	s_and_saveexec_b64 s[18:19], s[40:41]
	s_cbranch_execz .LBB0_2443
	v_lshl_add_u32 v19, v34, 4, s34
	s_waitcnt lgkmcnt(0)
	v_add_f32_e32 v0, v0, v18
	ds_write_b32 v19, v0 offset:6144

.LBB0_2445:
	v_lshlrev_b32_e32 v22, 16, v126
	v_and_b32_e32 v23, 0xffff0000, v126
	v_lshlrev_b32_e32 v24, 16, v127
	v_and_b32_e32 v25, 0xffff0000, v127
	s_waitcnt lgkmcnt(0)
	v_pk_mul_f32 v[16:17], v[16:17], v[0:1] op_sel_hi:[1,0]
	v_pk_mul_f32 v[14:15], v[14:15], v[0:1] op_sel_hi:[1,0]
	v_lshlrev_b32_e32 v26, 16, v128
	v_and_b32_e32 v27, 0xffff0000, v128
	v_lshlrev_b32_e32 v28, 16, v129
	v_and_b32_e32 v29, 0xffff0000, v129
	v_pk_fma_f32 v[16:17], v[184:185], v[16:17], v[24:25]
	v_pk_fma_f32 v[14:15], v[182:183], v[14:15], v[22:23]
	v_pk_mul_f32 v[12:13], v[12:13], v[0:1] op_sel_hi:[1,0]
	v_pk_mul_f32 v[10:11], v[10:11], v[0:1] op_sel_hi:[1,0]
	v_pk_fma_f32 v[22:23], v[180:181], v[12:13], v[28:29]
	v_pk_fma_f32 v[12:13], v[178:179], v[10:11], v[26:27]
	v_mul_f32_e32 v10, v15, v15
	v_mul_f32_e32 v11, v17, v17
	v_fmac_f32_e32 v10, v14, v14
	v_fmac_f32_e32 v11, v16, v16
	v_add_f32_e32 v10, v10, v11
	v_mul_f32_e32 v11, v13, v13
	v_mul_f32_e32 v19, v23, v23
	v_fmac_f32_e32 v11, v12, v12
	v_fmac_f32_e32 v19, v22, v22
	v_add_f32_e32 v11, v11, v19
	v_add_f32_e32 v19, v10, v11
	v_cvt_pk_bf16_f32 v10, v14, v15
	v_cvt_pk_bf16_f32 v11, v16, v17
	v_lshlrev_b32_e32 v14, 16, v122
	v_and_b32_e32 v15, 0xffff0000, v122
	v_lshlrev_b32_e32 v16, 16, v123
	v_and_b32_e32 v17, 0xffff0000, v123
	v_pk_mul_f32 v[8:9], v[8:9], v[0:1] op_sel_hi:[1,0]
	v_pk_mul_f32 v[6:7], v[6:7], v[0:1] op_sel_hi:[1,0]
	v_cvt_pk_bf16_f32 v12, v12, v13
	v_cvt_pk_bf16_f32 v13, v22, v23
	v_lshlrev_b32_e32 v22, 16, v124
	v_and_b32_e32 v23, 0xffff0000, v124
	v_pk_fma_f32 v[8:9], v[172:173], v[8:9], v[16:17]
	v_pk_fma_f32 v[6:7], v[170:171], v[6:7], v[14:15]
	v_pk_mul_f32 v[2:3], v[2:3], v[0:1] op_sel_hi:[1,0]
	v_lshlrev_b32_e32 v24, 16, v125
	v_and_b32_e32 v25, 0xffff0000, v125
	v_pk_mul_f32 v[4:5], v[4:5], v[0:1] op_sel_hi:[1,0]
	v_pk_fma_f32 v[16:17], v[166:167], v[2:3], v[22:23]
	v_mul_f32_e32 v0, v7, v7
	v_mul_f32_e32 v2, v9, v9
	v_pk_fma_f32 v[14:15], v[168:169], v[4:5], v[24:25]
	v_fmac_f32_e32 v0, v6, v6
	v_fmac_f32_e32 v2, v8, v8
	v_add_f32_e32 v0, v0, v2
	v_mul_f32_e32 v2, v17, v17
	v_mul_f32_e32 v3, v15, v15
	v_fmac_f32_e32 v2, v16, v16
	v_fmac_f32_e32 v3, v14, v14
	v_add_f32_e32 v2, v2, v3
	v_add_f32_e32 v0, v0, v2
	v_add_f32_e32 v0, v19, v0
	v_mov_b32_e32 v5, v0
	s_nop 1
	v_permlane16_swap_b32_e32 v5, v0
	v_add_u32_e32 v18, 0xb0, v240
	v_add_u32_e32 v20, s35, v18
	v_ashrrev_i32_e32 v21, 31, v20
	v_lshlrev_b64 v[20:21], 11, v[20:21]
	v_lshl_add_u64 v[2:3], s[6:7], 0, v[20:21]
	s_waitcnt lgkmcnt(0)
	v_add_f32_e32 v0, v0, v5
	v_lshl_add_u64 v[20:21], v[220:221], 1, v[2:3]
	v_mov_b32_e32 v2, v0
	s_nop 1
	v_permlane32_swap_b32_e32 v2, v0
	global_store_dwordx4 v[20:21], v[10:13], off
	v_cvt_pk_bf16_f32 v4, v6, v7
	v_cvt_pk_bf16_f32 v5, v8, v9
	v_cvt_pk_bf16_f32 v6, v16, v17
	v_cvt_pk_bf16_f32 v7, v14, v15
	global_store_dwordx4 v[20:21], v[4:7], off offset:256
	s_and_saveexec_b64 s[6:7], s[40:41]
	s_cbranch_execz .LBB0_2447
	v_lshl_add_u32 v3, v18, 4, s34
	s_waitcnt lgkmcnt(0)
	v_add_f32_e32 v0, v0, v2
	ds_write_b32 v3, v0 offset:6144

.LBB0_2475:
	s_lshl_b32 s8, s15, 5
	s_add_u32 s6, s6, s26
	s_addc_u32 s7, s7, s27
	s_add_i32 s4, s95, 64
	s_lshl_b32 s9, s14, 8
	v_lshrrev_b32_e32 v122, 1, v239
	s_or_b32 s8, s9, s8
	s_lshl_b32 s31, s4, 8
	v_and_or_b32 v220, v122, 24, s8
	v_add_u32_e32 v122, s31, v240
	v_ashrrev_i32_e32 v221, 31, v220
	v_ashrrev_i32_e32 v123, 31, v122
	v_lshl_add_u64 v[124:125], v[220:221], 1, s[6:7]
	v_lshlrev_b64 v[224:225], 11, v[122:123]
	v_lshl_add_u64 v[126:127], v[124:125], 0, v[224:225]
	s_barrier
	global_load_dwordx4 v[206:209], v[126:127], off
	global_load_dwordx4 v[202:205], v[126:127], off offset:256
	v_or_b32_e32 v126, 16, v122
	v_ashrrev_i32_e32 v127, 31, v126
	v_lshlrev_b64 v[126:127], 11, v[126:127]
	v_lshl_add_u64 v[126:127], v[124:125], 0, v[126:127]
	global_load_dwordx4 v[198:201], v[126:127], off
	global_load_dwordx4 v[194:197], v[126:127], off offset:256
	v_or_b32_e32 v126, 32, v122
	v_ashrrev_i32_e32 v127, 31, v126
	v_lshlrev_b64 v[126:127], 11, v[126:127]
	v_lshl_add_u64 v[126:127], v[124:125], 0, v[126:127]
	global_load_dwordx4 v[190:193], v[126:127], off
	global_load_dwordx4 v[186:189], v[126:127], off offset:256
	v_or_b32_e32 v126, 48, v122
	v_ashrrev_i32_e32 v127, 31, v126
	v_lshlrev_b64 v[126:127], 11, v[126:127]
	v_lshl_add_u64 v[126:127], v[124:125], 0, v[126:127]
	global_load_dwordx4 v[174:177], v[126:127], off
	global_load_dwordx4 v[162:165], v[126:127], off offset:256
	v_add_u32_e32 v126, 0x80, v122
	v_ashrrev_i32_e32 v127, 31, v126
	v_lshlrev_b64 v[126:127], 11, v[126:127]
	v_lshl_add_u64 v[126:127], v[124:125], 0, v[126:127]
	global_load_dwordx4 v[158:161], v[126:127], off
	global_load_dwordx4 v[154:157], v[126:127], off offset:256
	v_add_u32_e32 v126, 0x90, v122
	v_ashrrev_i32_e32 v127, 31, v126
	v_lshlrev_b64 v[126:127], 11, v[126:127]
	v_lshl_add_u64 v[126:127], v[124:125], 0, v[126:127]
	global_load_dwordx4 v[150:153], v[126:127], off
	global_load_dwordx4 v[146:149], v[126:127], off offset:256
	v_add_u32_e32 v126, 0xa0, v122
	v_add_u32_e32 v122, 0xb0, v122
	v_ashrrev_i32_e32 v127, 31, v126
	v_ashrrev_i32_e32 v123, 31, v122
	v_lshlrev_b64 v[126:127], 11, v[126:127]
	v_lshlrev_b64 v[122:123], 11, v[122:123]
	v_lshl_add_u64 v[126:127], v[124:125], 0, v[126:127]
	v_lshl_add_u64 v[122:123], v[124:125], 0, v[122:123]
	global_load_dwordx4 v[142:145], v[126:127], off
	global_load_dwordx4 v[138:141], v[126:127], off offset:256
	s_nop 0
	global_load_dwordx4 v[126:129], v[122:123], off
	s_nop 0
	global_load_dwordx4 v[122:125], v[122:123], off offset:256
	v_and_b32_e32 v167, 64, v231
	v_xor_b32_e32 v166, 16, v231
	v_add_u32_e32 v167, 64, v167
	v_cmp_lt_i32_e32 vcc, v166, v167
	v_mul_f32_e32 v168, v137, v137
	v_fmac_f32_e32 v168, v136, v136
	v_cndmask_b32_e32 v166, v231, v166, vcc
	v_lshlrev_b32_e32 v241, 2, v166
	v_mul_f32_e32 v166, v135, v135
	v_fmac_f32_e32 v166, v134, v134
	v_add_f32_e32 v166, v166, v168
	v_mul_f32_e32 v168, v131, v131
	v_mul_f32_e32 v169, v133, v133
	v_fmac_f32_e32 v168, v130, v130
	v_fmac_f32_e32 v169, v132, v132
	v_add_f32_e32 v168, v168, v169
	v_add_f32_e32 v166, v168, v166
	v_mul_f32_e32 v168, v119, v119
	v_mul_f32_e32 v169, v121, v121
	v_fmac_f32_e32 v168, v118, v118
	v_fmac_f32_e32 v169, v120, v120
	v_add_f32_e32 v168, v168, v169
	v_add_f32_e32 v166, v168, v166
	v_mul_f32_e32 v168, v115, v115
	v_mul_f32_e32 v169, v117, v117
	v_fmac_f32_e32 v168, v114, v114
	v_fmac_f32_e32 v169, v116, v116
	v_add_f32_e32 v168, v168, v169
	v_add_f32_e32 v166, v168, v166
	v_mov_b32_e32 v168, v166
	s_nop 1
	v_permlane16_swap_b32_e32 v168, v166
	v_xor_b32_e32 v169, 32, v231
	v_cmp_lt_i32_e32 vcc, v169, v167
	s_lshl_b32 s6, s15, 2
	s_add_i32 s30, s6, 0
	v_cndmask_b32_e32 v167, v231, v169, vcc
	v_lshlrev_b32_e32 v242, 2, v167
	s_waitcnt lgkmcnt(0)
	v_add_f32_e32 v167, v166, v168
	v_mov_b32_e32 v168, v167
	s_nop 1
	v_permlane32_swap_b32_e32 v168, v167
	v_and_b32_e32 v166, 63, v239
	v_cmp_gt_u32_e64 s[38:39], 16, v166
	s_and_saveexec_b64 s[6:7], s[38:39]
	s_load_dwordx2 s[90:91], s[0:1], 0xb0
	v_readlane_b32 s64, v252, 3
	v_readlane_b32 s65, v255, 10
	v_readlane_b32 s68, v255, 11
	s_movk_i32 s92, 0x2b20
	s_cbranch_execz .LBB0_2477
	s_lshl_b32 s8, s80, 10
	s_add_i32 s8, s30, s8
	s_waitcnt lgkmcnt(0)
	v_add_f32_e32 v167, v167, v168
	v_lshl_add_u32 v168, v0, 4, s8
	ds_write_b32 v168, v167
.LBB0_2477:
	s_or_b64 exec, exec, s[6:7]
	v_mul_f32_e32 v167, v111, v111
	s_waitcnt lgkmcnt(0)
	v_mul_f32_e32 v168, v113, v113
	v_fmac_f32_e32 v167, v110, v110
	v_fmac_f32_e32 v168, v112, v112
	v_add_f32_e32 v167, v167, v168
	v_mul_f32_e32 v168, v107, v107
	v_mul_f32_e32 v169, v109, v109
	v_fmac_f32_e32 v168, v106, v106
	v_fmac_f32_e32 v169, v108, v108
	v_add_f32_e32 v168, v168, v169
	v_add_f32_e32 v167, v168, v167
	v_mul_f32_e32 v168, v103, v103
	v_mul_f32_e32 v169, v105, v105
	v_fmac_f32_e32 v168, v102, v102
	v_fmac_f32_e32 v169, v104, v104
	v_add_f32_e32 v168, v168, v169
	v_add_f32_e32 v167, v168, v167
	v_mul_f32_e32 v168, v99, v99
	v_mul_f32_e32 v169, v101, v101
	v_fmac_f32_e32 v168, v98, v98
	v_fmac_f32_e32 v169, v100, v100
	v_add_f32_e32 v168, v168, v169
	v_add_f32_e32 v167, v168, v167
	v_mov_b32_e32 v168, v167
	s_nop 1
	v_permlane16_swap_b32_e32 v168, v167
	s_waitcnt lgkmcnt(0)
	v_add_f32_e32 v167, v167, v168
	v_mov_b32_e32 v168, v167
	s_nop 1
	v_permlane32_swap_b32_e32 v168, v167
	s_and_saveexec_b64 s[6:7], s[38:39]
	v_readlane_b32 s74, v255, 12
	v_readlane_b32 s95, v255, 13
	s_cbranch_execz .LBB0_2479
	s_lshl_b32 s8, s80, 10
	s_add_i32 s8, s30, s8
	s_waitcnt lgkmcnt(0)
	v_add_f32_e32 v167, v167, v168
	v_lshl_add_u32 v168, v0, 4, s8
	ds_write_b32 v168, v167 offset:256
.LBB0_2479:
	s_or_b64 exec, exec, s[6:7]
	v_mul_f32_e32 v167, v95, v95
	s_waitcnt lgkmcnt(0)
	v_mul_f32_e32 v168, v97, v97
	v_fmac_f32_e32 v167, v94, v94
	v_fmac_f32_e32 v168, v96, v96
	v_add_f32_e32 v167, v167, v168
	v_mul_f32_e32 v168, v91, v91
	v_mul_f32_e32 v169, v93, v93
	v_fmac_f32_e32 v168, v90, v90
	v_fmac_f32_e32 v169, v92, v92
	v_add_f32_e32 v168, v168, v169
	v_add_f32_e32 v167, v168, v167
	v_mul_f32_e32 v168, v87, v87
	v_mul_f32_e32 v169, v89, v89
	v_fmac_f32_e32 v168, v86, v86
	v_fmac_f32_e32 v169, v88, v88
	v_add_f32_e32 v168, v168, v169
	v_add_f32_e32 v167, v168, v167
	v_mul_f32_e32 v168, v83, v83
	v_mul_f32_e32 v169, v85, v85
	v_fmac_f32_e32 v168, v82, v82
	v_fmac_f32_e32 v169, v84, v84
	v_add_f32_e32 v168, v168, v169
	v_add_f32_e32 v167, v168, v167
	v_mov_b32_e32 v168, v167
	s_nop 1
	v_permlane16_swap_b32_e32 v168, v167
	s_waitcnt lgkmcnt(0)
	v_add_f32_e32 v167, v167, v168
	v_mov_b32_e32 v168, v167
	s_nop 1
	v_permlane32_swap_b32_e32 v168, v167
	s_and_saveexec_b64 s[6:7], s[38:39]
	s_cbranch_execz .LBB0_2481
	s_lshl_b32 s8, s80, 10
	s_add_i32 s8, s30, s8
	s_waitcnt lgkmcnt(0)
	v_add_f32_e32 v167, v167, v168
	v_lshl_add_u32 v168, v0, 4, s8
	ds_write_b32 v168, v167 offset:512
.LBB0_2481:
	s_or_b64 exec, exec, s[6:7]
	v_mul_f32_e32 v167, v79, v79
	s_waitcnt lgkmcnt(0)
	v_mul_f32_e32 v168, v81, v81
	v_fmac_f32_e32 v167, v78, v78
	v_fmac_f32_e32 v168, v80, v80
	v_add_f32_e32 v167, v167, v168
	v_mul_f32_e32 v168, v75, v75
	v_mul_f32_e32 v169, v77, v77
	v_fmac_f32_e32 v168, v74, v74
	v_fmac_f32_e32 v169, v76, v76
	v_add_f32_e32 v168, v168, v169
	v_add_f32_e32 v167, v168, v167
	v_mul_f32_e32 v168, v71, v71
	v_mul_f32_e32 v169, v73, v73
	v_fmac_f32_e32 v168, v70, v70
	v_fmac_f32_e32 v169, v72, v72
	v_add_f32_e32 v168, v168, v169
	v_add_f32_e32 v167, v168, v167
	v_mul_f32_e32 v168, v67, v67
	v_mul_f32_e32 v169, v69, v69
	v_fmac_f32_e32 v168, v66, v66
	v_fmac_f32_e32 v169, v68, v68
	v_add_f32_e32 v168, v168, v169
	v_add_f32_e32 v167, v168, v167
	v_mov_b32_e32 v168, v167
	s_nop 1
	v_permlane16_swap_b32_e32 v168, v167
	s_waitcnt lgkmcnt(0)
	v_add_f32_e32 v167, v167, v168
	v_mov_b32_e32 v168, v167
	s_nop 1
	v_permlane32_swap_b32_e32 v168, v167
	s_and_saveexec_b64 s[6:7], s[38:39]
	s_cbranch_execz .LBB0_2483
	s_lshl_b32 s8, s80, 10
	s_add_i32 s8, s30, s8
	s_waitcnt lgkmcnt(0)
	v_add_f32_e32 v167, v167, v168
	v_lshl_add_u32 v168, v0, 4, s8
	ds_write_b32 v168, v167 offset:768
.LBB0_2483:
	s_or_b64 exec, exec, s[6:7]
	v_mul_f32_e32 v167, v63, v63
	s_waitcnt lgkmcnt(0)
	v_mul_f32_e32 v168, v65, v65
	v_fmac_f32_e32 v167, v62, v62
	v_fmac_f32_e32 v168, v64, v64
	v_add_f32_e32 v167, v167, v168
	v_mul_f32_e32 v168, v59, v59
	v_mul_f32_e32 v169, v61, v61
	v_fmac_f32_e32 v168, v58, v58
	v_fmac_f32_e32 v169, v60, v60
	v_add_f32_e32 v168, v168, v169
	v_add_f32_e32 v167, v168, v167
	v_mul_f32_e32 v168, v55, v55
	v_mul_f32_e32 v169, v57, v57
	v_fmac_f32_e32 v168, v54, v54
	v_fmac_f32_e32 v169, v56, v56
	v_add_f32_e32 v168, v168, v169
	v_add_f32_e32 v167, v168, v167
	v_mul_f32_e32 v168, v51, v51
	v_mul_f32_e32 v169, v53, v53
	v_fmac_f32_e32 v168, v50, v50
	v_fmac_f32_e32 v169, v52, v52
	v_add_f32_e32 v168, v168, v169
	v_add_f32_e32 v167, v168, v167
	v_mov_b32_e32 v168, v167
	s_nop 1
	v_permlane16_swap_b32_e32 v168, v167
	s_waitcnt lgkmcnt(0)
	v_add_f32_e32 v167, v167, v168
	v_mov_b32_e32 v168, v167
	s_nop 1
	v_permlane32_swap_b32_e32 v168, v167
	s_and_saveexec_b64 s[6:7], s[38:39]
	s_cbranch_execz .LBB0_2485
	s_lshl_b32 s8, s80, 10
	s_add_i32 s8, s30, s8
	s_waitcnt lgkmcnt(0)
	v_add_f32_e32 v167, v167, v168
	v_lshl_add_u32 v168, v0, 4, s8
	ds_write_b32 v168, v167 offset:2048
.LBB0_2485:
	s_or_b64 exec, exec, s[6:7]
	v_mul_f32_e32 v167, v47, v47
	s_waitcnt lgkmcnt(0)
	v_mul_f32_e32 v168, v49, v49
	v_fmac_f32_e32 v167, v46, v46
	v_fmac_f32_e32 v168, v48, v48
	v_add_f32_e32 v167, v167, v168
	v_mul_f32_e32 v168, v43, v43
	v_mul_f32_e32 v169, v45, v45
	v_fmac_f32_e32 v168, v42, v42
	v_fmac_f32_e32 v169, v44, v44
	v_add_f32_e32 v168, v168, v169
	v_add_f32_e32 v167, v168, v167
	v_mul_f32_e32 v168, v39, v39
	v_mul_f32_e32 v169, v41, v41
	v_fmac_f32_e32 v168, v38, v38
	v_fmac_f32_e32 v169, v40, v40
	v_add_f32_e32 v168, v168, v169
	v_add_f32_e32 v167, v168, v167
	v_mul_f32_e32 v168, v35, v35
	v_mul_f32_e32 v169, v37, v37
	v_fmac_f32_e32 v168, v34, v34
	v_fmac_f32_e32 v169, v36, v36
	v_add_f32_e32 v168, v168, v169
	v_add_f32_e32 v167, v168, v167
	v_mov_b32_e32 v168, v167
	s_nop 1
	v_permlane16_swap_b32_e32 v168, v167
	s_waitcnt lgkmcnt(0)
	v_add_f32_e32 v167, v167, v168
	v_mov_b32_e32 v168, v167
	s_nop 1
	v_permlane32_swap_b32_e32 v168, v167
	s_and_saveexec_b64 s[6:7], s[38:39]
	s_cbranch_execz .LBB0_2487
	s_lshl_b32 s8, s80, 10
	s_add_i32 s8, s30, s8
	s_waitcnt lgkmcnt(0)
	v_add_f32_e32 v167, v167, v168
	v_lshl_add_u32 v168, v0, 4, s8
	ds_write_b32 v168, v167 offset:2304
.LBB0_2487:
	s_or_b64 exec, exec, s[6:7]
	v_mul_f32_e32 v167, v31, v31
	s_waitcnt lgkmcnt(0)
	v_mul_f32_e32 v168, v33, v33
	v_fmac_f32_e32 v167, v30, v30
	v_fmac_f32_e32 v168, v32, v32
	v_add_f32_e32 v167, v167, v168
	v_mul_f32_e32 v168, v27, v27
	v_mul_f32_e32 v169, v29, v29
	v_fmac_f32_e32 v168, v26, v26
	v_fmac_f32_e32 v169, v28, v28
	v_add_f32_e32 v168, v168, v169
	v_add_f32_e32 v167, v168, v167
	v_mul_f32_e32 v168, v23, v23
	v_mul_f32_e32 v169, v25, v25
	v_fmac_f32_e32 v168, v22, v22
	v_fmac_f32_e32 v169, v24, v24
	v_add_f32_e32 v168, v168, v169
	v_add_f32_e32 v167, v168, v167
	v_mul_f32_e32 v168, v19, v19
	v_mul_f32_e32 v169, v21, v21
	v_fmac_f32_e32 v168, v18, v18
	v_fmac_f32_e32 v169, v20, v20
	v_add_f32_e32 v168, v168, v169
	v_add_f32_e32 v167, v168, v167
	v_mov_b32_e32 v168, v167
	s_nop 1
	v_permlane16_swap_b32_e32 v168, v167
	s_waitcnt lgkmcnt(0)
	v_add_f32_e32 v167, v167, v168
	v_mov_b32_e32 v168, v167
	s_nop 1
	v_permlane32_swap_b32_e32 v168, v167
	s_and_saveexec_b64 s[6:7], s[38:39]
	s_cbranch_execz .LBB0_2489
	s_lshl_b32 s8, s80, 10
	s_add_i32 s8, s30, s8
	s_waitcnt lgkmcnt(0)
	v_add_f32_e32 v167, v167, v168
	v_lshl_add_u32 v168, v0, 4, s8
	ds_write_b32 v168, v167 offset:2560
.LBB0_2489:
	s_or_b64 exec, exec, s[6:7]
	v_mul_f32_e32 v167, v15, v15
	s_waitcnt lgkmcnt(0)
	v_mul_f32_e32 v168, v17, v17
	v_fmac_f32_e32 v167, v14, v14
	v_fmac_f32_e32 v168, v16, v16
	v_add_f32_e32 v167, v167, v168
	v_mul_f32_e32 v168, v11, v11
	v_mul_f32_e32 v169, v13, v13
	v_fmac_f32_e32 v168, v10, v10
	v_fmac_f32_e32 v169, v12, v12
	v_add_f32_e32 v168, v168, v169
	v_add_f32_e32 v167, v168, v167
	v_mul_f32_e32 v168, v7, v7
	v_mul_f32_e32 v169, v9, v9
	v_fmac_f32_e32 v168, v6, v6
	v_fmac_f32_e32 v169, v8, v8
	v_add_f32_e32 v168, v168, v169
	v_add_f32_e32 v167, v168, v167
	v_mul_f32_e32 v168, v3, v3
	v_mul_f32_e32 v169, v5, v5
	v_fmac_f32_e32 v168, v2, v2
	v_fmac_f32_e32 v169, v4, v4
	v_add_f32_e32 v168, v168, v169
	v_add_f32_e32 v167, v168, v167
	v_mov_b32_e32 v168, v167
	s_nop 1
	v_permlane16_swap_b32_e32 v168, v167
	s_waitcnt lgkmcnt(0)
	v_add_f32_e32 v167, v167, v168
	v_mov_b32_e32 v168, v167
	s_nop 1
	v_permlane32_swap_b32_e32 v168, v167
	s_and_saveexec_b64 s[6:7], s[38:39]
	s_cbranch_execz .LBB0_2491
	s_lshl_b32 s8, s80, 10
	s_add_i32 s8, s30, s8
	s_waitcnt lgkmcnt(0)
	v_add_f32_e32 v167, v167, v168
	v_lshl_add_u32 v0, v0, 4, s8
	ds_write_b32 v0, v167 offset:2816

.LBB0_2517:
	s_waitcnt vmcnt(0)
	v_lshlrev_b32_e32 v216, 16, v206
	v_and_b32_e32 v217, 0xffff0000, v206
	v_lshlrev_b32_e32 v206, 16, v207
	v_and_b32_e32 v207, 0xffff0000, v207
	s_waitcnt lgkmcnt(0)
	v_pk_mul_f32 v[136:137], v[136:137], v[0:1] op_sel_hi:[1,0]
	v_pk_mul_f32 v[134:135], v[134:135], v[0:1] op_sel_hi:[1,0]
	v_lshlrev_b32_e32 v218, 16, v208
	v_and_b32_e32 v219, 0xffff0000, v208
	v_lshlrev_b32_e32 v208, 16, v209
	v_and_b32_e32 v209, 0xffff0000, v209
	v_pk_fma_f32 v[136:137], v[184:185], v[136:137], v[206:207]
	v_pk_fma_f32 v[134:135], v[182:183], v[134:135], v[216:217]
	v_pk_mul_f32 v[132:133], v[132:133], v[0:1] op_sel_hi:[1,0]
	v_pk_mul_f32 v[130:131], v[130:131], v[0:1] op_sel_hi:[1,0]
	v_pk_fma_f32 v[206:207], v[180:181], v[132:133], v[208:209]
	v_pk_fma_f32 v[132:133], v[178:179], v[130:131], v[218:219]
	v_mul_f32_e32 v130, v135, v135
	v_mul_f32_e32 v131, v137, v137
	v_fmac_f32_e32 v130, v134, v134
	v_fmac_f32_e32 v131, v136, v136
	v_add_f32_e32 v130, v130, v131
	v_mul_f32_e32 v131, v133, v133
	v_mul_f32_e32 v208, v207, v207
	v_fmac_f32_e32 v131, v132, v132
	v_fmac_f32_e32 v208, v206, v206
	v_add_f32_e32 v131, v131, v208
	v_add_f32_e32 v208, v130, v131
	v_cvt_pk_bf16_f32 v130, v134, v135
	v_cvt_pk_bf16_f32 v131, v136, v137
	v_lshlrev_b32_e32 v134, 16, v202
	v_and_b32_e32 v135, 0xffff0000, v202
	v_lshlrev_b32_e32 v136, 16, v203
	v_and_b32_e32 v137, 0xffff0000, v203
	v_pk_mul_f32 v[120:121], v[120:121], v[0:1] op_sel_hi:[1,0]
	v_pk_mul_f32 v[118:119], v[118:119], v[0:1] op_sel_hi:[1,0]
	v_lshlrev_b32_e32 v202, 16, v204
	v_and_b32_e32 v203, 0xffff0000, v204
	v_pk_fma_f32 v[120:121], v[172:173], v[120:121], v[136:137]
	v_pk_fma_f32 v[118:119], v[170:171], v[118:119], v[134:135]
	v_pk_mul_f32 v[114:115], v[114:115], v[0:1] op_sel_hi:[1,0]
	v_lshlrev_b32_e32 v204, 16, v205
	v_and_b32_e32 v205, 0xffff0000, v205
	v_pk_mul_f32 v[116:117], v[116:117], v[0:1] op_sel_hi:[1,0]
	v_pk_fma_f32 v[136:137], v[166:167], v[114:115], v[202:203]
	v_mul_f32_e32 v0, v119, v119
	v_mul_f32_e32 v114, v121, v121
	v_pk_fma_f32 v[134:135], v[168:169], v[116:117], v[204:205]
	v_fmac_f32_e32 v0, v118, v118
	v_fmac_f32_e32 v114, v120, v120
	v_add_f32_e32 v0, v0, v114
	v_mul_f32_e32 v114, v137, v137
	v_mul_f32_e32 v115, v135, v135
	v_fmac_f32_e32 v114, v136, v136
	v_fmac_f32_e32 v115, v134, v134
	v_add_f32_e32 v114, v114, v115
	v_add_f32_e32 v0, v0, v114
	v_add_f32_e32 v0, v208, v0
	v_mov_b32_e32 v117, v0
	s_nop 1
	v_permlane16_swap_b32_e32 v117, v0
	s_add_u32 s6, s16, s18
	s_addc_u32 s7, s17, s19
	v_lshl_add_u64 v[114:115], s[6:7], 0, v[224:225]
	v_lshl_add_u64 v[202:203], v[220:221], 1, v[114:115]
	s_waitcnt lgkmcnt(0)
	v_add_f32_e32 v0, v0, v117
	v_mov_b32_e32 v114, v0
	s_nop 1
	v_permlane32_swap_b32_e32 v114, v0
	v_cvt_pk_bf16_f32 v132, v132, v133
	v_cvt_pk_bf16_f32 v133, v206, v207
	global_store_dwordx4 v[202:203], v[130:133], off
	v_cvt_pk_bf16_f32 v116, v118, v119
	v_cvt_pk_bf16_f32 v117, v120, v121
	v_cvt_pk_bf16_f32 v118, v136, v137
	v_cvt_pk_bf16_f32 v119, v134, v135
	global_store_dwordx4 v[202:203], v[116:119], off offset:256
	s_and_saveexec_b64 s[10:11], s[38:39]
	s_cbranch_execz .LBB0_2519
	v_lshl_add_u32 v115, v240, 4, s30
	s_waitcnt lgkmcnt(0)
	v_add_f32_e32 v0, v0, v114
	ds_write_b32 v115, v0 offset:6144

.LBB0_2521:
	v_lshlrev_b32_e32 v118, 16, v198
	v_and_b32_e32 v119, 0xffff0000, v198
	v_lshlrev_b32_e32 v120, 16, v199
	v_and_b32_e32 v121, 0xffff0000, v199
	s_waitcnt lgkmcnt(0)
	v_pk_mul_f32 v[112:113], v[112:113], v[0:1] op_sel_hi:[1,0]
	v_pk_mul_f32 v[110:111], v[110:111], v[0:1] op_sel_hi:[1,0]
	v_lshlrev_b32_e32 v130, 16, v200
	v_and_b32_e32 v131, 0xffff0000, v200
	v_lshlrev_b32_e32 v132, 16, v201
	v_and_b32_e32 v133, 0xffff0000, v201
	v_pk_fma_f32 v[112:113], v[184:185], v[112:113], v[120:121]
	v_pk_fma_f32 v[110:111], v[182:183], v[110:111], v[118:119]
	v_pk_mul_f32 v[108:109], v[108:109], v[0:1] op_sel_hi:[1,0]
	v_pk_mul_f32 v[106:107], v[106:107], v[0:1] op_sel_hi:[1,0]
	v_pk_fma_f32 v[118:119], v[180:181], v[108:109], v[132:133]
	v_pk_fma_f32 v[108:109], v[178:179], v[106:107], v[130:131]
	v_mul_f32_e32 v106, v111, v111
	v_mul_f32_e32 v107, v113, v113
	v_fmac_f32_e32 v106, v110, v110
	v_fmac_f32_e32 v107, v112, v112
	v_add_f32_e32 v106, v106, v107
	v_mul_f32_e32 v107, v109, v109
	v_mul_f32_e32 v115, v119, v119
	v_fmac_f32_e32 v107, v108, v108
	v_fmac_f32_e32 v115, v118, v118
	v_add_f32_e32 v107, v107, v115
	v_add_f32_e32 v115, v106, v107
	v_cvt_pk_bf16_f32 v106, v110, v111
	v_cvt_pk_bf16_f32 v107, v112, v113
	v_lshlrev_b32_e32 v110, 16, v194
	v_and_b32_e32 v111, 0xffff0000, v194
	v_lshlrev_b32_e32 v112, 16, v195
	v_and_b32_e32 v113, 0xffff0000, v195
	v_pk_mul_f32 v[104:105], v[104:105], v[0:1] op_sel_hi:[1,0]
	v_pk_mul_f32 v[102:103], v[102:103], v[0:1] op_sel_hi:[1,0]
	v_cvt_pk_bf16_f32 v108, v108, v109
	v_cvt_pk_bf16_f32 v109, v118, v119
	v_lshlrev_b32_e32 v118, 16, v196
	v_and_b32_e32 v119, 0xffff0000, v196
	v_pk_fma_f32 v[104:105], v[172:173], v[104:105], v[112:113]
	v_pk_fma_f32 v[102:103], v[170:171], v[102:103], v[110:111]
	v_pk_mul_f32 v[98:99], v[98:99], v[0:1] op_sel_hi:[1,0]
	v_lshlrev_b32_e32 v120, 16, v197
	v_and_b32_e32 v121, 0xffff0000, v197
	v_pk_mul_f32 v[100:101], v[100:101], v[0:1] op_sel_hi:[1,0]
	v_pk_fma_f32 v[112:113], v[166:167], v[98:99], v[118:119]
	v_mul_f32_e32 v0, v103, v103
	v_mul_f32_e32 v98, v105, v105
	v_pk_fma_f32 v[110:111], v[168:169], v[100:101], v[120:121]
	v_fmac_f32_e32 v0, v102, v102
	v_fmac_f32_e32 v98, v104, v104
	v_add_f32_e32 v0, v0, v98
	v_mul_f32_e32 v98, v113, v113
	v_mul_f32_e32 v99, v111, v111
	v_fmac_f32_e32 v98, v112, v112
	v_fmac_f32_e32 v99, v110, v110
	v_add_f32_e32 v98, v98, v99
	v_add_f32_e32 v0, v0, v98
	v_add_f32_e32 v0, v115, v0
	v_mov_b32_e32 v101, v0
	s_nop 1
	v_permlane16_swap_b32_e32 v101, v0
	v_or_b32_e32 v114, 16, v240
	v_add_u32_e32 v116, s31, v114
	v_ashrrev_i32_e32 v117, 31, v116
	v_lshlrev_b64 v[116:117], 11, v[116:117]
	v_lshl_add_u64 v[98:99], s[6:7], 0, v[116:117]
	s_waitcnt lgkmcnt(0)
	v_add_f32_e32 v0, v0, v101
	v_lshl_add_u64 v[116:117], v[220:221], 1, v[98:99]
	v_mov_b32_e32 v98, v0
	s_nop 1
	v_permlane32_swap_b32_e32 v98, v0
	global_store_dwordx4 v[116:117], v[106:109], off
	v_cvt_pk_bf16_f32 v100, v102, v103
	v_cvt_pk_bf16_f32 v101, v104, v105
	v_cvt_pk_bf16_f32 v102, v112, v113
	v_cvt_pk_bf16_f32 v103, v110, v111
	global_store_dwordx4 v[116:117], v[100:103], off offset:256
	s_and_saveexec_b64 s[10:11], s[38:39]
	s_cbranch_execz .LBB0_2523
	v_lshl_add_u32 v99, v114, 4, s30
	s_waitcnt lgkmcnt(0)
	v_add_f32_e32 v0, v0, v98
	ds_write_b32 v99, v0 offset:6144

.LBB0_2525:
	v_lshlrev_b32_e32 v102, 16, v190
	v_and_b32_e32 v103, 0xffff0000, v190
	v_lshlrev_b32_e32 v104, 16, v191
	v_and_b32_e32 v105, 0xffff0000, v191
	s_waitcnt lgkmcnt(0)
	v_pk_mul_f32 v[96:97], v[96:97], v[0:1] op_sel_hi:[1,0]
	v_pk_mul_f32 v[94:95], v[94:95], v[0:1] op_sel_hi:[1,0]
	v_lshlrev_b32_e32 v106, 16, v192
	v_and_b32_e32 v107, 0xffff0000, v192
	v_lshlrev_b32_e32 v108, 16, v193
	v_and_b32_e32 v109, 0xffff0000, v193
	v_pk_fma_f32 v[96:97], v[184:185], v[96:97], v[104:105]
	v_pk_fma_f32 v[94:95], v[182:183], v[94:95], v[102:103]
	v_pk_mul_f32 v[92:93], v[92:93], v[0:1] op_sel_hi:[1,0]
	v_pk_mul_f32 v[90:91], v[90:91], v[0:1] op_sel_hi:[1,0]
	v_pk_fma_f32 v[102:103], v[180:181], v[92:93], v[108:109]
	v_pk_fma_f32 v[92:93], v[178:179], v[90:91], v[106:107]
	v_mul_f32_e32 v90, v95, v95
	v_mul_f32_e32 v91, v97, v97
	v_fmac_f32_e32 v90, v94, v94
	v_fmac_f32_e32 v91, v96, v96
	v_add_f32_e32 v90, v90, v91
	v_mul_f32_e32 v91, v93, v93
	v_mul_f32_e32 v99, v103, v103
	v_fmac_f32_e32 v91, v92, v92
	v_fmac_f32_e32 v99, v102, v102
	v_add_f32_e32 v91, v91, v99
	v_add_f32_e32 v99, v90, v91
	v_cvt_pk_bf16_f32 v90, v94, v95
	v_cvt_pk_bf16_f32 v91, v96, v97
	v_lshlrev_b32_e32 v94, 16, v186
	v_and_b32_e32 v95, 0xffff0000, v186
	v_lshlrev_b32_e32 v96, 16, v187
	v_and_b32_e32 v97, 0xffff0000, v187
	v_pk_mul_f32 v[88:89], v[88:89], v[0:1] op_sel_hi:[1,0]
	v_pk_mul_f32 v[86:87], v[86:87], v[0:1] op_sel_hi:[1,0]
	v_cvt_pk_bf16_f32 v92, v92, v93
	v_cvt_pk_bf16_f32 v93, v102, v103
	v_lshlrev_b32_e32 v102, 16, v188
	v_and_b32_e32 v103, 0xffff0000, v188
	v_pk_fma_f32 v[88:89], v[172:173], v[88:89], v[96:97]
	v_pk_fma_f32 v[86:87], v[170:171], v[86:87], v[94:95]
	v_pk_mul_f32 v[82:83], v[82:83], v[0:1] op_sel_hi:[1,0]
	v_lshlrev_b32_e32 v104, 16, v189
	v_and_b32_e32 v105, 0xffff0000, v189
	v_pk_mul_f32 v[84:85], v[84:85], v[0:1] op_sel_hi:[1,0]
	v_pk_fma_f32 v[96:97], v[166:167], v[82:83], v[102:103]
	v_mul_f32_e32 v0, v87, v87
	v_mul_f32_e32 v82, v89, v89
	v_pk_fma_f32 v[94:95], v[168:169], v[84:85], v[104:105]
	v_fmac_f32_e32 v0, v86, v86
	v_fmac_f32_e32 v82, v88, v88
	v_add_f32_e32 v0, v0, v82
	v_mul_f32_e32 v82, v97, v97
	v_mul_f32_e32 v83, v95, v95
	v_fmac_f32_e32 v82, v96, v96
	v_fmac_f32_e32 v83, v94, v94
	v_add_f32_e32 v82, v82, v83
	v_add_f32_e32 v0, v0, v82
	v_add_f32_e32 v0, v99, v0
	v_mov_b32_e32 v85, v0
	s_nop 1
	v_permlane16_swap_b32_e32 v85, v0
	v_or_b32_e32 v98, 32, v240
	v_add_u32_e32 v100, s31, v98
	v_ashrrev_i32_e32 v101, 31, v100
	v_lshlrev_b64 v[100:101], 11, v[100:101]
	v_lshl_add_u64 v[82:83], s[6:7], 0, v[100:101]
	s_waitcnt lgkmcnt(0)
	v_add_f32_e32 v0, v0, v85
	v_lshl_add_u64 v[100:101], v[220:221], 1, v[82:83]
	v_mov_b32_e32 v82, v0
	s_nop 1
	v_permlane32_swap_b32_e32 v82, v0
	global_store_dwordx4 v[100:101], v[90:93], off
	v_cvt_pk_bf16_f32 v84, v86, v87
	v_cvt_pk_bf16_f32 v85, v88, v89
	v_cvt_pk_bf16_f32 v86, v96, v97
	v_cvt_pk_bf16_f32 v87, v94, v95
	global_store_dwordx4 v[100:101], v[84:87], off offset:256
	s_and_saveexec_b64 s[10:11], s[38:39]
	s_cbranch_execz .LBB0_2527
	v_lshl_add_u32 v83, v98, 4, s30
	s_waitcnt lgkmcnt(0)
	v_add_f32_e32 v0, v0, v82
	ds_write_b32 v83, v0 offset:6144

.LBB0_2529:
	v_lshlrev_b32_e32 v86, 16, v174
	v_and_b32_e32 v87, 0xffff0000, v174
	v_lshlrev_b32_e32 v88, 16, v175
	v_and_b32_e32 v89, 0xffff0000, v175
	s_waitcnt lgkmcnt(0)
	v_pk_mul_f32 v[80:81], v[80:81], v[0:1] op_sel_hi:[1,0]
	v_pk_mul_f32 v[78:79], v[78:79], v[0:1] op_sel_hi:[1,0]
	v_lshlrev_b32_e32 v90, 16, v176
	v_and_b32_e32 v91, 0xffff0000, v176
	v_lshlrev_b32_e32 v92, 16, v177
	v_and_b32_e32 v93, 0xffff0000, v177
	v_pk_fma_f32 v[80:81], v[184:185], v[80:81], v[88:89]
	v_pk_fma_f32 v[78:79], v[182:183], v[78:79], v[86:87]
	v_pk_mul_f32 v[76:77], v[76:77], v[0:1] op_sel_hi:[1,0]
	v_pk_mul_f32 v[74:75], v[74:75], v[0:1] op_sel_hi:[1,0]
	v_pk_fma_f32 v[86:87], v[180:181], v[76:77], v[92:93]
	v_pk_fma_f32 v[76:77], v[178:179], v[74:75], v[90:91]
	v_mul_f32_e32 v74, v79, v79
	v_mul_f32_e32 v75, v81, v81
	v_fmac_f32_e32 v74, v78, v78
	v_fmac_f32_e32 v75, v80, v80
	v_add_f32_e32 v74, v74, v75
	v_mul_f32_e32 v75, v77, v77
	v_mul_f32_e32 v83, v87, v87
	v_fmac_f32_e32 v75, v76, v76
	v_fmac_f32_e32 v83, v86, v86
	v_add_f32_e32 v75, v75, v83
	v_add_f32_e32 v83, v74, v75
	v_cvt_pk_bf16_f32 v74, v78, v79
	v_cvt_pk_bf16_f32 v75, v80, v81
	v_lshlrev_b32_e32 v78, 16, v162
	v_and_b32_e32 v79, 0xffff0000, v162
	v_lshlrev_b32_e32 v80, 16, v163
	v_and_b32_e32 v81, 0xffff0000, v163
	v_pk_mul_f32 v[72:73], v[72:73], v[0:1] op_sel_hi:[1,0]
	v_pk_mul_f32 v[70:71], v[70:71], v[0:1] op_sel_hi:[1,0]
	v_cvt_pk_bf16_f32 v76, v76, v77
	v_cvt_pk_bf16_f32 v77, v86, v87
	v_lshlrev_b32_e32 v86, 16, v164
	v_and_b32_e32 v87, 0xffff0000, v164
	v_pk_fma_f32 v[72:73], v[172:173], v[72:73], v[80:81]
	v_pk_fma_f32 v[70:71], v[170:171], v[70:71], v[78:79]
	v_pk_mul_f32 v[66:67], v[66:67], v[0:1] op_sel_hi:[1,0]
	v_lshlrev_b32_e32 v88, 16, v165
	v_and_b32_e32 v89, 0xffff0000, v165
	v_pk_mul_f32 v[68:69], v[68:69], v[0:1] op_sel_hi:[1,0]
	v_pk_fma_f32 v[80:81], v[166:167], v[66:67], v[86:87]
	v_mul_f32_e32 v0, v71, v71
	v_mul_f32_e32 v66, v73, v73
	v_pk_fma_f32 v[78:79], v[168:169], v[68:69], v[88:89]
	v_fmac_f32_e32 v0, v70, v70
	v_fmac_f32_e32 v66, v72, v72
	v_add_f32_e32 v0, v0, v66
	v_mul_f32_e32 v66, v81, v81
	v_mul_f32_e32 v67, v79, v79
	v_fmac_f32_e32 v66, v80, v80
	v_fmac_f32_e32 v67, v78, v78
	v_add_f32_e32 v66, v66, v67
	v_add_f32_e32 v0, v0, v66
	v_add_f32_e32 v0, v83, v0
	v_mov_b32_e32 v69, v0
	s_nop 1
	v_permlane16_swap_b32_e32 v69, v0
	v_or_b32_e32 v82, 48, v240
	v_add_u32_e32 v84, s31, v82
	v_ashrrev_i32_e32 v85, 31, v84
	v_lshlrev_b64 v[84:85], 11, v[84:85]
	v_lshl_add_u64 v[66:67], s[6:7], 0, v[84:85]
	s_waitcnt lgkmcnt(0)
	v_add_f32_e32 v0, v0, v69
	v_lshl_add_u64 v[84:85], v[220:221], 1, v[66:67]
	v_mov_b32_e32 v66, v0
	s_nop 1
	v_permlane32_swap_b32_e32 v66, v0
	global_store_dwordx4 v[84:85], v[74:77], off
	v_cvt_pk_bf16_f32 v68, v70, v71
	v_cvt_pk_bf16_f32 v69, v72, v73
	v_cvt_pk_bf16_f32 v70, v80, v81
	v_cvt_pk_bf16_f32 v71, v78, v79
	global_store_dwordx4 v[84:85], v[68:71], off offset:256
	s_and_saveexec_b64 s[10:11], s[38:39]
	s_cbranch_execz .LBB0_2531
	v_lshl_add_u32 v67, v82, 4, s30
	s_waitcnt lgkmcnt(0)
	v_add_f32_e32 v0, v0, v66
	ds_write_b32 v67, v0 offset:6144

.LBB0_2533:
	v_lshlrev_b32_e32 v70, 16, v158
	v_and_b32_e32 v71, 0xffff0000, v158
	v_lshlrev_b32_e32 v72, 16, v159
	v_and_b32_e32 v73, 0xffff0000, v159
	s_waitcnt lgkmcnt(0)
	v_pk_mul_f32 v[64:65], v[64:65], v[0:1] op_sel_hi:[1,0]
	v_pk_mul_f32 v[62:63], v[62:63], v[0:1] op_sel_hi:[1,0]
	v_lshlrev_b32_e32 v74, 16, v160
	v_and_b32_e32 v75, 0xffff0000, v160
	v_lshlrev_b32_e32 v76, 16, v161
	v_and_b32_e32 v77, 0xffff0000, v161
	v_pk_fma_f32 v[64:65], v[184:185], v[64:65], v[72:73]
	v_pk_fma_f32 v[62:63], v[182:183], v[62:63], v[70:71]
	v_pk_mul_f32 v[60:61], v[60:61], v[0:1] op_sel_hi:[1,0]
	v_pk_mul_f32 v[58:59], v[58:59], v[0:1] op_sel_hi:[1,0]
	v_pk_fma_f32 v[70:71], v[180:181], v[60:61], v[76:77]
	v_pk_fma_f32 v[60:61], v[178:179], v[58:59], v[74:75]
	v_mul_f32_e32 v58, v63, v63
	v_mul_f32_e32 v59, v65, v65
	v_fmac_f32_e32 v58, v62, v62
	v_fmac_f32_e32 v59, v64, v64
	v_add_f32_e32 v58, v58, v59
	v_mul_f32_e32 v59, v61, v61
	v_mul_f32_e32 v67, v71, v71
	v_fmac_f32_e32 v59, v60, v60
	v_fmac_f32_e32 v67, v70, v70
	v_add_f32_e32 v59, v59, v67
	v_add_f32_e32 v67, v58, v59
	v_cvt_pk_bf16_f32 v58, v62, v63
	v_cvt_pk_bf16_f32 v59, v64, v65
	v_lshlrev_b32_e32 v62, 16, v154
	v_and_b32_e32 v63, 0xffff0000, v154
	v_lshlrev_b32_e32 v64, 16, v155
	v_and_b32_e32 v65, 0xffff0000, v155
	v_pk_mul_f32 v[56:57], v[56:57], v[0:1] op_sel_hi:[1,0]
	v_pk_mul_f32 v[54:55], v[54:55], v[0:1] op_sel_hi:[1,0]
	v_cvt_pk_bf16_f32 v60, v60, v61
	v_cvt_pk_bf16_f32 v61, v70, v71
	v_lshlrev_b32_e32 v70, 16, v156
	v_and_b32_e32 v71, 0xffff0000, v156
	v_pk_fma_f32 v[56:57], v[172:173], v[56:57], v[64:65]
	v_pk_fma_f32 v[54:55], v[170:171], v[54:55], v[62:63]
	v_pk_mul_f32 v[50:51], v[50:51], v[0:1] op_sel_hi:[1,0]
	v_lshlrev_b32_e32 v72, 16, v157
	v_and_b32_e32 v73, 0xffff0000, v157
	v_pk_mul_f32 v[52:53], v[52:53], v[0:1] op_sel_hi:[1,0]
	v_pk_fma_f32 v[64:65], v[166:167], v[50:51], v[70:71]
	v_mul_f32_e32 v0, v55, v55
	v_mul_f32_e32 v50, v57, v57
	v_pk_fma_f32 v[62:63], v[168:169], v[52:53], v[72:73]
	v_fmac_f32_e32 v0, v54, v54
	v_fmac_f32_e32 v50, v56, v56
	v_add_f32_e32 v0, v0, v50
	v_mul_f32_e32 v50, v65, v65
	v_mul_f32_e32 v51, v63, v63
	v_fmac_f32_e32 v50, v64, v64
	v_fmac_f32_e32 v51, v62, v62
	v_add_f32_e32 v50, v50, v51
	v_add_f32_e32 v0, v0, v50
	v_add_f32_e32 v0, v67, v0
	v_mov_b32_e32 v53, v0
	s_nop 1
	v_permlane16_swap_b32_e32 v53, v0
	v_add_u32_e32 v66, 0x80, v240
	v_add_u32_e32 v68, s31, v66
	v_ashrrev_i32_e32 v69, 31, v68
	v_lshlrev_b64 v[68:69], 11, v[68:69]
	v_lshl_add_u64 v[50:51], s[6:7], 0, v[68:69]
	s_waitcnt lgkmcnt(0)
	v_add_f32_e32 v0, v0, v53
	v_lshl_add_u64 v[68:69], v[220:221], 1, v[50:51]
	v_mov_b32_e32 v50, v0
	s_nop 1
	v_permlane32_swap_b32_e32 v50, v0
	global_store_dwordx4 v[68:69], v[58:61], off
	v_cvt_pk_bf16_f32 v52, v54, v55
	v_cvt_pk_bf16_f32 v53, v56, v57
	v_cvt_pk_bf16_f32 v54, v64, v65
	v_cvt_pk_bf16_f32 v55, v62, v63
	global_store_dwordx4 v[68:69], v[52:55], off offset:256
	s_and_saveexec_b64 s[10:11], s[38:39]
	s_cbranch_execz .LBB0_2535
	v_lshl_add_u32 v51, v66, 4, s30
	s_waitcnt lgkmcnt(0)
	v_add_f32_e32 v0, v0, v50
	ds_write_b32 v51, v0 offset:6144

.LBB0_2537:
	v_lshlrev_b32_e32 v54, 16, v150
	v_and_b32_e32 v55, 0xffff0000, v150
	v_lshlrev_b32_e32 v56, 16, v151
	v_and_b32_e32 v57, 0xffff0000, v151
	s_waitcnt lgkmcnt(0)
	v_pk_mul_f32 v[48:49], v[48:49], v[0:1] op_sel_hi:[1,0]
	v_pk_mul_f32 v[46:47], v[46:47], v[0:1] op_sel_hi:[1,0]
	v_lshlrev_b32_e32 v58, 16, v152
	v_and_b32_e32 v59, 0xffff0000, v152
	v_lshlrev_b32_e32 v60, 16, v153
	v_and_b32_e32 v61, 0xffff0000, v153
	v_pk_fma_f32 v[48:49], v[184:185], v[48:49], v[56:57]
	v_pk_fma_f32 v[46:47], v[182:183], v[46:47], v[54:55]
	v_pk_mul_f32 v[44:45], v[44:45], v[0:1] op_sel_hi:[1,0]
	v_pk_mul_f32 v[42:43], v[42:43], v[0:1] op_sel_hi:[1,0]
	v_pk_fma_f32 v[54:55], v[180:181], v[44:45], v[60:61]
	v_pk_fma_f32 v[44:45], v[178:179], v[42:43], v[58:59]
	v_mul_f32_e32 v42, v47, v47
	v_mul_f32_e32 v43, v49, v49
	v_fmac_f32_e32 v42, v46, v46
	v_fmac_f32_e32 v43, v48, v48
	v_add_f32_e32 v42, v42, v43
	v_mul_f32_e32 v43, v45, v45
	v_mul_f32_e32 v51, v55, v55
	v_fmac_f32_e32 v43, v44, v44
	v_fmac_f32_e32 v51, v54, v54
	v_add_f32_e32 v43, v43, v51
	v_add_f32_e32 v51, v42, v43
	v_cvt_pk_bf16_f32 v42, v46, v47
	v_cvt_pk_bf16_f32 v43, v48, v49
	v_lshlrev_b32_e32 v46, 16, v146
	v_and_b32_e32 v47, 0xffff0000, v146
	v_lshlrev_b32_e32 v48, 16, v147
	v_and_b32_e32 v49, 0xffff0000, v147
	v_pk_mul_f32 v[40:41], v[40:41], v[0:1] op_sel_hi:[1,0]
	v_pk_mul_f32 v[38:39], v[38:39], v[0:1] op_sel_hi:[1,0]
	v_cvt_pk_bf16_f32 v44, v44, v45
	v_cvt_pk_bf16_f32 v45, v54, v55
	v_lshlrev_b32_e32 v54, 16, v148
	v_and_b32_e32 v55, 0xffff0000, v148
	v_pk_fma_f32 v[40:41], v[172:173], v[40:41], v[48:49]
	v_pk_fma_f32 v[38:39], v[170:171], v[38:39], v[46:47]
	v_pk_mul_f32 v[34:35], v[34:35], v[0:1] op_sel_hi:[1,0]
	v_lshlrev_b32_e32 v56, 16, v149
	v_and_b32_e32 v57, 0xffff0000, v149
	v_pk_mul_f32 v[36:37], v[36:37], v[0:1] op_sel_hi:[1,0]
	v_pk_fma_f32 v[48:49], v[166:167], v[34:35], v[54:55]
	v_mul_f32_e32 v0, v39, v39
	v_mul_f32_e32 v34, v41, v41
	v_pk_fma_f32 v[46:47], v[168:169], v[36:37], v[56:57]
	v_fmac_f32_e32 v0, v38, v38
	v_fmac_f32_e32 v34, v40, v40
	v_add_f32_e32 v0, v0, v34
	v_mul_f32_e32 v34, v49, v49
	v_mul_f32_e32 v35, v47, v47
	v_fmac_f32_e32 v34, v48, v48
	v_fmac_f32_e32 v35, v46, v46
	v_add_f32_e32 v34, v34, v35
	v_add_f32_e32 v0, v0, v34
	v_add_f32_e32 v0, v51, v0
	v_mov_b32_e32 v37, v0
	s_nop 1
	v_permlane16_swap_b32_e32 v37, v0
	v_add_u32_e32 v50, 0x90, v240
	v_add_u32_e32 v52, s31, v50
	v_ashrrev_i32_e32 v53, 31, v52
	v_lshlrev_b64 v[52:53], 11, v[52:53]
	v_lshl_add_u64 v[34:35], s[6:7], 0, v[52:53]
	s_waitcnt lgkmcnt(0)
	v_add_f32_e32 v0, v0, v37
	v_lshl_add_u64 v[52:53], v[220:221], 1, v[34:35]
	v_mov_b32_e32 v34, v0
	s_nop 1
	v_permlane32_swap_b32_e32 v34, v0
	global_store_dwordx4 v[52:53], v[42:45], off
	v_cvt_pk_bf16_f32 v36, v38, v39
	v_cvt_pk_bf16_f32 v37, v40, v41
	v_cvt_pk_bf16_f32 v38, v48, v49
	v_cvt_pk_bf16_f32 v39, v46, v47
	global_store_dwordx4 v[52:53], v[36:39], off offset:256
	s_and_saveexec_b64 s[10:11], s[38:39]
	s_cbranch_execz .LBB0_2539
	v_lshl_add_u32 v35, v50, 4, s30
	s_waitcnt lgkmcnt(0)
	v_add_f32_e32 v0, v0, v34
	ds_write_b32 v35, v0 offset:6144

.LBB0_2541:
	v_lshlrev_b32_e32 v38, 16, v142
	v_and_b32_e32 v39, 0xffff0000, v142
	v_lshlrev_b32_e32 v40, 16, v143
	v_and_b32_e32 v41, 0xffff0000, v143
	s_waitcnt lgkmcnt(0)
	v_pk_mul_f32 v[32:33], v[32:33], v[0:1] op_sel_hi:[1,0]
	v_pk_mul_f32 v[30:31], v[30:31], v[0:1] op_sel_hi:[1,0]
	v_lshlrev_b32_e32 v42, 16, v144
	v_and_b32_e32 v43, 0xffff0000, v144
	v_lshlrev_b32_e32 v44, 16, v145
	v_and_b32_e32 v45, 0xffff0000, v145
	v_pk_fma_f32 v[32:33], v[184:185], v[32:33], v[40:41]
	v_pk_fma_f32 v[30:31], v[182:183], v[30:31], v[38:39]
	v_pk_mul_f32 v[28:29], v[28:29], v[0:1] op_sel_hi:[1,0]
	v_pk_mul_f32 v[26:27], v[26:27], v[0:1] op_sel_hi:[1,0]
	v_pk_fma_f32 v[38:39], v[180:181], v[28:29], v[44:45]
	v_pk_fma_f32 v[28:29], v[178:179], v[26:27], v[42:43]
	v_mul_f32_e32 v26, v31, v31
	v_mul_f32_e32 v27, v33, v33
	v_fmac_f32_e32 v26, v30, v30
	v_fmac_f32_e32 v27, v32, v32
	v_add_f32_e32 v26, v26, v27
	v_mul_f32_e32 v27, v29, v29
	v_mul_f32_e32 v35, v39, v39
	v_fmac_f32_e32 v27, v28, v28
	v_fmac_f32_e32 v35, v38, v38
	v_add_f32_e32 v27, v27, v35
	v_add_f32_e32 v35, v26, v27
	v_cvt_pk_bf16_f32 v26, v30, v31
	v_cvt_pk_bf16_f32 v27, v32, v33
	v_lshlrev_b32_e32 v30, 16, v138
	v_and_b32_e32 v31, 0xffff0000, v138
	v_lshlrev_b32_e32 v32, 16, v139
	v_and_b32_e32 v33, 0xffff0000, v139
	v_pk_mul_f32 v[24:25], v[24:25], v[0:1] op_sel_hi:[1,0]
	v_pk_mul_f32 v[22:23], v[22:23], v[0:1] op_sel_hi:[1,0]
	v_cvt_pk_bf16_f32 v28, v28, v29
	v_cvt_pk_bf16_f32 v29, v38, v39
	v_lshlrev_b32_e32 v38, 16, v140
	v_and_b32_e32 v39, 0xffff0000, v140
	v_pk_fma_f32 v[24:25], v[172:173], v[24:25], v[32:33]
	v_pk_fma_f32 v[22:23], v[170:171], v[22:23], v[30:31]
	v_pk_mul_f32 v[18:19], v[18:19], v[0:1] op_sel_hi:[1,0]
	v_lshlrev_b32_e32 v40, 16, v141
	v_and_b32_e32 v41, 0xffff0000, v141
	v_pk_mul_f32 v[20:21], v[20:21], v[0:1] op_sel_hi:[1,0]
	v_pk_fma_f32 v[32:33], v[166:167], v[18:19], v[38:39]
	v_mul_f32_e32 v0, v23, v23
	v_mul_f32_e32 v18, v25, v25
	v_pk_fma_f32 v[30:31], v[168:169], v[20:21], v[40:41]
	v_fmac_f32_e32 v0, v22, v22
	v_fmac_f32_e32 v18, v24, v24
	v_add_f32_e32 v0, v0, v18
	v_mul_f32_e32 v18, v33, v33
	v_mul_f32_e32 v19, v31, v31
	v_fmac_f32_e32 v18, v32, v32
	v_fmac_f32_e32 v19, v30, v30
	v_add_f32_e32 v18, v18, v19
	v_add_f32_e32 v0, v0, v18
	v_add_f32_e32 v0, v35, v0
	v_mov_b32_e32 v21, v0
	s_nop 1
	v_permlane16_swap_b32_e32 v21, v0
	v_add_u32_e32 v34, 0xa0, v240
	v_add_u32_e32 v36, s31, v34
	v_ashrrev_i32_e32 v37, 31, v36
	v_lshlrev_b64 v[36:37], 11, v[36:37]
	v_lshl_add_u64 v[18:19], s[6:7], 0, v[36:37]
	s_waitcnt lgkmcnt(0)
	v_add_f32_e32 v0, v0, v21
	v_lshl_add_u64 v[36:37], v[220:221], 1, v[18:19]
	v_mov_b32_e32 v18, v0
	s_nop 1
	v_permlane32_swap_b32_e32 v18, v0
	global_store_dwordx4 v[36:37], v[26:29], off
	v_cvt_pk_bf16_f32 v20, v22, v23
	v_cvt_pk_bf16_f32 v21, v24, v25
	v_cvt_pk_bf16_f32 v22, v32, v33
	v_cvt_pk_bf16_f32 v23, v30, v31
	global_store_dwordx4 v[36:37], v[20:23], off offset:256
	s_and_saveexec_b64 s[10:11], s[38:39]
	s_cbranch_execz .LBB0_2543
	v_lshl_add_u32 v19, v34, 4, s30
	s_waitcnt lgkmcnt(0)
	v_add_f32_e32 v0, v0, v18
	ds_write_b32 v19, v0 offset:6144

.LBB0_2545:
	v_lshlrev_b32_e32 v22, 16, v126
	v_and_b32_e32 v23, 0xffff0000, v126
	v_lshlrev_b32_e32 v24, 16, v127
	v_and_b32_e32 v25, 0xffff0000, v127
	s_waitcnt lgkmcnt(0)
	v_pk_mul_f32 v[16:17], v[16:17], v[0:1] op_sel_hi:[1,0]
	v_pk_mul_f32 v[14:15], v[14:15], v[0:1] op_sel_hi:[1,0]
	v_lshlrev_b32_e32 v26, 16, v128
	v_and_b32_e32 v27, 0xffff0000, v128
	v_lshlrev_b32_e32 v28, 16, v129
	v_and_b32_e32 v29, 0xffff0000, v129
	v_pk_fma_f32 v[16:17], v[184:185], v[16:17], v[24:25]
	v_pk_fma_f32 v[14:15], v[182:183], v[14:15], v[22:23]
	v_pk_mul_f32 v[12:13], v[12:13], v[0:1] op_sel_hi:[1,0]
	v_pk_mul_f32 v[10:11], v[10:11], v[0:1] op_sel_hi:[1,0]
	v_pk_fma_f32 v[22:23], v[180:181], v[12:13], v[28:29]
	v_pk_fma_f32 v[12:13], v[178:179], v[10:11], v[26:27]
	v_mul_f32_e32 v10, v15, v15
	v_mul_f32_e32 v11, v17, v17
	v_fmac_f32_e32 v10, v14, v14
	v_fmac_f32_e32 v11, v16, v16
	v_add_f32_e32 v10, v10, v11
	v_mul_f32_e32 v11, v13, v13
	v_mul_f32_e32 v19, v23, v23
	v_fmac_f32_e32 v11, v12, v12
	v_fmac_f32_e32 v19, v22, v22
	v_add_f32_e32 v11, v11, v19
	v_add_f32_e32 v19, v10, v11
	v_cvt_pk_bf16_f32 v10, v14, v15
	v_cvt_pk_bf16_f32 v11, v16, v17
	v_lshlrev_b32_e32 v14, 16, v122
	v_and_b32_e32 v15, 0xffff0000, v122
	v_lshlrev_b32_e32 v16, 16, v123
	v_and_b32_e32 v17, 0xffff0000, v123
	v_pk_mul_f32 v[8:9], v[8:9], v[0:1] op_sel_hi:[1,0]
	v_pk_mul_f32 v[6:7], v[6:7], v[0:1] op_sel_hi:[1,0]
	v_cvt_pk_bf16_f32 v12, v12, v13
	v_cvt_pk_bf16_f32 v13, v22, v23
	v_lshlrev_b32_e32 v22, 16, v124
	v_and_b32_e32 v23, 0xffff0000, v124
	v_pk_fma_f32 v[8:9], v[172:173], v[8:9], v[16:17]
	v_pk_fma_f32 v[6:7], v[170:171], v[6:7], v[14:15]
	v_pk_mul_f32 v[2:3], v[2:3], v[0:1] op_sel_hi:[1,0]
	v_lshlrev_b32_e32 v24, 16, v125
	v_and_b32_e32 v25, 0xffff0000, v125
	v_pk_mul_f32 v[4:5], v[4:5], v[0:1] op_sel_hi:[1,0]
	v_pk_fma_f32 v[16:17], v[166:167], v[2:3], v[22:23]
	v_mul_f32_e32 v0, v7, v7
	v_mul_f32_e32 v2, v9, v9
	v_pk_fma_f32 v[14:15], v[168:169], v[4:5], v[24:25]
	v_fmac_f32_e32 v0, v6, v6
	v_fmac_f32_e32 v2, v8, v8
	v_add_f32_e32 v0, v0, v2
	v_mul_f32_e32 v2, v17, v17
	v_mul_f32_e32 v3, v15, v15
	v_fmac_f32_e32 v2, v16, v16
	v_fmac_f32_e32 v3, v14, v14
	v_add_f32_e32 v2, v2, v3
	v_add_f32_e32 v0, v0, v2
	v_add_f32_e32 v0, v19, v0
	v_mov_b32_e32 v5, v0
	s_nop 1
	v_permlane16_swap_b32_e32 v5, v0
	v_add_u32_e32 v18, 0xb0, v240
	v_add_u32_e32 v20, s31, v18
	v_ashrrev_i32_e32 v21, 31, v20
	v_lshlrev_b64 v[20:21], 11, v[20:21]
	v_lshl_add_u64 v[2:3], s[6:7], 0, v[20:21]
	s_waitcnt lgkmcnt(0)
	v_add_f32_e32 v0, v0, v5
	v_lshl_add_u64 v[20:21], v[220:221], 1, v[2:3]
	v_mov_b32_e32 v2, v0
	s_nop 1
	v_permlane32_swap_b32_e32 v2, v0
	global_store_dwordx4 v[20:21], v[10:13], off
	v_cvt_pk_bf16_f32 v4, v6, v7
	v_cvt_pk_bf16_f32 v5, v8, v9
	v_cvt_pk_bf16_f32 v6, v16, v17
	v_cvt_pk_bf16_f32 v7, v14, v15
	global_store_dwordx4 v[20:21], v[4:7], off offset:256
	s_and_saveexec_b64 s[6:7], s[38:39]
	s_cbranch_execz .LBB0_2547
	v_lshl_add_u32 v3, v18, 4, s30
	s_waitcnt lgkmcnt(0)
	v_add_f32_e32 v0, v0, v2
	ds_write_b32 v3, v0 offset:6144

.LBB0_2710:
	s_lshl_b32 s4, s62, 5
	s_lshl_b32 s24, s12, 8
	v_lshrrev_b32_e32 v118, 1, v0
	s_or_b32 s4, s24, s4
	v_and_or_b32 v220, v118, 24, s4
	s_lshl_b32 s29, s53, 8
	v_add_u32_e32 v118, s29, v240
	v_ashrrev_i32_e32 v221, 31, v220
	v_lshl_add_u64 v[120:121], v[220:221], 1, s[22:23]
	s_mov_b64 s[22:23], 0x4000000
	v_ashrrev_i32_e32 v119, 31, v118
	v_lshl_add_u64 v[120:121], v[120:121], 0, s[22:23]
	v_lshlrev_b64 v[224:225], 11, v[118:119]
	v_lshl_add_u64 v[126:127], v[120:121], 0, v[224:225]
	s_barrier
	global_load_dwordx4 v[206:209], v[126:127], off
	global_load_dwordx4 v[202:205], v[126:127], off offset:256
	v_or_b32_e32 v126, 16, v118
	v_ashrrev_i32_e32 v127, 31, v126
	v_lshlrev_b64 v[126:127], 11, v[126:127]
	v_lshl_add_u64 v[126:127], v[120:121], 0, v[126:127]
	global_load_dwordx4 v[198:201], v[126:127], off
	global_load_dwordx4 v[194:197], v[126:127], off offset:256
	v_or_b32_e32 v126, 32, v118
	v_ashrrev_i32_e32 v127, 31, v126
	v_lshlrev_b64 v[126:127], 11, v[126:127]
	v_lshl_add_u64 v[126:127], v[120:121], 0, v[126:127]
	global_load_dwordx4 v[190:193], v[126:127], off
	global_load_dwordx4 v[186:189], v[126:127], off offset:256
	v_or_b32_e32 v126, 48, v118
	v_ashrrev_i32_e32 v127, 31, v126
	v_lshlrev_b64 v[126:127], 11, v[126:127]
	v_lshl_add_u64 v[126:127], v[120:121], 0, v[126:127]
	global_load_dwordx4 v[174:177], v[126:127], off
	global_load_dwordx4 v[162:165], v[126:127], off offset:256
	v_add_u32_e32 v126, 0x80, v118
	v_ashrrev_i32_e32 v127, 31, v126
	v_lshlrev_b64 v[126:127], 11, v[126:127]
	v_lshl_add_u64 v[126:127], v[120:121], 0, v[126:127]
	global_load_dwordx4 v[158:161], v[126:127], off
	global_load_dwordx4 v[154:157], v[126:127], off offset:256
	v_add_u32_e32 v126, 0x90, v118
	v_ashrrev_i32_e32 v127, 31, v126
	v_lshlrev_b64 v[126:127], 11, v[126:127]
	v_lshl_add_u64 v[126:127], v[120:121], 0, v[126:127]
	global_load_dwordx4 v[150:153], v[126:127], off
	global_load_dwordx4 v[146:149], v[126:127], off offset:256
	v_add_u32_e32 v126, 0xa0, v118
	v_add_u32_e32 v118, 0xb0, v118
	v_ashrrev_i32_e32 v127, 31, v126
	v_ashrrev_i32_e32 v119, 31, v118
	v_lshlrev_b64 v[126:127], 11, v[126:127]
	v_lshlrev_b64 v[118:119], 11, v[118:119]
	v_lshl_add_u64 v[126:127], v[120:121], 0, v[126:127]
	v_lshl_add_u64 v[118:119], v[120:121], 0, v[118:119]
	global_load_dwordx4 v[142:145], v[126:127], off
	global_load_dwordx4 v[138:141], v[126:127], off offset:256
	s_nop 0
	global_load_dwordx4 v[126:129], v[118:119], off
	s_nop 0
	global_load_dwordx4 v[118:121], v[118:119], off offset:256
	v_and_b32_e32 v168, 64, v231
	v_xor_b32_e32 v167, 16, v231
	v_add_u32_e32 v168, 64, v168
	v_cmp_lt_i32_e32 vcc, v167, v168
	v_mul_f32_e32 v169, v137, v137
	v_fmac_f32_e32 v169, v136, v136
	v_cndmask_b32_e32 v167, v231, v167, vcc
	v_lshlrev_b32_e32 v241, 2, v167
	v_mul_f32_e32 v167, v135, v135
	v_fmac_f32_e32 v167, v134, v134
	v_add_f32_e32 v167, v167, v169
	v_mul_f32_e32 v169, v131, v131
	v_mul_f32_e32 v170, v133, v133
	v_fmac_f32_e32 v169, v130, v130
	v_fmac_f32_e32 v170, v132, v132
	v_add_f32_e32 v169, v169, v170
	v_add_f32_e32 v167, v169, v167
	v_mul_f32_e32 v169, v123, v123
	v_mul_f32_e32 v170, v125, v125
	v_fmac_f32_e32 v169, v122, v122
	v_fmac_f32_e32 v170, v124, v124
	v_add_f32_e32 v169, v169, v170
	v_add_f32_e32 v167, v169, v167
	v_mul_f32_e32 v169, v115, v115
	v_mul_f32_e32 v170, v117, v117
	v_fmac_f32_e32 v169, v114, v114
	v_fmac_f32_e32 v170, v116, v116
	v_add_f32_e32 v169, v169, v170
	v_add_f32_e32 v167, v169, v167
	v_mov_b32_e32 v169, v167
	s_nop 1
	v_permlane16_swap_b32_e32 v169, v167
	v_xor_b32_e32 v170, 32, v231
	v_cmp_lt_i32_e32 vcc, v170, v168
	s_lshl_b32 s4, s62, 2
	s_add_i32 s28, s4, 0
	v_cndmask_b32_e32 v168, v231, v170, vcc
	v_lshlrev_b32_e32 v242, 2, v168
	s_waitcnt lgkmcnt(0)
	v_add_f32_e32 v168, v167, v169
	v_mov_b32_e32 v169, v168
	s_nop 1
	v_permlane32_swap_b32_e32 v169, v168
	v_and_b32_e32 v167, 63, v0
	v_cmp_gt_u32_e64 s[40:41], 16, v167
	s_and_saveexec_b64 s[22:23], s[40:41]
	v_readlane_b32 s64, v252, 3
	v_readlane_b32 s65, v255, 10
	v_readlane_b32 s68, v255, 11
	v_readlane_b32 s70, v255, 14
	v_readlane_b32 s71, v255, 15
	s_cbranch_execz .LBB0_2712
	s_lshl_b32 s4, s52, 10
	s_add_i32 s4, s28, s4
	s_waitcnt lgkmcnt(0)
	v_add_f32_e32 v168, v168, v169
	v_lshl_add_u32 v169, v166, 4, s4
	ds_write_b32 v169, v168
.LBB0_2712:
	s_or_b64 exec, exec, s[22:23]
	v_mul_f32_e32 v168, v111, v111
	s_waitcnt lgkmcnt(0)
	v_mul_f32_e32 v169, v113, v113
	v_fmac_f32_e32 v168, v110, v110
	v_fmac_f32_e32 v169, v112, v112
	v_add_f32_e32 v168, v168, v169
	v_mul_f32_e32 v169, v107, v107
	v_mul_f32_e32 v170, v109, v109
	v_fmac_f32_e32 v169, v106, v106
	v_fmac_f32_e32 v170, v108, v108
	v_add_f32_e32 v169, v169, v170
	v_add_f32_e32 v168, v169, v168
	v_mul_f32_e32 v169, v103, v103
	v_mul_f32_e32 v170, v105, v105
	v_fmac_f32_e32 v169, v102, v102
	v_fmac_f32_e32 v170, v104, v104
	v_add_f32_e32 v169, v169, v170
	v_add_f32_e32 v168, v169, v168
	v_mul_f32_e32 v169, v99, v99
	v_mul_f32_e32 v170, v101, v101
	v_fmac_f32_e32 v169, v98, v98
	v_fmac_f32_e32 v170, v100, v100
	v_add_f32_e32 v169, v169, v170
	v_add_f32_e32 v168, v169, v168
	v_mov_b32_e32 v169, v168
	s_nop 1
	v_permlane16_swap_b32_e32 v169, v168
	s_waitcnt lgkmcnt(0)
	v_add_f32_e32 v168, v168, v169
	v_mov_b32_e32 v169, v168
	s_nop 1
	v_permlane32_swap_b32_e32 v169, v168
	s_and_saveexec_b64 s[22:23], s[40:41]
	s_cbranch_execz .LBB0_2714
	s_lshl_b32 s4, s52, 10
	s_add_i32 s4, s28, s4
	s_waitcnt lgkmcnt(0)
	v_add_f32_e32 v168, v168, v169
	v_lshl_add_u32 v169, v166, 4, s4
	ds_write_b32 v169, v168 offset:256
.LBB0_2714:
	s_or_b64 exec, exec, s[22:23]
	v_mul_f32_e32 v168, v95, v95
	s_waitcnt lgkmcnt(0)
	v_mul_f32_e32 v169, v97, v97
	v_fmac_f32_e32 v168, v94, v94
	v_fmac_f32_e32 v169, v96, v96
	v_add_f32_e32 v168, v168, v169
	v_mul_f32_e32 v169, v91, v91
	v_mul_f32_e32 v170, v93, v93
	v_fmac_f32_e32 v169, v90, v90
	v_fmac_f32_e32 v170, v92, v92
	v_add_f32_e32 v169, v169, v170
	v_add_f32_e32 v168, v169, v168
	v_mul_f32_e32 v169, v87, v87
	v_mul_f32_e32 v170, v89, v89
	v_fmac_f32_e32 v169, v86, v86
	v_fmac_f32_e32 v170, v88, v88
	v_add_f32_e32 v169, v169, v170
	v_add_f32_e32 v168, v169, v168
	v_mul_f32_e32 v169, v83, v83
	v_mul_f32_e32 v170, v85, v85
	v_fmac_f32_e32 v169, v82, v82
	v_fmac_f32_e32 v170, v84, v84
	v_add_f32_e32 v169, v169, v170
	v_add_f32_e32 v168, v169, v168
	v_mov_b32_e32 v169, v168
	s_nop 1
	v_permlane16_swap_b32_e32 v169, v168
	s_waitcnt lgkmcnt(0)
	v_add_f32_e32 v168, v168, v169
	v_mov_b32_e32 v169, v168
	s_nop 1
	v_permlane32_swap_b32_e32 v169, v168
	s_and_saveexec_b64 s[22:23], s[40:41]
	s_cbranch_execz .LBB0_2716
	s_lshl_b32 s4, s52, 10
	s_add_i32 s4, s28, s4
	s_waitcnt lgkmcnt(0)
	v_add_f32_e32 v168, v168, v169
	v_lshl_add_u32 v169, v166, 4, s4
	ds_write_b32 v169, v168 offset:512
.LBB0_2716:
	s_or_b64 exec, exec, s[22:23]
	v_mul_f32_e32 v168, v79, v79
	s_waitcnt lgkmcnt(0)
	v_mul_f32_e32 v169, v81, v81
	v_fmac_f32_e32 v168, v78, v78
	v_fmac_f32_e32 v169, v80, v80
	v_add_f32_e32 v168, v168, v169
	v_mul_f32_e32 v169, v75, v75
	v_mul_f32_e32 v170, v77, v77
	v_fmac_f32_e32 v169, v74, v74
	v_fmac_f32_e32 v170, v76, v76
	v_add_f32_e32 v169, v169, v170
	v_add_f32_e32 v168, v169, v168
	v_mul_f32_e32 v169, v71, v71
	v_mul_f32_e32 v170, v73, v73
	v_fmac_f32_e32 v169, v70, v70
	v_fmac_f32_e32 v170, v72, v72
	v_add_f32_e32 v169, v169, v170
	v_add_f32_e32 v168, v169, v168
	v_mul_f32_e32 v169, v67, v67
	v_mul_f32_e32 v170, v69, v69
	v_fmac_f32_e32 v169, v66, v66
	v_fmac_f32_e32 v170, v68, v68
	v_add_f32_e32 v169, v169, v170
	v_add_f32_e32 v168, v169, v168
	v_mov_b32_e32 v169, v168
	s_nop 1
	v_permlane16_swap_b32_e32 v169, v168
	s_waitcnt lgkmcnt(0)
	v_add_f32_e32 v168, v168, v169
	v_mov_b32_e32 v169, v168
	s_nop 1
	v_permlane32_swap_b32_e32 v169, v168
	s_and_saveexec_b64 s[22:23], s[40:41]
	s_cbranch_execz .LBB0_2718
	s_lshl_b32 s4, s52, 10
	s_add_i32 s4, s28, s4
	s_waitcnt lgkmcnt(0)
	v_add_f32_e32 v168, v168, v169
	v_lshl_add_u32 v169, v166, 4, s4
	ds_write_b32 v169, v168 offset:768
.LBB0_2718:
	s_or_b64 exec, exec, s[22:23]
	v_mul_f32_e32 v168, v63, v63
	s_waitcnt lgkmcnt(0)
	v_mul_f32_e32 v169, v65, v65
	v_fmac_f32_e32 v168, v62, v62
	v_fmac_f32_e32 v169, v64, v64
	v_add_f32_e32 v168, v168, v169
	v_mul_f32_e32 v169, v59, v59
	v_mul_f32_e32 v170, v61, v61
	v_fmac_f32_e32 v169, v58, v58
	v_fmac_f32_e32 v170, v60, v60
	v_add_f32_e32 v169, v169, v170
	v_add_f32_e32 v168, v169, v168
	v_mul_f32_e32 v169, v55, v55
	v_mul_f32_e32 v170, v57, v57
	v_fmac_f32_e32 v169, v54, v54
	v_fmac_f32_e32 v170, v56, v56
	v_add_f32_e32 v169, v169, v170
	v_add_f32_e32 v168, v169, v168
	v_mul_f32_e32 v169, v51, v51
	v_mul_f32_e32 v170, v53, v53
	v_fmac_f32_e32 v169, v50, v50
	v_fmac_f32_e32 v170, v52, v52
	v_add_f32_e32 v169, v169, v170
	v_add_f32_e32 v168, v169, v168
	v_mov_b32_e32 v169, v168
	s_nop 1
	v_permlane16_swap_b32_e32 v169, v168
	s_waitcnt lgkmcnt(0)
	v_add_f32_e32 v168, v168, v169
	v_mov_b32_e32 v169, v168
	s_nop 1
	v_permlane32_swap_b32_e32 v169, v168
	s_and_saveexec_b64 s[22:23], s[40:41]
	s_cbranch_execz .LBB0_2720
	s_lshl_b32 s4, s52, 10
	s_add_i32 s4, s28, s4
	s_waitcnt lgkmcnt(0)
	v_add_f32_e32 v168, v168, v169
	v_lshl_add_u32 v169, v166, 4, s4
	ds_write_b32 v169, v168 offset:2048
.LBB0_2720:
	s_or_b64 exec, exec, s[22:23]
	v_mul_f32_e32 v168, v47, v47
	s_waitcnt lgkmcnt(0)
	v_mul_f32_e32 v169, v49, v49
	v_fmac_f32_e32 v168, v46, v46
	v_fmac_f32_e32 v169, v48, v48
	v_add_f32_e32 v168, v168, v169
	v_mul_f32_e32 v169, v43, v43
	v_mul_f32_e32 v170, v45, v45
	v_fmac_f32_e32 v169, v42, v42
	v_fmac_f32_e32 v170, v44, v44
	v_add_f32_e32 v169, v169, v170
	v_add_f32_e32 v168, v169, v168
	v_mul_f32_e32 v169, v39, v39
	v_mul_f32_e32 v170, v41, v41
	v_fmac_f32_e32 v169, v38, v38
	v_fmac_f32_e32 v170, v40, v40
	v_add_f32_e32 v169, v169, v170
	v_add_f32_e32 v168, v169, v168
	v_mul_f32_e32 v169, v35, v35
	v_mul_f32_e32 v170, v37, v37
	v_fmac_f32_e32 v169, v34, v34
	v_fmac_f32_e32 v170, v36, v36
	v_add_f32_e32 v169, v169, v170
	v_add_f32_e32 v168, v169, v168
	v_mov_b32_e32 v169, v168
	s_nop 1
	v_permlane16_swap_b32_e32 v169, v168
	s_waitcnt lgkmcnt(0)
	v_add_f32_e32 v168, v168, v169
	v_mov_b32_e32 v169, v168
	s_nop 1
	v_permlane32_swap_b32_e32 v169, v168
	s_and_saveexec_b64 s[22:23], s[40:41]
	s_cbranch_execz .LBB0_2722
	s_lshl_b32 s4, s52, 10
	s_add_i32 s4, s28, s4
	s_waitcnt lgkmcnt(0)
	v_add_f32_e32 v168, v168, v169
	v_lshl_add_u32 v169, v166, 4, s4
	ds_write_b32 v169, v168 offset:2304
.LBB0_2722:
	s_or_b64 exec, exec, s[22:23]
	v_mul_f32_e32 v168, v31, v31
	s_waitcnt lgkmcnt(0)
	v_mul_f32_e32 v169, v33, v33
	v_fmac_f32_e32 v168, v30, v30
	v_fmac_f32_e32 v169, v32, v32
	v_add_f32_e32 v168, v168, v169
	v_mul_f32_e32 v169, v27, v27
	v_mul_f32_e32 v170, v29, v29
	v_fmac_f32_e32 v169, v26, v26
	v_fmac_f32_e32 v170, v28, v28
	v_add_f32_e32 v169, v169, v170
	v_add_f32_e32 v168, v169, v168
	v_mul_f32_e32 v169, v23, v23
	v_mul_f32_e32 v170, v25, v25
	v_fmac_f32_e32 v169, v22, v22
	v_fmac_f32_e32 v170, v24, v24
	v_add_f32_e32 v169, v169, v170
	v_add_f32_e32 v168, v169, v168
	v_mul_f32_e32 v169, v19, v19
	v_mul_f32_e32 v170, v21, v21
	v_fmac_f32_e32 v169, v18, v18
	v_fmac_f32_e32 v170, v20, v20
	v_add_f32_e32 v169, v169, v170
	v_add_f32_e32 v168, v169, v168
	v_mov_b32_e32 v169, v168
	s_nop 1
	v_permlane16_swap_b32_e32 v169, v168
	s_waitcnt lgkmcnt(0)
	v_add_f32_e32 v168, v168, v169
	v_mov_b32_e32 v169, v168
	s_nop 1
	v_permlane32_swap_b32_e32 v169, v168
	s_and_saveexec_b64 s[22:23], s[40:41]
	s_cbranch_execz .LBB0_2724
	s_lshl_b32 s4, s52, 10
	s_add_i32 s4, s28, s4
	s_waitcnt lgkmcnt(0)
	v_add_f32_e32 v168, v168, v169
	v_lshl_add_u32 v169, v166, 4, s4
	ds_write_b32 v169, v168 offset:2560
.LBB0_2724:
	s_or_b64 exec, exec, s[22:23]
	v_mul_f32_e32 v168, v15, v15
	s_waitcnt lgkmcnt(0)
	v_mul_f32_e32 v169, v17, v17
	v_fmac_f32_e32 v168, v14, v14
	v_fmac_f32_e32 v169, v16, v16
	v_add_f32_e32 v168, v168, v169
	v_mul_f32_e32 v169, v11, v11
	v_mul_f32_e32 v170, v13, v13
	v_fmac_f32_e32 v169, v10, v10
	v_fmac_f32_e32 v170, v12, v12
	v_add_f32_e32 v169, v169, v170
	v_add_f32_e32 v168, v169, v168
	v_mul_f32_e32 v169, v7, v7
	v_mul_f32_e32 v170, v9, v9
	v_fmac_f32_e32 v169, v6, v6
	v_fmac_f32_e32 v170, v8, v8
	v_add_f32_e32 v169, v169, v170
	v_add_f32_e32 v168, v169, v168
	v_mul_f32_e32 v169, v3, v3
	v_mul_f32_e32 v170, v5, v5
	v_fmac_f32_e32 v169, v2, v2
	v_fmac_f32_e32 v170, v4, v4
	v_add_f32_e32 v169, v169, v170
	v_add_f32_e32 v168, v169, v168
	v_mov_b32_e32 v169, v168
	s_nop 1
	v_permlane16_swap_b32_e32 v169, v168
	s_waitcnt lgkmcnt(0)
	v_add_f32_e32 v168, v168, v169
	v_mov_b32_e32 v169, v168
	s_nop 1
	v_permlane32_swap_b32_e32 v169, v168
	s_and_saveexec_b64 s[22:23], s[40:41]
	s_cbranch_execz .LBB0_2726
	s_lshl_b32 s4, s52, 10
	s_add_i32 s4, s28, s4
	s_waitcnt lgkmcnt(0)
	v_add_f32_e32 v168, v168, v169
	v_lshl_add_u32 v166, v166, 4, s4
	ds_write_b32 v166, v168 offset:2816

.LBB0_2752:
	s_waitcnt vmcnt(0)
	v_lshlrev_b32_e32 v216, 16, v206
	v_and_b32_e32 v217, 0xffff0000, v206
	v_lshlrev_b32_e32 v206, 16, v207
	v_and_b32_e32 v207, 0xffff0000, v207
	s_waitcnt lgkmcnt(0)
	v_pk_mul_f32 v[136:137], v[136:137], v[0:1] op_sel_hi:[1,0]
	v_pk_mul_f32 v[134:135], v[134:135], v[0:1] op_sel_hi:[1,0]
	v_lshlrev_b32_e32 v218, 16, v208
	v_and_b32_e32 v219, 0xffff0000, v208
	v_lshlrev_b32_e32 v208, 16, v209
	v_and_b32_e32 v209, 0xffff0000, v209
	v_pk_fma_f32 v[136:137], v[184:185], v[136:137], v[206:207]
	v_pk_fma_f32 v[134:135], v[182:183], v[134:135], v[216:217]
	v_pk_mul_f32 v[132:133], v[132:133], v[0:1] op_sel_hi:[1,0]
	v_pk_mul_f32 v[130:131], v[130:131], v[0:1] op_sel_hi:[1,0]
	v_pk_fma_f32 v[206:207], v[180:181], v[132:133], v[208:209]
	v_pk_fma_f32 v[132:133], v[178:179], v[130:131], v[218:219]
	v_mul_f32_e32 v130, v135, v135
	v_mul_f32_e32 v131, v137, v137
	v_fmac_f32_e32 v130, v134, v134
	v_fmac_f32_e32 v131, v136, v136
	v_add_f32_e32 v130, v130, v131
	v_mul_f32_e32 v131, v133, v133
	v_mul_f32_e32 v208, v207, v207
	v_fmac_f32_e32 v131, v132, v132
	v_fmac_f32_e32 v208, v206, v206
	v_add_f32_e32 v131, v131, v208
	v_add_f32_e32 v208, v130, v131
	v_cvt_pk_bf16_f32 v130, v134, v135
	v_cvt_pk_bf16_f32 v131, v136, v137
	v_lshlrev_b32_e32 v134, 16, v202
	v_and_b32_e32 v135, 0xffff0000, v202
	v_lshlrev_b32_e32 v136, 16, v203
	v_and_b32_e32 v137, 0xffff0000, v203
	v_pk_mul_f32 v[124:125], v[124:125], v[0:1] op_sel_hi:[1,0]
	v_pk_mul_f32 v[122:123], v[122:123], v[0:1] op_sel_hi:[1,0]
	v_lshlrev_b32_e32 v202, 16, v204
	v_and_b32_e32 v203, 0xffff0000, v204
	v_pk_fma_f32 v[124:125], v[172:173], v[124:125], v[136:137]
	v_pk_fma_f32 v[122:123], v[170:171], v[122:123], v[134:135]
	v_pk_mul_f32 v[114:115], v[114:115], v[0:1] op_sel_hi:[1,0]
	v_lshlrev_b32_e32 v204, 16, v205
	v_and_b32_e32 v205, 0xffff0000, v205
	v_pk_mul_f32 v[116:117], v[116:117], v[0:1] op_sel_hi:[1,0]
	v_pk_fma_f32 v[134:135], v[166:167], v[114:115], v[202:203]
	v_mul_f32_e32 v0, v123, v123
	v_mul_f32_e32 v114, v125, v125
	v_pk_fma_f32 v[116:117], v[168:169], v[116:117], v[204:205]
	v_fmac_f32_e32 v0, v122, v122
	v_fmac_f32_e32 v114, v124, v124
	v_add_f32_e32 v0, v0, v114
	v_mul_f32_e32 v114, v135, v135
	v_mul_f32_e32 v115, v117, v117
	v_fmac_f32_e32 v114, v134, v134
	v_fmac_f32_e32 v115, v116, v116
	v_add_f32_e32 v114, v114, v115
	v_add_f32_e32 v0, v0, v114
	v_add_f32_e32 v0, v208, v0
	v_mov_b32_e32 v202, v0
	s_nop 1
	v_permlane16_swap_b32_e32 v202, v0
	s_add_u32 s14, s14, 0x4000000
	s_addc_u32 s15, s15, 0
	v_lshl_add_u64 v[114:115], s[14:15], 0, v[224:225]
	v_lshl_add_u64 v[136:137], v[220:221], 1, v[114:115]
	s_waitcnt lgkmcnt(0)
	v_add_f32_e32 v0, v0, v202
	v_mov_b32_e32 v114, v0
	s_nop 1
	v_permlane32_swap_b32_e32 v114, v0
	v_cvt_pk_bf16_f32 v132, v132, v133
	v_cvt_pk_bf16_f32 v133, v206, v207
	global_store_dwordx4 v[136:137], v[130:133], off
	v_cvt_pk_bf16_f32 v122, v122, v123
	v_cvt_pk_bf16_f32 v123, v124, v125
	v_cvt_pk_bf16_f32 v124, v134, v135
	v_cvt_pk_bf16_f32 v125, v116, v117
	global_store_dwordx4 v[136:137], v[122:125], off offset:256
	s_and_saveexec_b64 s[16:17], s[40:41]
	s_cbranch_execz .LBB0_2754
	v_lshl_add_u32 v115, v240, 4, s28
	s_waitcnt lgkmcnt(0)
	v_add_f32_e32 v0, v0, v114
	ds_write_b32 v115, v0 offset:6144

.LBB0_2756:
	v_lshlrev_b32_e32 v122, 16, v198
	v_and_b32_e32 v123, 0xffff0000, v198
	v_lshlrev_b32_e32 v124, 16, v199
	v_and_b32_e32 v125, 0xffff0000, v199
	s_waitcnt lgkmcnt(0)
	v_pk_mul_f32 v[112:113], v[112:113], v[0:1] op_sel_hi:[1,0]
	v_pk_mul_f32 v[110:111], v[110:111], v[0:1] op_sel_hi:[1,0]
	v_lshlrev_b32_e32 v130, 16, v200
	v_and_b32_e32 v131, 0xffff0000, v200
	v_lshlrev_b32_e32 v132, 16, v201
	v_and_b32_e32 v133, 0xffff0000, v201
	v_pk_fma_f32 v[112:113], v[184:185], v[112:113], v[124:125]
	v_pk_fma_f32 v[110:111], v[182:183], v[110:111], v[122:123]
	v_pk_mul_f32 v[108:109], v[108:109], v[0:1] op_sel_hi:[1,0]
	v_pk_mul_f32 v[106:107], v[106:107], v[0:1] op_sel_hi:[1,0]
	v_pk_fma_f32 v[122:123], v[180:181], v[108:109], v[132:133]
	v_pk_fma_f32 v[108:109], v[178:179], v[106:107], v[130:131]
	v_mul_f32_e32 v106, v111, v111
	v_mul_f32_e32 v107, v113, v113
	v_fmac_f32_e32 v106, v110, v110
	v_fmac_f32_e32 v107, v112, v112
	v_add_f32_e32 v106, v106, v107
	v_mul_f32_e32 v107, v109, v109
	v_mul_f32_e32 v115, v123, v123
	v_fmac_f32_e32 v107, v108, v108
	v_fmac_f32_e32 v115, v122, v122
	v_add_f32_e32 v107, v107, v115
	v_add_f32_e32 v115, v106, v107
	v_cvt_pk_bf16_f32 v106, v110, v111
	v_cvt_pk_bf16_f32 v107, v112, v113
	v_lshlrev_b32_e32 v110, 16, v194
	v_and_b32_e32 v111, 0xffff0000, v194
	v_lshlrev_b32_e32 v112, 16, v195
	v_and_b32_e32 v113, 0xffff0000, v195
	v_pk_mul_f32 v[104:105], v[104:105], v[0:1] op_sel_hi:[1,0]
	v_pk_mul_f32 v[102:103], v[102:103], v[0:1] op_sel_hi:[1,0]
	v_cvt_pk_bf16_f32 v108, v108, v109
	v_cvt_pk_bf16_f32 v109, v122, v123
	v_lshlrev_b32_e32 v122, 16, v196
	v_and_b32_e32 v123, 0xffff0000, v196
	v_pk_fma_f32 v[104:105], v[172:173], v[104:105], v[112:113]
	v_pk_fma_f32 v[102:103], v[170:171], v[102:103], v[110:111]
	v_pk_mul_f32 v[98:99], v[98:99], v[0:1] op_sel_hi:[1,0]
	v_lshlrev_b32_e32 v124, 16, v197
	v_and_b32_e32 v125, 0xffff0000, v197
	v_pk_mul_f32 v[100:101], v[100:101], v[0:1] op_sel_hi:[1,0]
	v_pk_fma_f32 v[112:113], v[166:167], v[98:99], v[122:123]
	v_mul_f32_e32 v0, v103, v103
	v_mul_f32_e32 v98, v105, v105
	v_pk_fma_f32 v[110:111], v[168:169], v[100:101], v[124:125]
	v_fmac_f32_e32 v0, v102, v102
	v_fmac_f32_e32 v98, v104, v104
	v_add_f32_e32 v0, v0, v98
	v_mul_f32_e32 v98, v113, v113
	v_mul_f32_e32 v99, v111, v111
	v_fmac_f32_e32 v98, v112, v112
	v_fmac_f32_e32 v99, v110, v110
	v_add_f32_e32 v98, v98, v99
	v_add_f32_e32 v0, v0, v98
	v_add_f32_e32 v0, v115, v0
	v_mov_b32_e32 v101, v0
	s_nop 1
	v_permlane16_swap_b32_e32 v101, v0
	v_or_b32_e32 v114, 16, v240
	v_add_u32_e32 v116, s29, v114
	v_ashrrev_i32_e32 v117, 31, v116
	v_lshlrev_b64 v[116:117], 11, v[116:117]
	v_lshl_add_u64 v[98:99], s[14:15], 0, v[116:117]
	s_waitcnt lgkmcnt(0)
	v_add_f32_e32 v0, v0, v101
	v_lshl_add_u64 v[116:117], v[220:221], 1, v[98:99]
	v_mov_b32_e32 v98, v0
	s_nop 1
	v_permlane32_swap_b32_e32 v98, v0
	global_store_dwordx4 v[116:117], v[106:109], off
	v_cvt_pk_bf16_f32 v100, v102, v103
	v_cvt_pk_bf16_f32 v101, v104, v105
	v_cvt_pk_bf16_f32 v102, v112, v113
	v_cvt_pk_bf16_f32 v103, v110, v111
	global_store_dwordx4 v[116:117], v[100:103], off offset:256
	s_and_saveexec_b64 s[16:17], s[40:41]
	s_cbranch_execz .LBB0_2758
	v_lshl_add_u32 v99, v114, 4, s28
	s_waitcnt lgkmcnt(0)
	v_add_f32_e32 v0, v0, v98
	ds_write_b32 v99, v0 offset:6144

.LBB0_2760:
	v_lshlrev_b32_e32 v102, 16, v190
	v_and_b32_e32 v103, 0xffff0000, v190
	v_lshlrev_b32_e32 v104, 16, v191
	v_and_b32_e32 v105, 0xffff0000, v191
	s_waitcnt lgkmcnt(0)
	v_pk_mul_f32 v[96:97], v[96:97], v[0:1] op_sel_hi:[1,0]
	v_pk_mul_f32 v[94:95], v[94:95], v[0:1] op_sel_hi:[1,0]
	v_lshlrev_b32_e32 v106, 16, v192
	v_and_b32_e32 v107, 0xffff0000, v192
	v_lshlrev_b32_e32 v108, 16, v193
	v_and_b32_e32 v109, 0xffff0000, v193
	v_pk_fma_f32 v[96:97], v[184:185], v[96:97], v[104:105]
	v_pk_fma_f32 v[94:95], v[182:183], v[94:95], v[102:103]
	v_pk_mul_f32 v[92:93], v[92:93], v[0:1] op_sel_hi:[1,0]
	v_pk_mul_f32 v[90:91], v[90:91], v[0:1] op_sel_hi:[1,0]
	v_pk_fma_f32 v[102:103], v[180:181], v[92:93], v[108:109]
	v_pk_fma_f32 v[92:93], v[178:179], v[90:91], v[106:107]
	v_mul_f32_e32 v90, v95, v95
	v_mul_f32_e32 v91, v97, v97
	v_fmac_f32_e32 v90, v94, v94
	v_fmac_f32_e32 v91, v96, v96
	v_add_f32_e32 v90, v90, v91
	v_mul_f32_e32 v91, v93, v93
	v_mul_f32_e32 v99, v103, v103
	v_fmac_f32_e32 v91, v92, v92
	v_fmac_f32_e32 v99, v102, v102
	v_add_f32_e32 v91, v91, v99
	v_add_f32_e32 v99, v90, v91
	v_cvt_pk_bf16_f32 v90, v94, v95
	v_cvt_pk_bf16_f32 v91, v96, v97
	v_lshlrev_b32_e32 v94, 16, v186
	v_and_b32_e32 v95, 0xffff0000, v186
	v_lshlrev_b32_e32 v96, 16, v187
	v_and_b32_e32 v97, 0xffff0000, v187
	v_pk_mul_f32 v[88:89], v[88:89], v[0:1] op_sel_hi:[1,0]
	v_pk_mul_f32 v[86:87], v[86:87], v[0:1] op_sel_hi:[1,0]
	v_cvt_pk_bf16_f32 v92, v92, v93
	v_cvt_pk_bf16_f32 v93, v102, v103
	v_lshlrev_b32_e32 v102, 16, v188
	v_and_b32_e32 v103, 0xffff0000, v188
	v_pk_fma_f32 v[88:89], v[172:173], v[88:89], v[96:97]
	v_pk_fma_f32 v[86:87], v[170:171], v[86:87], v[94:95]
	v_pk_mul_f32 v[82:83], v[82:83], v[0:1] op_sel_hi:[1,0]
	v_lshlrev_b32_e32 v104, 16, v189
	v_and_b32_e32 v105, 0xffff0000, v189
	v_pk_mul_f32 v[84:85], v[84:85], v[0:1] op_sel_hi:[1,0]
	v_pk_fma_f32 v[96:97], v[166:167], v[82:83], v[102:103]
	v_mul_f32_e32 v0, v87, v87
	v_mul_f32_e32 v82, v89, v89
	v_pk_fma_f32 v[94:95], v[168:169], v[84:85], v[104:105]
	v_fmac_f32_e32 v0, v86, v86
	v_fmac_f32_e32 v82, v88, v88
	v_add_f32_e32 v0, v0, v82
	v_mul_f32_e32 v82, v97, v97
	v_mul_f32_e32 v83, v95, v95
	v_fmac_f32_e32 v82, v96, v96
	v_fmac_f32_e32 v83, v94, v94
	v_add_f32_e32 v82, v82, v83
	v_add_f32_e32 v0, v0, v82
	v_add_f32_e32 v0, v99, v0
	v_mov_b32_e32 v85, v0
	s_nop 1
	v_permlane16_swap_b32_e32 v85, v0
	v_or_b32_e32 v98, 32, v240
	v_add_u32_e32 v100, s29, v98
	v_ashrrev_i32_e32 v101, 31, v100
	v_lshlrev_b64 v[100:101], 11, v[100:101]
	v_lshl_add_u64 v[82:83], s[14:15], 0, v[100:101]
	s_waitcnt lgkmcnt(0)
	v_add_f32_e32 v0, v0, v85
	v_lshl_add_u64 v[100:101], v[220:221], 1, v[82:83]
	v_mov_b32_e32 v82, v0
	s_nop 1
	v_permlane32_swap_b32_e32 v82, v0
	global_store_dwordx4 v[100:101], v[90:93], off
	v_cvt_pk_bf16_f32 v84, v86, v87
	v_cvt_pk_bf16_f32 v85, v88, v89
	v_cvt_pk_bf16_f32 v86, v96, v97
	v_cvt_pk_bf16_f32 v87, v94, v95
	global_store_dwordx4 v[100:101], v[84:87], off offset:256
	s_and_saveexec_b64 s[16:17], s[40:41]
	s_cbranch_execz .LBB0_2762
	v_lshl_add_u32 v83, v98, 4, s28
	s_waitcnt lgkmcnt(0)
	v_add_f32_e32 v0, v0, v82
	ds_write_b32 v83, v0 offset:6144

.LBB0_2764:
	v_lshlrev_b32_e32 v86, 16, v174
	v_and_b32_e32 v87, 0xffff0000, v174
	v_lshlrev_b32_e32 v88, 16, v175
	v_and_b32_e32 v89, 0xffff0000, v175
	s_waitcnt lgkmcnt(0)
	v_pk_mul_f32 v[80:81], v[80:81], v[0:1] op_sel_hi:[1,0]
	v_pk_mul_f32 v[78:79], v[78:79], v[0:1] op_sel_hi:[1,0]
	v_lshlrev_b32_e32 v90, 16, v176
	v_and_b32_e32 v91, 0xffff0000, v176
	v_lshlrev_b32_e32 v92, 16, v177
	v_and_b32_e32 v93, 0xffff0000, v177
	v_pk_fma_f32 v[80:81], v[184:185], v[80:81], v[88:89]
	v_pk_fma_f32 v[78:79], v[182:183], v[78:79], v[86:87]
	v_pk_mul_f32 v[76:77], v[76:77], v[0:1] op_sel_hi:[1,0]
	v_pk_mul_f32 v[74:75], v[74:75], v[0:1] op_sel_hi:[1,0]
	v_pk_fma_f32 v[86:87], v[180:181], v[76:77], v[92:93]
	v_pk_fma_f32 v[76:77], v[178:179], v[74:75], v[90:91]
	v_mul_f32_e32 v74, v79, v79
	v_mul_f32_e32 v75, v81, v81
	v_fmac_f32_e32 v74, v78, v78
	v_fmac_f32_e32 v75, v80, v80
	v_add_f32_e32 v74, v74, v75
	v_mul_f32_e32 v75, v77, v77
	v_mul_f32_e32 v83, v87, v87
	v_fmac_f32_e32 v75, v76, v76
	v_fmac_f32_e32 v83, v86, v86
	v_add_f32_e32 v75, v75, v83
	v_add_f32_e32 v83, v74, v75
	v_cvt_pk_bf16_f32 v74, v78, v79
	v_cvt_pk_bf16_f32 v75, v80, v81
	v_lshlrev_b32_e32 v78, 16, v162
	v_and_b32_e32 v79, 0xffff0000, v162
	v_lshlrev_b32_e32 v80, 16, v163
	v_and_b32_e32 v81, 0xffff0000, v163
	v_pk_mul_f32 v[72:73], v[72:73], v[0:1] op_sel_hi:[1,0]
	v_pk_mul_f32 v[70:71], v[70:71], v[0:1] op_sel_hi:[1,0]
	v_cvt_pk_bf16_f32 v76, v76, v77
	v_cvt_pk_bf16_f32 v77, v86, v87
	v_lshlrev_b32_e32 v86, 16, v164
	v_and_b32_e32 v87, 0xffff0000, v164
	v_pk_fma_f32 v[72:73], v[172:173], v[72:73], v[80:81]
	v_pk_fma_f32 v[70:71], v[170:171], v[70:71], v[78:79]
	v_pk_mul_f32 v[66:67], v[66:67], v[0:1] op_sel_hi:[1,0]
	v_lshlrev_b32_e32 v88, 16, v165
	v_and_b32_e32 v89, 0xffff0000, v165
	v_pk_mul_f32 v[68:69], v[68:69], v[0:1] op_sel_hi:[1,0]
	v_pk_fma_f32 v[80:81], v[166:167], v[66:67], v[86:87]
	v_mul_f32_e32 v0, v71, v71
	v_mul_f32_e32 v66, v73, v73
	v_pk_fma_f32 v[78:79], v[168:169], v[68:69], v[88:89]
	v_fmac_f32_e32 v0, v70, v70
	v_fmac_f32_e32 v66, v72, v72
	v_add_f32_e32 v0, v0, v66
	v_mul_f32_e32 v66, v81, v81
	v_mul_f32_e32 v67, v79, v79
	v_fmac_f32_e32 v66, v80, v80
	v_fmac_f32_e32 v67, v78, v78
	v_add_f32_e32 v66, v66, v67
	v_add_f32_e32 v0, v0, v66
	v_add_f32_e32 v0, v83, v0
	v_mov_b32_e32 v69, v0
	s_nop 1
	v_permlane16_swap_b32_e32 v69, v0
	v_or_b32_e32 v82, 48, v240
	v_add_u32_e32 v84, s29, v82
	v_ashrrev_i32_e32 v85, 31, v84
	v_lshlrev_b64 v[84:85], 11, v[84:85]
	v_lshl_add_u64 v[66:67], s[14:15], 0, v[84:85]
	s_waitcnt lgkmcnt(0)
	v_add_f32_e32 v0, v0, v69
	v_lshl_add_u64 v[84:85], v[220:221], 1, v[66:67]
	v_mov_b32_e32 v66, v0
	s_nop 1
	v_permlane32_swap_b32_e32 v66, v0
	global_store_dwordx4 v[84:85], v[74:77], off
	v_cvt_pk_bf16_f32 v68, v70, v71
	v_cvt_pk_bf16_f32 v69, v72, v73
	v_cvt_pk_bf16_f32 v70, v80, v81
	v_cvt_pk_bf16_f32 v71, v78, v79
	global_store_dwordx4 v[84:85], v[68:71], off offset:256
	s_and_saveexec_b64 s[16:17], s[40:41]
	s_cbranch_execz .LBB0_2766
	v_lshl_add_u32 v67, v82, 4, s28
	s_waitcnt lgkmcnt(0)
	v_add_f32_e32 v0, v0, v66
	ds_write_b32 v67, v0 offset:6144

.LBB0_2768:
	v_lshlrev_b32_e32 v70, 16, v158
	v_and_b32_e32 v71, 0xffff0000, v158
	v_lshlrev_b32_e32 v72, 16, v159
	v_and_b32_e32 v73, 0xffff0000, v159
	s_waitcnt lgkmcnt(0)
	v_pk_mul_f32 v[64:65], v[64:65], v[0:1] op_sel_hi:[1,0]
	v_pk_mul_f32 v[62:63], v[62:63], v[0:1] op_sel_hi:[1,0]
	v_lshlrev_b32_e32 v74, 16, v160
	v_and_b32_e32 v75, 0xffff0000, v160
	v_lshlrev_b32_e32 v76, 16, v161
	v_and_b32_e32 v77, 0xffff0000, v161
	v_pk_fma_f32 v[64:65], v[184:185], v[64:65], v[72:73]
	v_pk_fma_f32 v[62:63], v[182:183], v[62:63], v[70:71]
	v_pk_mul_f32 v[60:61], v[60:61], v[0:1] op_sel_hi:[1,0]
	v_pk_mul_f32 v[58:59], v[58:59], v[0:1] op_sel_hi:[1,0]
	v_pk_fma_f32 v[70:71], v[180:181], v[60:61], v[76:77]
	v_pk_fma_f32 v[60:61], v[178:179], v[58:59], v[74:75]
	v_mul_f32_e32 v58, v63, v63
	v_mul_f32_e32 v59, v65, v65
	v_fmac_f32_e32 v58, v62, v62
	v_fmac_f32_e32 v59, v64, v64
	v_add_f32_e32 v58, v58, v59
	v_mul_f32_e32 v59, v61, v61
	v_mul_f32_e32 v67, v71, v71
	v_fmac_f32_e32 v59, v60, v60
	v_fmac_f32_e32 v67, v70, v70
	v_add_f32_e32 v59, v59, v67
	v_add_f32_e32 v67, v58, v59
	v_cvt_pk_bf16_f32 v58, v62, v63
	v_cvt_pk_bf16_f32 v59, v64, v65
	v_lshlrev_b32_e32 v62, 16, v154
	v_and_b32_e32 v63, 0xffff0000, v154
	v_lshlrev_b32_e32 v64, 16, v155
	v_and_b32_e32 v65, 0xffff0000, v155
	v_pk_mul_f32 v[56:57], v[56:57], v[0:1] op_sel_hi:[1,0]
	v_pk_mul_f32 v[54:55], v[54:55], v[0:1] op_sel_hi:[1,0]
	v_cvt_pk_bf16_f32 v60, v60, v61
	v_cvt_pk_bf16_f32 v61, v70, v71
	v_lshlrev_b32_e32 v70, 16, v156
	v_and_b32_e32 v71, 0xffff0000, v156
	v_pk_fma_f32 v[56:57], v[172:173], v[56:57], v[64:65]
	v_pk_fma_f32 v[54:55], v[170:171], v[54:55], v[62:63]
	v_pk_mul_f32 v[50:51], v[50:51], v[0:1] op_sel_hi:[1,0]
	v_lshlrev_b32_e32 v72, 16, v157
	v_and_b32_e32 v73, 0xffff0000, v157
	v_pk_mul_f32 v[52:53], v[52:53], v[0:1] op_sel_hi:[1,0]
	v_pk_fma_f32 v[64:65], v[166:167], v[50:51], v[70:71]
	v_mul_f32_e32 v0, v55, v55
	v_mul_f32_e32 v50, v57, v57
	v_pk_fma_f32 v[62:63], v[168:169], v[52:53], v[72:73]
	v_fmac_f32_e32 v0, v54, v54
	v_fmac_f32_e32 v50, v56, v56
	v_add_f32_e32 v0, v0, v50
	v_mul_f32_e32 v50, v65, v65
	v_mul_f32_e32 v51, v63, v63
	v_fmac_f32_e32 v50, v64, v64
	v_fmac_f32_e32 v51, v62, v62
	v_add_f32_e32 v50, v50, v51
	v_add_f32_e32 v0, v0, v50
	v_add_f32_e32 v0, v67, v0
	v_mov_b32_e32 v53, v0
	s_nop 1
	v_permlane16_swap_b32_e32 v53, v0
	v_add_u32_e32 v66, 0x80, v240
	v_add_u32_e32 v68, s29, v66
	v_ashrrev_i32_e32 v69, 31, v68
	v_lshlrev_b64 v[68:69], 11, v[68:69]
	v_lshl_add_u64 v[50:51], s[14:15], 0, v[68:69]
	s_waitcnt lgkmcnt(0)
	v_add_f32_e32 v0, v0, v53
	v_lshl_add_u64 v[68:69], v[220:221], 1, v[50:51]
	v_mov_b32_e32 v50, v0
	s_nop 1
	v_permlane32_swap_b32_e32 v50, v0
	global_store_dwordx4 v[68:69], v[58:61], off
	v_cvt_pk_bf16_f32 v52, v54, v55
	v_cvt_pk_bf16_f32 v53, v56, v57
	v_cvt_pk_bf16_f32 v54, v64, v65
	v_cvt_pk_bf16_f32 v55, v62, v63
	global_store_dwordx4 v[68:69], v[52:55], off offset:256
	s_and_saveexec_b64 s[16:17], s[40:41]
	s_cbranch_execz .LBB0_2770
	v_lshl_add_u32 v51, v66, 4, s28
	s_waitcnt lgkmcnt(0)
	v_add_f32_e32 v0, v0, v50
	ds_write_b32 v51, v0 offset:6144

.LBB0_2772:
	v_lshlrev_b32_e32 v54, 16, v150
	v_and_b32_e32 v55, 0xffff0000, v150
	v_lshlrev_b32_e32 v56, 16, v151
	v_and_b32_e32 v57, 0xffff0000, v151
	s_waitcnt lgkmcnt(0)
	v_pk_mul_f32 v[48:49], v[48:49], v[0:1] op_sel_hi:[1,0]
	v_pk_mul_f32 v[46:47], v[46:47], v[0:1] op_sel_hi:[1,0]
	v_lshlrev_b32_e32 v58, 16, v152
	v_and_b32_e32 v59, 0xffff0000, v152
	v_lshlrev_b32_e32 v60, 16, v153
	v_and_b32_e32 v61, 0xffff0000, v153
	v_pk_fma_f32 v[48:49], v[184:185], v[48:49], v[56:57]
	v_pk_fma_f32 v[46:47], v[182:183], v[46:47], v[54:55]
	v_pk_mul_f32 v[44:45], v[44:45], v[0:1] op_sel_hi:[1,0]
	v_pk_mul_f32 v[42:43], v[42:43], v[0:1] op_sel_hi:[1,0]
	v_pk_fma_f32 v[54:55], v[180:181], v[44:45], v[60:61]
	v_pk_fma_f32 v[44:45], v[178:179], v[42:43], v[58:59]
	v_mul_f32_e32 v42, v47, v47
	v_mul_f32_e32 v43, v49, v49
	v_fmac_f32_e32 v42, v46, v46
	v_fmac_f32_e32 v43, v48, v48
	v_add_f32_e32 v42, v42, v43
	v_mul_f32_e32 v43, v45, v45
	v_mul_f32_e32 v51, v55, v55
	v_fmac_f32_e32 v43, v44, v44
	v_fmac_f32_e32 v51, v54, v54
	v_add_f32_e32 v43, v43, v51
	v_add_f32_e32 v51, v42, v43
	v_cvt_pk_bf16_f32 v42, v46, v47
	v_cvt_pk_bf16_f32 v43, v48, v49
	v_lshlrev_b32_e32 v46, 16, v146
	v_and_b32_e32 v47, 0xffff0000, v146
	v_lshlrev_b32_e32 v48, 16, v147
	v_and_b32_e32 v49, 0xffff0000, v147
	v_pk_mul_f32 v[40:41], v[40:41], v[0:1] op_sel_hi:[1,0]
	v_pk_mul_f32 v[38:39], v[38:39], v[0:1] op_sel_hi:[1,0]
	v_cvt_pk_bf16_f32 v44, v44, v45
	v_cvt_pk_bf16_f32 v45, v54, v55
	v_lshlrev_b32_e32 v54, 16, v148
	v_and_b32_e32 v55, 0xffff0000, v148
	v_pk_fma_f32 v[40:41], v[172:173], v[40:41], v[48:49]
	v_pk_fma_f32 v[38:39], v[170:171], v[38:39], v[46:47]
	v_pk_mul_f32 v[34:35], v[34:35], v[0:1] op_sel_hi:[1,0]
	v_lshlrev_b32_e32 v56, 16, v149
	v_and_b32_e32 v57, 0xffff0000, v149
	v_pk_mul_f32 v[36:37], v[36:37], v[0:1] op_sel_hi:[1,0]
	v_pk_fma_f32 v[48:49], v[166:167], v[34:35], v[54:55]
	v_mul_f32_e32 v0, v39, v39
	v_mul_f32_e32 v34, v41, v41
	v_pk_fma_f32 v[46:47], v[168:169], v[36:37], v[56:57]
	v_fmac_f32_e32 v0, v38, v38
	v_fmac_f32_e32 v34, v40, v40
	v_add_f32_e32 v0, v0, v34
	v_mul_f32_e32 v34, v49, v49
	v_mul_f32_e32 v35, v47, v47
	v_fmac_f32_e32 v34, v48, v48
	v_fmac_f32_e32 v35, v46, v46
	v_add_f32_e32 v34, v34, v35
	v_add_f32_e32 v0, v0, v34
	v_add_f32_e32 v0, v51, v0
	v_mov_b32_e32 v37, v0
	s_nop 1
	v_permlane16_swap_b32_e32 v37, v0
	v_add_u32_e32 v50, 0x90, v240
	v_add_u32_e32 v52, s29, v50
	v_ashrrev_i32_e32 v53, 31, v52
	v_lshlrev_b64 v[52:53], 11, v[52:53]
	v_lshl_add_u64 v[34:35], s[14:15], 0, v[52:53]
	s_waitcnt lgkmcnt(0)
	v_add_f32_e32 v0, v0, v37
	v_lshl_add_u64 v[52:53], v[220:221], 1, v[34:35]
	v_mov_b32_e32 v34, v0
	s_nop 1
	v_permlane32_swap_b32_e32 v34, v0
	global_store_dwordx4 v[52:53], v[42:45], off
	v_cvt_pk_bf16_f32 v36, v38, v39
	v_cvt_pk_bf16_f32 v37, v40, v41
	v_cvt_pk_bf16_f32 v38, v48, v49
	v_cvt_pk_bf16_f32 v39, v46, v47
	global_store_dwordx4 v[52:53], v[36:39], off offset:256
	s_and_saveexec_b64 s[16:17], s[40:41]
	s_cbranch_execz .LBB0_2774
	v_lshl_add_u32 v35, v50, 4, s28
	s_waitcnt lgkmcnt(0)
	v_add_f32_e32 v0, v0, v34
	ds_write_b32 v35, v0 offset:6144

.LBB0_2776:
	v_lshlrev_b32_e32 v38, 16, v142
	v_and_b32_e32 v39, 0xffff0000, v142
	v_lshlrev_b32_e32 v40, 16, v143
	v_and_b32_e32 v41, 0xffff0000, v143
	s_waitcnt lgkmcnt(0)
	v_pk_mul_f32 v[32:33], v[32:33], v[0:1] op_sel_hi:[1,0]
	v_pk_mul_f32 v[30:31], v[30:31], v[0:1] op_sel_hi:[1,0]
	v_lshlrev_b32_e32 v42, 16, v144
	v_and_b32_e32 v43, 0xffff0000, v144
	v_lshlrev_b32_e32 v44, 16, v145
	v_and_b32_e32 v45, 0xffff0000, v145
	v_pk_fma_f32 v[32:33], v[184:185], v[32:33], v[40:41]
	v_pk_fma_f32 v[30:31], v[182:183], v[30:31], v[38:39]
	v_pk_mul_f32 v[28:29], v[28:29], v[0:1] op_sel_hi:[1,0]
	v_pk_mul_f32 v[26:27], v[26:27], v[0:1] op_sel_hi:[1,0]
	v_pk_fma_f32 v[38:39], v[180:181], v[28:29], v[44:45]
	v_pk_fma_f32 v[28:29], v[178:179], v[26:27], v[42:43]
	v_mul_f32_e32 v26, v31, v31
	v_mul_f32_e32 v27, v33, v33
	v_fmac_f32_e32 v26, v30, v30
	v_fmac_f32_e32 v27, v32, v32
	v_add_f32_e32 v26, v26, v27
	v_mul_f32_e32 v27, v29, v29
	v_mul_f32_e32 v35, v39, v39
	v_fmac_f32_e32 v27, v28, v28
	v_fmac_f32_e32 v35, v38, v38
	v_add_f32_e32 v27, v27, v35
	v_add_f32_e32 v35, v26, v27
	v_cvt_pk_bf16_f32 v26, v30, v31
	v_cvt_pk_bf16_f32 v27, v32, v33
	v_lshlrev_b32_e32 v30, 16, v138
	v_and_b32_e32 v31, 0xffff0000, v138
	v_lshlrev_b32_e32 v32, 16, v139
	v_and_b32_e32 v33, 0xffff0000, v139
	v_pk_mul_f32 v[24:25], v[24:25], v[0:1] op_sel_hi:[1,0]
	v_pk_mul_f32 v[22:23], v[22:23], v[0:1] op_sel_hi:[1,0]
	v_cvt_pk_bf16_f32 v28, v28, v29
	v_cvt_pk_bf16_f32 v29, v38, v39
	v_lshlrev_b32_e32 v38, 16, v140
	v_and_b32_e32 v39, 0xffff0000, v140
	v_pk_fma_f32 v[24:25], v[172:173], v[24:25], v[32:33]
	v_pk_fma_f32 v[22:23], v[170:171], v[22:23], v[30:31]
	v_pk_mul_f32 v[18:19], v[18:19], v[0:1] op_sel_hi:[1,0]
	v_lshlrev_b32_e32 v40, 16, v141
	v_and_b32_e32 v41, 0xffff0000, v141
	v_pk_mul_f32 v[20:21], v[20:21], v[0:1] op_sel_hi:[1,0]
	v_pk_fma_f32 v[32:33], v[166:167], v[18:19], v[38:39]
	v_mul_f32_e32 v0, v23, v23
	v_mul_f32_e32 v18, v25, v25
	v_pk_fma_f32 v[30:31], v[168:169], v[20:21], v[40:41]
	v_fmac_f32_e32 v0, v22, v22
	v_fmac_f32_e32 v18, v24, v24
	v_add_f32_e32 v0, v0, v18
	v_mul_f32_e32 v18, v33, v33
	v_mul_f32_e32 v19, v31, v31
	v_fmac_f32_e32 v18, v32, v32
	v_fmac_f32_e32 v19, v30, v30
	v_add_f32_e32 v18, v18, v19
	v_add_f32_e32 v0, v0, v18
	v_add_f32_e32 v0, v35, v0
	v_mov_b32_e32 v21, v0
	s_nop 1
	v_permlane16_swap_b32_e32 v21, v0
	v_add_u32_e32 v34, 0xa0, v240
	v_add_u32_e32 v36, s29, v34
	v_ashrrev_i32_e32 v37, 31, v36
	v_lshlrev_b64 v[36:37], 11, v[36:37]
	v_lshl_add_u64 v[18:19], s[14:15], 0, v[36:37]
	s_waitcnt lgkmcnt(0)
	v_add_f32_e32 v0, v0, v21
	v_lshl_add_u64 v[36:37], v[220:221], 1, v[18:19]
	v_mov_b32_e32 v18, v0
	s_nop 1
	v_permlane32_swap_b32_e32 v18, v0
	global_store_dwordx4 v[36:37], v[26:29], off
	v_cvt_pk_bf16_f32 v20, v22, v23
	v_cvt_pk_bf16_f32 v21, v24, v25
	v_cvt_pk_bf16_f32 v22, v32, v33
	v_cvt_pk_bf16_f32 v23, v30, v31
	global_store_dwordx4 v[36:37], v[20:23], off offset:256
	s_and_saveexec_b64 s[16:17], s[40:41]
	s_cbranch_execz .LBB0_2778
	v_lshl_add_u32 v19, v34, 4, s28
	s_waitcnt lgkmcnt(0)
	v_add_f32_e32 v0, v0, v18
	ds_write_b32 v19, v0 offset:6144

.LBB0_2780:
	v_lshlrev_b32_e32 v22, 16, v126
	v_and_b32_e32 v23, 0xffff0000, v126
	v_lshlrev_b32_e32 v24, 16, v127
	v_and_b32_e32 v25, 0xffff0000, v127
	s_waitcnt lgkmcnt(0)
	v_pk_mul_f32 v[16:17], v[16:17], v[0:1] op_sel_hi:[1,0]
	v_pk_mul_f32 v[14:15], v[14:15], v[0:1] op_sel_hi:[1,0]
	v_lshlrev_b32_e32 v26, 16, v128
	v_and_b32_e32 v27, 0xffff0000, v128
	v_lshlrev_b32_e32 v28, 16, v129
	v_and_b32_e32 v29, 0xffff0000, v129
	v_pk_fma_f32 v[16:17], v[184:185], v[16:17], v[24:25]
	v_pk_fma_f32 v[14:15], v[182:183], v[14:15], v[22:23]
	v_pk_mul_f32 v[12:13], v[12:13], v[0:1] op_sel_hi:[1,0]
	v_pk_mul_f32 v[10:11], v[10:11], v[0:1] op_sel_hi:[1,0]
	v_pk_fma_f32 v[22:23], v[180:181], v[12:13], v[28:29]
	v_pk_fma_f32 v[12:13], v[178:179], v[10:11], v[26:27]
	v_mul_f32_e32 v10, v15, v15
	v_mul_f32_e32 v11, v17, v17
	v_fmac_f32_e32 v10, v14, v14
	v_fmac_f32_e32 v11, v16, v16
	v_add_f32_e32 v10, v10, v11
	v_mul_f32_e32 v11, v13, v13
	v_mul_f32_e32 v19, v23, v23
	v_fmac_f32_e32 v11, v12, v12
	v_fmac_f32_e32 v19, v22, v22
	v_add_f32_e32 v11, v11, v19
	v_add_f32_e32 v19, v10, v11
	v_cvt_pk_bf16_f32 v10, v14, v15
	v_cvt_pk_bf16_f32 v11, v16, v17
	v_lshlrev_b32_e32 v14, 16, v118
	v_and_b32_e32 v15, 0xffff0000, v118
	v_lshlrev_b32_e32 v16, 16, v119
	v_and_b32_e32 v17, 0xffff0000, v119
	v_pk_mul_f32 v[8:9], v[8:9], v[0:1] op_sel_hi:[1,0]
	v_pk_mul_f32 v[6:7], v[6:7], v[0:1] op_sel_hi:[1,0]
	v_cvt_pk_bf16_f32 v12, v12, v13
	v_cvt_pk_bf16_f32 v13, v22, v23
	v_lshlrev_b32_e32 v22, 16, v120
	v_and_b32_e32 v23, 0xffff0000, v120
	v_pk_fma_f32 v[8:9], v[172:173], v[8:9], v[16:17]
	v_pk_fma_f32 v[6:7], v[170:171], v[6:7], v[14:15]
	v_pk_mul_f32 v[2:3], v[2:3], v[0:1] op_sel_hi:[1,0]
	v_lshlrev_b32_e32 v24, 16, v121
	v_and_b32_e32 v25, 0xffff0000, v121
	v_pk_mul_f32 v[4:5], v[4:5], v[0:1] op_sel_hi:[1,0]
	v_pk_fma_f32 v[16:17], v[166:167], v[2:3], v[22:23]
	v_mul_f32_e32 v0, v7, v7
	v_mul_f32_e32 v2, v9, v9
	v_pk_fma_f32 v[14:15], v[168:169], v[4:5], v[24:25]
	v_fmac_f32_e32 v0, v6, v6
	v_fmac_f32_e32 v2, v8, v8
	v_add_f32_e32 v0, v0, v2
	v_mul_f32_e32 v2, v17, v17
	v_mul_f32_e32 v3, v15, v15
	v_fmac_f32_e32 v2, v16, v16
	v_fmac_f32_e32 v3, v14, v14
	v_add_f32_e32 v2, v2, v3
	v_add_f32_e32 v0, v0, v2
	v_add_f32_e32 v0, v19, v0
	v_mov_b32_e32 v5, v0
	s_nop 1
	v_permlane16_swap_b32_e32 v5, v0
	v_add_u32_e32 v18, 0xb0, v240
	v_add_u32_e32 v20, s29, v18
	v_ashrrev_i32_e32 v21, 31, v20
	v_lshlrev_b64 v[20:21], 11, v[20:21]
	v_lshl_add_u64 v[2:3], s[14:15], 0, v[20:21]
	s_waitcnt lgkmcnt(0)
	v_add_f32_e32 v0, v0, v5
	v_lshl_add_u64 v[20:21], v[220:221], 1, v[2:3]
	v_mov_b32_e32 v2, v0
	s_nop 1
	v_permlane32_swap_b32_e32 v2, v0
	global_store_dwordx4 v[20:21], v[10:13], off
	v_cvt_pk_bf16_f32 v4, v6, v7
	v_cvt_pk_bf16_f32 v5, v8, v9
	v_cvt_pk_bf16_f32 v6, v16, v17
	v_cvt_pk_bf16_f32 v7, v14, v15
	global_store_dwordx4 v[20:21], v[4:7], off offset:256
	s_and_saveexec_b64 s[14:15], s[40:41]
	s_cbranch_execz .LBB0_2782
	v_lshl_add_u32 v3, v18, 4, s28
	s_waitcnt lgkmcnt(0)
	v_add_f32_e32 v0, v0, v2
	ds_write_b32 v3, v0 offset:6144

.LBB0_2803:
	s_lshl_b32 s24, s52, 5
	s_lshl_b32 s25, s12, 8
	v_lshrrev_b32_e32 v118, 1, v0
	s_add_i32 s4, s80, 64
	s_or_b32 s24, s25, s24
	v_and_or_b32 v220, v118, 24, s24
	s_lshl_b32 s29, s4, 8
	v_add_u32_e32 v118, s29, v240
	v_ashrrev_i32_e32 v221, 31, v220
	v_lshl_add_u64 v[120:121], v[220:221], 1, s[22:23]
	s_mov_b64 s[22:23], 0x4000000
	v_ashrrev_i32_e32 v119, 31, v118
	v_lshl_add_u64 v[120:121], v[120:121], 0, s[22:23]
	v_lshlrev_b64 v[224:225], 11, v[118:119]
	v_lshl_add_u64 v[126:127], v[120:121], 0, v[224:225]
	s_barrier
	global_load_dwordx4 v[206:209], v[126:127], off
	global_load_dwordx4 v[202:205], v[126:127], off offset:256
	v_or_b32_e32 v126, 16, v118
	v_ashrrev_i32_e32 v127, 31, v126
	v_lshlrev_b64 v[126:127], 11, v[126:127]
	v_lshl_add_u64 v[126:127], v[120:121], 0, v[126:127]
	global_load_dwordx4 v[198:201], v[126:127], off
	global_load_dwordx4 v[194:197], v[126:127], off offset:256
	v_or_b32_e32 v126, 32, v118
	v_ashrrev_i32_e32 v127, 31, v126
	v_lshlrev_b64 v[126:127], 11, v[126:127]
	v_lshl_add_u64 v[126:127], v[120:121], 0, v[126:127]
	global_load_dwordx4 v[190:193], v[126:127], off
	global_load_dwordx4 v[186:189], v[126:127], off offset:256
	v_or_b32_e32 v126, 48, v118
	v_ashrrev_i32_e32 v127, 31, v126
	v_lshlrev_b64 v[126:127], 11, v[126:127]
	v_lshl_add_u64 v[126:127], v[120:121], 0, v[126:127]
	global_load_dwordx4 v[174:177], v[126:127], off
	global_load_dwordx4 v[162:165], v[126:127], off offset:256
	v_add_u32_e32 v126, 0x80, v118
	v_ashrrev_i32_e32 v127, 31, v126
	v_lshlrev_b64 v[126:127], 11, v[126:127]
	v_lshl_add_u64 v[126:127], v[120:121], 0, v[126:127]
	global_load_dwordx4 v[158:161], v[126:127], off
	global_load_dwordx4 v[154:157], v[126:127], off offset:256
	v_add_u32_e32 v126, 0x90, v118
	v_ashrrev_i32_e32 v127, 31, v126
	v_lshlrev_b64 v[126:127], 11, v[126:127]
	v_lshl_add_u64 v[126:127], v[120:121], 0, v[126:127]
	global_load_dwordx4 v[150:153], v[126:127], off
	global_load_dwordx4 v[146:149], v[126:127], off offset:256
	v_add_u32_e32 v126, 0xa0, v118
	v_add_u32_e32 v118, 0xb0, v118
	v_ashrrev_i32_e32 v127, 31, v126
	v_ashrrev_i32_e32 v119, 31, v118
	v_lshlrev_b64 v[126:127], 11, v[126:127]
	v_lshlrev_b64 v[118:119], 11, v[118:119]
	v_lshl_add_u64 v[126:127], v[120:121], 0, v[126:127]
	v_lshl_add_u64 v[118:119], v[120:121], 0, v[118:119]
	global_load_dwordx4 v[142:145], v[126:127], off
	global_load_dwordx4 v[138:141], v[126:127], off offset:256
	s_nop 0
	global_load_dwordx4 v[126:129], v[118:119], off
	s_nop 0
	global_load_dwordx4 v[118:121], v[118:119], off offset:256
	v_and_b32_e32 v168, 64, v231
	v_xor_b32_e32 v167, 16, v231
	v_add_u32_e32 v168, 64, v168
	v_cmp_lt_i32_e32 vcc, v167, v168
	v_mul_f32_e32 v169, v137, v137
	v_fmac_f32_e32 v169, v136, v136
	v_cndmask_b32_e32 v167, v231, v167, vcc
	v_lshlrev_b32_e32 v241, 2, v167
	v_mul_f32_e32 v167, v135, v135
	v_fmac_f32_e32 v167, v134, v134
	v_add_f32_e32 v167, v167, v169
	v_mul_f32_e32 v169, v131, v131
	v_mul_f32_e32 v170, v133, v133
	v_fmac_f32_e32 v169, v130, v130
	v_fmac_f32_e32 v170, v132, v132
	v_add_f32_e32 v169, v169, v170
	v_add_f32_e32 v167, v169, v167
	v_mul_f32_e32 v169, v123, v123
	v_mul_f32_e32 v170, v125, v125
	v_fmac_f32_e32 v169, v122, v122
	v_fmac_f32_e32 v170, v124, v124
	v_add_f32_e32 v169, v169, v170
	v_add_f32_e32 v167, v169, v167
	v_mul_f32_e32 v169, v115, v115
	v_mul_f32_e32 v170, v117, v117
	v_fmac_f32_e32 v169, v114, v114
	v_fmac_f32_e32 v170, v116, v116
	v_add_f32_e32 v169, v169, v170
	v_add_f32_e32 v167, v169, v167
	v_mov_b32_e32 v169, v167
	s_nop 1
	v_permlane16_swap_b32_e32 v169, v167
	v_xor_b32_e32 v170, 32, v231
	v_cmp_lt_i32_e32 vcc, v170, v168
	s_lshl_b32 s22, s52, 2
	s_add_i32 s28, s22, 0
	v_cndmask_b32_e32 v168, v231, v170, vcc
	v_lshlrev_b32_e32 v242, 2, v168
	s_waitcnt lgkmcnt(0)
	v_add_f32_e32 v168, v167, v169
	v_mov_b32_e32 v169, v168
	s_nop 1
	v_permlane32_swap_b32_e32 v169, v168
	v_and_b32_e32 v167, 63, v0
	v_cmp_gt_u32_e64 s[40:41], 16, v167
	s_and_saveexec_b64 s[22:23], s[40:41]
	v_readlane_b32 s64, v252, 3
	v_readlane_b32 s65, v255, 10
	v_readlane_b32 s68, v255, 11
	v_readlane_b32 s70, v255, 14
	v_readlane_b32 s71, v255, 15
	s_cbranch_execz .LBB0_2805
	s_lshl_b32 s24, s48, 10
	s_add_i32 s24, s28, s24
	s_waitcnt lgkmcnt(0)
	v_add_f32_e32 v168, v168, v169
	v_lshl_add_u32 v169, v166, 4, s24
	ds_write_b32 v169, v168
.LBB0_2805:
	s_or_b64 exec, exec, s[22:23]
	v_mul_f32_e32 v168, v111, v111
	s_waitcnt lgkmcnt(0)
	v_mul_f32_e32 v169, v113, v113
	v_fmac_f32_e32 v168, v110, v110
	v_fmac_f32_e32 v169, v112, v112
	v_add_f32_e32 v168, v168, v169
	v_mul_f32_e32 v169, v107, v107
	v_mul_f32_e32 v170, v109, v109
	v_fmac_f32_e32 v169, v106, v106
	v_fmac_f32_e32 v170, v108, v108
	v_add_f32_e32 v169, v169, v170
	v_add_f32_e32 v168, v169, v168
	v_mul_f32_e32 v169, v103, v103
	v_mul_f32_e32 v170, v105, v105
	v_fmac_f32_e32 v169, v102, v102
	v_fmac_f32_e32 v170, v104, v104
	v_add_f32_e32 v169, v169, v170
	v_add_f32_e32 v168, v169, v168
	v_mul_f32_e32 v169, v99, v99
	v_mul_f32_e32 v170, v101, v101
	v_fmac_f32_e32 v169, v98, v98
	v_fmac_f32_e32 v170, v100, v100
	v_add_f32_e32 v169, v169, v170
	v_add_f32_e32 v168, v169, v168
	v_mov_b32_e32 v169, v168
	s_nop 1
	v_permlane16_swap_b32_e32 v169, v168
	s_waitcnt lgkmcnt(0)
	v_add_f32_e32 v168, v168, v169
	v_mov_b32_e32 v169, v168
	s_nop 1
	v_permlane32_swap_b32_e32 v169, v168
	s_and_saveexec_b64 s[22:23], s[40:41]
	s_cbranch_execz .LBB0_2807
	s_lshl_b32 s24, s48, 10
	s_add_i32 s24, s28, s24
	s_waitcnt lgkmcnt(0)
	v_add_f32_e32 v168, v168, v169
	v_lshl_add_u32 v169, v166, 4, s24
	ds_write_b32 v169, v168 offset:256
.LBB0_2807:
	s_or_b64 exec, exec, s[22:23]
	v_mul_f32_e32 v168, v95, v95
	s_waitcnt lgkmcnt(0)
	v_mul_f32_e32 v169, v97, v97
	v_fmac_f32_e32 v168, v94, v94
	v_fmac_f32_e32 v169, v96, v96
	v_add_f32_e32 v168, v168, v169
	v_mul_f32_e32 v169, v91, v91
	v_mul_f32_e32 v170, v93, v93
	v_fmac_f32_e32 v169, v90, v90
	v_fmac_f32_e32 v170, v92, v92
	v_add_f32_e32 v169, v169, v170
	v_add_f32_e32 v168, v169, v168
	v_mul_f32_e32 v169, v87, v87
	v_mul_f32_e32 v170, v89, v89
	v_fmac_f32_e32 v169, v86, v86
	v_fmac_f32_e32 v170, v88, v88
	v_add_f32_e32 v169, v169, v170
	v_add_f32_e32 v168, v169, v168
	v_mul_f32_e32 v169, v83, v83
	v_mul_f32_e32 v170, v85, v85
	v_fmac_f32_e32 v169, v82, v82
	v_fmac_f32_e32 v170, v84, v84
	v_add_f32_e32 v169, v169, v170
	v_add_f32_e32 v168, v169, v168
	v_mov_b32_e32 v169, v168
	s_nop 1
	v_permlane16_swap_b32_e32 v169, v168
	s_waitcnt lgkmcnt(0)
	v_add_f32_e32 v168, v168, v169
	v_mov_b32_e32 v169, v168
	s_nop 1
	v_permlane32_swap_b32_e32 v169, v168
	s_and_saveexec_b64 s[22:23], s[40:41]
	s_cbranch_execz .LBB0_2809
	s_lshl_b32 s24, s48, 10
	s_add_i32 s24, s28, s24
	s_waitcnt lgkmcnt(0)
	v_add_f32_e32 v168, v168, v169
	v_lshl_add_u32 v169, v166, 4, s24
	ds_write_b32 v169, v168 offset:512
.LBB0_2809:
	s_or_b64 exec, exec, s[22:23]
	v_mul_f32_e32 v168, v79, v79
	s_waitcnt lgkmcnt(0)
	v_mul_f32_e32 v169, v81, v81
	v_fmac_f32_e32 v168, v78, v78
	v_fmac_f32_e32 v169, v80, v80
	v_add_f32_e32 v168, v168, v169
	v_mul_f32_e32 v169, v75, v75
	v_mul_f32_e32 v170, v77, v77
	v_fmac_f32_e32 v169, v74, v74
	v_fmac_f32_e32 v170, v76, v76
	v_add_f32_e32 v169, v169, v170
	v_add_f32_e32 v168, v169, v168
	v_mul_f32_e32 v169, v71, v71
	v_mul_f32_e32 v170, v73, v73
	v_fmac_f32_e32 v169, v70, v70
	v_fmac_f32_e32 v170, v72, v72
	v_add_f32_e32 v169, v169, v170
	v_add_f32_e32 v168, v169, v168
	v_mul_f32_e32 v169, v67, v67
	v_mul_f32_e32 v170, v69, v69
	v_fmac_f32_e32 v169, v66, v66
	v_fmac_f32_e32 v170, v68, v68
	v_add_f32_e32 v169, v169, v170
	v_add_f32_e32 v168, v169, v168
	v_mov_b32_e32 v169, v168
	s_nop 1
	v_permlane16_swap_b32_e32 v169, v168
	s_waitcnt lgkmcnt(0)
	v_add_f32_e32 v168, v168, v169
	v_mov_b32_e32 v169, v168
	s_nop 1
	v_permlane32_swap_b32_e32 v169, v168
	s_and_saveexec_b64 s[22:23], s[40:41]
	s_cbranch_execz .LBB0_2811
	s_lshl_b32 s24, s48, 10
	s_add_i32 s24, s28, s24
	s_waitcnt lgkmcnt(0)
	v_add_f32_e32 v168, v168, v169
	v_lshl_add_u32 v169, v166, 4, s24
	ds_write_b32 v169, v168 offset:768
.LBB0_2811:
	s_or_b64 exec, exec, s[22:23]
	v_mul_f32_e32 v168, v63, v63
	s_waitcnt lgkmcnt(0)
	v_mul_f32_e32 v169, v65, v65
	v_fmac_f32_e32 v168, v62, v62
	v_fmac_f32_e32 v169, v64, v64
	v_add_f32_e32 v168, v168, v169
	v_mul_f32_e32 v169, v59, v59
	v_mul_f32_e32 v170, v61, v61
	v_fmac_f32_e32 v169, v58, v58
	v_fmac_f32_e32 v170, v60, v60
	v_add_f32_e32 v169, v169, v170
	v_add_f32_e32 v168, v169, v168
	v_mul_f32_e32 v169, v55, v55
	v_mul_f32_e32 v170, v57, v57
	v_fmac_f32_e32 v169, v54, v54
	v_fmac_f32_e32 v170, v56, v56
	v_add_f32_e32 v169, v169, v170
	v_add_f32_e32 v168, v169, v168
	v_mul_f32_e32 v169, v51, v51
	v_mul_f32_e32 v170, v53, v53
	v_fmac_f32_e32 v169, v50, v50
	v_fmac_f32_e32 v170, v52, v52
	v_add_f32_e32 v169, v169, v170
	v_add_f32_e32 v168, v169, v168
	v_mov_b32_e32 v169, v168
	s_nop 1
	v_permlane16_swap_b32_e32 v169, v168
	s_waitcnt lgkmcnt(0)
	v_add_f32_e32 v168, v168, v169
	v_mov_b32_e32 v169, v168
	s_nop 1
	v_permlane32_swap_b32_e32 v169, v168
	s_and_saveexec_b64 s[22:23], s[40:41]
	s_cbranch_execz .LBB0_2813
	s_lshl_b32 s24, s48, 10
	s_add_i32 s24, s28, s24
	s_waitcnt lgkmcnt(0)
	v_add_f32_e32 v168, v168, v169
	v_lshl_add_u32 v169, v166, 4, s24
	ds_write_b32 v169, v168 offset:2048
.LBB0_2813:
	s_or_b64 exec, exec, s[22:23]
	v_mul_f32_e32 v168, v47, v47
	s_waitcnt lgkmcnt(0)
	v_mul_f32_e32 v169, v49, v49
	v_fmac_f32_e32 v168, v46, v46
	v_fmac_f32_e32 v169, v48, v48
	v_add_f32_e32 v168, v168, v169
	v_mul_f32_e32 v169, v43, v43
	v_mul_f32_e32 v170, v45, v45
	v_fmac_f32_e32 v169, v42, v42
	v_fmac_f32_e32 v170, v44, v44
	v_add_f32_e32 v169, v169, v170
	v_add_f32_e32 v168, v169, v168
	v_mul_f32_e32 v169, v39, v39
	v_mul_f32_e32 v170, v41, v41
	v_fmac_f32_e32 v169, v38, v38
	v_fmac_f32_e32 v170, v40, v40
	v_add_f32_e32 v169, v169, v170
	v_add_f32_e32 v168, v169, v168
	v_mul_f32_e32 v169, v35, v35
	v_mul_f32_e32 v170, v37, v37
	v_fmac_f32_e32 v169, v34, v34
	v_fmac_f32_e32 v170, v36, v36
	v_add_f32_e32 v169, v169, v170
	v_add_f32_e32 v168, v169, v168
	v_mov_b32_e32 v169, v168
	s_nop 1
	v_permlane16_swap_b32_e32 v169, v168
	s_waitcnt lgkmcnt(0)
	v_add_f32_e32 v168, v168, v169
	v_mov_b32_e32 v169, v168
	s_nop 1
	v_permlane32_swap_b32_e32 v169, v168
	s_and_saveexec_b64 s[22:23], s[40:41]
	s_cbranch_execz .LBB0_2815
	s_lshl_b32 s24, s48, 10
	s_add_i32 s24, s28, s24
	s_waitcnt lgkmcnt(0)
	v_add_f32_e32 v168, v168, v169
	v_lshl_add_u32 v169, v166, 4, s24
	ds_write_b32 v169, v168 offset:2304
.LBB0_2815:
	s_or_b64 exec, exec, s[22:23]
	v_mul_f32_e32 v168, v31, v31
	s_waitcnt lgkmcnt(0)
	v_mul_f32_e32 v169, v33, v33
	v_fmac_f32_e32 v168, v30, v30
	v_fmac_f32_e32 v169, v32, v32
	v_add_f32_e32 v168, v168, v169
	v_mul_f32_e32 v169, v27, v27
	v_mul_f32_e32 v170, v29, v29
	v_fmac_f32_e32 v169, v26, v26
	v_fmac_f32_e32 v170, v28, v28
	v_add_f32_e32 v169, v169, v170
	v_add_f32_e32 v168, v169, v168
	v_mul_f32_e32 v169, v23, v23
	v_mul_f32_e32 v170, v25, v25
	v_fmac_f32_e32 v169, v22, v22
	v_fmac_f32_e32 v170, v24, v24
	v_add_f32_e32 v169, v169, v170
	v_add_f32_e32 v168, v169, v168
	v_mul_f32_e32 v169, v19, v19
	v_mul_f32_e32 v170, v21, v21
	v_fmac_f32_e32 v169, v18, v18
	v_fmac_f32_e32 v170, v20, v20
	v_add_f32_e32 v169, v169, v170
	v_add_f32_e32 v168, v169, v168
	v_mov_b32_e32 v169, v168
	s_nop 1
	v_permlane16_swap_b32_e32 v169, v168
	s_waitcnt lgkmcnt(0)
	v_add_f32_e32 v168, v168, v169
	v_mov_b32_e32 v169, v168
	s_nop 1
	v_permlane32_swap_b32_e32 v169, v168
	s_and_saveexec_b64 s[22:23], s[40:41]
	s_cbranch_execz .LBB0_2817
	s_lshl_b32 s24, s48, 10
	s_add_i32 s24, s28, s24
	s_waitcnt lgkmcnt(0)
	v_add_f32_e32 v168, v168, v169
	v_lshl_add_u32 v169, v166, 4, s24
	ds_write_b32 v169, v168 offset:2560
.LBB0_2817:
	s_or_b64 exec, exec, s[22:23]
	v_mul_f32_e32 v168, v15, v15
	s_waitcnt lgkmcnt(0)
	v_mul_f32_e32 v169, v17, v17
	v_fmac_f32_e32 v168, v14, v14
	v_fmac_f32_e32 v169, v16, v16
	v_add_f32_e32 v168, v168, v169
	v_mul_f32_e32 v169, v11, v11
	v_mul_f32_e32 v170, v13, v13
	v_fmac_f32_e32 v169, v10, v10
	v_fmac_f32_e32 v170, v12, v12
	v_add_f32_e32 v169, v169, v170
	v_add_f32_e32 v168, v169, v168
	v_mul_f32_e32 v169, v7, v7
	v_mul_f32_e32 v170, v9, v9
	v_fmac_f32_e32 v169, v6, v6
	v_fmac_f32_e32 v170, v8, v8
	v_add_f32_e32 v169, v169, v170
	v_add_f32_e32 v168, v169, v168
	v_mul_f32_e32 v169, v3, v3
	v_mul_f32_e32 v170, v5, v5
	v_fmac_f32_e32 v169, v2, v2
	v_fmac_f32_e32 v170, v4, v4
	v_add_f32_e32 v169, v169, v170
	v_add_f32_e32 v168, v169, v168
	v_mov_b32_e32 v169, v168
	s_nop 1
	v_permlane16_swap_b32_e32 v169, v168
	s_waitcnt lgkmcnt(0)
	v_add_f32_e32 v168, v168, v169
	v_mov_b32_e32 v169, v168
	s_nop 1
	v_permlane32_swap_b32_e32 v169, v168
	s_and_saveexec_b64 s[22:23], s[40:41]
	s_cbranch_execz .LBB0_2819
	s_lshl_b32 s24, s48, 10
	s_add_i32 s24, s28, s24
	s_waitcnt lgkmcnt(0)
	v_add_f32_e32 v168, v168, v169
	v_lshl_add_u32 v166, v166, 4, s24
	ds_write_b32 v166, v168 offset:2816

.LBB0_2845:
	s_waitcnt vmcnt(0)
	v_lshlrev_b32_e32 v216, 16, v206
	v_and_b32_e32 v217, 0xffff0000, v206
	v_lshlrev_b32_e32 v206, 16, v207
	v_and_b32_e32 v207, 0xffff0000, v207
	s_waitcnt lgkmcnt(0)
	v_pk_mul_f32 v[136:137], v[136:137], v[0:1] op_sel_hi:[1,0]
	v_pk_mul_f32 v[134:135], v[134:135], v[0:1] op_sel_hi:[1,0]
	v_lshlrev_b32_e32 v218, 16, v208
	v_and_b32_e32 v219, 0xffff0000, v208
	v_lshlrev_b32_e32 v208, 16, v209
	v_and_b32_e32 v209, 0xffff0000, v209
	v_pk_fma_f32 v[136:137], v[184:185], v[136:137], v[206:207]
	v_pk_fma_f32 v[134:135], v[182:183], v[134:135], v[216:217]
	v_pk_mul_f32 v[132:133], v[132:133], v[0:1] op_sel_hi:[1,0]
	v_pk_mul_f32 v[130:131], v[130:131], v[0:1] op_sel_hi:[1,0]
	v_pk_fma_f32 v[206:207], v[180:181], v[132:133], v[208:209]
	v_pk_fma_f32 v[132:133], v[178:179], v[130:131], v[218:219]
	v_mul_f32_e32 v130, v135, v135
	v_mul_f32_e32 v131, v137, v137
	v_fmac_f32_e32 v130, v134, v134
	v_fmac_f32_e32 v131, v136, v136
	v_add_f32_e32 v130, v130, v131
	v_mul_f32_e32 v131, v133, v133
	v_mul_f32_e32 v208, v207, v207
	v_fmac_f32_e32 v131, v132, v132
	v_fmac_f32_e32 v208, v206, v206
	v_add_f32_e32 v131, v131, v208
	v_add_f32_e32 v208, v130, v131
	v_cvt_pk_bf16_f32 v130, v134, v135
	v_cvt_pk_bf16_f32 v131, v136, v137
	v_lshlrev_b32_e32 v134, 16, v202
	v_and_b32_e32 v135, 0xffff0000, v202
	v_lshlrev_b32_e32 v136, 16, v203
	v_and_b32_e32 v137, 0xffff0000, v203
	v_pk_mul_f32 v[124:125], v[124:125], v[0:1] op_sel_hi:[1,0]
	v_pk_mul_f32 v[122:123], v[122:123], v[0:1] op_sel_hi:[1,0]
	v_lshlrev_b32_e32 v202, 16, v204
	v_and_b32_e32 v203, 0xffff0000, v204
	v_pk_fma_f32 v[124:125], v[172:173], v[124:125], v[136:137]
	v_pk_fma_f32 v[122:123], v[170:171], v[122:123], v[134:135]
	v_pk_mul_f32 v[114:115], v[114:115], v[0:1] op_sel_hi:[1,0]
	v_lshlrev_b32_e32 v204, 16, v205
	v_and_b32_e32 v205, 0xffff0000, v205
	v_pk_mul_f32 v[116:117], v[116:117], v[0:1] op_sel_hi:[1,0]
	v_pk_fma_f32 v[134:135], v[166:167], v[114:115], v[202:203]
	v_mul_f32_e32 v0, v123, v123
	v_mul_f32_e32 v114, v125, v125
	v_pk_fma_f32 v[116:117], v[168:169], v[116:117], v[204:205]
	v_fmac_f32_e32 v0, v122, v122
	v_fmac_f32_e32 v114, v124, v124
	v_add_f32_e32 v0, v0, v114
	v_mul_f32_e32 v114, v135, v135
	v_mul_f32_e32 v115, v117, v117
	v_fmac_f32_e32 v114, v134, v134
	v_fmac_f32_e32 v115, v116, v116
	v_add_f32_e32 v114, v114, v115
	v_add_f32_e32 v0, v0, v114
	v_add_f32_e32 v0, v208, v0
	v_mov_b32_e32 v202, v0
	s_nop 1
	v_permlane16_swap_b32_e32 v202, v0
	s_add_u32 s6, s14, 0x4000000
	s_addc_u32 s7, s15, 0
	v_lshl_add_u64 v[114:115], s[6:7], 0, v[224:225]
	v_lshl_add_u64 v[136:137], v[220:221], 1, v[114:115]
	s_waitcnt lgkmcnt(0)
	v_add_f32_e32 v0, v0, v202
	v_mov_b32_e32 v114, v0
	s_nop 1
	v_permlane32_swap_b32_e32 v114, v0
	v_cvt_pk_bf16_f32 v132, v132, v133
	v_cvt_pk_bf16_f32 v133, v206, v207
	global_store_dwordx4 v[136:137], v[130:133], off
	v_cvt_pk_bf16_f32 v122, v122, v123
	v_cvt_pk_bf16_f32 v123, v124, v125
	v_cvt_pk_bf16_f32 v124, v134, v135
	v_cvt_pk_bf16_f32 v125, v116, v117
	global_store_dwordx4 v[136:137], v[122:125], off offset:256
	s_and_saveexec_b64 s[14:15], s[40:41]
	s_cbranch_execz .LBB0_2847
	v_lshl_add_u32 v115, v240, 4, s28
	s_waitcnt lgkmcnt(0)
	v_add_f32_e32 v0, v0, v114
	ds_write_b32 v115, v0 offset:6144

.LBB0_2849:
	v_lshlrev_b32_e32 v122, 16, v198
	v_and_b32_e32 v123, 0xffff0000, v198
	v_lshlrev_b32_e32 v124, 16, v199
	v_and_b32_e32 v125, 0xffff0000, v199
	s_waitcnt lgkmcnt(0)
	v_pk_mul_f32 v[112:113], v[112:113], v[0:1] op_sel_hi:[1,0]
	v_pk_mul_f32 v[110:111], v[110:111], v[0:1] op_sel_hi:[1,0]
	v_lshlrev_b32_e32 v130, 16, v200
	v_and_b32_e32 v131, 0xffff0000, v200
	v_lshlrev_b32_e32 v132, 16, v201
	v_and_b32_e32 v133, 0xffff0000, v201
	v_pk_fma_f32 v[112:113], v[184:185], v[112:113], v[124:125]
	v_pk_fma_f32 v[110:111], v[182:183], v[110:111], v[122:123]
	v_pk_mul_f32 v[108:109], v[108:109], v[0:1] op_sel_hi:[1,0]
	v_pk_mul_f32 v[106:107], v[106:107], v[0:1] op_sel_hi:[1,0]
	v_pk_fma_f32 v[122:123], v[180:181], v[108:109], v[132:133]
	v_pk_fma_f32 v[108:109], v[178:179], v[106:107], v[130:131]
	v_mul_f32_e32 v106, v111, v111
	v_mul_f32_e32 v107, v113, v113
	v_fmac_f32_e32 v106, v110, v110
	v_fmac_f32_e32 v107, v112, v112
	v_add_f32_e32 v106, v106, v107
	v_mul_f32_e32 v107, v109, v109
	v_mul_f32_e32 v115, v123, v123
	v_fmac_f32_e32 v107, v108, v108
	v_fmac_f32_e32 v115, v122, v122
	v_add_f32_e32 v107, v107, v115
	v_add_f32_e32 v115, v106, v107
	v_cvt_pk_bf16_f32 v106, v110, v111
	v_cvt_pk_bf16_f32 v107, v112, v113
	v_lshlrev_b32_e32 v110, 16, v194
	v_and_b32_e32 v111, 0xffff0000, v194
	v_lshlrev_b32_e32 v112, 16, v195
	v_and_b32_e32 v113, 0xffff0000, v195
	v_pk_mul_f32 v[104:105], v[104:105], v[0:1] op_sel_hi:[1,0]
	v_pk_mul_f32 v[102:103], v[102:103], v[0:1] op_sel_hi:[1,0]
	v_cvt_pk_bf16_f32 v108, v108, v109
	v_cvt_pk_bf16_f32 v109, v122, v123
	v_lshlrev_b32_e32 v122, 16, v196
	v_and_b32_e32 v123, 0xffff0000, v196
	v_pk_fma_f32 v[104:105], v[172:173], v[104:105], v[112:113]
	v_pk_fma_f32 v[102:103], v[170:171], v[102:103], v[110:111]
	v_pk_mul_f32 v[98:99], v[98:99], v[0:1] op_sel_hi:[1,0]
	v_lshlrev_b32_e32 v124, 16, v197
	v_and_b32_e32 v125, 0xffff0000, v197
	v_pk_mul_f32 v[100:101], v[100:101], v[0:1] op_sel_hi:[1,0]
	v_pk_fma_f32 v[112:113], v[166:167], v[98:99], v[122:123]
	v_mul_f32_e32 v0, v103, v103
	v_mul_f32_e32 v98, v105, v105
	v_pk_fma_f32 v[110:111], v[168:169], v[100:101], v[124:125]
	v_fmac_f32_e32 v0, v102, v102
	v_fmac_f32_e32 v98, v104, v104
	v_add_f32_e32 v0, v0, v98
	v_mul_f32_e32 v98, v113, v113
	v_mul_f32_e32 v99, v111, v111
	v_fmac_f32_e32 v98, v112, v112
	v_fmac_f32_e32 v99, v110, v110
	v_add_f32_e32 v98, v98, v99
	v_add_f32_e32 v0, v0, v98
	v_add_f32_e32 v0, v115, v0
	v_mov_b32_e32 v101, v0
	s_nop 1
	v_permlane16_swap_b32_e32 v101, v0
	v_or_b32_e32 v114, 16, v240
	v_add_u32_e32 v116, s29, v114
	v_ashrrev_i32_e32 v117, 31, v116
	v_lshlrev_b64 v[116:117], 11, v[116:117]
	v_lshl_add_u64 v[98:99], s[6:7], 0, v[116:117]
	s_waitcnt lgkmcnt(0)
	v_add_f32_e32 v0, v0, v101
	v_lshl_add_u64 v[116:117], v[220:221], 1, v[98:99]
	v_mov_b32_e32 v98, v0
	s_nop 1
	v_permlane32_swap_b32_e32 v98, v0
	global_store_dwordx4 v[116:117], v[106:109], off
	v_cvt_pk_bf16_f32 v100, v102, v103
	v_cvt_pk_bf16_f32 v101, v104, v105
	v_cvt_pk_bf16_f32 v102, v112, v113
	v_cvt_pk_bf16_f32 v103, v110, v111
	global_store_dwordx4 v[116:117], v[100:103], off offset:256
	s_and_saveexec_b64 s[14:15], s[40:41]
	s_cbranch_execz .LBB0_2851
	v_lshl_add_u32 v99, v114, 4, s28
	s_waitcnt lgkmcnt(0)
	v_add_f32_e32 v0, v0, v98
	ds_write_b32 v99, v0 offset:6144

.LBB0_2853:
	v_lshlrev_b32_e32 v102, 16, v190
	v_and_b32_e32 v103, 0xffff0000, v190
	v_lshlrev_b32_e32 v104, 16, v191
	v_and_b32_e32 v105, 0xffff0000, v191
	s_waitcnt lgkmcnt(0)
	v_pk_mul_f32 v[96:97], v[96:97], v[0:1] op_sel_hi:[1,0]
	v_pk_mul_f32 v[94:95], v[94:95], v[0:1] op_sel_hi:[1,0]
	v_lshlrev_b32_e32 v106, 16, v192
	v_and_b32_e32 v107, 0xffff0000, v192
	v_lshlrev_b32_e32 v108, 16, v193
	v_and_b32_e32 v109, 0xffff0000, v193
	v_pk_fma_f32 v[96:97], v[184:185], v[96:97], v[104:105]
	v_pk_fma_f32 v[94:95], v[182:183], v[94:95], v[102:103]
	v_pk_mul_f32 v[92:93], v[92:93], v[0:1] op_sel_hi:[1,0]
	v_pk_mul_f32 v[90:91], v[90:91], v[0:1] op_sel_hi:[1,0]
	v_pk_fma_f32 v[102:103], v[180:181], v[92:93], v[108:109]
	v_pk_fma_f32 v[92:93], v[178:179], v[90:91], v[106:107]
	v_mul_f32_e32 v90, v95, v95
	v_mul_f32_e32 v91, v97, v97
	v_fmac_f32_e32 v90, v94, v94
	v_fmac_f32_e32 v91, v96, v96
	v_add_f32_e32 v90, v90, v91
	v_mul_f32_e32 v91, v93, v93
	v_mul_f32_e32 v99, v103, v103
	v_fmac_f32_e32 v91, v92, v92
	v_fmac_f32_e32 v99, v102, v102
	v_add_f32_e32 v91, v91, v99
	v_add_f32_e32 v99, v90, v91
	v_cvt_pk_bf16_f32 v90, v94, v95
	v_cvt_pk_bf16_f32 v91, v96, v97
	v_lshlrev_b32_e32 v94, 16, v186
	v_and_b32_e32 v95, 0xffff0000, v186
	v_lshlrev_b32_e32 v96, 16, v187
	v_and_b32_e32 v97, 0xffff0000, v187
	v_pk_mul_f32 v[88:89], v[88:89], v[0:1] op_sel_hi:[1,0]
	v_pk_mul_f32 v[86:87], v[86:87], v[0:1] op_sel_hi:[1,0]
	v_cvt_pk_bf16_f32 v92, v92, v93
	v_cvt_pk_bf16_f32 v93, v102, v103
	v_lshlrev_b32_e32 v102, 16, v188
	v_and_b32_e32 v103, 0xffff0000, v188
	v_pk_fma_f32 v[88:89], v[172:173], v[88:89], v[96:97]
	v_pk_fma_f32 v[86:87], v[170:171], v[86:87], v[94:95]
	v_pk_mul_f32 v[82:83], v[82:83], v[0:1] op_sel_hi:[1,0]
	v_lshlrev_b32_e32 v104, 16, v189
	v_and_b32_e32 v105, 0xffff0000, v189
	v_pk_mul_f32 v[84:85], v[84:85], v[0:1] op_sel_hi:[1,0]
	v_pk_fma_f32 v[96:97], v[166:167], v[82:83], v[102:103]
	v_mul_f32_e32 v0, v87, v87
	v_mul_f32_e32 v82, v89, v89
	v_pk_fma_f32 v[94:95], v[168:169], v[84:85], v[104:105]
	v_fmac_f32_e32 v0, v86, v86
	v_fmac_f32_e32 v82, v88, v88
	v_add_f32_e32 v0, v0, v82
	v_mul_f32_e32 v82, v97, v97
	v_mul_f32_e32 v83, v95, v95
	v_fmac_f32_e32 v82, v96, v96
	v_fmac_f32_e32 v83, v94, v94
	v_add_f32_e32 v82, v82, v83
	v_add_f32_e32 v0, v0, v82
	v_add_f32_e32 v0, v99, v0
	v_mov_b32_e32 v85, v0
	s_nop 1
	v_permlane16_swap_b32_e32 v85, v0
	v_or_b32_e32 v98, 32, v240
	v_add_u32_e32 v100, s29, v98
	v_ashrrev_i32_e32 v101, 31, v100
	v_lshlrev_b64 v[100:101], 11, v[100:101]
	v_lshl_add_u64 v[82:83], s[6:7], 0, v[100:101]
	s_waitcnt lgkmcnt(0)
	v_add_f32_e32 v0, v0, v85
	v_lshl_add_u64 v[100:101], v[220:221], 1, v[82:83]
	v_mov_b32_e32 v82, v0
	s_nop 1
	v_permlane32_swap_b32_e32 v82, v0
	global_store_dwordx4 v[100:101], v[90:93], off
	v_cvt_pk_bf16_f32 v84, v86, v87
	v_cvt_pk_bf16_f32 v85, v88, v89
	v_cvt_pk_bf16_f32 v86, v96, v97
	v_cvt_pk_bf16_f32 v87, v94, v95
	global_store_dwordx4 v[100:101], v[84:87], off offset:256
	s_and_saveexec_b64 s[14:15], s[40:41]
	s_cbranch_execz .LBB0_2855
	v_lshl_add_u32 v83, v98, 4, s28
	s_waitcnt lgkmcnt(0)
	v_add_f32_e32 v0, v0, v82
	ds_write_b32 v83, v0 offset:6144

.LBB0_2857:
	v_lshlrev_b32_e32 v86, 16, v174
	v_and_b32_e32 v87, 0xffff0000, v174
	v_lshlrev_b32_e32 v88, 16, v175
	v_and_b32_e32 v89, 0xffff0000, v175
	s_waitcnt lgkmcnt(0)
	v_pk_mul_f32 v[80:81], v[80:81], v[0:1] op_sel_hi:[1,0]
	v_pk_mul_f32 v[78:79], v[78:79], v[0:1] op_sel_hi:[1,0]
	v_lshlrev_b32_e32 v90, 16, v176
	v_and_b32_e32 v91, 0xffff0000, v176
	v_lshlrev_b32_e32 v92, 16, v177
	v_and_b32_e32 v93, 0xffff0000, v177
	v_pk_fma_f32 v[80:81], v[184:185], v[80:81], v[88:89]
	v_pk_fma_f32 v[78:79], v[182:183], v[78:79], v[86:87]
	v_pk_mul_f32 v[76:77], v[76:77], v[0:1] op_sel_hi:[1,0]
	v_pk_mul_f32 v[74:75], v[74:75], v[0:1] op_sel_hi:[1,0]
	v_pk_fma_f32 v[86:87], v[180:181], v[76:77], v[92:93]
	v_pk_fma_f32 v[76:77], v[178:179], v[74:75], v[90:91]
	v_mul_f32_e32 v74, v79, v79
	v_mul_f32_e32 v75, v81, v81
	v_fmac_f32_e32 v74, v78, v78
	v_fmac_f32_e32 v75, v80, v80
	v_add_f32_e32 v74, v74, v75
	v_mul_f32_e32 v75, v77, v77
	v_mul_f32_e32 v83, v87, v87
	v_fmac_f32_e32 v75, v76, v76
	v_fmac_f32_e32 v83, v86, v86
	v_add_f32_e32 v75, v75, v83
	v_add_f32_e32 v83, v74, v75
	v_cvt_pk_bf16_f32 v74, v78, v79
	v_cvt_pk_bf16_f32 v75, v80, v81
	v_lshlrev_b32_e32 v78, 16, v162
	v_and_b32_e32 v79, 0xffff0000, v162
	v_lshlrev_b32_e32 v80, 16, v163
	v_and_b32_e32 v81, 0xffff0000, v163
	v_pk_mul_f32 v[72:73], v[72:73], v[0:1] op_sel_hi:[1,0]
	v_pk_mul_f32 v[70:71], v[70:71], v[0:1] op_sel_hi:[1,0]
	v_cvt_pk_bf16_f32 v76, v76, v77
	v_cvt_pk_bf16_f32 v77, v86, v87
	v_lshlrev_b32_e32 v86, 16, v164
	v_and_b32_e32 v87, 0xffff0000, v164
	v_pk_fma_f32 v[72:73], v[172:173], v[72:73], v[80:81]
	v_pk_fma_f32 v[70:71], v[170:171], v[70:71], v[78:79]
	v_pk_mul_f32 v[66:67], v[66:67], v[0:1] op_sel_hi:[1,0]
	v_lshlrev_b32_e32 v88, 16, v165
	v_and_b32_e32 v89, 0xffff0000, v165
	v_pk_mul_f32 v[68:69], v[68:69], v[0:1] op_sel_hi:[1,0]
	v_pk_fma_f32 v[80:81], v[166:167], v[66:67], v[86:87]
	v_mul_f32_e32 v0, v71, v71
	v_mul_f32_e32 v66, v73, v73
	v_pk_fma_f32 v[78:79], v[168:169], v[68:69], v[88:89]
	v_fmac_f32_e32 v0, v70, v70
	v_fmac_f32_e32 v66, v72, v72
	v_add_f32_e32 v0, v0, v66
	v_mul_f32_e32 v66, v81, v81
	v_mul_f32_e32 v67, v79, v79
	v_fmac_f32_e32 v66, v80, v80
	v_fmac_f32_e32 v67, v78, v78
	v_add_f32_e32 v66, v66, v67
	v_add_f32_e32 v0, v0, v66
	v_add_f32_e32 v0, v83, v0
	v_mov_b32_e32 v69, v0
	s_nop 1
	v_permlane16_swap_b32_e32 v69, v0
	v_or_b32_e32 v82, 48, v240
	v_add_u32_e32 v84, s29, v82
	v_ashrrev_i32_e32 v85, 31, v84
	v_lshlrev_b64 v[84:85], 11, v[84:85]
	v_lshl_add_u64 v[66:67], s[6:7], 0, v[84:85]
	s_waitcnt lgkmcnt(0)
	v_add_f32_e32 v0, v0, v69
	v_lshl_add_u64 v[84:85], v[220:221], 1, v[66:67]
	v_mov_b32_e32 v66, v0
	s_nop 1
	v_permlane32_swap_b32_e32 v66, v0
	global_store_dwordx4 v[84:85], v[74:77], off
	v_cvt_pk_bf16_f32 v68, v70, v71
	v_cvt_pk_bf16_f32 v69, v72, v73
	v_cvt_pk_bf16_f32 v70, v80, v81
	v_cvt_pk_bf16_f32 v71, v78, v79
	global_store_dwordx4 v[84:85], v[68:71], off offset:256
	s_and_saveexec_b64 s[14:15], s[40:41]
	s_cbranch_execz .LBB0_2859
	v_lshl_add_u32 v67, v82, 4, s28
	s_waitcnt lgkmcnt(0)
	v_add_f32_e32 v0, v0, v66
	ds_write_b32 v67, v0 offset:6144

.LBB0_2861:
	v_lshlrev_b32_e32 v70, 16, v158
	v_and_b32_e32 v71, 0xffff0000, v158
	v_lshlrev_b32_e32 v72, 16, v159
	v_and_b32_e32 v73, 0xffff0000, v159
	s_waitcnt lgkmcnt(0)
	v_pk_mul_f32 v[64:65], v[64:65], v[0:1] op_sel_hi:[1,0]
	v_pk_mul_f32 v[62:63], v[62:63], v[0:1] op_sel_hi:[1,0]
	v_lshlrev_b32_e32 v74, 16, v160
	v_and_b32_e32 v75, 0xffff0000, v160
	v_lshlrev_b32_e32 v76, 16, v161
	v_and_b32_e32 v77, 0xffff0000, v161
	v_pk_fma_f32 v[64:65], v[184:185], v[64:65], v[72:73]
	v_pk_fma_f32 v[62:63], v[182:183], v[62:63], v[70:71]
	v_pk_mul_f32 v[60:61], v[60:61], v[0:1] op_sel_hi:[1,0]
	v_pk_mul_f32 v[58:59], v[58:59], v[0:1] op_sel_hi:[1,0]
	v_pk_fma_f32 v[70:71], v[180:181], v[60:61], v[76:77]
	v_pk_fma_f32 v[60:61], v[178:179], v[58:59], v[74:75]
	v_mul_f32_e32 v58, v63, v63
	v_mul_f32_e32 v59, v65, v65
	v_fmac_f32_e32 v58, v62, v62
	v_fmac_f32_e32 v59, v64, v64
	v_add_f32_e32 v58, v58, v59
	v_mul_f32_e32 v59, v61, v61
	v_mul_f32_e32 v67, v71, v71
	v_fmac_f32_e32 v59, v60, v60
	v_fmac_f32_e32 v67, v70, v70
	v_add_f32_e32 v59, v59, v67
	v_add_f32_e32 v67, v58, v59
	v_cvt_pk_bf16_f32 v58, v62, v63
	v_cvt_pk_bf16_f32 v59, v64, v65
	v_lshlrev_b32_e32 v62, 16, v154
	v_and_b32_e32 v63, 0xffff0000, v154
	v_lshlrev_b32_e32 v64, 16, v155
	v_and_b32_e32 v65, 0xffff0000, v155
	v_pk_mul_f32 v[56:57], v[56:57], v[0:1] op_sel_hi:[1,0]
	v_pk_mul_f32 v[54:55], v[54:55], v[0:1] op_sel_hi:[1,0]
	v_cvt_pk_bf16_f32 v60, v60, v61
	v_cvt_pk_bf16_f32 v61, v70, v71
	v_lshlrev_b32_e32 v70, 16, v156
	v_and_b32_e32 v71, 0xffff0000, v156
	v_pk_fma_f32 v[56:57], v[172:173], v[56:57], v[64:65]
	v_pk_fma_f32 v[54:55], v[170:171], v[54:55], v[62:63]
	v_pk_mul_f32 v[50:51], v[50:51], v[0:1] op_sel_hi:[1,0]
	v_lshlrev_b32_e32 v72, 16, v157
	v_and_b32_e32 v73, 0xffff0000, v157
	v_pk_mul_f32 v[52:53], v[52:53], v[0:1] op_sel_hi:[1,0]
	v_pk_fma_f32 v[64:65], v[166:167], v[50:51], v[70:71]
	v_mul_f32_e32 v0, v55, v55
	v_mul_f32_e32 v50, v57, v57
	v_pk_fma_f32 v[62:63], v[168:169], v[52:53], v[72:73]
	v_fmac_f32_e32 v0, v54, v54
	v_fmac_f32_e32 v50, v56, v56
	v_add_f32_e32 v0, v0, v50
	v_mul_f32_e32 v50, v65, v65
	v_mul_f32_e32 v51, v63, v63
	v_fmac_f32_e32 v50, v64, v64
	v_fmac_f32_e32 v51, v62, v62
	v_add_f32_e32 v50, v50, v51
	v_add_f32_e32 v0, v0, v50
	v_add_f32_e32 v0, v67, v0
	v_mov_b32_e32 v53, v0
	s_nop 1
	v_permlane16_swap_b32_e32 v53, v0
	v_add_u32_e32 v66, 0x80, v240
	v_add_u32_e32 v68, s29, v66
	v_ashrrev_i32_e32 v69, 31, v68
	v_lshlrev_b64 v[68:69], 11, v[68:69]
	v_lshl_add_u64 v[50:51], s[6:7], 0, v[68:69]
	s_waitcnt lgkmcnt(0)
	v_add_f32_e32 v0, v0, v53
	v_lshl_add_u64 v[68:69], v[220:221], 1, v[50:51]
	v_mov_b32_e32 v50, v0
	s_nop 1
	v_permlane32_swap_b32_e32 v50, v0
	global_store_dwordx4 v[68:69], v[58:61], off
	v_cvt_pk_bf16_f32 v52, v54, v55
	v_cvt_pk_bf16_f32 v53, v56, v57
	v_cvt_pk_bf16_f32 v54, v64, v65
	v_cvt_pk_bf16_f32 v55, v62, v63
	global_store_dwordx4 v[68:69], v[52:55], off offset:256
	s_and_saveexec_b64 s[14:15], s[40:41]
	s_cbranch_execz .LBB0_2863
	v_lshl_add_u32 v51, v66, 4, s28
	s_waitcnt lgkmcnt(0)
	v_add_f32_e32 v0, v0, v50
	ds_write_b32 v51, v0 offset:6144

.LBB0_2865:
	v_lshlrev_b32_e32 v54, 16, v150
	v_and_b32_e32 v55, 0xffff0000, v150
	v_lshlrev_b32_e32 v56, 16, v151
	v_and_b32_e32 v57, 0xffff0000, v151
	s_waitcnt lgkmcnt(0)
	v_pk_mul_f32 v[48:49], v[48:49], v[0:1] op_sel_hi:[1,0]
	v_pk_mul_f32 v[46:47], v[46:47], v[0:1] op_sel_hi:[1,0]
	v_lshlrev_b32_e32 v58, 16, v152
	v_and_b32_e32 v59, 0xffff0000, v152
	v_lshlrev_b32_e32 v60, 16, v153
	v_and_b32_e32 v61, 0xffff0000, v153
	v_pk_fma_f32 v[48:49], v[184:185], v[48:49], v[56:57]
	v_pk_fma_f32 v[46:47], v[182:183], v[46:47], v[54:55]
	v_pk_mul_f32 v[44:45], v[44:45], v[0:1] op_sel_hi:[1,0]
	v_pk_mul_f32 v[42:43], v[42:43], v[0:1] op_sel_hi:[1,0]
	v_pk_fma_f32 v[54:55], v[180:181], v[44:45], v[60:61]
	v_pk_fma_f32 v[44:45], v[178:179], v[42:43], v[58:59]
	v_mul_f32_e32 v42, v47, v47
	v_mul_f32_e32 v43, v49, v49
	v_fmac_f32_e32 v42, v46, v46
	v_fmac_f32_e32 v43, v48, v48
	v_add_f32_e32 v42, v42, v43
	v_mul_f32_e32 v43, v45, v45
	v_mul_f32_e32 v51, v55, v55
	v_fmac_f32_e32 v43, v44, v44
	v_fmac_f32_e32 v51, v54, v54
	v_add_f32_e32 v43, v43, v51
	v_add_f32_e32 v51, v42, v43
	v_cvt_pk_bf16_f32 v42, v46, v47
	v_cvt_pk_bf16_f32 v43, v48, v49
	v_lshlrev_b32_e32 v46, 16, v146
	v_and_b32_e32 v47, 0xffff0000, v146
	v_lshlrev_b32_e32 v48, 16, v147
	v_and_b32_e32 v49, 0xffff0000, v147
	v_pk_mul_f32 v[40:41], v[40:41], v[0:1] op_sel_hi:[1,0]
	v_pk_mul_f32 v[38:39], v[38:39], v[0:1] op_sel_hi:[1,0]
	v_cvt_pk_bf16_f32 v44, v44, v45
	v_cvt_pk_bf16_f32 v45, v54, v55
	v_lshlrev_b32_e32 v54, 16, v148
	v_and_b32_e32 v55, 0xffff0000, v148
	v_pk_fma_f32 v[40:41], v[172:173], v[40:41], v[48:49]
	v_pk_fma_f32 v[38:39], v[170:171], v[38:39], v[46:47]
	v_pk_mul_f32 v[34:35], v[34:35], v[0:1] op_sel_hi:[1,0]
	v_lshlrev_b32_e32 v56, 16, v149
	v_and_b32_e32 v57, 0xffff0000, v149
	v_pk_mul_f32 v[36:37], v[36:37], v[0:1] op_sel_hi:[1,0]
	v_pk_fma_f32 v[48:49], v[166:167], v[34:35], v[54:55]
	v_mul_f32_e32 v0, v39, v39
	v_mul_f32_e32 v34, v41, v41
	v_pk_fma_f32 v[46:47], v[168:169], v[36:37], v[56:57]
	v_fmac_f32_e32 v0, v38, v38
	v_fmac_f32_e32 v34, v40, v40
	v_add_f32_e32 v0, v0, v34
	v_mul_f32_e32 v34, v49, v49
	v_mul_f32_e32 v35, v47, v47
	v_fmac_f32_e32 v34, v48, v48
	v_fmac_f32_e32 v35, v46, v46
	v_add_f32_e32 v34, v34, v35
	v_add_f32_e32 v0, v0, v34
	v_add_f32_e32 v0, v51, v0
	v_mov_b32_e32 v37, v0
	s_nop 1
	v_permlane16_swap_b32_e32 v37, v0
	v_add_u32_e32 v50, 0x90, v240
	v_add_u32_e32 v52, s29, v50
	v_ashrrev_i32_e32 v53, 31, v52
	v_lshlrev_b64 v[52:53], 11, v[52:53]
	v_lshl_add_u64 v[34:35], s[6:7], 0, v[52:53]
	s_waitcnt lgkmcnt(0)
	v_add_f32_e32 v0, v0, v37
	v_lshl_add_u64 v[52:53], v[220:221], 1, v[34:35]
	v_mov_b32_e32 v34, v0
	s_nop 1
	v_permlane32_swap_b32_e32 v34, v0
	global_store_dwordx4 v[52:53], v[42:45], off
	v_cvt_pk_bf16_f32 v36, v38, v39
	v_cvt_pk_bf16_f32 v37, v40, v41
	v_cvt_pk_bf16_f32 v38, v48, v49
	v_cvt_pk_bf16_f32 v39, v46, v47
	global_store_dwordx4 v[52:53], v[36:39], off offset:256
	s_and_saveexec_b64 s[14:15], s[40:41]
	s_cbranch_execz .LBB0_2867
	v_lshl_add_u32 v35, v50, 4, s28
	s_waitcnt lgkmcnt(0)
	v_add_f32_e32 v0, v0, v34
	ds_write_b32 v35, v0 offset:6144

.LBB0_2869:
	v_lshlrev_b32_e32 v38, 16, v142
	v_and_b32_e32 v39, 0xffff0000, v142
	v_lshlrev_b32_e32 v40, 16, v143
	v_and_b32_e32 v41, 0xffff0000, v143
	s_waitcnt lgkmcnt(0)
	v_pk_mul_f32 v[32:33], v[32:33], v[0:1] op_sel_hi:[1,0]
	v_pk_mul_f32 v[30:31], v[30:31], v[0:1] op_sel_hi:[1,0]
	v_lshlrev_b32_e32 v42, 16, v144
	v_and_b32_e32 v43, 0xffff0000, v144
	v_lshlrev_b32_e32 v44, 16, v145
	v_and_b32_e32 v45, 0xffff0000, v145
	v_pk_fma_f32 v[32:33], v[184:185], v[32:33], v[40:41]
	v_pk_fma_f32 v[30:31], v[182:183], v[30:31], v[38:39]
	v_pk_mul_f32 v[28:29], v[28:29], v[0:1] op_sel_hi:[1,0]
	v_pk_mul_f32 v[26:27], v[26:27], v[0:1] op_sel_hi:[1,0]
	v_pk_fma_f32 v[38:39], v[180:181], v[28:29], v[44:45]
	v_pk_fma_f32 v[28:29], v[178:179], v[26:27], v[42:43]
	v_mul_f32_e32 v26, v31, v31
	v_mul_f32_e32 v27, v33, v33
	v_fmac_f32_e32 v26, v30, v30
	v_fmac_f32_e32 v27, v32, v32
	v_add_f32_e32 v26, v26, v27
	v_mul_f32_e32 v27, v29, v29
	v_mul_f32_e32 v35, v39, v39
	v_fmac_f32_e32 v27, v28, v28
	v_fmac_f32_e32 v35, v38, v38
	v_add_f32_e32 v27, v27, v35
	v_add_f32_e32 v35, v26, v27
	v_cvt_pk_bf16_f32 v26, v30, v31
	v_cvt_pk_bf16_f32 v27, v32, v33
	v_lshlrev_b32_e32 v30, 16, v138
	v_and_b32_e32 v31, 0xffff0000, v138
	v_lshlrev_b32_e32 v32, 16, v139
	v_and_b32_e32 v33, 0xffff0000, v139
	v_pk_mul_f32 v[24:25], v[24:25], v[0:1] op_sel_hi:[1,0]
	v_pk_mul_f32 v[22:23], v[22:23], v[0:1] op_sel_hi:[1,0]
	v_cvt_pk_bf16_f32 v28, v28, v29
	v_cvt_pk_bf16_f32 v29, v38, v39
	v_lshlrev_b32_e32 v38, 16, v140
	v_and_b32_e32 v39, 0xffff0000, v140
	v_pk_fma_f32 v[24:25], v[172:173], v[24:25], v[32:33]
	v_pk_fma_f32 v[22:23], v[170:171], v[22:23], v[30:31]
	v_pk_mul_f32 v[18:19], v[18:19], v[0:1] op_sel_hi:[1,0]
	v_lshlrev_b32_e32 v40, 16, v141
	v_and_b32_e32 v41, 0xffff0000, v141
	v_pk_mul_f32 v[20:21], v[20:21], v[0:1] op_sel_hi:[1,0]
	v_pk_fma_f32 v[32:33], v[166:167], v[18:19], v[38:39]
	v_mul_f32_e32 v0, v23, v23
	v_mul_f32_e32 v18, v25, v25
	v_pk_fma_f32 v[30:31], v[168:169], v[20:21], v[40:41]
	v_fmac_f32_e32 v0, v22, v22
	v_fmac_f32_e32 v18, v24, v24
	v_add_f32_e32 v0, v0, v18
	v_mul_f32_e32 v18, v33, v33
	v_mul_f32_e32 v19, v31, v31
	v_fmac_f32_e32 v18, v32, v32
	v_fmac_f32_e32 v19, v30, v30
	v_add_f32_e32 v18, v18, v19
	v_add_f32_e32 v0, v0, v18
	v_add_f32_e32 v0, v35, v0
	v_mov_b32_e32 v21, v0
	s_nop 1
	v_permlane16_swap_b32_e32 v21, v0
	v_add_u32_e32 v34, 0xa0, v240
	v_add_u32_e32 v36, s29, v34
	v_ashrrev_i32_e32 v37, 31, v36
	v_lshlrev_b64 v[36:37], 11, v[36:37]
	v_lshl_add_u64 v[18:19], s[6:7], 0, v[36:37]
	s_waitcnt lgkmcnt(0)
	v_add_f32_e32 v0, v0, v21
	v_lshl_add_u64 v[36:37], v[220:221], 1, v[18:19]
	v_mov_b32_e32 v18, v0
	s_nop 1
	v_permlane32_swap_b32_e32 v18, v0
	global_store_dwordx4 v[36:37], v[26:29], off
	v_cvt_pk_bf16_f32 v20, v22, v23
	v_cvt_pk_bf16_f32 v21, v24, v25
	v_cvt_pk_bf16_f32 v22, v32, v33
	v_cvt_pk_bf16_f32 v23, v30, v31
	global_store_dwordx4 v[36:37], v[20:23], off offset:256
	s_and_saveexec_b64 s[14:15], s[40:41]
	s_cbranch_execz .LBB0_2871
	v_lshl_add_u32 v19, v34, 4, s28
	s_waitcnt lgkmcnt(0)
	v_add_f32_e32 v0, v0, v18
	ds_write_b32 v19, v0 offset:6144

.LBB0_2898:
	s_lshl_b32 s4, s53, 5
	s_lshl_b32 s24, s20, 8
	v_lshrrev_b32_e32 v122, 1, v0
	s_or_b32 s4, s24, s4
	v_and_or_b32 v220, v122, 24, s4
	s_lshl_b32 s27, s52, 8
	v_add_u32_e32 v222, s27, v224
	v_ashrrev_i32_e32 v221, 31, v220
	v_lshl_add_u64 v[122:123], v[220:221], 1, s[22:23]
	s_mov_b64 s[22:23], 0x1bc00000
	v_ashrrev_i32_e32 v223, 31, v222
	v_lshl_add_u64 v[122:123], v[122:123], 0, s[22:23]
	v_lshlrev_b64 v[124:125], 11, v[222:223]
	v_lshl_add_u64 v[124:125], v[122:123], 0, v[124:125]
	s_barrier
	global_load_dwordx4 v[206:209], v[124:125], off
	global_load_dwordx4 v[202:205], v[124:125], off offset:256
	v_or_b32_e32 v124, 16, v222
	v_ashrrev_i32_e32 v125, 31, v124
	v_lshlrev_b64 v[124:125], 11, v[124:125]
	v_lshl_add_u64 v[124:125], v[122:123], 0, v[124:125]
	global_load_dwordx4 v[198:201], v[124:125], off
	global_load_dwordx4 v[194:197], v[124:125], off offset:256
	v_or_b32_e32 v124, 32, v222
	v_ashrrev_i32_e32 v125, 31, v124
	v_lshlrev_b64 v[124:125], 11, v[124:125]
	v_lshl_add_u64 v[124:125], v[122:123], 0, v[124:125]
	global_load_dwordx4 v[190:193], v[124:125], off
	global_load_dwordx4 v[186:189], v[124:125], off offset:256
	v_or_b32_e32 v124, 48, v222
	v_ashrrev_i32_e32 v125, 31, v124
	v_lshlrev_b64 v[124:125], 11, v[124:125]
	v_lshl_add_u64 v[124:125], v[122:123], 0, v[124:125]
	global_load_dwordx4 v[174:177], v[124:125], off
	global_load_dwordx4 v[162:165], v[124:125], off offset:256
	v_add_u32_e32 v124, 0x80, v222
	v_ashrrev_i32_e32 v125, 31, v124
	v_lshlrev_b64 v[124:125], 11, v[124:125]
	v_lshl_add_u64 v[124:125], v[122:123], 0, v[124:125]
	global_load_dwordx4 v[158:161], v[124:125], off
	global_load_dwordx4 v[154:157], v[124:125], off offset:256
	v_add_u32_e32 v124, 0x90, v222
	v_ashrrev_i32_e32 v125, 31, v124
	v_lshlrev_b64 v[124:125], 11, v[124:125]
	v_lshl_add_u64 v[124:125], v[122:123], 0, v[124:125]
	global_load_dwordx4 v[150:153], v[124:125], off
	global_load_dwordx4 v[146:149], v[124:125], off offset:256
	v_add_u32_e32 v124, 0xa0, v222
	v_ashrrev_i32_e32 v125, 31, v124
	v_lshlrev_b64 v[124:125], 11, v[124:125]
	v_lshl_add_u64 v[124:125], v[122:123], 0, v[124:125]
	global_load_dwordx4 v[142:145], v[124:125], off
	global_load_dwordx4 v[138:141], v[124:125], off offset:256
	v_add_u32_e32 v124, 0xb0, v222
	v_ashrrev_i32_e32 v125, 31, v124
	v_lshlrev_b64 v[124:125], 11, v[124:125]
	v_lshl_add_u64 v[122:123], v[122:123], 0, v[124:125]
	global_load_dwordx4 v[126:129], v[122:123], off
	s_nop 0
	global_load_dwordx4 v[122:125], v[122:123], off offset:256
	v_and_b32_e32 v168, 64, v231
	v_xor_b32_e32 v167, 16, v231
	v_add_u32_e32 v168, 64, v168
	v_cmp_lt_i32_e32 vcc, v167, v168
	v_mul_f32_e32 v169, v137, v137
	v_fmac_f32_e32 v169, v136, v136
	v_cndmask_b32_e32 v167, v231, v167, vcc
	v_lshlrev_b32_e32 v225, 2, v167
	v_mul_f32_e32 v167, v135, v135
	v_fmac_f32_e32 v167, v134, v134
	v_add_f32_e32 v167, v167, v169
	v_mul_f32_e32 v169, v131, v131
	v_mul_f32_e32 v170, v133, v133
	v_fmac_f32_e32 v169, v130, v130
	v_fmac_f32_e32 v170, v132, v132
	v_add_f32_e32 v169, v169, v170
	v_add_f32_e32 v167, v169, v167
	v_mul_f32_e32 v169, v119, v119
	v_mul_f32_e32 v170, v121, v121
	v_fmac_f32_e32 v169, v118, v118
	v_fmac_f32_e32 v170, v120, v120
	v_add_f32_e32 v169, v169, v170
	v_add_f32_e32 v167, v169, v167
	v_mul_f32_e32 v169, v115, v115
	v_mul_f32_e32 v170, v117, v117
	v_fmac_f32_e32 v169, v114, v114
	v_fmac_f32_e32 v170, v116, v116
	v_add_f32_e32 v169, v169, v170
	v_add_f32_e32 v167, v169, v167
	v_mov_b32_e32 v169, v167
	s_nop 1
	v_permlane16_swap_b32_e32 v169, v167
	v_xor_b32_e32 v170, 32, v231
	v_cmp_lt_i32_e32 vcc, v170, v168
	s_lshl_b32 s4, s53, 2
	s_add_i32 s26, s4, 0
	v_cndmask_b32_e32 v168, v231, v170, vcc
	v_lshlrev_b32_e32 v240, 2, v168
	s_waitcnt lgkmcnt(0)
	v_add_f32_e32 v167, v167, v169
	v_mov_b32_e32 v169, v167
	s_nop 1
	v_permlane32_swap_b32_e32 v169, v167
	v_and_b32_e32 v168, 63, v0
	v_cmp_gt_u32_e64 s[40:41], 16, v168
	s_and_saveexec_b64 s[22:23], s[40:41]
	v_readlane_b32 s64, v252, 3
	v_readlane_b32 s65, v255, 10
	v_readlane_b32 s68, v255, 11
	v_readlane_b32 s70, v255, 14
	v_readlane_b32 s71, v255, 15
	s_cbranch_execz .LBB0_2900
	s_lshl_b32 s4, s49, 10
	s_add_i32 s4, s26, s4
	s_waitcnt lgkmcnt(0)
	v_add_f32_e32 v167, v167, v169
	v_lshl_add_u32 v169, v166, 4, s4
	ds_write_b32 v169, v167
.LBB0_2900:
	s_or_b64 exec, exec, s[22:23]
	v_mul_f32_e32 v167, v111, v111
	s_waitcnt lgkmcnt(0)
	v_mul_f32_e32 v169, v113, v113
	v_fmac_f32_e32 v167, v110, v110
	v_fmac_f32_e32 v169, v112, v112
	v_add_f32_e32 v167, v167, v169
	v_mul_f32_e32 v169, v107, v107
	v_mul_f32_e32 v170, v109, v109
	v_fmac_f32_e32 v169, v106, v106
	v_fmac_f32_e32 v170, v108, v108
	v_add_f32_e32 v169, v169, v170
	v_add_f32_e32 v167, v169, v167
	v_mul_f32_e32 v169, v103, v103
	v_mul_f32_e32 v170, v105, v105
	v_fmac_f32_e32 v169, v102, v102
	v_fmac_f32_e32 v170, v104, v104
	v_add_f32_e32 v169, v169, v170
	v_add_f32_e32 v167, v169, v167
	v_mul_f32_e32 v169, v99, v99
	v_mul_f32_e32 v170, v101, v101
	v_fmac_f32_e32 v169, v98, v98
	v_fmac_f32_e32 v170, v100, v100
	v_add_f32_e32 v169, v169, v170
	v_add_f32_e32 v167, v169, v167
	v_mov_b32_e32 v169, v167
	s_nop 1
	v_permlane16_swap_b32_e32 v169, v167
	s_waitcnt lgkmcnt(0)
	v_add_f32_e32 v167, v167, v169
	v_mov_b32_e32 v169, v167
	s_nop 1
	v_permlane32_swap_b32_e32 v169, v167
	s_and_saveexec_b64 s[22:23], s[40:41]
	s_cbranch_execz .LBB0_2902
	s_lshl_b32 s4, s49, 10
	s_add_i32 s4, s26, s4
	s_waitcnt lgkmcnt(0)
	v_add_f32_e32 v167, v167, v169
	v_lshl_add_u32 v169, v166, 4, s4
	ds_write_b32 v169, v167 offset:256
.LBB0_2902:
	s_or_b64 exec, exec, s[22:23]
	v_mul_f32_e32 v167, v95, v95
	s_waitcnt lgkmcnt(0)
	v_mul_f32_e32 v169, v97, v97
	v_fmac_f32_e32 v167, v94, v94
	v_fmac_f32_e32 v169, v96, v96
	v_add_f32_e32 v167, v167, v169
	v_mul_f32_e32 v169, v91, v91
	v_mul_f32_e32 v170, v93, v93
	v_fmac_f32_e32 v169, v90, v90
	v_fmac_f32_e32 v170, v92, v92
	v_add_f32_e32 v169, v169, v170
	v_add_f32_e32 v167, v169, v167
	v_mul_f32_e32 v169, v87, v87
	v_mul_f32_e32 v170, v89, v89
	v_fmac_f32_e32 v169, v86, v86
	v_fmac_f32_e32 v170, v88, v88
	v_add_f32_e32 v169, v169, v170
	v_add_f32_e32 v167, v169, v167
	v_mul_f32_e32 v169, v83, v83
	v_mul_f32_e32 v170, v85, v85
	v_fmac_f32_e32 v169, v82, v82
	v_fmac_f32_e32 v170, v84, v84
	v_add_f32_e32 v169, v169, v170
	v_add_f32_e32 v167, v169, v167
	v_mov_b32_e32 v169, v167
	s_nop 1
	v_permlane16_swap_b32_e32 v169, v167
	s_waitcnt lgkmcnt(0)
	v_add_f32_e32 v167, v167, v169
	v_mov_b32_e32 v169, v167
	s_nop 1
	v_permlane32_swap_b32_e32 v169, v167
	s_and_saveexec_b64 s[22:23], s[40:41]
	s_cbranch_execz .LBB0_2904
	s_lshl_b32 s4, s49, 10
	s_add_i32 s4, s26, s4
	s_waitcnt lgkmcnt(0)
	v_add_f32_e32 v167, v167, v169
	v_lshl_add_u32 v169, v166, 4, s4
	ds_write_b32 v169, v167 offset:512
.LBB0_2904:
	s_or_b64 exec, exec, s[22:23]
	v_mul_f32_e32 v167, v79, v79
	s_waitcnt lgkmcnt(0)
	v_mul_f32_e32 v169, v81, v81
	v_fmac_f32_e32 v167, v78, v78
	v_fmac_f32_e32 v169, v80, v80
	v_add_f32_e32 v167, v167, v169
	v_mul_f32_e32 v169, v75, v75
	v_mul_f32_e32 v170, v77, v77
	v_fmac_f32_e32 v169, v74, v74
	v_fmac_f32_e32 v170, v76, v76
	v_add_f32_e32 v169, v169, v170
	v_add_f32_e32 v167, v169, v167
	v_mul_f32_e32 v169, v71, v71
	v_mul_f32_e32 v170, v73, v73
	v_fmac_f32_e32 v169, v70, v70
	v_fmac_f32_e32 v170, v72, v72
	v_add_f32_e32 v169, v169, v170
	v_add_f32_e32 v167, v169, v167
	v_mul_f32_e32 v169, v67, v67
	v_mul_f32_e32 v170, v69, v69
	v_fmac_f32_e32 v169, v66, v66
	v_fmac_f32_e32 v170, v68, v68
	v_add_f32_e32 v169, v169, v170
	v_add_f32_e32 v167, v169, v167
	v_mov_b32_e32 v169, v167
	s_nop 1
	v_permlane16_swap_b32_e32 v169, v167
	s_waitcnt lgkmcnt(0)
	v_add_f32_e32 v167, v167, v169
	v_mov_b32_e32 v169, v167
	s_nop 1
	v_permlane32_swap_b32_e32 v169, v167
	s_and_saveexec_b64 s[22:23], s[40:41]
	s_cbranch_execz .LBB0_2906
	s_lshl_b32 s4, s49, 10
	s_add_i32 s4, s26, s4
	s_waitcnt lgkmcnt(0)
	v_add_f32_e32 v167, v167, v169
	v_lshl_add_u32 v169, v166, 4, s4
	ds_write_b32 v169, v167 offset:768
.LBB0_2906:
	s_or_b64 exec, exec, s[22:23]
	v_mul_f32_e32 v167, v63, v63
	s_waitcnt lgkmcnt(0)
	v_mul_f32_e32 v169, v65, v65
	v_fmac_f32_e32 v167, v62, v62
	v_fmac_f32_e32 v169, v64, v64
	v_add_f32_e32 v167, v167, v169
	v_mul_f32_e32 v169, v59, v59
	v_mul_f32_e32 v170, v61, v61
	v_fmac_f32_e32 v169, v58, v58
	v_fmac_f32_e32 v170, v60, v60
	v_add_f32_e32 v169, v169, v170
	v_add_f32_e32 v167, v169, v167
	v_mul_f32_e32 v169, v55, v55
	v_mul_f32_e32 v170, v57, v57
	v_fmac_f32_e32 v169, v54, v54
	v_fmac_f32_e32 v170, v56, v56
	v_add_f32_e32 v169, v169, v170
	v_add_f32_e32 v167, v169, v167
	v_mul_f32_e32 v169, v51, v51
	v_mul_f32_e32 v170, v53, v53
	v_fmac_f32_e32 v169, v50, v50
	v_fmac_f32_e32 v170, v52, v52
	v_add_f32_e32 v169, v169, v170
	v_add_f32_e32 v167, v169, v167
	v_mov_b32_e32 v169, v167
	s_nop 1
	v_permlane16_swap_b32_e32 v169, v167
	s_waitcnt lgkmcnt(0)
	v_add_f32_e32 v167, v167, v169
	v_mov_b32_e32 v169, v167
	s_nop 1
	v_permlane32_swap_b32_e32 v169, v167
	s_and_saveexec_b64 s[22:23], s[40:41]
	s_cbranch_execz .LBB0_2908
	s_lshl_b32 s4, s49, 10
	s_add_i32 s4, s26, s4
	s_waitcnt lgkmcnt(0)
	v_add_f32_e32 v167, v167, v169
	v_lshl_add_u32 v169, v166, 4, s4
	ds_write_b32 v169, v167 offset:2048
.LBB0_2908:
	s_or_b64 exec, exec, s[22:23]
	v_mul_f32_e32 v167, v47, v47
	s_waitcnt lgkmcnt(0)
	v_mul_f32_e32 v169, v49, v49
	v_fmac_f32_e32 v167, v46, v46
	v_fmac_f32_e32 v169, v48, v48
	v_add_f32_e32 v167, v167, v169
	v_mul_f32_e32 v169, v43, v43
	v_mul_f32_e32 v170, v45, v45
	v_fmac_f32_e32 v169, v42, v42
	v_fmac_f32_e32 v170, v44, v44
	v_add_f32_e32 v169, v169, v170
	v_add_f32_e32 v167, v169, v167
	v_mul_f32_e32 v169, v39, v39
	v_mul_f32_e32 v170, v41, v41
	v_fmac_f32_e32 v169, v38, v38
	v_fmac_f32_e32 v170, v40, v40
	v_add_f32_e32 v169, v169, v170
	v_add_f32_e32 v167, v169, v167
	v_mul_f32_e32 v169, v35, v35
	v_mul_f32_e32 v170, v37, v37
	v_fmac_f32_e32 v169, v34, v34
	v_fmac_f32_e32 v170, v36, v36
	v_add_f32_e32 v169, v169, v170
	v_add_f32_e32 v167, v169, v167
	v_mov_b32_e32 v169, v167
	s_nop 1
	v_permlane16_swap_b32_e32 v169, v167
	s_waitcnt lgkmcnt(0)
	v_add_f32_e32 v167, v167, v169
	v_mov_b32_e32 v169, v167
	s_nop 1
	v_permlane32_swap_b32_e32 v169, v167
	s_and_saveexec_b64 s[22:23], s[40:41]
	s_cbranch_execz .LBB0_2910
	s_lshl_b32 s4, s49, 10
	s_add_i32 s4, s26, s4
	s_waitcnt lgkmcnt(0)
	v_add_f32_e32 v167, v167, v169
	v_lshl_add_u32 v169, v166, 4, s4
	ds_write_b32 v169, v167 offset:2304
.LBB0_2910:
	s_or_b64 exec, exec, s[22:23]
	v_mul_f32_e32 v167, v31, v31
	s_waitcnt lgkmcnt(0)
	v_mul_f32_e32 v169, v33, v33
	v_fmac_f32_e32 v167, v30, v30
	v_fmac_f32_e32 v169, v32, v32
	v_add_f32_e32 v167, v167, v169
	v_mul_f32_e32 v169, v27, v27
	v_mul_f32_e32 v170, v29, v29
	v_fmac_f32_e32 v169, v26, v26
	v_fmac_f32_e32 v170, v28, v28
	v_add_f32_e32 v169, v169, v170
	v_add_f32_e32 v167, v169, v167
	v_mul_f32_e32 v169, v23, v23
	v_mul_f32_e32 v170, v25, v25
	v_fmac_f32_e32 v169, v22, v22
	v_fmac_f32_e32 v170, v24, v24
	v_add_f32_e32 v169, v169, v170
	v_add_f32_e32 v167, v169, v167
	v_mul_f32_e32 v169, v19, v19
	v_mul_f32_e32 v170, v21, v21
	v_fmac_f32_e32 v169, v18, v18
	v_fmac_f32_e32 v170, v20, v20
	v_add_f32_e32 v169, v169, v170
	v_add_f32_e32 v167, v169, v167
	v_mov_b32_e32 v169, v167
	s_nop 1
	v_permlane16_swap_b32_e32 v169, v167
	s_waitcnt lgkmcnt(0)
	v_add_f32_e32 v167, v167, v169
	v_mov_b32_e32 v169, v167
	s_nop 1
	v_permlane32_swap_b32_e32 v169, v167
	s_and_saveexec_b64 s[22:23], s[40:41]
	s_cbranch_execz .LBB0_2912
	s_lshl_b32 s4, s49, 10
	s_add_i32 s4, s26, s4
	s_waitcnt lgkmcnt(0)
	v_add_f32_e32 v167, v167, v169
	v_lshl_add_u32 v169, v166, 4, s4
	ds_write_b32 v169, v167 offset:2560
.LBB0_2912:
	s_or_b64 exec, exec, s[22:23]
	v_mul_f32_e32 v167, v15, v15
	s_waitcnt lgkmcnt(0)
	v_mul_f32_e32 v169, v17, v17
	v_fmac_f32_e32 v167, v14, v14
	v_fmac_f32_e32 v169, v16, v16
	v_add_f32_e32 v167, v167, v169
	v_mul_f32_e32 v169, v11, v11
	v_mul_f32_e32 v170, v13, v13
	v_fmac_f32_e32 v169, v10, v10
	v_fmac_f32_e32 v170, v12, v12
	v_add_f32_e32 v169, v169, v170
	v_add_f32_e32 v167, v169, v167
	v_mul_f32_e32 v169, v7, v7
	v_mul_f32_e32 v170, v9, v9
	v_fmac_f32_e32 v169, v6, v6
	v_fmac_f32_e32 v170, v8, v8
	v_add_f32_e32 v169, v169, v170
	v_add_f32_e32 v167, v169, v167
	v_mul_f32_e32 v169, v3, v3
	v_mul_f32_e32 v170, v5, v5
	v_fmac_f32_e32 v169, v2, v2
	v_fmac_f32_e32 v170, v4, v4
	v_add_f32_e32 v169, v169, v170
	v_add_f32_e32 v167, v169, v167
	v_mov_b32_e32 v169, v167
	s_nop 1
	v_permlane16_swap_b32_e32 v169, v167
	s_waitcnt lgkmcnt(0)
	v_add_f32_e32 v167, v167, v169
	v_mov_b32_e32 v169, v167
	s_nop 1
	v_permlane32_swap_b32_e32 v169, v167
	s_and_saveexec_b64 s[22:23], s[40:41]
	s_cbranch_execz .LBB0_2914
	s_lshl_b32 s4, s49, 10
	s_add_i32 s4, s26, s4
	s_waitcnt lgkmcnt(0)
	v_add_f32_e32 v167, v167, v169
	v_lshl_add_u32 v166, v166, 4, s4
	ds_write_b32 v166, v167 offset:2816

.LBB0_2940:
	s_waitcnt vmcnt(0)
	v_lshlrev_b32_e32 v218, 16, v206
	v_and_b32_e32 v219, 0xffff0000, v206
	v_lshlrev_b32_e32 v206, 16, v207
	v_and_b32_e32 v207, 0xffff0000, v207
	s_waitcnt lgkmcnt(0)
	v_pk_mul_f32 v[136:137], v[136:137], v[0:1] op_sel_hi:[1,0]
	v_pk_mul_f32 v[134:135], v[134:135], v[0:1] op_sel_hi:[1,0]
	v_pk_fma_f32 v[136:137], v[184:185], v[136:137], v[206:207]
	v_pk_fma_f32 v[134:135], v[182:183], v[134:135], v[218:219]
	v_lshlrev_b32_e32 v242, 16, v208
	v_and_b32_e32 v243, 0xffff0000, v208
	v_lshlrev_b32_e32 v208, 16, v209
	v_and_b32_e32 v209, 0xffff0000, v209
	v_pk_mul_f32 v[132:133], v[132:133], v[0:1] op_sel_hi:[1,0]
	v_pk_mul_f32 v[130:131], v[130:131], v[0:1] op_sel_hi:[1,0]
	v_mul_f32_e32 v206, v135, v135
	v_mul_f32_e32 v207, v137, v137
	v_pk_fma_f32 v[132:133], v[180:181], v[132:133], v[208:209]
	v_pk_fma_f32 v[130:131], v[178:179], v[130:131], v[242:243]
	v_fmac_f32_e32 v206, v134, v134
	v_fmac_f32_e32 v207, v136, v136
	v_add_f32_e32 v206, v206, v207
	v_mul_f32_e32 v207, v131, v131
	v_mul_f32_e32 v208, v133, v133
	v_fmac_f32_e32 v207, v130, v130
	v_fmac_f32_e32 v208, v132, v132
	v_add_f32_e32 v207, v207, v208
	s_movk_i32 s4, 0x4000
	v_add_f32_e32 v206, v206, v207
	v_mov_b32_e32 v207, s13
	v_mov_b32_e32 v208, s11
	v_cmp_gt_i32_e32 vcc, s4, v222
	v_and_b32_e32 v209, 0xffff0000, v202
	v_pk_mul_f32 v[120:121], v[120:121], v[0:1] op_sel_hi:[1,0]
	v_cndmask_b32_e32 v207, v207, v208, vcc
	v_lshlrev_b32_e32 v208, 16, v202
	v_lshlrev_b32_e32 v202, 16, v203
	v_and_b32_e32 v203, 0xffff0000, v203
	v_pk_mul_f32 v[118:119], v[118:119], v[0:1] op_sel_hi:[1,0]
	v_lshlrev_b32_e32 v218, 16, v204
	v_and_b32_e32 v219, 0xffff0000, v204
	v_pk_fma_f32 v[120:121], v[172:173], v[120:121], v[202:203]
	v_pk_fma_f32 v[118:119], v[170:171], v[118:119], v[208:209]
	v_pk_mul_f32 v[114:115], v[114:115], v[0:1] op_sel_hi:[1,0]
	v_lshlrev_b32_e32 v204, 16, v205
	v_and_b32_e32 v205, 0xffff0000, v205
	v_pk_mul_f32 v[116:117], v[116:117], v[0:1] op_sel_hi:[1,0]
	v_pk_fma_f32 v[202:203], v[166:167], v[114:115], v[218:219]
	v_mul_f32_e32 v0, v119, v119
	v_mul_f32_e32 v114, v121, v121
	v_pk_fma_f32 v[204:205], v[168:169], v[116:117], v[204:205]
	v_fmac_f32_e32 v0, v118, v118
	v_fmac_f32_e32 v114, v120, v120
	v_add_f32_e32 v0, v0, v114
	v_mul_f32_e32 v114, v203, v203
	v_mul_f32_e32 v115, v205, v205
	v_fmac_f32_e32 v114, v202, v202
	v_fmac_f32_e32 v115, v204, v204
	v_add_f32_e32 v114, v114, v115
	v_add_f32_e32 v0, v0, v114
	v_add_f32_e32 v0, v206, v0
	v_mov_b32_e32 v208, v0
	s_nop 1
	v_permlane16_swap_b32_e32 v208, v0
	v_lshlrev_b64 v[216:217], 12, v[222:223]
	v_mov_b32_e32 v222, s12
	v_mov_b32_e32 v114, s10
	v_cndmask_b32_e32 v206, v222, v114, vcc
	v_lshl_add_u64 v[114:115], v[206:207], 0, v[216:217]
	s_waitcnt lgkmcnt(0)
	v_add_f32_e32 v0, v0, v208
	v_lshl_add_u64 v[116:117], v[220:221], 2, v[114:115]
	v_mov_b32_e32 v114, v0
	s_nop 1
	v_permlane32_swap_b32_e32 v114, v0
	global_store_dwordx4 v[116:117], v[134:137], off
	global_store_dwordx4 v[116:117], v[130:133], off offset:16
	global_store_dwordx4 v[116:117], v[118:121], off offset:512
	global_store_dwordx4 v[116:117], v[202:205], off offset:528
	s_and_saveexec_b64 s[14:15], s[40:41]
	s_cbranch_execz .LBB0_2942
	v_lshl_add_u32 v115, v224, 4, s26
	s_waitcnt lgkmcnt(0)
	v_add_f32_e32 v0, v0, v114
	ds_write_b32 v115, v0 offset:6144

.LBB0_2944:
	s_waitcnt lgkmcnt(0)
	v_or_b32_e32 v114, 16, v224
	v_add_u32_e32 v116, s27, v114
	v_lshlrev_b32_e32 v118, 16, v198
	v_and_b32_e32 v119, 0xffff0000, v198
	v_lshlrev_b32_e32 v130, 16, v199
	v_and_b32_e32 v131, 0xffff0000, v199
	v_pk_mul_f32 v[112:113], v[112:113], v[0:1] op_sel_hi:[1,0]
	v_pk_mul_f32 v[110:111], v[110:111], v[0:1] op_sel_hi:[1,0]
	v_ashrrev_i32_e32 v117, 31, v116
	v_pk_fma_f32 v[112:113], v[184:185], v[112:113], v[130:131]
	v_pk_fma_f32 v[110:111], v[182:183], v[110:111], v[118:119]
	v_lshlrev_b64 v[120:121], 12, v[116:117]
	v_lshlrev_b32_e32 v132, 16, v200
	v_and_b32_e32 v133, 0xffff0000, v200
	v_lshlrev_b32_e32 v134, 16, v201
	v_and_b32_e32 v135, 0xffff0000, v201
	v_pk_mul_f32 v[108:109], v[108:109], v[0:1] op_sel_hi:[1,0]
	v_pk_mul_f32 v[106:107], v[106:107], v[0:1] op_sel_hi:[1,0]
	v_mul_f32_e32 v115, v111, v111
	v_mul_f32_e32 v117, v113, v113
	v_pk_fma_f32 v[108:109], v[180:181], v[108:109], v[134:135]
	v_pk_fma_f32 v[106:107], v[178:179], v[106:107], v[132:133]
	v_fmac_f32_e32 v115, v110, v110
	v_fmac_f32_e32 v117, v112, v112
	v_add_f32_e32 v115, v115, v117
	v_mul_f32_e32 v117, v107, v107
	v_mul_f32_e32 v118, v109, v109
	v_fmac_f32_e32 v117, v106, v106
	v_fmac_f32_e32 v118, v108, v108
	v_add_f32_e32 v117, v117, v118
	v_add_f32_e32 v115, v115, v117
	v_mov_b32_e32 v117, s13
	v_mov_b32_e32 v118, s11
	v_cmp_gt_i32_e32 vcc, s4, v116
	v_lshlrev_b32_e32 v116, 16, v194
	v_and_b32_e32 v119, 0xffff0000, v195
	v_cndmask_b32_e32 v131, v117, v118, vcc
	v_and_b32_e32 v117, 0xffff0000, v194
	v_lshlrev_b32_e32 v118, 16, v195
	v_pk_mul_f32 v[104:105], v[104:105], v[0:1] op_sel_hi:[1,0]
	v_pk_mul_f32 v[102:103], v[102:103], v[0:1] op_sel_hi:[1,0]
	v_lshlrev_b32_e32 v132, 16, v196
	v_and_b32_e32 v133, 0xffff0000, v196
	v_pk_fma_f32 v[104:105], v[172:173], v[104:105], v[118:119]
	v_pk_fma_f32 v[102:103], v[170:171], v[102:103], v[116:117]
	v_pk_mul_f32 v[98:99], v[98:99], v[0:1] op_sel_hi:[1,0]
	v_lshlrev_b32_e32 v134, 16, v197
	v_and_b32_e32 v135, 0xffff0000, v197
	v_pk_mul_f32 v[100:101], v[100:101], v[0:1] op_sel_hi:[1,0]
	v_pk_fma_f32 v[116:117], v[166:167], v[98:99], v[132:133]
	v_mul_f32_e32 v0, v103, v103
	v_mul_f32_e32 v98, v105, v105
	v_pk_fma_f32 v[118:119], v[168:169], v[100:101], v[134:135]
	v_fmac_f32_e32 v0, v102, v102
	v_fmac_f32_e32 v98, v104, v104
	v_add_f32_e32 v0, v0, v98
	v_mul_f32_e32 v98, v117, v117
	v_mul_f32_e32 v99, v119, v119
	v_fmac_f32_e32 v98, v116, v116
	v_fmac_f32_e32 v99, v118, v118
	v_add_f32_e32 v98, v98, v99
	v_add_f32_e32 v0, v0, v98
	v_add_f32_e32 v0, v115, v0
	v_mov_b32_e32 v115, v0
	s_nop 1
	v_permlane16_swap_b32_e32 v115, v0
	v_mov_b32_e32 v130, s12
	v_mov_b32_e32 v98, s10
	v_cndmask_b32_e32 v130, v130, v98, vcc
	v_lshl_add_u64 v[98:99], v[130:131], 0, v[120:121]
	s_waitcnt lgkmcnt(0)
	v_add_f32_e32 v0, v0, v115
	v_lshl_add_u64 v[100:101], v[220:221], 2, v[98:99]
	v_mov_b32_e32 v98, v0
	s_nop 1
	v_permlane32_swap_b32_e32 v98, v0
	global_store_dwordx4 v[100:101], v[110:113], off
	global_store_dwordx4 v[100:101], v[106:109], off offset:16
	global_store_dwordx4 v[100:101], v[102:105], off offset:512
	global_store_dwordx4 v[100:101], v[116:119], off offset:528
	s_and_saveexec_b64 s[14:15], s[40:41]
	s_cbranch_execz .LBB0_2946
	v_lshl_add_u32 v99, v114, 4, s26
	s_waitcnt lgkmcnt(0)
	v_add_f32_e32 v0, v0, v98
	ds_write_b32 v99, v0 offset:6144

.LBB0_2948:
	s_waitcnt lgkmcnt(0)
	v_or_b32_e32 v98, 32, v224
	v_add_u32_e32 v100, s27, v98
	v_lshlrev_b32_e32 v102, 16, v190
	v_and_b32_e32 v103, 0xffff0000, v190
	v_lshlrev_b32_e32 v106, 16, v191
	v_and_b32_e32 v107, 0xffff0000, v191
	v_pk_mul_f32 v[96:97], v[96:97], v[0:1] op_sel_hi:[1,0]
	v_pk_mul_f32 v[94:95], v[94:95], v[0:1] op_sel_hi:[1,0]
	v_ashrrev_i32_e32 v101, 31, v100
	v_pk_fma_f32 v[96:97], v[184:185], v[96:97], v[106:107]
	v_pk_fma_f32 v[94:95], v[182:183], v[94:95], v[102:103]
	v_lshlrev_b64 v[104:105], 12, v[100:101]
	v_lshlrev_b32_e32 v108, 16, v192
	v_and_b32_e32 v109, 0xffff0000, v192
	v_lshlrev_b32_e32 v110, 16, v193
	v_and_b32_e32 v111, 0xffff0000, v193
	v_pk_mul_f32 v[92:93], v[92:93], v[0:1] op_sel_hi:[1,0]
	v_pk_mul_f32 v[90:91], v[90:91], v[0:1] op_sel_hi:[1,0]
	v_mul_f32_e32 v99, v95, v95
	v_mul_f32_e32 v101, v97, v97
	v_pk_fma_f32 v[92:93], v[180:181], v[92:93], v[110:111]
	v_pk_fma_f32 v[90:91], v[178:179], v[90:91], v[108:109]
	v_fmac_f32_e32 v99, v94, v94
	v_fmac_f32_e32 v101, v96, v96
	v_add_f32_e32 v99, v99, v101
	v_mul_f32_e32 v101, v91, v91
	v_mul_f32_e32 v102, v93, v93
	v_fmac_f32_e32 v101, v90, v90
	v_fmac_f32_e32 v102, v92, v92
	v_add_f32_e32 v101, v101, v102
	v_add_f32_e32 v99, v99, v101
	v_mov_b32_e32 v101, s13
	v_mov_b32_e32 v102, s11
	v_cmp_gt_i32_e32 vcc, s4, v100
	v_lshlrev_b32_e32 v100, 16, v186
	v_and_b32_e32 v103, 0xffff0000, v187
	v_cndmask_b32_e32 v107, v101, v102, vcc
	v_and_b32_e32 v101, 0xffff0000, v186
	v_lshlrev_b32_e32 v102, 16, v187
	v_pk_mul_f32 v[88:89], v[88:89], v[0:1] op_sel_hi:[1,0]
	v_pk_mul_f32 v[86:87], v[86:87], v[0:1] op_sel_hi:[1,0]
	v_lshlrev_b32_e32 v108, 16, v188
	v_and_b32_e32 v109, 0xffff0000, v188
	v_pk_fma_f32 v[88:89], v[172:173], v[88:89], v[102:103]
	v_pk_fma_f32 v[86:87], v[170:171], v[86:87], v[100:101]
	v_pk_mul_f32 v[82:83], v[82:83], v[0:1] op_sel_hi:[1,0]
	v_lshlrev_b32_e32 v110, 16, v189
	v_and_b32_e32 v111, 0xffff0000, v189
	v_pk_mul_f32 v[84:85], v[84:85], v[0:1] op_sel_hi:[1,0]
	v_pk_fma_f32 v[100:101], v[166:167], v[82:83], v[108:109]
	v_mul_f32_e32 v0, v87, v87
	v_mul_f32_e32 v82, v89, v89
	v_pk_fma_f32 v[102:103], v[168:169], v[84:85], v[110:111]
	v_fmac_f32_e32 v0, v86, v86
	v_fmac_f32_e32 v82, v88, v88
	v_add_f32_e32 v0, v0, v82
	v_mul_f32_e32 v82, v101, v101
	v_mul_f32_e32 v83, v103, v103
	v_fmac_f32_e32 v82, v100, v100
	v_fmac_f32_e32 v83, v102, v102
	v_add_f32_e32 v82, v82, v83
	v_add_f32_e32 v0, v0, v82
	v_add_f32_e32 v0, v99, v0
	v_mov_b32_e32 v99, v0
	s_nop 1
	v_permlane16_swap_b32_e32 v99, v0
	v_mov_b32_e32 v106, s12
	v_mov_b32_e32 v82, s10
	v_cndmask_b32_e32 v106, v106, v82, vcc
	v_lshl_add_u64 v[82:83], v[106:107], 0, v[104:105]
	s_waitcnt lgkmcnt(0)
	v_add_f32_e32 v0, v0, v99
	v_lshl_add_u64 v[84:85], v[220:221], 2, v[82:83]
	v_mov_b32_e32 v82, v0
	s_nop 1
	v_permlane32_swap_b32_e32 v82, v0
	global_store_dwordx4 v[84:85], v[94:97], off
	global_store_dwordx4 v[84:85], v[90:93], off offset:16
	global_store_dwordx4 v[84:85], v[86:89], off offset:512
	global_store_dwordx4 v[84:85], v[100:103], off offset:528
	s_and_saveexec_b64 s[14:15], s[40:41]
	s_cbranch_execz .LBB0_2950
	v_lshl_add_u32 v83, v98, 4, s26
	s_waitcnt lgkmcnt(0)
	v_add_f32_e32 v0, v0, v82
	ds_write_b32 v83, v0 offset:6144

.LBB0_2952:
	s_waitcnt lgkmcnt(0)
	v_or_b32_e32 v82, 48, v224
	v_add_u32_e32 v84, s27, v82
	v_lshlrev_b32_e32 v86, 16, v174
	v_and_b32_e32 v87, 0xffff0000, v174
	v_lshlrev_b32_e32 v90, 16, v175
	v_and_b32_e32 v91, 0xffff0000, v175
	v_pk_mul_f32 v[80:81], v[80:81], v[0:1] op_sel_hi:[1,0]
	v_pk_mul_f32 v[78:79], v[78:79], v[0:1] op_sel_hi:[1,0]
	v_ashrrev_i32_e32 v85, 31, v84
	v_pk_fma_f32 v[80:81], v[184:185], v[80:81], v[90:91]
	v_pk_fma_f32 v[78:79], v[182:183], v[78:79], v[86:87]
	v_lshlrev_b64 v[88:89], 12, v[84:85]
	v_lshlrev_b32_e32 v92, 16, v176
	v_and_b32_e32 v93, 0xffff0000, v176
	v_lshlrev_b32_e32 v94, 16, v177
	v_and_b32_e32 v95, 0xffff0000, v177
	v_pk_mul_f32 v[76:77], v[76:77], v[0:1] op_sel_hi:[1,0]
	v_pk_mul_f32 v[74:75], v[74:75], v[0:1] op_sel_hi:[1,0]
	v_mul_f32_e32 v83, v79, v79
	v_mul_f32_e32 v85, v81, v81
	v_pk_fma_f32 v[76:77], v[180:181], v[76:77], v[94:95]
	v_pk_fma_f32 v[74:75], v[178:179], v[74:75], v[92:93]
	v_fmac_f32_e32 v83, v78, v78
	v_fmac_f32_e32 v85, v80, v80
	v_add_f32_e32 v83, v83, v85
	v_mul_f32_e32 v85, v75, v75
	v_mul_f32_e32 v86, v77, v77
	v_fmac_f32_e32 v85, v74, v74
	v_fmac_f32_e32 v86, v76, v76
	v_add_f32_e32 v85, v85, v86
	v_add_f32_e32 v83, v83, v85
	v_mov_b32_e32 v85, s13
	v_mov_b32_e32 v86, s11
	v_cmp_gt_i32_e32 vcc, s4, v84
	v_lshlrev_b32_e32 v84, 16, v162
	v_and_b32_e32 v87, 0xffff0000, v163
	v_cndmask_b32_e32 v91, v85, v86, vcc
	v_and_b32_e32 v85, 0xffff0000, v162
	v_lshlrev_b32_e32 v86, 16, v163
	v_pk_mul_f32 v[72:73], v[72:73], v[0:1] op_sel_hi:[1,0]
	v_pk_mul_f32 v[70:71], v[70:71], v[0:1] op_sel_hi:[1,0]
	v_lshlrev_b32_e32 v92, 16, v164
	v_and_b32_e32 v93, 0xffff0000, v164
	v_pk_fma_f32 v[72:73], v[172:173], v[72:73], v[86:87]
	v_pk_fma_f32 v[70:71], v[170:171], v[70:71], v[84:85]
	v_pk_mul_f32 v[66:67], v[66:67], v[0:1] op_sel_hi:[1,0]
	v_lshlrev_b32_e32 v94, 16, v165
	v_and_b32_e32 v95, 0xffff0000, v165
	v_pk_mul_f32 v[68:69], v[68:69], v[0:1] op_sel_hi:[1,0]
	v_pk_fma_f32 v[84:85], v[166:167], v[66:67], v[92:93]
	v_mul_f32_e32 v0, v71, v71
	v_mul_f32_e32 v66, v73, v73
	v_pk_fma_f32 v[86:87], v[168:169], v[68:69], v[94:95]
	v_fmac_f32_e32 v0, v70, v70
	v_fmac_f32_e32 v66, v72, v72
	v_add_f32_e32 v0, v0, v66
	v_mul_f32_e32 v66, v85, v85
	v_mul_f32_e32 v67, v87, v87
	v_fmac_f32_e32 v66, v84, v84
	v_fmac_f32_e32 v67, v86, v86
	v_add_f32_e32 v66, v66, v67
	v_add_f32_e32 v0, v0, v66
	v_add_f32_e32 v0, v83, v0
	v_mov_b32_e32 v83, v0
	s_nop 1
	v_permlane16_swap_b32_e32 v83, v0
	v_mov_b32_e32 v90, s12
	v_mov_b32_e32 v66, s10
	v_cndmask_b32_e32 v90, v90, v66, vcc
	v_lshl_add_u64 v[66:67], v[90:91], 0, v[88:89]
	s_waitcnt lgkmcnt(0)
	v_add_f32_e32 v0, v0, v83
	v_lshl_add_u64 v[68:69], v[220:221], 2, v[66:67]
	v_mov_b32_e32 v66, v0
	s_nop 1
	v_permlane32_swap_b32_e32 v66, v0
	global_store_dwordx4 v[68:69], v[78:81], off
	global_store_dwordx4 v[68:69], v[74:77], off offset:16
	global_store_dwordx4 v[68:69], v[70:73], off offset:512
	global_store_dwordx4 v[68:69], v[84:87], off offset:528
	s_and_saveexec_b64 s[14:15], s[40:41]
	s_cbranch_execz .LBB0_2954
	v_lshl_add_u32 v67, v82, 4, s26
	s_waitcnt lgkmcnt(0)
	v_add_f32_e32 v0, v0, v66
	ds_write_b32 v67, v0 offset:6144

.LBB0_2956:
	s_waitcnt lgkmcnt(0)
	v_add_u32_e32 v66, 0x80, v224
	v_add_u32_e32 v68, s27, v66
	v_lshlrev_b32_e32 v70, 16, v158
	v_and_b32_e32 v71, 0xffff0000, v158
	v_lshlrev_b32_e32 v74, 16, v159
	v_and_b32_e32 v75, 0xffff0000, v159
	v_pk_mul_f32 v[64:65], v[64:65], v[0:1] op_sel_hi:[1,0]
	v_pk_mul_f32 v[62:63], v[62:63], v[0:1] op_sel_hi:[1,0]
	v_ashrrev_i32_e32 v69, 31, v68
	v_pk_fma_f32 v[64:65], v[184:185], v[64:65], v[74:75]
	v_pk_fma_f32 v[62:63], v[182:183], v[62:63], v[70:71]
	v_lshlrev_b64 v[72:73], 12, v[68:69]
	v_lshlrev_b32_e32 v76, 16, v160
	v_and_b32_e32 v77, 0xffff0000, v160
	v_lshlrev_b32_e32 v78, 16, v161
	v_and_b32_e32 v79, 0xffff0000, v161
	v_pk_mul_f32 v[60:61], v[60:61], v[0:1] op_sel_hi:[1,0]
	v_pk_mul_f32 v[58:59], v[58:59], v[0:1] op_sel_hi:[1,0]
	v_mul_f32_e32 v67, v63, v63
	v_mul_f32_e32 v69, v65, v65
	v_pk_fma_f32 v[60:61], v[180:181], v[60:61], v[78:79]
	v_pk_fma_f32 v[58:59], v[178:179], v[58:59], v[76:77]
	v_fmac_f32_e32 v67, v62, v62
	v_fmac_f32_e32 v69, v64, v64
	v_add_f32_e32 v67, v67, v69
	v_mul_f32_e32 v69, v59, v59
	v_mul_f32_e32 v70, v61, v61
	v_fmac_f32_e32 v69, v58, v58
	v_fmac_f32_e32 v70, v60, v60
	v_add_f32_e32 v69, v69, v70
	v_add_f32_e32 v67, v67, v69
	v_mov_b32_e32 v69, s13
	v_mov_b32_e32 v70, s11
	v_cmp_gt_i32_e32 vcc, s4, v68
	v_lshlrev_b32_e32 v68, 16, v154
	v_and_b32_e32 v71, 0xffff0000, v155
	v_cndmask_b32_e32 v75, v69, v70, vcc
	v_and_b32_e32 v69, 0xffff0000, v154
	v_lshlrev_b32_e32 v70, 16, v155
	v_pk_mul_f32 v[56:57], v[56:57], v[0:1] op_sel_hi:[1,0]
	v_pk_mul_f32 v[54:55], v[54:55], v[0:1] op_sel_hi:[1,0]
	v_lshlrev_b32_e32 v76, 16, v156
	v_and_b32_e32 v77, 0xffff0000, v156
	v_pk_fma_f32 v[56:57], v[172:173], v[56:57], v[70:71]
	v_pk_fma_f32 v[54:55], v[170:171], v[54:55], v[68:69]
	v_pk_mul_f32 v[50:51], v[50:51], v[0:1] op_sel_hi:[1,0]
	v_lshlrev_b32_e32 v78, 16, v157
	v_and_b32_e32 v79, 0xffff0000, v157
	v_pk_mul_f32 v[52:53], v[52:53], v[0:1] op_sel_hi:[1,0]
	v_pk_fma_f32 v[68:69], v[166:167], v[50:51], v[76:77]
	v_mul_f32_e32 v0, v55, v55
	v_mul_f32_e32 v50, v57, v57
	v_pk_fma_f32 v[70:71], v[168:169], v[52:53], v[78:79]
	v_fmac_f32_e32 v0, v54, v54
	v_fmac_f32_e32 v50, v56, v56
	v_add_f32_e32 v0, v0, v50
	v_mul_f32_e32 v50, v69, v69
	v_mul_f32_e32 v51, v71, v71
	v_fmac_f32_e32 v50, v68, v68
	v_fmac_f32_e32 v51, v70, v70
	v_add_f32_e32 v50, v50, v51
	v_add_f32_e32 v0, v0, v50
	v_add_f32_e32 v0, v67, v0
	v_mov_b32_e32 v67, v0
	s_nop 1
	v_permlane16_swap_b32_e32 v67, v0
	v_mov_b32_e32 v74, s12
	v_mov_b32_e32 v50, s10
	v_cndmask_b32_e32 v74, v74, v50, vcc
	v_lshl_add_u64 v[50:51], v[74:75], 0, v[72:73]
	s_waitcnt lgkmcnt(0)
	v_add_f32_e32 v0, v0, v67
	v_lshl_add_u64 v[52:53], v[220:221], 2, v[50:51]
	v_mov_b32_e32 v50, v0
	s_nop 1
	v_permlane32_swap_b32_e32 v50, v0
	global_store_dwordx4 v[52:53], v[62:65], off
	global_store_dwordx4 v[52:53], v[58:61], off offset:16
	global_store_dwordx4 v[52:53], v[54:57], off offset:512
	global_store_dwordx4 v[52:53], v[68:71], off offset:528
	s_and_saveexec_b64 s[14:15], s[40:41]
	s_cbranch_execz .LBB0_2958
	v_lshl_add_u32 v51, v66, 4, s26
	s_waitcnt lgkmcnt(0)
	v_add_f32_e32 v0, v0, v50
	ds_write_b32 v51, v0 offset:6144

.LBB0_2960:
	s_waitcnt lgkmcnt(0)
	v_add_u32_e32 v50, 0x90, v224
	v_add_u32_e32 v52, s27, v50
	v_lshlrev_b32_e32 v54, 16, v150
	v_and_b32_e32 v55, 0xffff0000, v150
	v_lshlrev_b32_e32 v58, 16, v151
	v_and_b32_e32 v59, 0xffff0000, v151
	v_pk_mul_f32 v[48:49], v[48:49], v[0:1] op_sel_hi:[1,0]
	v_pk_mul_f32 v[46:47], v[46:47], v[0:1] op_sel_hi:[1,0]
	v_ashrrev_i32_e32 v53, 31, v52
	v_pk_fma_f32 v[48:49], v[184:185], v[48:49], v[58:59]
	v_pk_fma_f32 v[46:47], v[182:183], v[46:47], v[54:55]
	v_lshlrev_b64 v[56:57], 12, v[52:53]
	v_lshlrev_b32_e32 v60, 16, v152
	v_and_b32_e32 v61, 0xffff0000, v152
	v_lshlrev_b32_e32 v62, 16, v153
	v_and_b32_e32 v63, 0xffff0000, v153
	v_pk_mul_f32 v[44:45], v[44:45], v[0:1] op_sel_hi:[1,0]
	v_pk_mul_f32 v[42:43], v[42:43], v[0:1] op_sel_hi:[1,0]
	v_mul_f32_e32 v51, v47, v47
	v_mul_f32_e32 v53, v49, v49
	v_pk_fma_f32 v[44:45], v[180:181], v[44:45], v[62:63]
	v_pk_fma_f32 v[42:43], v[178:179], v[42:43], v[60:61]
	v_fmac_f32_e32 v51, v46, v46
	v_fmac_f32_e32 v53, v48, v48
	v_add_f32_e32 v51, v51, v53
	v_mul_f32_e32 v53, v43, v43
	v_mul_f32_e32 v54, v45, v45
	v_fmac_f32_e32 v53, v42, v42
	v_fmac_f32_e32 v54, v44, v44
	v_add_f32_e32 v53, v53, v54
	v_add_f32_e32 v51, v51, v53
	v_mov_b32_e32 v53, s13
	v_mov_b32_e32 v54, s11
	v_cmp_gt_i32_e32 vcc, s4, v52
	v_lshlrev_b32_e32 v52, 16, v146
	v_and_b32_e32 v55, 0xffff0000, v147
	v_cndmask_b32_e32 v59, v53, v54, vcc
	v_and_b32_e32 v53, 0xffff0000, v146
	v_lshlrev_b32_e32 v54, 16, v147
	v_pk_mul_f32 v[40:41], v[40:41], v[0:1] op_sel_hi:[1,0]
	v_pk_mul_f32 v[38:39], v[38:39], v[0:1] op_sel_hi:[1,0]
	v_lshlrev_b32_e32 v60, 16, v148
	v_and_b32_e32 v61, 0xffff0000, v148
	v_pk_fma_f32 v[40:41], v[172:173], v[40:41], v[54:55]
	v_pk_fma_f32 v[38:39], v[170:171], v[38:39], v[52:53]
	v_pk_mul_f32 v[34:35], v[34:35], v[0:1] op_sel_hi:[1,0]
	v_lshlrev_b32_e32 v62, 16, v149
	v_and_b32_e32 v63, 0xffff0000, v149
	v_pk_mul_f32 v[36:37], v[36:37], v[0:1] op_sel_hi:[1,0]
	v_pk_fma_f32 v[52:53], v[166:167], v[34:35], v[60:61]
	v_mul_f32_e32 v0, v39, v39
	v_mul_f32_e32 v34, v41, v41
	v_pk_fma_f32 v[54:55], v[168:169], v[36:37], v[62:63]
	v_fmac_f32_e32 v0, v38, v38
	v_fmac_f32_e32 v34, v40, v40
	v_add_f32_e32 v0, v0, v34
	v_mul_f32_e32 v34, v53, v53
	v_mul_f32_e32 v35, v55, v55
	v_fmac_f32_e32 v34, v52, v52
	v_fmac_f32_e32 v35, v54, v54
	v_add_f32_e32 v34, v34, v35
	v_add_f32_e32 v0, v0, v34
	v_add_f32_e32 v0, v51, v0
	v_mov_b32_e32 v51, v0
	s_nop 1
	v_permlane16_swap_b32_e32 v51, v0
	v_mov_b32_e32 v58, s12
	v_mov_b32_e32 v34, s10
	v_cndmask_b32_e32 v58, v58, v34, vcc
	v_lshl_add_u64 v[34:35], v[58:59], 0, v[56:57]
	s_waitcnt lgkmcnt(0)
	v_add_f32_e32 v0, v0, v51
	v_lshl_add_u64 v[36:37], v[220:221], 2, v[34:35]
	v_mov_b32_e32 v34, v0
	s_nop 1
	v_permlane32_swap_b32_e32 v34, v0
	global_store_dwordx4 v[36:37], v[46:49], off
	global_store_dwordx4 v[36:37], v[42:45], off offset:16
	global_store_dwordx4 v[36:37], v[38:41], off offset:512
	global_store_dwordx4 v[36:37], v[52:55], off offset:528
	s_and_saveexec_b64 s[14:15], s[40:41]
	s_cbranch_execz .LBB0_2962
	v_lshl_add_u32 v35, v50, 4, s26
	s_waitcnt lgkmcnt(0)
	v_add_f32_e32 v0, v0, v34
	ds_write_b32 v35, v0 offset:6144

.LBB0_2964:
	s_waitcnt lgkmcnt(0)
	v_add_u32_e32 v34, 0xa0, v224
	v_add_u32_e32 v36, s27, v34
	v_lshlrev_b32_e32 v38, 16, v142
	v_and_b32_e32 v39, 0xffff0000, v142
	v_lshlrev_b32_e32 v42, 16, v143
	v_and_b32_e32 v43, 0xffff0000, v143
	v_pk_mul_f32 v[32:33], v[32:33], v[0:1] op_sel_hi:[1,0]
	v_pk_mul_f32 v[30:31], v[30:31], v[0:1] op_sel_hi:[1,0]
	v_ashrrev_i32_e32 v37, 31, v36
	v_pk_fma_f32 v[32:33], v[184:185], v[32:33], v[42:43]
	v_pk_fma_f32 v[30:31], v[182:183], v[30:31], v[38:39]
	v_lshlrev_b64 v[40:41], 12, v[36:37]
	v_lshlrev_b32_e32 v44, 16, v144
	v_and_b32_e32 v45, 0xffff0000, v144
	v_lshlrev_b32_e32 v46, 16, v145
	v_and_b32_e32 v47, 0xffff0000, v145
	v_pk_mul_f32 v[28:29], v[28:29], v[0:1] op_sel_hi:[1,0]
	v_pk_mul_f32 v[26:27], v[26:27], v[0:1] op_sel_hi:[1,0]
	v_mul_f32_e32 v35, v31, v31
	v_mul_f32_e32 v37, v33, v33
	v_pk_fma_f32 v[28:29], v[180:181], v[28:29], v[46:47]
	v_pk_fma_f32 v[26:27], v[178:179], v[26:27], v[44:45]
	v_fmac_f32_e32 v35, v30, v30
	v_fmac_f32_e32 v37, v32, v32
	v_add_f32_e32 v35, v35, v37
	v_mul_f32_e32 v37, v27, v27
	v_mul_f32_e32 v38, v29, v29
	v_fmac_f32_e32 v37, v26, v26
	v_fmac_f32_e32 v38, v28, v28
	v_add_f32_e32 v37, v37, v38
	v_add_f32_e32 v35, v35, v37
	v_mov_b32_e32 v37, s13
	v_mov_b32_e32 v38, s11
	v_cmp_gt_i32_e32 vcc, s4, v36
	v_lshlrev_b32_e32 v36, 16, v138
	v_and_b32_e32 v39, 0xffff0000, v139
	v_cndmask_b32_e32 v43, v37, v38, vcc
	v_and_b32_e32 v37, 0xffff0000, v138
	v_lshlrev_b32_e32 v38, 16, v139
	v_pk_mul_f32 v[24:25], v[24:25], v[0:1] op_sel_hi:[1,0]
	v_pk_mul_f32 v[22:23], v[22:23], v[0:1] op_sel_hi:[1,0]
	v_lshlrev_b32_e32 v44, 16, v140
	v_and_b32_e32 v45, 0xffff0000, v140
	v_pk_fma_f32 v[24:25], v[172:173], v[24:25], v[38:39]
	v_pk_fma_f32 v[22:23], v[170:171], v[22:23], v[36:37]
	v_pk_mul_f32 v[18:19], v[18:19], v[0:1] op_sel_hi:[1,0]
	v_lshlrev_b32_e32 v46, 16, v141
	v_and_b32_e32 v47, 0xffff0000, v141
	v_pk_mul_f32 v[20:21], v[20:21], v[0:1] op_sel_hi:[1,0]
	v_pk_fma_f32 v[36:37], v[166:167], v[18:19], v[44:45]
	v_mul_f32_e32 v0, v23, v23
	v_mul_f32_e32 v18, v25, v25
	v_pk_fma_f32 v[38:39], v[168:169], v[20:21], v[46:47]
	v_fmac_f32_e32 v0, v22, v22
	v_fmac_f32_e32 v18, v24, v24
	v_add_f32_e32 v0, v0, v18
	v_mul_f32_e32 v18, v37, v37
	v_mul_f32_e32 v19, v39, v39
	v_fmac_f32_e32 v18, v36, v36
	v_fmac_f32_e32 v19, v38, v38
	v_add_f32_e32 v18, v18, v19
	v_add_f32_e32 v0, v0, v18
	v_add_f32_e32 v0, v35, v0
	v_mov_b32_e32 v35, v0
	s_nop 1
	v_permlane16_swap_b32_e32 v35, v0
	v_mov_b32_e32 v42, s12
	v_mov_b32_e32 v18, s10
	v_cndmask_b32_e32 v42, v42, v18, vcc
	v_lshl_add_u64 v[18:19], v[42:43], 0, v[40:41]
	s_waitcnt lgkmcnt(0)
	v_add_f32_e32 v0, v0, v35
	v_lshl_add_u64 v[20:21], v[220:221], 2, v[18:19]
	v_mov_b32_e32 v18, v0
	s_nop 1
	v_permlane32_swap_b32_e32 v18, v0
	global_store_dwordx4 v[20:21], v[30:33], off
	global_store_dwordx4 v[20:21], v[26:29], off offset:16
	global_store_dwordx4 v[20:21], v[22:25], off offset:512
	global_store_dwordx4 v[20:21], v[36:39], off offset:528
	s_and_saveexec_b64 s[14:15], s[40:41]
	s_cbranch_execz .LBB0_2966
	v_lshl_add_u32 v19, v34, 4, s26
	s_waitcnt lgkmcnt(0)
	v_add_f32_e32 v0, v0, v18
	ds_write_b32 v19, v0 offset:6144

.LBB0_2968:
	s_waitcnt lgkmcnt(0)
	v_add_u32_e32 v18, 0xb0, v224
	v_add_u32_e32 v20, s27, v18
	v_lshlrev_b32_e32 v22, 16, v126
	v_and_b32_e32 v23, 0xffff0000, v126
	v_lshlrev_b32_e32 v26, 16, v127
	v_and_b32_e32 v27, 0xffff0000, v127
	v_pk_mul_f32 v[16:17], v[16:17], v[0:1] op_sel_hi:[1,0]
	v_pk_mul_f32 v[14:15], v[14:15], v[0:1] op_sel_hi:[1,0]
	v_ashrrev_i32_e32 v21, 31, v20
	v_pk_fma_f32 v[16:17], v[184:185], v[16:17], v[26:27]
	v_pk_fma_f32 v[14:15], v[182:183], v[14:15], v[22:23]
	v_lshlrev_b64 v[24:25], 12, v[20:21]
	v_lshlrev_b32_e32 v28, 16, v128
	v_and_b32_e32 v29, 0xffff0000, v128
	v_lshlrev_b32_e32 v30, 16, v129
	v_and_b32_e32 v31, 0xffff0000, v129
	v_pk_mul_f32 v[12:13], v[12:13], v[0:1] op_sel_hi:[1,0]
	v_pk_mul_f32 v[10:11], v[10:11], v[0:1] op_sel_hi:[1,0]
	v_mul_f32_e32 v19, v15, v15
	v_mul_f32_e32 v21, v17, v17
	v_pk_fma_f32 v[12:13], v[180:181], v[12:13], v[30:31]
	v_pk_fma_f32 v[10:11], v[178:179], v[10:11], v[28:29]
	v_fmac_f32_e32 v19, v14, v14
	v_fmac_f32_e32 v21, v16, v16
	v_add_f32_e32 v19, v19, v21
	v_mul_f32_e32 v21, v11, v11
	v_mul_f32_e32 v22, v13, v13
	v_fmac_f32_e32 v21, v10, v10
	v_fmac_f32_e32 v22, v12, v12
	v_add_f32_e32 v21, v21, v22
	v_add_f32_e32 v19, v19, v21
	v_mov_b32_e32 v21, s13
	v_mov_b32_e32 v22, s11
	v_cmp_gt_i32_e32 vcc, s4, v20
	v_lshlrev_b32_e32 v20, 16, v122
	v_and_b32_e32 v23, 0xffff0000, v123
	v_cndmask_b32_e32 v27, v21, v22, vcc
	v_and_b32_e32 v21, 0xffff0000, v122
	v_lshlrev_b32_e32 v22, 16, v123
	v_pk_mul_f32 v[8:9], v[8:9], v[0:1] op_sel_hi:[1,0]
	v_pk_mul_f32 v[6:7], v[6:7], v[0:1] op_sel_hi:[1,0]
	v_lshlrev_b32_e32 v28, 16, v124
	v_and_b32_e32 v29, 0xffff0000, v124
	v_pk_fma_f32 v[8:9], v[172:173], v[8:9], v[22:23]
	v_pk_fma_f32 v[6:7], v[170:171], v[6:7], v[20:21]
	v_pk_mul_f32 v[2:3], v[2:3], v[0:1] op_sel_hi:[1,0]
	v_lshlrev_b32_e32 v30, 16, v125
	v_and_b32_e32 v31, 0xffff0000, v125
	v_pk_mul_f32 v[4:5], v[4:5], v[0:1] op_sel_hi:[1,0]
	v_pk_fma_f32 v[20:21], v[166:167], v[2:3], v[28:29]
	v_mul_f32_e32 v0, v7, v7
	v_mul_f32_e32 v2, v9, v9
	v_pk_fma_f32 v[22:23], v[168:169], v[4:5], v[30:31]
	v_fmac_f32_e32 v0, v6, v6
	v_fmac_f32_e32 v2, v8, v8
	v_add_f32_e32 v0, v0, v2
	v_mul_f32_e32 v2, v21, v21
	v_mul_f32_e32 v3, v23, v23
	v_fmac_f32_e32 v2, v20, v20
	v_fmac_f32_e32 v3, v22, v22
	v_add_f32_e32 v2, v2, v3
	v_add_f32_e32 v0, v0, v2
	v_add_f32_e32 v0, v19, v0
	v_mov_b32_e32 v19, v0
	s_nop 1
	v_permlane16_swap_b32_e32 v19, v0
	v_mov_b32_e32 v26, s12
	v_mov_b32_e32 v2, s10
	v_cndmask_b32_e32 v26, v26, v2, vcc
	v_lshl_add_u64 v[2:3], v[26:27], 0, v[24:25]
	s_waitcnt lgkmcnt(0)
	v_add_f32_e32 v0, v0, v19
	v_lshl_add_u64 v[4:5], v[220:221], 2, v[2:3]
	v_mov_b32_e32 v2, v0
	s_nop 1
	v_permlane32_swap_b32_e32 v2, v0
	global_store_dwordx4 v[4:5], v[14:17], off
	global_store_dwordx4 v[4:5], v[10:13], off offset:16
	global_store_dwordx4 v[4:5], v[6:9], off offset:512
	global_store_dwordx4 v[4:5], v[20:23], off offset:528
	s_and_saveexec_b64 s[10:11], s[40:41]
	s_cbranch_execz .LBB0_2970
	v_lshl_add_u32 v3, v18, 4, s26
	s_waitcnt lgkmcnt(0)
	v_add_f32_e32 v0, v0, v2
	ds_write_b32 v3, v0 offset:6144

.LBB0_2989:
	s_lshl_b32 s24, s48, 5
	s_lshl_b32 s25, s20, 8
	v_lshrrev_b32_e32 v122, 1, v239
	s_add_i32 s4, s78, 64
	s_or_b32 s24, s25, s24
	v_and_or_b32 v220, v122, 24, s24
	s_lshl_b32 s27, s4, 8
	v_add_u32_e32 v222, s27, v224
	v_ashrrev_i32_e32 v221, 31, v220
	v_lshl_add_u64 v[122:123], v[220:221], 1, s[22:23]
	s_mov_b64 s[22:23], 0x1bc00000
	v_ashrrev_i32_e32 v223, 31, v222
	v_lshl_add_u64 v[122:123], v[122:123], 0, s[22:23]
	v_lshlrev_b64 v[124:125], 11, v[222:223]
	v_lshl_add_u64 v[124:125], v[122:123], 0, v[124:125]
	s_barrier
	global_load_dwordx4 v[206:209], v[124:125], off
	global_load_dwordx4 v[202:205], v[124:125], off offset:256
	v_or_b32_e32 v124, 16, v222
	v_ashrrev_i32_e32 v125, 31, v124
	v_lshlrev_b64 v[124:125], 11, v[124:125]
	v_lshl_add_u64 v[124:125], v[122:123], 0, v[124:125]
	global_load_dwordx4 v[198:201], v[124:125], off
	global_load_dwordx4 v[194:197], v[124:125], off offset:256
	v_or_b32_e32 v124, 32, v222
	v_ashrrev_i32_e32 v125, 31, v124
	v_lshlrev_b64 v[124:125], 11, v[124:125]
	v_lshl_add_u64 v[124:125], v[122:123], 0, v[124:125]
	global_load_dwordx4 v[190:193], v[124:125], off
	global_load_dwordx4 v[186:189], v[124:125], off offset:256
	v_or_b32_e32 v124, 48, v222
	v_ashrrev_i32_e32 v125, 31, v124
	v_lshlrev_b64 v[124:125], 11, v[124:125]
	v_lshl_add_u64 v[124:125], v[122:123], 0, v[124:125]
	global_load_dwordx4 v[174:177], v[124:125], off
	global_load_dwordx4 v[162:165], v[124:125], off offset:256
	v_add_u32_e32 v124, 0x80, v222
	v_ashrrev_i32_e32 v125, 31, v124
	v_lshlrev_b64 v[124:125], 11, v[124:125]
	v_lshl_add_u64 v[124:125], v[122:123], 0, v[124:125]
	global_load_dwordx4 v[158:161], v[124:125], off
	global_load_dwordx4 v[154:157], v[124:125], off offset:256
	v_add_u32_e32 v124, 0x90, v222
	v_ashrrev_i32_e32 v125, 31, v124
	v_lshlrev_b64 v[124:125], 11, v[124:125]
	v_lshl_add_u64 v[124:125], v[122:123], 0, v[124:125]
	global_load_dwordx4 v[150:153], v[124:125], off
	global_load_dwordx4 v[146:149], v[124:125], off offset:256
	v_add_u32_e32 v124, 0xa0, v222
	v_ashrrev_i32_e32 v125, 31, v124
	v_lshlrev_b64 v[124:125], 11, v[124:125]
	v_lshl_add_u64 v[124:125], v[122:123], 0, v[124:125]
	global_load_dwordx4 v[142:145], v[124:125], off
	global_load_dwordx4 v[138:141], v[124:125], off offset:256
	v_add_u32_e32 v124, 0xb0, v222
	v_ashrrev_i32_e32 v125, 31, v124
	v_lshlrev_b64 v[124:125], 11, v[124:125]
	v_lshl_add_u64 v[122:123], v[122:123], 0, v[124:125]
	global_load_dwordx4 v[126:129], v[122:123], off
	s_nop 0
	global_load_dwordx4 v[122:125], v[122:123], off offset:256
	v_and_b32_e32 v167, 64, v231
	v_xor_b32_e32 v166, 16, v231
	v_add_u32_e32 v167, 64, v167
	v_cmp_lt_i32_e32 vcc, v166, v167
	v_mul_f32_e32 v168, v137, v137
	v_fmac_f32_e32 v168, v136, v136
	v_cndmask_b32_e32 v166, v231, v166, vcc
	v_lshlrev_b32_e32 v225, 2, v166
	v_mul_f32_e32 v166, v135, v135
	v_fmac_f32_e32 v166, v134, v134
	v_add_f32_e32 v166, v166, v168
	v_mul_f32_e32 v168, v131, v131
	v_mul_f32_e32 v169, v133, v133
	v_fmac_f32_e32 v168, v130, v130
	v_fmac_f32_e32 v169, v132, v132
	v_add_f32_e32 v168, v168, v169
	v_add_f32_e32 v166, v168, v166
	v_mul_f32_e32 v168, v119, v119
	v_mul_f32_e32 v169, v121, v121
	v_fmac_f32_e32 v168, v118, v118
	v_fmac_f32_e32 v169, v120, v120
	v_add_f32_e32 v168, v168, v169
	v_add_f32_e32 v166, v168, v166
	v_mul_f32_e32 v168, v115, v115
	v_mul_f32_e32 v169, v117, v117
	v_fmac_f32_e32 v168, v114, v114
	v_fmac_f32_e32 v169, v116, v116
	v_add_f32_e32 v168, v168, v169
	v_add_f32_e32 v166, v168, v166
	v_mov_b32_e32 v168, v166
	s_nop 1
	v_permlane16_swap_b32_e32 v168, v166
	v_xor_b32_e32 v169, 32, v231
	v_cmp_lt_i32_e32 vcc, v169, v167
	s_lshl_b32 s22, s48, 2
	s_add_i32 s26, s22, 0
	v_cndmask_b32_e32 v167, v231, v169, vcc
	v_lshlrev_b32_e32 v240, 2, v167
	s_waitcnt lgkmcnt(0)
	v_add_f32_e32 v166, v166, v168
	v_mov_b32_e32 v167, v166
	s_nop 1
	v_permlane32_swap_b32_e32 v167, v166
	v_and_b32_e32 v168, 63, v239
	v_cmp_gt_u32_e64 s[38:39], 16, v168
	s_and_saveexec_b64 s[22:23], s[38:39]
	v_readlane_b32 s64, v252, 3
	v_readlane_b32 s65, v255, 10
	v_readlane_b32 s68, v255, 11
	s_cbranch_execz .LBB0_2991
	s_lshl_b32 s24, s47, 10
	s_add_i32 s24, s26, s24
	s_waitcnt lgkmcnt(0)
	v_add_f32_e32 v166, v166, v167
	v_lshl_add_u32 v167, v0, 4, s24
	ds_write_b32 v167, v166
.LBB0_2991:
	s_or_b64 exec, exec, s[22:23]
	v_mul_f32_e32 v166, v111, v111
	s_waitcnt lgkmcnt(0)
	v_mul_f32_e32 v167, v113, v113
	v_fmac_f32_e32 v166, v110, v110
	v_fmac_f32_e32 v167, v112, v112
	v_add_f32_e32 v166, v166, v167
	v_mul_f32_e32 v167, v107, v107
	v_mul_f32_e32 v169, v109, v109
	v_fmac_f32_e32 v167, v106, v106
	v_fmac_f32_e32 v169, v108, v108
	v_add_f32_e32 v167, v167, v169
	v_add_f32_e32 v166, v167, v166
	v_mul_f32_e32 v167, v103, v103
	v_mul_f32_e32 v169, v105, v105
	v_fmac_f32_e32 v167, v102, v102
	v_fmac_f32_e32 v169, v104, v104
	v_add_f32_e32 v167, v167, v169
	v_add_f32_e32 v166, v167, v166
	v_mul_f32_e32 v167, v99, v99
	v_mul_f32_e32 v169, v101, v101
	v_fmac_f32_e32 v167, v98, v98
	v_fmac_f32_e32 v169, v100, v100
	v_add_f32_e32 v167, v167, v169
	v_add_f32_e32 v166, v167, v166
	v_mov_b32_e32 v167, v166
	s_nop 1
	v_permlane16_swap_b32_e32 v167, v166
	s_waitcnt lgkmcnt(0)
	v_add_f32_e32 v166, v166, v167
	v_mov_b32_e32 v167, v166
	s_nop 1
	v_permlane32_swap_b32_e32 v167, v166
	s_and_saveexec_b64 s[22:23], s[38:39]
	v_readlane_b32 s70, v255, 14
	v_readlane_b32 s71, v255, 15
	s_cbranch_execz .LBB0_2993
	s_lshl_b32 s24, s47, 10
	s_add_i32 s24, s26, s24
	s_waitcnt lgkmcnt(0)
	v_add_f32_e32 v166, v166, v167
	v_lshl_add_u32 v167, v0, 4, s24
	ds_write_b32 v167, v166 offset:256
.LBB0_2993:
	s_or_b64 exec, exec, s[22:23]
	v_mul_f32_e32 v166, v95, v95
	s_waitcnt lgkmcnt(0)
	v_mul_f32_e32 v167, v97, v97
	v_fmac_f32_e32 v166, v94, v94
	v_fmac_f32_e32 v167, v96, v96
	v_add_f32_e32 v166, v166, v167
	v_mul_f32_e32 v167, v91, v91
	v_mul_f32_e32 v169, v93, v93
	v_fmac_f32_e32 v167, v90, v90
	v_fmac_f32_e32 v169, v92, v92
	v_add_f32_e32 v167, v167, v169
	v_add_f32_e32 v166, v167, v166
	v_mul_f32_e32 v167, v87, v87
	v_mul_f32_e32 v169, v89, v89
	v_fmac_f32_e32 v167, v86, v86
	v_fmac_f32_e32 v169, v88, v88
	v_add_f32_e32 v167, v167, v169
	v_add_f32_e32 v166, v167, v166
	v_mul_f32_e32 v167, v83, v83
	v_mul_f32_e32 v169, v85, v85
	v_fmac_f32_e32 v167, v82, v82
	v_fmac_f32_e32 v169, v84, v84
	v_add_f32_e32 v167, v167, v169
	v_add_f32_e32 v166, v167, v166
	v_mov_b32_e32 v167, v166
	s_nop 1
	v_permlane16_swap_b32_e32 v167, v166
	s_waitcnt lgkmcnt(0)
	v_add_f32_e32 v166, v166, v167
	v_mov_b32_e32 v167, v166
	s_nop 1
	v_permlane32_swap_b32_e32 v167, v166
	s_and_saveexec_b64 s[22:23], s[38:39]
	s_cbranch_execz .LBB0_2995
	s_lshl_b32 s24, s47, 10
	s_add_i32 s24, s26, s24
	s_waitcnt lgkmcnt(0)
	v_add_f32_e32 v166, v166, v167
	v_lshl_add_u32 v167, v0, 4, s24
	ds_write_b32 v167, v166 offset:512
.LBB0_2995:
	s_or_b64 exec, exec, s[22:23]
	v_mul_f32_e32 v166, v79, v79
	s_waitcnt lgkmcnt(0)
	v_mul_f32_e32 v167, v81, v81
	v_fmac_f32_e32 v166, v78, v78
	v_fmac_f32_e32 v167, v80, v80
	v_add_f32_e32 v166, v166, v167
	v_mul_f32_e32 v167, v75, v75
	v_mul_f32_e32 v169, v77, v77
	v_fmac_f32_e32 v167, v74, v74
	v_fmac_f32_e32 v169, v76, v76
	v_add_f32_e32 v167, v167, v169
	v_add_f32_e32 v166, v167, v166
	v_mul_f32_e32 v167, v71, v71
	v_mul_f32_e32 v169, v73, v73
	v_fmac_f32_e32 v167, v70, v70
	v_fmac_f32_e32 v169, v72, v72
	v_add_f32_e32 v167, v167, v169
	v_add_f32_e32 v166, v167, v166
	v_mul_f32_e32 v167, v67, v67
	v_mul_f32_e32 v169, v69, v69
	v_fmac_f32_e32 v167, v66, v66
	v_fmac_f32_e32 v169, v68, v68
	v_add_f32_e32 v167, v167, v169
	v_add_f32_e32 v166, v167, v166
	v_mov_b32_e32 v167, v166
	s_nop 1
	v_permlane16_swap_b32_e32 v167, v166
	s_waitcnt lgkmcnt(0)
	v_add_f32_e32 v166, v166, v167
	v_mov_b32_e32 v167, v166
	s_nop 1
	v_permlane32_swap_b32_e32 v167, v166
	s_and_saveexec_b64 s[22:23], s[38:39]
	s_cbranch_execz .LBB0_2997
	s_lshl_b32 s24, s47, 10
	s_add_i32 s24, s26, s24
	s_waitcnt lgkmcnt(0)
	v_add_f32_e32 v166, v166, v167
	v_lshl_add_u32 v167, v0, 4, s24
	ds_write_b32 v167, v166 offset:768
.LBB0_2997:
	s_or_b64 exec, exec, s[22:23]
	v_mul_f32_e32 v166, v63, v63
	s_waitcnt lgkmcnt(0)
	v_mul_f32_e32 v167, v65, v65
	v_fmac_f32_e32 v166, v62, v62
	v_fmac_f32_e32 v167, v64, v64
	v_add_f32_e32 v166, v166, v167
	v_mul_f32_e32 v167, v59, v59
	v_mul_f32_e32 v169, v61, v61
	v_fmac_f32_e32 v167, v58, v58
	v_fmac_f32_e32 v169, v60, v60
	v_add_f32_e32 v167, v167, v169
	v_add_f32_e32 v166, v167, v166
	v_mul_f32_e32 v167, v55, v55
	v_mul_f32_e32 v169, v57, v57
	v_fmac_f32_e32 v167, v54, v54
	v_fmac_f32_e32 v169, v56, v56
	v_add_f32_e32 v167, v167, v169
	v_add_f32_e32 v166, v167, v166
	v_mul_f32_e32 v167, v51, v51
	v_mul_f32_e32 v169, v53, v53
	v_fmac_f32_e32 v167, v50, v50
	v_fmac_f32_e32 v169, v52, v52
	v_add_f32_e32 v167, v167, v169
	v_add_f32_e32 v166, v167, v166
	v_mov_b32_e32 v167, v166
	s_nop 1
	v_permlane16_swap_b32_e32 v167, v166
	s_waitcnt lgkmcnt(0)
	v_add_f32_e32 v166, v166, v167
	v_mov_b32_e32 v167, v166
	s_nop 1
	v_permlane32_swap_b32_e32 v167, v166
	s_and_saveexec_b64 s[22:23], s[38:39]
	s_cbranch_execz .LBB0_2999
	s_lshl_b32 s24, s47, 10
	s_add_i32 s24, s26, s24
	s_waitcnt lgkmcnt(0)
	v_add_f32_e32 v166, v166, v167
	v_lshl_add_u32 v167, v0, 4, s24
	ds_write_b32 v167, v166 offset:2048
.LBB0_2999:
	s_or_b64 exec, exec, s[22:23]
	v_mul_f32_e32 v166, v47, v47
	s_waitcnt lgkmcnt(0)
	v_mul_f32_e32 v167, v49, v49
	v_fmac_f32_e32 v166, v46, v46
	v_fmac_f32_e32 v167, v48, v48
	v_add_f32_e32 v166, v166, v167
	v_mul_f32_e32 v167, v43, v43
	v_mul_f32_e32 v169, v45, v45
	v_fmac_f32_e32 v167, v42, v42
	v_fmac_f32_e32 v169, v44, v44
	v_add_f32_e32 v167, v167, v169
	v_add_f32_e32 v166, v167, v166
	v_mul_f32_e32 v167, v39, v39
	v_mul_f32_e32 v169, v41, v41
	v_fmac_f32_e32 v167, v38, v38
	v_fmac_f32_e32 v169, v40, v40
	v_add_f32_e32 v167, v167, v169
	v_add_f32_e32 v166, v167, v166
	v_mul_f32_e32 v167, v35, v35
	v_mul_f32_e32 v169, v37, v37
	v_fmac_f32_e32 v167, v34, v34
	v_fmac_f32_e32 v169, v36, v36
	v_add_f32_e32 v167, v167, v169
	v_add_f32_e32 v166, v167, v166
	v_mov_b32_e32 v167, v166
	s_nop 1
	v_permlane16_swap_b32_e32 v167, v166
	s_waitcnt lgkmcnt(0)
	v_add_f32_e32 v166, v166, v167
	v_mov_b32_e32 v167, v166
	s_nop 1
	v_permlane32_swap_b32_e32 v167, v166
	s_and_saveexec_b64 s[22:23], s[38:39]
	s_cbranch_execz .LBB0_3001
	s_lshl_b32 s24, s47, 10
	s_add_i32 s24, s26, s24
	s_waitcnt lgkmcnt(0)
	v_add_f32_e32 v166, v166, v167
	v_lshl_add_u32 v167, v0, 4, s24
	ds_write_b32 v167, v166 offset:2304
.LBB0_3001:
	s_or_b64 exec, exec, s[22:23]
	v_mul_f32_e32 v166, v31, v31
	s_waitcnt lgkmcnt(0)
	v_mul_f32_e32 v167, v33, v33
	v_fmac_f32_e32 v166, v30, v30
	v_fmac_f32_e32 v167, v32, v32
	v_add_f32_e32 v166, v166, v167
	v_mul_f32_e32 v167, v27, v27
	v_mul_f32_e32 v169, v29, v29
	v_fmac_f32_e32 v167, v26, v26
	v_fmac_f32_e32 v169, v28, v28
	v_add_f32_e32 v167, v167, v169
	v_add_f32_e32 v166, v167, v166
	v_mul_f32_e32 v167, v23, v23
	v_mul_f32_e32 v169, v25, v25
	v_fmac_f32_e32 v167, v22, v22
	v_fmac_f32_e32 v169, v24, v24
	v_add_f32_e32 v167, v167, v169
	v_add_f32_e32 v166, v167, v166
	v_mul_f32_e32 v167, v19, v19
	v_mul_f32_e32 v169, v21, v21
	v_fmac_f32_e32 v167, v18, v18
	v_fmac_f32_e32 v169, v20, v20
	v_add_f32_e32 v167, v167, v169
	v_add_f32_e32 v166, v167, v166
	v_mov_b32_e32 v167, v166
	s_nop 1
	v_permlane16_swap_b32_e32 v167, v166
	s_waitcnt lgkmcnt(0)
	v_add_f32_e32 v166, v166, v167
	v_mov_b32_e32 v167, v166
	s_nop 1
	v_permlane32_swap_b32_e32 v167, v166
	s_and_saveexec_b64 s[22:23], s[38:39]
	s_cbranch_execz .LBB0_3003
	s_lshl_b32 s24, s47, 10
	s_add_i32 s24, s26, s24
	s_waitcnt lgkmcnt(0)
	v_add_f32_e32 v166, v166, v167
	v_lshl_add_u32 v167, v0, 4, s24
	ds_write_b32 v167, v166 offset:2560
.LBB0_3003:
	s_or_b64 exec, exec, s[22:23]
	v_mul_f32_e32 v166, v15, v15
	s_waitcnt lgkmcnt(0)
	v_mul_f32_e32 v167, v17, v17
	v_fmac_f32_e32 v166, v14, v14
	v_fmac_f32_e32 v167, v16, v16
	v_add_f32_e32 v166, v166, v167
	v_mul_f32_e32 v167, v11, v11
	v_mul_f32_e32 v169, v13, v13
	v_fmac_f32_e32 v167, v10, v10
	v_fmac_f32_e32 v169, v12, v12
	v_add_f32_e32 v167, v167, v169
	v_add_f32_e32 v166, v167, v166
	v_mul_f32_e32 v167, v7, v7
	v_mul_f32_e32 v169, v9, v9
	v_fmac_f32_e32 v167, v6, v6
	v_fmac_f32_e32 v169, v8, v8
	v_add_f32_e32 v167, v167, v169
	v_add_f32_e32 v166, v167, v166
	v_mul_f32_e32 v167, v3, v3
	v_mul_f32_e32 v169, v5, v5
	v_fmac_f32_e32 v167, v2, v2
	v_fmac_f32_e32 v169, v4, v4
	v_add_f32_e32 v167, v167, v169
	v_add_f32_e32 v166, v167, v166
	v_mov_b32_e32 v167, v166
	s_nop 1
	v_permlane16_swap_b32_e32 v167, v166
	s_waitcnt lgkmcnt(0)
	v_add_f32_e32 v166, v166, v167
	v_mov_b32_e32 v167, v166
	s_nop 1
	v_permlane32_swap_b32_e32 v167, v166
	s_and_saveexec_b64 s[22:23], s[38:39]
	s_cbranch_execz .LBB0_3005
	s_lshl_b32 s24, s47, 10
	s_add_i32 s24, s26, s24
	s_waitcnt lgkmcnt(0)
	v_add_f32_e32 v166, v166, v167
	v_lshl_add_u32 v0, v0, 4, s24
	ds_write_b32 v0, v166 offset:2816

.LBB0_3031:
	s_waitcnt vmcnt(0)
	v_lshlrev_b32_e32 v218, 16, v206
	v_and_b32_e32 v219, 0xffff0000, v206
	v_lshlrev_b32_e32 v206, 16, v207
	v_and_b32_e32 v207, 0xffff0000, v207
	s_waitcnt lgkmcnt(0)
	v_pk_mul_f32 v[136:137], v[136:137], v[0:1] op_sel_hi:[1,0]
	v_pk_mul_f32 v[134:135], v[134:135], v[0:1] op_sel_hi:[1,0]
	v_pk_fma_f32 v[136:137], v[184:185], v[136:137], v[206:207]
	v_pk_fma_f32 v[134:135], v[182:183], v[134:135], v[218:219]
	v_lshlrev_b32_e32 v242, 16, v208
	v_and_b32_e32 v243, 0xffff0000, v208
	v_lshlrev_b32_e32 v208, 16, v209
	v_and_b32_e32 v209, 0xffff0000, v209
	v_pk_mul_f32 v[132:133], v[132:133], v[0:1] op_sel_hi:[1,0]
	v_pk_mul_f32 v[130:131], v[130:131], v[0:1] op_sel_hi:[1,0]
	v_mul_f32_e32 v206, v135, v135
	v_mul_f32_e32 v207, v137, v137
	v_pk_fma_f32 v[132:133], v[180:181], v[132:133], v[208:209]
	v_pk_fma_f32 v[130:131], v[178:179], v[130:131], v[242:243]
	v_fmac_f32_e32 v206, v134, v134
	v_fmac_f32_e32 v207, v136, v136
	v_add_f32_e32 v206, v206, v207
	v_mul_f32_e32 v207, v131, v131
	v_mul_f32_e32 v208, v133, v133
	v_fmac_f32_e32 v207, v130, v130
	v_fmac_f32_e32 v208, v132, v132
	v_add_f32_e32 v207, v207, v208
	s_movk_i32 s4, 0x4000
	v_add_f32_e32 v206, v206, v207
	v_mov_b32_e32 v207, s13
	v_mov_b32_e32 v208, s11
	v_cmp_gt_i32_e32 vcc, s4, v222
	v_and_b32_e32 v209, 0xffff0000, v202
	v_pk_mul_f32 v[120:121], v[120:121], v[0:1] op_sel_hi:[1,0]
	v_cndmask_b32_e32 v207, v207, v208, vcc
	v_lshlrev_b32_e32 v208, 16, v202
	v_lshlrev_b32_e32 v202, 16, v203
	v_and_b32_e32 v203, 0xffff0000, v203
	v_pk_mul_f32 v[118:119], v[118:119], v[0:1] op_sel_hi:[1,0]
	v_lshlrev_b32_e32 v218, 16, v204
	v_and_b32_e32 v219, 0xffff0000, v204
	v_pk_fma_f32 v[120:121], v[172:173], v[120:121], v[202:203]
	v_pk_fma_f32 v[118:119], v[170:171], v[118:119], v[208:209]
	v_pk_mul_f32 v[114:115], v[114:115], v[0:1] op_sel_hi:[1,0]
	v_lshlrev_b32_e32 v204, 16, v205
	v_and_b32_e32 v205, 0xffff0000, v205
	v_pk_mul_f32 v[116:117], v[116:117], v[0:1] op_sel_hi:[1,0]
	v_pk_fma_f32 v[202:203], v[166:167], v[114:115], v[218:219]
	v_mul_f32_e32 v0, v119, v119
	v_mul_f32_e32 v114, v121, v121
	v_pk_fma_f32 v[204:205], v[168:169], v[116:117], v[204:205]
	v_fmac_f32_e32 v0, v118, v118
	v_fmac_f32_e32 v114, v120, v120
	v_add_f32_e32 v0, v0, v114
	v_mul_f32_e32 v114, v203, v203
	v_mul_f32_e32 v115, v205, v205
	v_fmac_f32_e32 v114, v202, v202
	v_fmac_f32_e32 v115, v204, v204
	v_add_f32_e32 v114, v114, v115
	v_add_f32_e32 v0, v0, v114
	v_add_f32_e32 v0, v206, v0
	v_mov_b32_e32 v208, v0
	s_nop 1
	v_permlane16_swap_b32_e32 v208, v0
	v_lshlrev_b64 v[216:217], 12, v[222:223]
	v_mov_b32_e32 v222, s12
	v_mov_b32_e32 v114, s10
	v_cndmask_b32_e32 v206, v222, v114, vcc
	v_lshl_add_u64 v[114:115], v[206:207], 0, v[216:217]
	s_waitcnt lgkmcnt(0)
	v_add_f32_e32 v0, v0, v208
	v_lshl_add_u64 v[116:117], v[220:221], 2, v[114:115]
	v_mov_b32_e32 v114, v0
	s_nop 1
	v_permlane32_swap_b32_e32 v114, v0
	global_store_dwordx4 v[116:117], v[134:137], off
	global_store_dwordx4 v[116:117], v[130:133], off offset:16
	global_store_dwordx4 v[116:117], v[118:121], off offset:512
	global_store_dwordx4 v[116:117], v[202:205], off offset:528
	s_and_saveexec_b64 s[6:7], s[38:39]
	s_cbranch_execz .LBB0_3033
	v_lshl_add_u32 v115, v224, 4, s26
	s_waitcnt lgkmcnt(0)
	v_add_f32_e32 v0, v0, v114
	ds_write_b32 v115, v0 offset:6144

.LBB0_3035:
	s_waitcnt lgkmcnt(0)
	v_or_b32_e32 v114, 16, v224
	v_add_u32_e32 v116, s27, v114
	v_lshlrev_b32_e32 v118, 16, v198
	v_and_b32_e32 v119, 0xffff0000, v198
	v_lshlrev_b32_e32 v130, 16, v199
	v_and_b32_e32 v131, 0xffff0000, v199
	v_pk_mul_f32 v[112:113], v[112:113], v[0:1] op_sel_hi:[1,0]
	v_pk_mul_f32 v[110:111], v[110:111], v[0:1] op_sel_hi:[1,0]
	v_ashrrev_i32_e32 v117, 31, v116
	v_pk_fma_f32 v[112:113], v[184:185], v[112:113], v[130:131]
	v_pk_fma_f32 v[110:111], v[182:183], v[110:111], v[118:119]
	v_lshlrev_b64 v[120:121], 12, v[116:117]
	v_lshlrev_b32_e32 v132, 16, v200
	v_and_b32_e32 v133, 0xffff0000, v200
	v_lshlrev_b32_e32 v134, 16, v201
	v_and_b32_e32 v135, 0xffff0000, v201
	v_pk_mul_f32 v[108:109], v[108:109], v[0:1] op_sel_hi:[1,0]
	v_pk_mul_f32 v[106:107], v[106:107], v[0:1] op_sel_hi:[1,0]
	v_mul_f32_e32 v115, v111, v111
	v_mul_f32_e32 v117, v113, v113
	v_pk_fma_f32 v[108:109], v[180:181], v[108:109], v[134:135]
	v_pk_fma_f32 v[106:107], v[178:179], v[106:107], v[132:133]
	v_fmac_f32_e32 v115, v110, v110
	v_fmac_f32_e32 v117, v112, v112
	v_add_f32_e32 v115, v115, v117
	v_mul_f32_e32 v117, v107, v107
	v_mul_f32_e32 v118, v109, v109
	v_fmac_f32_e32 v117, v106, v106
	v_fmac_f32_e32 v118, v108, v108
	v_add_f32_e32 v117, v117, v118
	v_add_f32_e32 v115, v115, v117
	v_mov_b32_e32 v117, s13
	v_mov_b32_e32 v118, s11
	v_cmp_gt_i32_e32 vcc, s4, v116
	v_lshlrev_b32_e32 v116, 16, v194
	v_and_b32_e32 v119, 0xffff0000, v195
	v_cndmask_b32_e32 v131, v117, v118, vcc
	v_and_b32_e32 v117, 0xffff0000, v194
	v_lshlrev_b32_e32 v118, 16, v195
	v_pk_mul_f32 v[104:105], v[104:105], v[0:1] op_sel_hi:[1,0]
	v_pk_mul_f32 v[102:103], v[102:103], v[0:1] op_sel_hi:[1,0]
	v_lshlrev_b32_e32 v132, 16, v196
	v_and_b32_e32 v133, 0xffff0000, v196
	v_pk_fma_f32 v[104:105], v[172:173], v[104:105], v[118:119]
	v_pk_fma_f32 v[102:103], v[170:171], v[102:103], v[116:117]
	v_pk_mul_f32 v[98:99], v[98:99], v[0:1] op_sel_hi:[1,0]
	v_lshlrev_b32_e32 v134, 16, v197
	v_and_b32_e32 v135, 0xffff0000, v197
	v_pk_mul_f32 v[100:101], v[100:101], v[0:1] op_sel_hi:[1,0]
	v_pk_fma_f32 v[116:117], v[166:167], v[98:99], v[132:133]
	v_mul_f32_e32 v0, v103, v103
	v_mul_f32_e32 v98, v105, v105
	v_pk_fma_f32 v[118:119], v[168:169], v[100:101], v[134:135]
	v_fmac_f32_e32 v0, v102, v102
	v_fmac_f32_e32 v98, v104, v104
	v_add_f32_e32 v0, v0, v98
	v_mul_f32_e32 v98, v117, v117
	v_mul_f32_e32 v99, v119, v119
	v_fmac_f32_e32 v98, v116, v116
	v_fmac_f32_e32 v99, v118, v118
	v_add_f32_e32 v98, v98, v99
	v_add_f32_e32 v0, v0, v98
	v_add_f32_e32 v0, v115, v0
	v_mov_b32_e32 v115, v0
	s_nop 1
	v_permlane16_swap_b32_e32 v115, v0
	v_mov_b32_e32 v130, s12
	v_mov_b32_e32 v98, s10
	v_cndmask_b32_e32 v130, v130, v98, vcc
	v_lshl_add_u64 v[98:99], v[130:131], 0, v[120:121]
	s_waitcnt lgkmcnt(0)
	v_add_f32_e32 v0, v0, v115
	v_lshl_add_u64 v[100:101], v[220:221], 2, v[98:99]
	v_mov_b32_e32 v98, v0
	s_nop 1
	v_permlane32_swap_b32_e32 v98, v0
	global_store_dwordx4 v[100:101], v[110:113], off
	global_store_dwordx4 v[100:101], v[106:109], off offset:16
	global_store_dwordx4 v[100:101], v[102:105], off offset:512
	global_store_dwordx4 v[100:101], v[116:119], off offset:528
	s_and_saveexec_b64 s[6:7], s[38:39]
	s_cbranch_execz .LBB0_3037
	v_lshl_add_u32 v99, v114, 4, s26
	s_waitcnt lgkmcnt(0)
	v_add_f32_e32 v0, v0, v98
	ds_write_b32 v99, v0 offset:6144

.LBB0_3039:
	s_waitcnt lgkmcnt(0)
	v_or_b32_e32 v98, 32, v224
	v_add_u32_e32 v100, s27, v98
	v_lshlrev_b32_e32 v102, 16, v190
	v_and_b32_e32 v103, 0xffff0000, v190
	v_lshlrev_b32_e32 v106, 16, v191
	v_and_b32_e32 v107, 0xffff0000, v191
	v_pk_mul_f32 v[96:97], v[96:97], v[0:1] op_sel_hi:[1,0]
	v_pk_mul_f32 v[94:95], v[94:95], v[0:1] op_sel_hi:[1,0]
	v_ashrrev_i32_e32 v101, 31, v100
	v_pk_fma_f32 v[96:97], v[184:185], v[96:97], v[106:107]
	v_pk_fma_f32 v[94:95], v[182:183], v[94:95], v[102:103]
	v_lshlrev_b64 v[104:105], 12, v[100:101]
	v_lshlrev_b32_e32 v108, 16, v192
	v_and_b32_e32 v109, 0xffff0000, v192
	v_lshlrev_b32_e32 v110, 16, v193
	v_and_b32_e32 v111, 0xffff0000, v193
	v_pk_mul_f32 v[92:93], v[92:93], v[0:1] op_sel_hi:[1,0]
	v_pk_mul_f32 v[90:91], v[90:91], v[0:1] op_sel_hi:[1,0]
	v_mul_f32_e32 v99, v95, v95
	v_mul_f32_e32 v101, v97, v97
	v_pk_fma_f32 v[92:93], v[180:181], v[92:93], v[110:111]
	v_pk_fma_f32 v[90:91], v[178:179], v[90:91], v[108:109]
	v_fmac_f32_e32 v99, v94, v94
	v_fmac_f32_e32 v101, v96, v96
	v_add_f32_e32 v99, v99, v101
	v_mul_f32_e32 v101, v91, v91
	v_mul_f32_e32 v102, v93, v93
	v_fmac_f32_e32 v101, v90, v90
	v_fmac_f32_e32 v102, v92, v92
	v_add_f32_e32 v101, v101, v102
	v_add_f32_e32 v99, v99, v101
	v_mov_b32_e32 v101, s13
	v_mov_b32_e32 v102, s11
	v_cmp_gt_i32_e32 vcc, s4, v100
	v_lshlrev_b32_e32 v100, 16, v186
	v_and_b32_e32 v103, 0xffff0000, v187
	v_cndmask_b32_e32 v107, v101, v102, vcc
	v_and_b32_e32 v101, 0xffff0000, v186
	v_lshlrev_b32_e32 v102, 16, v187
	v_pk_mul_f32 v[88:89], v[88:89], v[0:1] op_sel_hi:[1,0]
	v_pk_mul_f32 v[86:87], v[86:87], v[0:1] op_sel_hi:[1,0]
	v_lshlrev_b32_e32 v108, 16, v188
	v_and_b32_e32 v109, 0xffff0000, v188
	v_pk_fma_f32 v[88:89], v[172:173], v[88:89], v[102:103]
	v_pk_fma_f32 v[86:87], v[170:171], v[86:87], v[100:101]
	v_pk_mul_f32 v[82:83], v[82:83], v[0:1] op_sel_hi:[1,0]
	v_lshlrev_b32_e32 v110, 16, v189
	v_and_b32_e32 v111, 0xffff0000, v189
	v_pk_mul_f32 v[84:85], v[84:85], v[0:1] op_sel_hi:[1,0]
	v_pk_fma_f32 v[100:101], v[166:167], v[82:83], v[108:109]
	v_mul_f32_e32 v0, v87, v87
	v_mul_f32_e32 v82, v89, v89
	v_pk_fma_f32 v[102:103], v[168:169], v[84:85], v[110:111]
	v_fmac_f32_e32 v0, v86, v86
	v_fmac_f32_e32 v82, v88, v88
	v_add_f32_e32 v0, v0, v82
	v_mul_f32_e32 v82, v101, v101
	v_mul_f32_e32 v83, v103, v103
	v_fmac_f32_e32 v82, v100, v100
	v_fmac_f32_e32 v83, v102, v102
	v_add_f32_e32 v82, v82, v83
	v_add_f32_e32 v0, v0, v82
	v_add_f32_e32 v0, v99, v0
	v_mov_b32_e32 v99, v0
	s_nop 1
	v_permlane16_swap_b32_e32 v99, v0
	v_mov_b32_e32 v106, s12
	v_mov_b32_e32 v82, s10
	v_cndmask_b32_e32 v106, v106, v82, vcc
	v_lshl_add_u64 v[82:83], v[106:107], 0, v[104:105]
	s_waitcnt lgkmcnt(0)
	v_add_f32_e32 v0, v0, v99
	v_lshl_add_u64 v[84:85], v[220:221], 2, v[82:83]
	v_mov_b32_e32 v82, v0
	s_nop 1
	v_permlane32_swap_b32_e32 v82, v0
	global_store_dwordx4 v[84:85], v[94:97], off
	global_store_dwordx4 v[84:85], v[90:93], off offset:16
	global_store_dwordx4 v[84:85], v[86:89], off offset:512
	global_store_dwordx4 v[84:85], v[100:103], off offset:528
	s_and_saveexec_b64 s[6:7], s[38:39]
	s_cbranch_execz .LBB0_3041
	v_lshl_add_u32 v83, v98, 4, s26
	s_waitcnt lgkmcnt(0)
	v_add_f32_e32 v0, v0, v82
	ds_write_b32 v83, v0 offset:6144

.LBB0_3043:
	s_waitcnt lgkmcnt(0)
	v_or_b32_e32 v82, 48, v224
	v_add_u32_e32 v84, s27, v82
	v_lshlrev_b32_e32 v86, 16, v174
	v_and_b32_e32 v87, 0xffff0000, v174
	v_lshlrev_b32_e32 v90, 16, v175
	v_and_b32_e32 v91, 0xffff0000, v175
	v_pk_mul_f32 v[80:81], v[80:81], v[0:1] op_sel_hi:[1,0]
	v_pk_mul_f32 v[78:79], v[78:79], v[0:1] op_sel_hi:[1,0]
	v_ashrrev_i32_e32 v85, 31, v84
	v_pk_fma_f32 v[80:81], v[184:185], v[80:81], v[90:91]
	v_pk_fma_f32 v[78:79], v[182:183], v[78:79], v[86:87]
	v_lshlrev_b64 v[88:89], 12, v[84:85]
	v_lshlrev_b32_e32 v92, 16, v176
	v_and_b32_e32 v93, 0xffff0000, v176
	v_lshlrev_b32_e32 v94, 16, v177
	v_and_b32_e32 v95, 0xffff0000, v177
	v_pk_mul_f32 v[76:77], v[76:77], v[0:1] op_sel_hi:[1,0]
	v_pk_mul_f32 v[74:75], v[74:75], v[0:1] op_sel_hi:[1,0]
	v_mul_f32_e32 v83, v79, v79
	v_mul_f32_e32 v85, v81, v81
	v_pk_fma_f32 v[76:77], v[180:181], v[76:77], v[94:95]
	v_pk_fma_f32 v[74:75], v[178:179], v[74:75], v[92:93]
	v_fmac_f32_e32 v83, v78, v78
	v_fmac_f32_e32 v85, v80, v80
	v_add_f32_e32 v83, v83, v85
	v_mul_f32_e32 v85, v75, v75
	v_mul_f32_e32 v86, v77, v77
	v_fmac_f32_e32 v85, v74, v74
	v_fmac_f32_e32 v86, v76, v76
	v_add_f32_e32 v85, v85, v86
	v_add_f32_e32 v83, v83, v85
	v_mov_b32_e32 v85, s13
	v_mov_b32_e32 v86, s11
	v_cmp_gt_i32_e32 vcc, s4, v84
	v_lshlrev_b32_e32 v84, 16, v162
	v_and_b32_e32 v87, 0xffff0000, v163
	v_cndmask_b32_e32 v91, v85, v86, vcc
	v_and_b32_e32 v85, 0xffff0000, v162
	v_lshlrev_b32_e32 v86, 16, v163
	v_pk_mul_f32 v[72:73], v[72:73], v[0:1] op_sel_hi:[1,0]
	v_pk_mul_f32 v[70:71], v[70:71], v[0:1] op_sel_hi:[1,0]
	v_lshlrev_b32_e32 v92, 16, v164
	v_and_b32_e32 v93, 0xffff0000, v164
	v_pk_fma_f32 v[72:73], v[172:173], v[72:73], v[86:87]
	v_pk_fma_f32 v[70:71], v[170:171], v[70:71], v[84:85]
	v_pk_mul_f32 v[66:67], v[66:67], v[0:1] op_sel_hi:[1,0]
	v_lshlrev_b32_e32 v94, 16, v165
	v_and_b32_e32 v95, 0xffff0000, v165
	v_pk_mul_f32 v[68:69], v[68:69], v[0:1] op_sel_hi:[1,0]
	v_pk_fma_f32 v[84:85], v[166:167], v[66:67], v[92:93]
	v_mul_f32_e32 v0, v71, v71
	v_mul_f32_e32 v66, v73, v73
	v_pk_fma_f32 v[86:87], v[168:169], v[68:69], v[94:95]
	v_fmac_f32_e32 v0, v70, v70
	v_fmac_f32_e32 v66, v72, v72
	v_add_f32_e32 v0, v0, v66
	v_mul_f32_e32 v66, v85, v85
	v_mul_f32_e32 v67, v87, v87
	v_fmac_f32_e32 v66, v84, v84
	v_fmac_f32_e32 v67, v86, v86
	v_add_f32_e32 v66, v66, v67
	v_add_f32_e32 v0, v0, v66
	v_add_f32_e32 v0, v83, v0
	v_mov_b32_e32 v83, v0
	s_nop 1
	v_permlane16_swap_b32_e32 v83, v0
	v_mov_b32_e32 v90, s12
	v_mov_b32_e32 v66, s10
	v_cndmask_b32_e32 v90, v90, v66, vcc
	v_lshl_add_u64 v[66:67], v[90:91], 0, v[88:89]
	s_waitcnt lgkmcnt(0)
	v_add_f32_e32 v0, v0, v83
	v_lshl_add_u64 v[68:69], v[220:221], 2, v[66:67]
	v_mov_b32_e32 v66, v0
	s_nop 1
	v_permlane32_swap_b32_e32 v66, v0
	global_store_dwordx4 v[68:69], v[78:81], off
	global_store_dwordx4 v[68:69], v[74:77], off offset:16
	global_store_dwordx4 v[68:69], v[70:73], off offset:512
	global_store_dwordx4 v[68:69], v[84:87], off offset:528
	s_and_saveexec_b64 s[6:7], s[38:39]
	s_cbranch_execz .LBB0_3045
	v_lshl_add_u32 v67, v82, 4, s26
	s_waitcnt lgkmcnt(0)
	v_add_f32_e32 v0, v0, v66
	ds_write_b32 v67, v0 offset:6144

.LBB0_3047:
	s_waitcnt lgkmcnt(0)
	v_add_u32_e32 v66, 0x80, v224
	v_add_u32_e32 v68, s27, v66
	v_lshlrev_b32_e32 v70, 16, v158
	v_and_b32_e32 v71, 0xffff0000, v158
	v_lshlrev_b32_e32 v74, 16, v159
	v_and_b32_e32 v75, 0xffff0000, v159
	v_pk_mul_f32 v[64:65], v[64:65], v[0:1] op_sel_hi:[1,0]
	v_pk_mul_f32 v[62:63], v[62:63], v[0:1] op_sel_hi:[1,0]
	v_ashrrev_i32_e32 v69, 31, v68
	v_pk_fma_f32 v[64:65], v[184:185], v[64:65], v[74:75]
	v_pk_fma_f32 v[62:63], v[182:183], v[62:63], v[70:71]
	v_lshlrev_b64 v[72:73], 12, v[68:69]
	v_lshlrev_b32_e32 v76, 16, v160
	v_and_b32_e32 v77, 0xffff0000, v160
	v_lshlrev_b32_e32 v78, 16, v161
	v_and_b32_e32 v79, 0xffff0000, v161
	v_pk_mul_f32 v[60:61], v[60:61], v[0:1] op_sel_hi:[1,0]
	v_pk_mul_f32 v[58:59], v[58:59], v[0:1] op_sel_hi:[1,0]
	v_mul_f32_e32 v67, v63, v63
	v_mul_f32_e32 v69, v65, v65
	v_pk_fma_f32 v[60:61], v[180:181], v[60:61], v[78:79]
	v_pk_fma_f32 v[58:59], v[178:179], v[58:59], v[76:77]
	v_fmac_f32_e32 v67, v62, v62
	v_fmac_f32_e32 v69, v64, v64
	v_add_f32_e32 v67, v67, v69
	v_mul_f32_e32 v69, v59, v59
	v_mul_f32_e32 v70, v61, v61
	v_fmac_f32_e32 v69, v58, v58
	v_fmac_f32_e32 v70, v60, v60
	v_add_f32_e32 v69, v69, v70
	v_add_f32_e32 v67, v67, v69
	v_mov_b32_e32 v69, s13
	v_mov_b32_e32 v70, s11
	v_cmp_gt_i32_e32 vcc, s4, v68
	v_lshlrev_b32_e32 v68, 16, v154
	v_and_b32_e32 v71, 0xffff0000, v155
	v_cndmask_b32_e32 v75, v69, v70, vcc
	v_and_b32_e32 v69, 0xffff0000, v154
	v_lshlrev_b32_e32 v70, 16, v155
	v_pk_mul_f32 v[56:57], v[56:57], v[0:1] op_sel_hi:[1,0]
	v_pk_mul_f32 v[54:55], v[54:55], v[0:1] op_sel_hi:[1,0]
	v_lshlrev_b32_e32 v76, 16, v156
	v_and_b32_e32 v77, 0xffff0000, v156
	v_pk_fma_f32 v[56:57], v[172:173], v[56:57], v[70:71]
	v_pk_fma_f32 v[54:55], v[170:171], v[54:55], v[68:69]
	v_pk_mul_f32 v[50:51], v[50:51], v[0:1] op_sel_hi:[1,0]
	v_lshlrev_b32_e32 v78, 16, v157
	v_and_b32_e32 v79, 0xffff0000, v157
	v_pk_mul_f32 v[52:53], v[52:53], v[0:1] op_sel_hi:[1,0]
	v_pk_fma_f32 v[68:69], v[166:167], v[50:51], v[76:77]
	v_mul_f32_e32 v0, v55, v55
	v_mul_f32_e32 v50, v57, v57
	v_pk_fma_f32 v[70:71], v[168:169], v[52:53], v[78:79]
	v_fmac_f32_e32 v0, v54, v54
	v_fmac_f32_e32 v50, v56, v56
	v_add_f32_e32 v0, v0, v50
	v_mul_f32_e32 v50, v69, v69
	v_mul_f32_e32 v51, v71, v71
	v_fmac_f32_e32 v50, v68, v68
	v_fmac_f32_e32 v51, v70, v70
	v_add_f32_e32 v50, v50, v51
	v_add_f32_e32 v0, v0, v50
	v_add_f32_e32 v0, v67, v0
	v_mov_b32_e32 v67, v0
	s_nop 1
	v_permlane16_swap_b32_e32 v67, v0
	v_mov_b32_e32 v74, s12
	v_mov_b32_e32 v50, s10
	v_cndmask_b32_e32 v74, v74, v50, vcc
	v_lshl_add_u64 v[50:51], v[74:75], 0, v[72:73]
	s_waitcnt lgkmcnt(0)
	v_add_f32_e32 v0, v0, v67
	v_lshl_add_u64 v[52:53], v[220:221], 2, v[50:51]
	v_mov_b32_e32 v50, v0
	s_nop 1
	v_permlane32_swap_b32_e32 v50, v0
	global_store_dwordx4 v[52:53], v[62:65], off
	global_store_dwordx4 v[52:53], v[58:61], off offset:16
	global_store_dwordx4 v[52:53], v[54:57], off offset:512
	global_store_dwordx4 v[52:53], v[68:71], off offset:528
	s_and_saveexec_b64 s[6:7], s[38:39]
	s_cbranch_execz .LBB0_3049
	v_lshl_add_u32 v51, v66, 4, s26
	s_waitcnt lgkmcnt(0)
	v_add_f32_e32 v0, v0, v50
	ds_write_b32 v51, v0 offset:6144

.LBB0_3051:
	s_waitcnt lgkmcnt(0)
	v_add_u32_e32 v50, 0x90, v224
	v_add_u32_e32 v52, s27, v50
	v_lshlrev_b32_e32 v54, 16, v150
	v_and_b32_e32 v55, 0xffff0000, v150
	v_lshlrev_b32_e32 v58, 16, v151
	v_and_b32_e32 v59, 0xffff0000, v151
	v_pk_mul_f32 v[48:49], v[48:49], v[0:1] op_sel_hi:[1,0]
	v_pk_mul_f32 v[46:47], v[46:47], v[0:1] op_sel_hi:[1,0]
	v_ashrrev_i32_e32 v53, 31, v52
	v_pk_fma_f32 v[48:49], v[184:185], v[48:49], v[58:59]
	v_pk_fma_f32 v[46:47], v[182:183], v[46:47], v[54:55]
	v_lshlrev_b64 v[56:57], 12, v[52:53]
	v_lshlrev_b32_e32 v60, 16, v152
	v_and_b32_e32 v61, 0xffff0000, v152
	v_lshlrev_b32_e32 v62, 16, v153
	v_and_b32_e32 v63, 0xffff0000, v153
	v_pk_mul_f32 v[44:45], v[44:45], v[0:1] op_sel_hi:[1,0]
	v_pk_mul_f32 v[42:43], v[42:43], v[0:1] op_sel_hi:[1,0]
	v_mul_f32_e32 v51, v47, v47
	v_mul_f32_e32 v53, v49, v49
	v_pk_fma_f32 v[44:45], v[180:181], v[44:45], v[62:63]
	v_pk_fma_f32 v[42:43], v[178:179], v[42:43], v[60:61]
	v_fmac_f32_e32 v51, v46, v46
	v_fmac_f32_e32 v53, v48, v48
	v_add_f32_e32 v51, v51, v53
	v_mul_f32_e32 v53, v43, v43
	v_mul_f32_e32 v54, v45, v45
	v_fmac_f32_e32 v53, v42, v42
	v_fmac_f32_e32 v54, v44, v44
	v_add_f32_e32 v53, v53, v54
	v_add_f32_e32 v51, v51, v53
	v_mov_b32_e32 v53, s13
	v_mov_b32_e32 v54, s11
	v_cmp_gt_i32_e32 vcc, s4, v52
	v_lshlrev_b32_e32 v52, 16, v146
	v_and_b32_e32 v55, 0xffff0000, v147
	v_cndmask_b32_e32 v59, v53, v54, vcc
	v_and_b32_e32 v53, 0xffff0000, v146
	v_lshlrev_b32_e32 v54, 16, v147
	v_pk_mul_f32 v[40:41], v[40:41], v[0:1] op_sel_hi:[1,0]
	v_pk_mul_f32 v[38:39], v[38:39], v[0:1] op_sel_hi:[1,0]
	v_lshlrev_b32_e32 v60, 16, v148
	v_and_b32_e32 v61, 0xffff0000, v148
	v_pk_fma_f32 v[40:41], v[172:173], v[40:41], v[54:55]
	v_pk_fma_f32 v[38:39], v[170:171], v[38:39], v[52:53]
	v_pk_mul_f32 v[34:35], v[34:35], v[0:1] op_sel_hi:[1,0]
	v_lshlrev_b32_e32 v62, 16, v149
	v_and_b32_e32 v63, 0xffff0000, v149
	v_pk_mul_f32 v[36:37], v[36:37], v[0:1] op_sel_hi:[1,0]
	v_pk_fma_f32 v[52:53], v[166:167], v[34:35], v[60:61]
	v_mul_f32_e32 v0, v39, v39
	v_mul_f32_e32 v34, v41, v41
	v_pk_fma_f32 v[54:55], v[168:169], v[36:37], v[62:63]
	v_fmac_f32_e32 v0, v38, v38
	v_fmac_f32_e32 v34, v40, v40
	v_add_f32_e32 v0, v0, v34
	v_mul_f32_e32 v34, v53, v53
	v_mul_f32_e32 v35, v55, v55
	v_fmac_f32_e32 v34, v52, v52
	v_fmac_f32_e32 v35, v54, v54
	v_add_f32_e32 v34, v34, v35
	v_add_f32_e32 v0, v0, v34
	v_add_f32_e32 v0, v51, v0
	v_mov_b32_e32 v51, v0
	s_nop 1
	v_permlane16_swap_b32_e32 v51, v0
	v_mov_b32_e32 v58, s12
	v_mov_b32_e32 v34, s10
	v_cndmask_b32_e32 v58, v58, v34, vcc
	v_lshl_add_u64 v[34:35], v[58:59], 0, v[56:57]
	s_waitcnt lgkmcnt(0)
	v_add_f32_e32 v0, v0, v51
	v_lshl_add_u64 v[36:37], v[220:221], 2, v[34:35]
	v_mov_b32_e32 v34, v0
	s_nop 1
	v_permlane32_swap_b32_e32 v34, v0
	global_store_dwordx4 v[36:37], v[46:49], off
	global_store_dwordx4 v[36:37], v[42:45], off offset:16
	global_store_dwordx4 v[36:37], v[38:41], off offset:512
	global_store_dwordx4 v[36:37], v[52:55], off offset:528
	s_and_saveexec_b64 s[6:7], s[38:39]
	s_cbranch_execz .LBB0_3053
	v_lshl_add_u32 v35, v50, 4, s26
	s_waitcnt lgkmcnt(0)
	v_add_f32_e32 v0, v0, v34
	ds_write_b32 v35, v0 offset:6144

.LBB0_3055:
	s_waitcnt lgkmcnt(0)
	v_add_u32_e32 v34, 0xa0, v224
	v_add_u32_e32 v36, s27, v34
	v_lshlrev_b32_e32 v38, 16, v142
	v_and_b32_e32 v39, 0xffff0000, v142
	v_lshlrev_b32_e32 v42, 16, v143
	v_and_b32_e32 v43, 0xffff0000, v143
	v_pk_mul_f32 v[32:33], v[32:33], v[0:1] op_sel_hi:[1,0]
	v_pk_mul_f32 v[30:31], v[30:31], v[0:1] op_sel_hi:[1,0]
	v_ashrrev_i32_e32 v37, 31, v36
	v_pk_fma_f32 v[32:33], v[184:185], v[32:33], v[42:43]
	v_pk_fma_f32 v[30:31], v[182:183], v[30:31], v[38:39]
	v_lshlrev_b64 v[40:41], 12, v[36:37]
	v_lshlrev_b32_e32 v44, 16, v144
	v_and_b32_e32 v45, 0xffff0000, v144
	v_lshlrev_b32_e32 v46, 16, v145
	v_and_b32_e32 v47, 0xffff0000, v145
	v_pk_mul_f32 v[28:29], v[28:29], v[0:1] op_sel_hi:[1,0]
	v_pk_mul_f32 v[26:27], v[26:27], v[0:1] op_sel_hi:[1,0]
	v_mul_f32_e32 v35, v31, v31
	v_mul_f32_e32 v37, v33, v33
	v_pk_fma_f32 v[28:29], v[180:181], v[28:29], v[46:47]
	v_pk_fma_f32 v[26:27], v[178:179], v[26:27], v[44:45]
	v_fmac_f32_e32 v35, v30, v30
	v_fmac_f32_e32 v37, v32, v32
	v_add_f32_e32 v35, v35, v37
	v_mul_f32_e32 v37, v27, v27
	v_mul_f32_e32 v38, v29, v29
	v_fmac_f32_e32 v37, v26, v26
	v_fmac_f32_e32 v38, v28, v28
	v_add_f32_e32 v37, v37, v38
	v_add_f32_e32 v35, v35, v37
	v_mov_b32_e32 v37, s13
	v_mov_b32_e32 v38, s11
	v_cmp_gt_i32_e32 vcc, s4, v36
	v_lshlrev_b32_e32 v36, 16, v138
	v_and_b32_e32 v39, 0xffff0000, v139
	v_cndmask_b32_e32 v43, v37, v38, vcc
	v_and_b32_e32 v37, 0xffff0000, v138
	v_lshlrev_b32_e32 v38, 16, v139
	v_pk_mul_f32 v[24:25], v[24:25], v[0:1] op_sel_hi:[1,0]
	v_pk_mul_f32 v[22:23], v[22:23], v[0:1] op_sel_hi:[1,0]
	v_lshlrev_b32_e32 v44, 16, v140
	v_and_b32_e32 v45, 0xffff0000, v140
	v_pk_fma_f32 v[24:25], v[172:173], v[24:25], v[38:39]
	v_pk_fma_f32 v[22:23], v[170:171], v[22:23], v[36:37]
	v_pk_mul_f32 v[18:19], v[18:19], v[0:1] op_sel_hi:[1,0]
	v_lshlrev_b32_e32 v46, 16, v141
	v_and_b32_e32 v47, 0xffff0000, v141
	v_pk_mul_f32 v[20:21], v[20:21], v[0:1] op_sel_hi:[1,0]
	v_pk_fma_f32 v[36:37], v[166:167], v[18:19], v[44:45]
	v_mul_f32_e32 v0, v23, v23
	v_mul_f32_e32 v18, v25, v25
	v_pk_fma_f32 v[38:39], v[168:169], v[20:21], v[46:47]
	v_fmac_f32_e32 v0, v22, v22
	v_fmac_f32_e32 v18, v24, v24
	v_add_f32_e32 v0, v0, v18
	v_mul_f32_e32 v18, v37, v37
	v_mul_f32_e32 v19, v39, v39
	v_fmac_f32_e32 v18, v36, v36
	v_fmac_f32_e32 v19, v38, v38
	v_add_f32_e32 v18, v18, v19
	v_add_f32_e32 v0, v0, v18
	v_add_f32_e32 v0, v35, v0
	v_mov_b32_e32 v35, v0
	s_nop 1
	v_permlane16_swap_b32_e32 v35, v0
	v_mov_b32_e32 v42, s12
	v_mov_b32_e32 v18, s10
	v_cndmask_b32_e32 v42, v42, v18, vcc
	v_lshl_add_u64 v[18:19], v[42:43], 0, v[40:41]
	s_waitcnt lgkmcnt(0)
	v_add_f32_e32 v0, v0, v35
	v_lshl_add_u64 v[20:21], v[220:221], 2, v[18:19]
	v_mov_b32_e32 v18, v0
	s_nop 1
	v_permlane32_swap_b32_e32 v18, v0
	global_store_dwordx4 v[20:21], v[30:33], off
	global_store_dwordx4 v[20:21], v[26:29], off offset:16
	global_store_dwordx4 v[20:21], v[22:25], off offset:512
	global_store_dwordx4 v[20:21], v[36:39], off offset:528
	s_and_saveexec_b64 s[6:7], s[38:39]
	s_cbranch_execz .LBB0_3057
	v_lshl_add_u32 v19, v34, 4, s26
	s_waitcnt lgkmcnt(0)
	v_add_f32_e32 v0, v0, v18
	ds_write_b32 v19, v0 offset:6144

.LBB0_3059:
	s_waitcnt lgkmcnt(0)
	v_add_u32_e32 v18, 0xb0, v224
	v_add_u32_e32 v20, s27, v18
	v_lshlrev_b32_e32 v22, 16, v126
	v_and_b32_e32 v23, 0xffff0000, v126
	v_lshlrev_b32_e32 v26, 16, v127
	v_and_b32_e32 v27, 0xffff0000, v127
	v_pk_mul_f32 v[16:17], v[16:17], v[0:1] op_sel_hi:[1,0]
	v_pk_mul_f32 v[14:15], v[14:15], v[0:1] op_sel_hi:[1,0]
	v_ashrrev_i32_e32 v21, 31, v20
	v_pk_fma_f32 v[16:17], v[184:185], v[16:17], v[26:27]
	v_pk_fma_f32 v[14:15], v[182:183], v[14:15], v[22:23]
	v_lshlrev_b64 v[24:25], 12, v[20:21]
	v_lshlrev_b32_e32 v28, 16, v128
	v_and_b32_e32 v29, 0xffff0000, v128
	v_lshlrev_b32_e32 v30, 16, v129
	v_and_b32_e32 v31, 0xffff0000, v129
	v_pk_mul_f32 v[12:13], v[12:13], v[0:1] op_sel_hi:[1,0]
	v_pk_mul_f32 v[10:11], v[10:11], v[0:1] op_sel_hi:[1,0]
	v_mul_f32_e32 v19, v15, v15
	v_mul_f32_e32 v21, v17, v17
	v_pk_fma_f32 v[12:13], v[180:181], v[12:13], v[30:31]
	v_pk_fma_f32 v[10:11], v[178:179], v[10:11], v[28:29]
	v_fmac_f32_e32 v19, v14, v14
	v_fmac_f32_e32 v21, v16, v16
	v_add_f32_e32 v19, v19, v21
	v_mul_f32_e32 v21, v11, v11
	v_mul_f32_e32 v22, v13, v13
	v_fmac_f32_e32 v21, v10, v10
	v_fmac_f32_e32 v22, v12, v12
	v_add_f32_e32 v21, v21, v22
	v_add_f32_e32 v19, v19, v21
	v_mov_b32_e32 v21, s13
	v_mov_b32_e32 v22, s11
	v_cmp_gt_i32_e32 vcc, s4, v20
	v_lshlrev_b32_e32 v20, 16, v122
	v_and_b32_e32 v23, 0xffff0000, v123
	v_cndmask_b32_e32 v27, v21, v22, vcc
	v_and_b32_e32 v21, 0xffff0000, v122
	v_lshlrev_b32_e32 v22, 16, v123
	v_pk_mul_f32 v[8:9], v[8:9], v[0:1] op_sel_hi:[1,0]
	v_pk_mul_f32 v[6:7], v[6:7], v[0:1] op_sel_hi:[1,0]
	v_lshlrev_b32_e32 v28, 16, v124
	v_and_b32_e32 v29, 0xffff0000, v124
	v_pk_fma_f32 v[8:9], v[172:173], v[8:9], v[22:23]
	v_pk_fma_f32 v[6:7], v[170:171], v[6:7], v[20:21]
	v_pk_mul_f32 v[2:3], v[2:3], v[0:1] op_sel_hi:[1,0]
	v_lshlrev_b32_e32 v30, 16, v125
	v_and_b32_e32 v31, 0xffff0000, v125
	v_pk_mul_f32 v[4:5], v[4:5], v[0:1] op_sel_hi:[1,0]
	v_pk_fma_f32 v[20:21], v[166:167], v[2:3], v[28:29]
	v_mul_f32_e32 v0, v7, v7
	v_mul_f32_e32 v2, v9, v9
	v_pk_fma_f32 v[22:23], v[168:169], v[4:5], v[30:31]
	v_fmac_f32_e32 v0, v6, v6
	v_fmac_f32_e32 v2, v8, v8
	v_add_f32_e32 v0, v0, v2
	v_mul_f32_e32 v2, v21, v21
	v_mul_f32_e32 v3, v23, v23
	v_fmac_f32_e32 v2, v20, v20
	v_fmac_f32_e32 v3, v22, v22
	v_add_f32_e32 v2, v2, v3
	v_add_f32_e32 v0, v0, v2
	v_add_f32_e32 v0, v19, v0
	v_mov_b32_e32 v19, v0
	s_nop 1
	v_permlane16_swap_b32_e32 v19, v0
	v_mov_b32_e32 v26, s12
	v_mov_b32_e32 v2, s10
	v_cndmask_b32_e32 v26, v26, v2, vcc
	v_lshl_add_u64 v[2:3], v[26:27], 0, v[24:25]
	s_waitcnt lgkmcnt(0)
	v_add_f32_e32 v0, v0, v19
	v_lshl_add_u64 v[4:5], v[220:221], 2, v[2:3]
	v_mov_b32_e32 v2, v0
	s_nop 1
	v_permlane32_swap_b32_e32 v2, v0
	global_store_dwordx4 v[4:5], v[14:17], off
	global_store_dwordx4 v[4:5], v[10:13], off offset:16
	global_store_dwordx4 v[4:5], v[6:9], off offset:512
	global_store_dwordx4 v[4:5], v[20:23], off offset:528
	s_and_saveexec_b64 s[6:7], s[38:39]
	s_cbranch_execz .LBB0_3061
	v_lshl_add_u32 v3, v18, 4, s26
	s_waitcnt lgkmcnt(0)
	v_add_f32_e32 v0, v0, v2
	ds_write_b32 v3, v0 offset:6144
